# speedup vs baseline: 1.0345x; 1.0345x over previous
.LBB0_23:
	s_cbranch_execz .LBB0_3
	s_branch .LBB0_4
	.p2alignl 8, 3212836864

.LBB1_13:
	s_endpgm
	.p2alignl 8, 3212836864

_Z10scan_pass1PKDF16_S0_PKfS0_S2_S2_PDF16_PfS4_S2_S3_:
	s_mov_b32 s5, s3
	s_load_dwordx8 s[16:23], s[0:1], 0x0
	s_lshl_b32 s3, s4, 11
	s_lshl_b32 s6, s5, 5
	v_and_b32_e32 v60, 63, v0
	s_add_i32 s6, s3, s6
	v_lshl_or_b32 v14, s6, 3, v60
	v_and_b32_e32 v1, 0xc0, v0
	v_ashrrev_i32_e32 v15, 31, v14
	v_lshl_or_b32 v61, s2, 8, v1
	s_waitcnt lgkmcnt(0)
	v_lshl_add_u64 v[2:3], v[14:15], 4, s[16:17]
	global_load_dwordx4 v[2:5], v[2:3], off
	v_lshl_or_b32 v56, v61, 3, v60
	v_or_b32_e32 v10, 0x100, v56
	v_ashrrev_i32_e32 v57, 31, v56
	v_ashrrev_i32_e32 v11, 31, v10
	v_or_b32_e32 v16, 64, v14
	v_lshl_add_u64 v[6:7], v[56:57], 4, s[18:19]
	v_lshl_add_u64 v[10:11], v[10:11], 4, s[18:19]
	v_ashrrev_i32_e32 v17, 31, v16
	global_load_dwordx4 v[6:9], v[6:7], off
	v_lshl_add_u64 v[16:17], v[16:17], 4, s[16:17]
	global_load_dwordx4 v[10:13], v[10:11], off
	s_ashr_i32 s7, s6, 31
	global_load_dwordx4 v[36:39], v[16:17], off
	v_or_b32_e32 v16, 64, v56
	v_ashrrev_i32_e32 v17, 31, v16
	v_lshl_add_u64 v[16:17], v[16:17], 4, s[18:19]
	global_load_dwordx4 v[52:55], v[16:17], off
	v_or_b32_e32 v16, 0x140, v56
	v_ashrrev_i32_e32 v17, 31, v16
	v_lshl_add_u64 v[16:17], v[16:17], 4, s[18:19]
	global_load_dwordx4 v[48:51], v[16:17], off
	v_or_b32_e32 v16, 0x80, v14
	v_ashrrev_i32_e32 v17, 31, v16
	v_lshl_add_u64 v[16:17], v[16:17], 4, s[16:17]
	global_load_dwordx4 v[32:35], v[16:17], off
	v_or_b32_e32 v16, 0x80, v56
	v_ashrrev_i32_e32 v17, 31, v16
	v_lshl_add_u64 v[16:17], v[16:17], 4, s[18:19]
	global_load_dwordx4 v[44:47], v[16:17], off
	v_or_b32_e32 v16, 0x180, v56
	v_ashrrev_i32_e32 v17, 31, v16
	v_lshl_add_u64 v[16:17], v[16:17], 4, s[18:19]
	global_load_dwordx4 v[40:43], v[16:17], off
	s_load_dwordx4 s[24:27], s[0:1], 0x40
	s_load_dwordx2 s[28:29], s[0:1], 0x50
	s_load_dwordx8 s[8:15], s[0:1], 0x20
	s_lshl_b64 s[0:1], s[6:7], 7
	v_or_b32_e32 v14, 0xc0, v14
	v_ashrrev_i32_e32 v15, 31, v14
	v_lshl_add_u64 v[14:15], v[14:15], 4, s[16:17]
	s_waitcnt lgkmcnt(0)
	s_add_u32 s0, s8, s0
	s_addc_u32 s1, s9, s1
	s_lshl_b32 s4, s4, 6
	v_lshlrev_b32_e32 v91, 4, v0
	global_load_dwordx4 v[64:67], v[14:15], off
	global_load_dwordx4 v[68:71], v91, s[0:1]
	s_add_i32 s0, s4, s5
	s_mov_b32 s3, 0
	s_ashr_i32 s1, s0, 31
	s_lshl_b64 s[8:9], s[2:3], 11
	s_lshl_b64 s[4:5], s[0:1], 14
	s_add_u32 s2, s4, s8
	s_addc_u32 s4, s5, s9
	v_lshl_or_b32 v92, v0, 3, s2
	v_mov_b32_e32 v93, s4
	v_lshl_add_u64 v[0:1], v[92:93], 2, s[26:27]
	global_load_dwordx4 v[72:75], v[0:1], off offset:16 nt
	global_load_dwordx4 v[76:79], v[0:1], off nt
	v_or_b32_e32 v58, 0xc0, v56
	v_or_b32_e32 v56, 0x1c0, v56
	v_ashrrev_i32_e32 v59, 31, v58
	v_ashrrev_i32_e32 v57, 31, v56
	v_lshl_add_u64 v[58:59], v[58:59], 4, s[18:19]
	v_lshl_add_u64 v[56:57], v[56:57], 4, s[18:19]
	global_load_dwordx4 v[84:87], v[58:59], off
	global_load_dwordx4 v[80:83], v[56:57], off
	s_ashr_i32 s4, s6, 3
	s_ashr_i32 s5, s4, 31
	s_or_b32 s8, s4, 1
	s_or_b32 s16, s4, 2
	s_or_b32 s18, s4, 3
	s_lshl_b64 s[4:5], s[4:5], 15
	s_ashr_i32 s9, s8, 31
	s_ashr_i32 s17, s16, 31
	s_ashr_i32 s19, s18, 31
	s_mov_b32 s2, 0x41800000
	s_waitcnt vmcnt(13)
	v_mfma_f32_32x32x16_f16 v[16:31], v[2:5], v[6:9], 0
	s_waitcnt vmcnt(3)
	v_mul_f32_e64 v72, v72, s2
	v_mul_f32_e64 v73, v73, s2
	v_mfma_f32_32x32x16_f16 v[0:15], v[2:5], v[10:13], 0
	s_waitcnt vmcnt(2)
	v_mul_f32_e64 v76, v76, s2
	v_mul_f32_e64 v77, v77, s2
	v_mfma_f32_32x32x16_f16 v[16:31], v[36:39], v[52:55], v[16:31]
	v_or_b32_e32 v52, v61, v60
	v_ashrrev_i32_e32 v53, 31, v52
	v_lshlrev_b64 v[94:95], 4, v[52:53]
	v_lshl_add_u64 v[54:55], s[22:23], 0, v[94:95]
	v_lshlrev_b64 v[88:89], 2, v[52:53]
	v_mfma_f32_32x32x16_f16 v[0:15], v[36:39], v[48:51], v[0:15]
	v_lshl_add_u64 v[36:37], v[54:55], 0, s[4:5]
	s_lshl_b64 s[4:5], s[8:9], 15
	s_lshl_b64 s[8:9], s[16:17], 15
	global_load_dwordx4 v[60:63], v[36:37], off
	s_lshl_b64 s[16:17], s[18:19], 15
	v_lshl_add_u64 v[48:49], v[54:55], 0, s[4:5]
	v_lshl_add_u64 v[50:51], v[54:55], 0, s[8:9]
	v_mfma_f32_32x32x16_f16 v[16:31], v[32:35], v[44:47], v[16:31]
	v_lshl_add_u64 v[96:97], v[54:55], 0, s[16:17]
	v_mfma_f32_32x32x16_f16 v[0:15], v[32:35], v[40:43], v[0:15]
	v_lshlrev_b64 v[32:33], 6, v[52:53]
	v_lshl_add_u64 v[44:45], s[10:11], 0, v[32:33]
	v_lshl_add_u64 v[52:53], s[20:21], 0, v[88:89]
	global_load_dwordx4 v[32:35], v[44:45], off offset:48
	global_load_dwordx4 v[36:39], v[44:45], off offset:32
	global_load_dwordx4 v[40:43], v[44:45], off offset:16
	s_nop 0
	global_load_dwordx4 v[44:47], v[44:45], off
	s_nop 0
	global_load_dword v90, v[52:53], off
	global_load_dwordx4 v[56:59], v[48:49], off
	s_nop 0
	global_load_dwordx4 v[52:55], v[50:51], off
	s_nop 0
	global_load_dwordx4 v[48:51], v[96:97], off
	ds_write_b128 v91, v[68:71]
	v_pk_mul_f32 v[68:69], v[78:79], s[2:3] op_sel_hi:[1,0]
	v_pk_mul_f32 v[70:71], v[74:75], s[2:3] op_sel_hi:[1,0]
	s_waitcnt vmcnt(10)
	v_mfma_f32_32x32x16_f16 v[16:31], v[64:67], v[84:87], v[16:31]
	v_cvt_pk_f16_f32 v71, v70, v71
	v_cvt_pk_f16_f32 v69, v68, v69
	v_cvt_pk_f16_f32 v70, v72, v73
	v_cvt_pk_f16_f32 v68, v76, v77
	v_lshl_add_u64 v[72:73], v[92:93], 1, s[28:29]
	s_mov_b32 s2, s3
	global_store_dwordx4 v[72:73], v[68:71], off
	s_waitcnt vmcnt(10)
	v_mfma_f32_32x32x16_f16 v[0:15], v[64:67], v[80:83], v[0:15]
	v_mov_b32_e32 v67, 0
	s_waitcnt lgkmcnt(0)
	s_barrier
	v_mov_b64_e32 v[76:77], s[2:3]
	ds_read_b128 v[68:71], v67
	ds_read_b128 v[72:75], v67 offset:16
	s_nop 5
	v_permlane32_swap_b32_e32 v16, v0
	v_permlane32_swap_b32_e32 v17, v1
	v_permlane32_swap_b32_e32 v18, v2
	v_permlane32_swap_b32_e32 v19, v3
	v_permlane32_swap_b32_e32 v20, v4
	v_permlane32_swap_b32_e32 v21, v5
	v_permlane32_swap_b32_e32 v22, v6
	v_permlane32_swap_b32_e32 v23, v7
	v_permlane32_swap_b32_e32 v24, v8
	v_permlane32_swap_b32_e32 v25, v9
	v_permlane32_swap_b32_e32 v26, v10
	v_permlane32_swap_b32_e32 v27, v11
	v_permlane32_swap_b32_e32 v28, v12
	v_permlane32_swap_b32_e32 v29, v13
	v_permlane32_swap_b32_e32 v30, v14
	v_permlane32_swap_b32_e32 v31, v15
	s_ashr_i32 s2, s6, 2
	v_lshl_add_u64 v[64:65], s[24:25], 0, v[94:95]
	s_waitcnt vmcnt(9)
	v_cvt_f32_f16_e32 v66, v60
	v_mul_f32_e32 v66, 0x3c800000, v66
	s_mov_b32 s4, 0x3d800000
	s_waitcnt vmcnt(4)
	v_pk_fma_f32 v[16:17], v[16:17], s[4:5], v[90:91] op_sel_hi:[1,0,0]
	s_mov_b32 s5, 0x41f00000
	v_min_f32_e32 v78, 0x41f00000, v16
	v_min_f32_e32 v79, 0x41f00000, v17
	v_mul_f32_e32 v78, 0x3fb8aa3b, v78
	v_mul_f32_e32 v79, 0x3fb8aa3b, v79
	v_exp_f32_e32 v78, v78
	v_exp_f32_e32 v79, v79
	s_mov_b32 s6, 0x3f317218
	v_cmp_lt_f32_e32 vcc, s5, v16
	v_add_f32_e32 v78, 1.0, v78
	v_add_f32_e32 v79, 1.0, v79
	v_log_f32_e32 v78, v78
	v_log_f32_e32 v79, v79
	s_nop 0
	v_pk_mul_f32 v[78:79], v[78:79], s[6:7] op_sel_hi:[1,0]
	s_nop 0
	v_cndmask_b32_e32 v16, v78, v16, vcc
	v_pk_mul_f32 v[80:81], v[16:17], v[44:45] op_sel_hi:[0,1]
	v_exp_f32_e32 v80, v80
	v_exp_f32_e32 v81, v81
	v_pk_mul_f32 v[82:83], v[16:17], v[46:47] op_sel_hi:[0,1]
	v_exp_f32_e32 v82, v82
	v_exp_f32_e32 v83, v83
	v_mul_f32_e32 v78, v16, v66
	v_pk_mul_f32 v[80:81], v[80:81], 0 op_sel_hi:[1,0]
	v_pk_mul_f32 v[84:85], v[16:17], v[42:43] op_sel_hi:[0,1]
	s_waitcnt lgkmcnt(1)
	v_pk_fma_f32 v[80:81], v[78:79], v[68:69], v[80:81] op_sel_hi:[0,1,1]
	v_pk_mul_f32 v[68:69], v[82:83], 0 op_sel_hi:[1,0]
	v_pk_mul_f32 v[82:83], v[16:17], v[40:41] op_sel_hi:[0,1]
	v_exp_f32_e32 v82, v82
	v_exp_f32_e32 v83, v83
	v_exp_f32_e32 v84, v84
	v_exp_f32_e32 v85, v85
	v_pk_fma_f32 v[86:87], v[78:79], v[70:71], v[68:69] op_sel_hi:[0,1,1]
	v_pk_mul_f32 v[68:69], v[82:83], 0 op_sel_hi:[1,0]
	v_cmp_lt_f32_e32 vcc, s5, v17
	s_waitcnt lgkmcnt(0)
	v_pk_fma_f32 v[82:83], v[78:79], v[72:73], v[68:69] op_sel_hi:[0,1,1]
	v_pk_mul_f32 v[68:69], v[84:85], 0 op_sel_hi:[1,0]
	v_cndmask_b32_e32 v66, v79, v17, vcc
	v_pk_fma_f32 v[84:85], v[78:79], v[74:75], v[68:69] op_sel_hi:[0,1,1]
	ds_read_b128 v[68:71], v67 offset:32
	ds_read_b128 v[72:75], v67 offset:48
	v_pk_mul_f32 v[76:77], v[16:17], v[36:37] op_sel_hi:[0,1]
	v_exp_f32_e32 v76, v76
	v_exp_f32_e32 v77, v77
	v_pk_mul_f32 v[92:93], v[16:17], v[38:39] op_sel_hi:[0,1]
	v_exp_f32_e32 v92, v92
	v_exp_f32_e32 v93, v93
	v_pk_mul_f32 v[76:77], v[76:77], 0 op_sel_hi:[1,0]
	s_waitcnt lgkmcnt(1)
	v_pk_fma_f32 v[76:77], v[78:79], v[68:69], v[76:77] op_sel_hi:[0,1,1]
	v_pk_mul_f32 v[68:69], v[92:93], 0 op_sel_hi:[1,0]
	s_nop 0
	v_pk_fma_f32 v[92:93], v[78:79], v[70:71], v[68:69] op_sel_hi:[0,1,1]
	v_pk_mul_f32 v[68:69], v[16:17], v[32:33] op_sel_hi:[0,1]
	v_exp_f32_e32 v68, v68
	v_exp_f32_e32 v69, v69
	v_pk_mul_f32 v[70:71], v[16:17], v[34:35] op_sel_hi:[0,1]
	v_exp_f32_e32 v70, v70
	v_exp_f32_e32 v71, v71
	v_pk_mul_f32 v[68:69], v[68:69], 0 op_sel_hi:[1,0]
	v_cvt_f32_f16_sdwa v17, v60 dst_sel:DWORD dst_unused:UNUSED_PAD src0_sel:WORD_1
	s_waitcnt lgkmcnt(0)
	v_pk_fma_f32 v[94:95], v[78:79], v[72:73], v[68:69] op_sel_hi:[0,1,1]
	v_pk_mul_f32 v[68:69], v[70:71], 0 op_sel_hi:[1,0]
	v_mul_f32_e32 v17, 0x3c800000, v17
	v_pk_fma_f32 v[78:79], v[78:79], v[74:75], v[68:69] op_sel_hi:[0,1,1]
	ds_read_b128 v[68:71], v67 offset:128
	v_pk_mul_f32 v[72:73], v[66:67], v[44:45] op_sel_hi:[0,1]
	v_exp_f32_e32 v96, v72
	v_exp_f32_e32 v97, v73
	v_pk_mul_f32 v[72:73], v[66:67], v[46:47] op_sel_hi:[0,1]
	v_exp_f32_e32 v98, v72
	v_exp_f32_e32 v99, v73
	v_mul_f32_e32 v60, v66, v17
	v_pk_mul_f32 v[80:81], v[80:81], v[96:97]
	ds_read_b128 v[72:75], v67 offset:144
	s_waitcnt lgkmcnt(1)
	v_pk_fma_f32 v[80:81], v[60:61], v[68:69], v[80:81] op_sel_hi:[0,1,1]
	v_pk_mul_f32 v[68:69], v[86:87], v[98:99]
	v_pk_mul_f32 v[86:87], v[66:67], v[40:41] op_sel_hi:[0,1]
	v_exp_f32_e32 v86, v86
	v_exp_f32_e32 v87, v87
	v_pk_mul_f32 v[96:97], v[66:67], v[42:43] op_sel_hi:[0,1]
	v_exp_f32_e32 v96, v96
	v_exp_f32_e32 v97, v97
	v_pk_fma_f32 v[98:99], v[60:61], v[70:71], v[68:69] op_sel_hi:[0,1,1]
	v_pk_mul_f32 v[68:69], v[82:83], v[86:87]
	s_waitcnt lgkmcnt(0)
	v_pk_fma_f32 v[82:83], v[60:61], v[72:73], v[68:69] op_sel_hi:[0,1,1]
	v_pk_mul_f32 v[68:69], v[84:85], v[96:97]
	s_nop 0
	v_pk_fma_f32 v[84:85], v[60:61], v[74:75], v[68:69] op_sel_hi:[0,1,1]
	ds_read_b128 v[68:71], v67 offset:160
	ds_read_b128 v[72:75], v67 offset:176
	v_pk_mul_f32 v[86:87], v[66:67], v[36:37] op_sel_hi:[0,1]
	v_exp_f32_e32 v86, v86
	v_exp_f32_e32 v87, v87
	v_pk_mul_f32 v[96:97], v[66:67], v[38:39] op_sel_hi:[0,1]
	v_exp_f32_e32 v96, v96
	v_exp_f32_e32 v97, v97
	v_pk_mul_f32 v[76:77], v[76:77], v[86:87]
	v_pk_mul_f32 v[86:87], v[66:67], v[32:33] op_sel_hi:[0,1]
	s_waitcnt lgkmcnt(1)
	v_pk_fma_f32 v[76:77], v[60:61], v[68:69], v[76:77] op_sel_hi:[0,1,1]
	v_pk_mul_f32 v[68:69], v[92:93], v[96:97]
	v_exp_f32_e32 v86, v86
	v_exp_f32_e32 v87, v87
	v_pk_mul_f32 v[92:93], v[66:67], v[34:35] op_sel_hi:[0,1]
	v_exp_f32_e32 v92, v92
	v_exp_f32_e32 v93, v93
	v_pk_fma_f32 v[96:97], v[60:61], v[70:71], v[68:69] op_sel_hi:[0,1,1]
	v_pk_mul_f32 v[68:69], v[94:95], v[86:87]
	v_cvt_f32_f16_e32 v17, v61
	s_waitcnt lgkmcnt(0)
	v_pk_fma_f32 v[86:87], v[60:61], v[72:73], v[68:69] op_sel_hi:[0,1,1]
	v_pk_mul_f32 v[68:69], v[78:79], v[92:93]
	v_mul_f32_e32 v17, 0x3c800000, v17
	v_pk_fma_f32 v[78:79], v[60:61], v[74:75], v[68:69] op_sel_hi:[0,1,1]
	ds_read_b128 v[68:71], v67 offset:256
	ds_read_b128 v[72:75], v67 offset:272
	v_pk_fma_f32 v[18:19], v[18:19], s[4:5], v[90:91] op_sel_hi:[1,0,0]
	s_nop 0
	v_min_f32_e32 v60, 0x41f00000, v18
	v_mul_f32_e32 v60, 0x3fb8aa3b, v60
	v_min_f32_e32 v91, 0x41f00000, v19
	v_exp_f32_e32 v60, v60
	v_mul_f32_e32 v91, 0x3fb8aa3b, v91
	v_exp_f32_e32 v91, v91
	v_cmp_lt_f32_e32 vcc, s5, v19
	v_add_f32_e32 v60, 1.0, v60
	v_log_f32_e32 v92, v60
	v_add_f32_e32 v60, 1.0, v91
	v_log_f32_e32 v93, v60
	s_nop 0
	v_pk_mul_f32 v[92:93], v[92:93], s[6:7] op_sel_hi:[1,0]
	s_nop 0
	v_cndmask_b32_e32 v19, v93, v19, vcc
	v_cmp_lt_f32_e32 vcc, s5, v18
	s_nop 1
	v_cndmask_b32_e32 v18, v92, v18, vcc
	v_pk_mul_f32 v[92:93], v[18:19], v[44:45] op_sel_hi:[0,1]
	v_exp_f32_e32 v92, v92
	v_exp_f32_e32 v93, v93
	v_pk_mul_f32 v[94:95], v[18:19], v[46:47] op_sel_hi:[0,1]
	v_exp_f32_e32 v94, v94
	v_exp_f32_e32 v95, v95
	v_mul_f32_e32 v60, v18, v17
	v_pk_mul_f32 v[80:81], v[80:81], v[92:93]
	v_pk_mul_f32 v[92:93], v[18:19], v[40:41] op_sel_hi:[0,1]
	s_waitcnt lgkmcnt(1)
	v_pk_fma_f32 v[80:81], v[60:61], v[68:69], v[80:81] op_sel_hi:[0,1,1]
	v_pk_mul_f32 v[68:69], v[98:99], v[94:95]
	v_exp_f32_e32 v92, v92
	v_exp_f32_e32 v93, v93
	v_pk_mul_f32 v[94:95], v[18:19], v[42:43] op_sel_hi:[0,1]
	v_exp_f32_e32 v94, v94
	v_exp_f32_e32 v95, v95
	v_pk_fma_f32 v[98:99], v[60:61], v[70:71], v[68:69] op_sel_hi:[0,1,1]
	v_pk_mul_f32 v[68:69], v[82:83], v[92:93]
	s_waitcnt lgkmcnt(0)
	v_pk_fma_f32 v[82:83], v[60:61], v[72:73], v[68:69] op_sel_hi:[0,1,1]
	v_pk_mul_f32 v[68:69], v[84:85], v[94:95]
	v_pk_mul_f32 v[72:73], v[18:19], v[36:37] op_sel_hi:[0,1]
	v_pk_fma_f32 v[84:85], v[60:61], v[74:75], v[68:69] op_sel_hi:[0,1,1]
	ds_read_b128 v[68:71], v67 offset:288
	v_exp_f32_e32 v92, v72
	v_exp_f32_e32 v93, v73
	v_pk_mul_f32 v[72:73], v[18:19], v[38:39] op_sel_hi:[0,1]
	v_exp_f32_e32 v94, v72
	v_exp_f32_e32 v95, v73
	v_pk_mul_f32 v[76:77], v[76:77], v[92:93]
	v_pk_mul_f32 v[92:93], v[18:19], v[32:33] op_sel_hi:[0,1]
	ds_read_b128 v[72:75], v67 offset:304
	s_waitcnt lgkmcnt(1)
	v_pk_fma_f32 v[76:77], v[60:61], v[68:69], v[76:77] op_sel_hi:[0,1,1]
	v_pk_mul_f32 v[68:69], v[96:97], v[94:95]
	v_exp_f32_e32 v92, v92
	v_exp_f32_e32 v93, v93
	v_pk_mul_f32 v[94:95], v[18:19], v[34:35] op_sel_hi:[0,1]
	v_exp_f32_e32 v94, v94
	v_exp_f32_e32 v95, v95
	v_pk_fma_f32 v[96:97], v[60:61], v[70:71], v[68:69] op_sel_hi:[0,1,1]
	v_pk_mul_f32 v[68:69], v[86:87], v[92:93]
	s_waitcnt lgkmcnt(0)
	v_pk_fma_f32 v[86:87], v[60:61], v[72:73], v[68:69] op_sel_hi:[0,1,1]
	v_pk_mul_f32 v[68:69], v[78:79], v[94:95]
	s_nop 0
	v_pk_fma_f32 v[78:79], v[60:61], v[74:75], v[68:69] op_sel_hi:[0,1,1]
	v_cvt_f32_f16_sdwa v68, v61 dst_sel:DWORD dst_unused:UNUSED_PAD src0_sel:WORD_1
	s_ashr_i32 s3, s2, 31
	s_lshl_b64 s[8:9], s[2:3], 15
	v_mov_b32_e32 v92, v19
	v_lshl_add_u64 v[60:61], v[64:65], 0, s[8:9]
	v_mov_b32_e32 v17, v66
	v_pk_mul_f32 v[72:73], v[92:93], v[44:45] op_sel_hi:[0,1]
	global_store_dwordx4 v[60:61], v[16:19], off
	v_exp_f32_e32 v94, v72
	v_exp_f32_e32 v95, v73
	v_mul_f32_e32 v17, 0x3c800000, v68
	ds_read_b128 v[68:71], v67 offset:384
	v_pk_mul_f32 v[72:73], v[92:93], v[46:47] op_sel_hi:[0,1]
	v_exp_f32_e32 v100, v72
	v_exp_f32_e32 v101, v73
	v_mul_f32_e32 v60, v19, v17
	v_pk_mul_f32 v[80:81], v[80:81], v[94:95]
	v_pk_mul_f32 v[94:95], v[92:93], v[40:41] op_sel_hi:[0,1]
	ds_read_b128 v[72:75], v67 offset:400
	s_waitcnt lgkmcnt(1)
	v_pk_fma_f32 v[80:81], v[60:61], v[68:69], v[80:81] op_sel_hi:[0,1,1]
	v_pk_mul_f32 v[68:69], v[98:99], v[100:101]
	v_exp_f32_e32 v94, v94
	v_exp_f32_e32 v95, v95
	v_pk_mul_f32 v[98:99], v[92:93], v[42:43] op_sel_hi:[0,1]
	v_exp_f32_e32 v98, v98
	v_exp_f32_e32 v99, v99
	v_pk_fma_f32 v[100:101], v[60:61], v[70:71], v[68:69] op_sel_hi:[0,1,1]
	v_pk_mul_f32 v[68:69], v[82:83], v[94:95]
	s_waitcnt lgkmcnt(0)
	v_pk_fma_f32 v[82:83], v[60:61], v[72:73], v[68:69] op_sel_hi:[0,1,1]
	v_pk_mul_f32 v[68:69], v[84:85], v[98:99]
	s_nop 0
	v_pk_fma_f32 v[84:85], v[60:61], v[74:75], v[68:69] op_sel_hi:[0,1,1]
	ds_read_b128 v[68:71], v67 offset:416
	ds_read_b128 v[72:75], v67 offset:432
	v_pk_mul_f32 v[94:95], v[92:93], v[36:37] op_sel_hi:[0,1]
	v_exp_f32_e32 v94, v94
	v_exp_f32_e32 v95, v95
	v_pk_mul_f32 v[98:99], v[92:93], v[38:39] op_sel_hi:[0,1]
	v_exp_f32_e32 v98, v98
	v_exp_f32_e32 v99, v99
	v_pk_mul_f32 v[76:77], v[76:77], v[94:95]
	v_pk_mul_f32 v[94:95], v[92:93], v[32:33] op_sel_hi:[0,1]
	v_exp_f32_e32 v94, v94
	v_exp_f32_e32 v95, v95
	v_pk_mul_f32 v[92:93], v[92:93], v[34:35] op_sel_hi:[0,1]
	v_exp_f32_e32 v92, v92
	v_exp_f32_e32 v93, v93
	s_waitcnt lgkmcnt(1)
	v_pk_fma_f32 v[76:77], v[60:61], v[68:69], v[76:77] op_sel_hi:[0,1,1]
	v_pk_mul_f32 v[68:69], v[96:97], v[98:99]
	v_cvt_f32_f16_e32 v17, v62
	v_pk_fma_f32 v[96:97], v[60:61], v[70:71], v[68:69] op_sel_hi:[0,1,1]
	v_pk_mul_f32 v[68:69], v[86:87], v[94:95]
	v_mul_f32_e32 v17, 0x3c800000, v17
	s_waitcnt lgkmcnt(0)
	v_pk_fma_f32 v[86:87], v[60:61], v[72:73], v[68:69] op_sel_hi:[0,1,1]
	v_pk_mul_f32 v[68:69], v[78:79], v[92:93]
	s_nop 0
	v_pk_fma_f32 v[78:79], v[60:61], v[74:75], v[68:69] op_sel_hi:[0,1,1]
	ds_read_b128 v[68:71], v67 offset:512
	ds_read_b128 v[72:75], v67 offset:528
	v_pk_fma_f32 v[0:1], v[0:1], s[4:5], v[90:91] op_sel_hi:[1,0,0]
	s_nop 0
	v_min_f32_e32 v60, 0x41f00000, v0
	v_min_f32_e32 v61, 0x41f00000, v1
	v_mul_f32_e32 v60, 0x3fb8aa3b, v60
	v_mul_f32_e32 v61, 0x3fb8aa3b, v61
	v_exp_f32_e32 v60, v60
	v_exp_f32_e32 v61, v61
	v_cmp_lt_f32_e32 vcc, s5, v0
	v_add_f32_e32 v60, 1.0, v60
	v_add_f32_e32 v61, 1.0, v61
	v_log_f32_e32 v60, v60
	v_log_f32_e32 v61, v61
	s_nop 0
	v_pk_mul_f32 v[60:61], v[60:61], s[6:7] op_sel_hi:[1,0]
	s_nop 0
	v_cndmask_b32_e32 v0, v60, v0, vcc
	v_pk_mul_f32 v[92:93], v[0:1], v[44:45] op_sel_hi:[0,1]
	v_exp_f32_e32 v92, v92
	v_exp_f32_e32 v93, v93
	v_pk_mul_f32 v[94:95], v[0:1], v[46:47] op_sel_hi:[0,1]
	v_exp_f32_e32 v94, v94
	v_exp_f32_e32 v95, v95
	v_mul_f32_e32 v98, v0, v17
	v_pk_mul_f32 v[80:81], v[80:81], v[92:93]
	v_pk_mul_f32 v[92:93], v[0:1], v[40:41] op_sel_hi:[0,1]
	s_waitcnt lgkmcnt(1)
	v_pk_fma_f32 v[80:81], v[98:99], v[68:69], v[80:81] op_sel_hi:[0,1,1]
	v_pk_mul_f32 v[68:69], v[100:101], v[94:95]
	v_exp_f32_e32 v92, v92
	v_exp_f32_e32 v93, v93
	v_pk_mul_f32 v[94:95], v[0:1], v[42:43] op_sel_hi:[0,1]
	v_exp_f32_e32 v94, v94
	v_exp_f32_e32 v95, v95
	v_pk_fma_f32 v[100:101], v[98:99], v[70:71], v[68:69] op_sel_hi:[0,1,1]
	v_pk_mul_f32 v[68:69], v[82:83], v[92:93]
	v_cmp_lt_f32_e32 vcc, s5, v1
	s_waitcnt lgkmcnt(0)
	v_pk_fma_f32 v[82:83], v[98:99], v[72:73], v[68:69] op_sel_hi:[0,1,1]
	v_pk_mul_f32 v[68:69], v[84:85], v[94:95]
	v_cndmask_b32_e32 v60, v61, v1, vcc
	v_pk_fma_f32 v[84:85], v[98:99], v[74:75], v[68:69] op_sel_hi:[0,1,1]
	ds_read_b128 v[68:71], v67 offset:544
	ds_read_b128 v[72:75], v67 offset:560
	v_pk_mul_f32 v[92:93], v[0:1], v[36:37] op_sel_hi:[0,1]
	v_exp_f32_e32 v92, v92
	v_exp_f32_e32 v93, v93
	v_pk_mul_f32 v[94:95], v[0:1], v[38:39] op_sel_hi:[0,1]
	v_exp_f32_e32 v94, v94
	v_exp_f32_e32 v95, v95
	v_pk_mul_f32 v[76:77], v[76:77], v[92:93]
	s_waitcnt lgkmcnt(1)
	v_pk_fma_f32 v[76:77], v[98:99], v[68:69], v[76:77] op_sel_hi:[0,1,1]
	v_pk_mul_f32 v[68:69], v[96:97], v[94:95]
	s_nop 0
	v_pk_fma_f32 v[92:93], v[98:99], v[70:71], v[68:69] op_sel_hi:[0,1,1]
	v_pk_mul_f32 v[68:69], v[0:1], v[32:33] op_sel_hi:[0,1]
	v_exp_f32_e32 v68, v68
	v_exp_f32_e32 v69, v69
	v_pk_mul_f32 v[70:71], v[0:1], v[34:35] op_sel_hi:[0,1]
	v_exp_f32_e32 v70, v70
	v_exp_f32_e32 v71, v71
	v_pk_mul_f32 v[68:69], v[86:87], v[68:69]
	v_cvt_f32_f16_sdwa v1, v62 dst_sel:DWORD dst_unused:UNUSED_PAD src0_sel:WORD_1
	s_waitcnt lgkmcnt(0)
	v_pk_fma_f32 v[86:87], v[98:99], v[72:73], v[68:69] op_sel_hi:[0,1,1]
	v_pk_mul_f32 v[68:69], v[78:79], v[70:71]
	v_pk_mul_f32 v[72:73], v[60:61], v[44:45] op_sel_hi:[0,1]
	v_pk_fma_f32 v[78:79], v[98:99], v[74:75], v[68:69] op_sel_hi:[0,1,1]
	ds_read_b128 v[68:71], v67 offset:640
	v_exp_f32_e32 v94, v72
	v_exp_f32_e32 v95, v73
	v_pk_mul_f32 v[72:73], v[60:61], v[46:47] op_sel_hi:[0,1]
	v_exp_f32_e32 v96, v72
	v_exp_f32_e32 v97, v73
	v_mul_f32_e32 v1, 0x3c800000, v1
	v_mul_f32_e32 v62, v60, v1
	v_pk_mul_f32 v[80:81], v[80:81], v[94:95]
	v_pk_mul_f32 v[94:95], v[60:61], v[40:41] op_sel_hi:[0,1]
	ds_read_b128 v[72:75], v67 offset:656
	s_waitcnt lgkmcnt(1)
	v_pk_fma_f32 v[80:81], v[62:63], v[68:69], v[80:81] op_sel_hi:[0,1,1]
	v_pk_mul_f32 v[68:69], v[100:101], v[96:97]
	v_exp_f32_e32 v94, v94
	v_exp_f32_e32 v95, v95
	v_pk_mul_f32 v[96:97], v[60:61], v[42:43] op_sel_hi:[0,1]
	v_exp_f32_e32 v96, v96
	v_exp_f32_e32 v97, v97
	v_pk_fma_f32 v[98:99], v[62:63], v[70:71], v[68:69] op_sel_hi:[0,1,1]
	v_pk_mul_f32 v[68:69], v[82:83], v[94:95]
	s_waitcnt lgkmcnt(0)
	v_pk_fma_f32 v[82:83], v[62:63], v[72:73], v[68:69] op_sel_hi:[0,1,1]
	v_pk_mul_f32 v[68:69], v[84:85], v[96:97]
	s_nop 0
	v_pk_fma_f32 v[84:85], v[62:63], v[74:75], v[68:69] op_sel_hi:[0,1,1]
	ds_read_b128 v[68:71], v67 offset:672
	ds_read_b128 v[72:75], v67 offset:688
	v_pk_mul_f32 v[94:95], v[60:61], v[36:37] op_sel_hi:[0,1]
	v_exp_f32_e32 v94, v94
	v_exp_f32_e32 v95, v95
	v_pk_mul_f32 v[96:97], v[60:61], v[38:39] op_sel_hi:[0,1]
	v_exp_f32_e32 v96, v96
	v_exp_f32_e32 v97, v97
	v_pk_mul_f32 v[76:77], v[76:77], v[94:95]
	v_pk_mul_f32 v[94:95], v[60:61], v[34:35] op_sel_hi:[0,1]
	s_waitcnt lgkmcnt(1)
	v_pk_fma_f32 v[76:77], v[62:63], v[68:69], v[76:77] op_sel_hi:[0,1,1]
	v_pk_mul_f32 v[68:69], v[92:93], v[96:97]
	v_pk_mul_f32 v[92:93], v[60:61], v[32:33] op_sel_hi:[0,1]
	v_exp_f32_e32 v92, v92
	v_exp_f32_e32 v93, v93
	v_exp_f32_e32 v94, v94
	v_exp_f32_e32 v95, v95
	v_pk_fma_f32 v[96:97], v[62:63], v[70:71], v[68:69] op_sel_hi:[0,1,1]
	v_pk_mul_f32 v[68:69], v[86:87], v[92:93]
	v_cvt_f32_f16_e32 v1, v63
	s_waitcnt lgkmcnt(0)
	v_pk_fma_f32 v[86:87], v[62:63], v[72:73], v[68:69] op_sel_hi:[0,1,1]
	v_pk_mul_f32 v[68:69], v[78:79], v[94:95]
	v_mul_f32_e32 v1, 0x3c800000, v1
	v_pk_fma_f32 v[78:79], v[62:63], v[74:75], v[68:69] op_sel_hi:[0,1,1]
	ds_read_b128 v[68:71], v67 offset:768
	ds_read_b128 v[72:75], v67 offset:784
	v_pk_fma_f32 v[2:3], v[2:3], s[4:5], v[90:91] op_sel_hi:[1,0,0]
	s_nop 0
	v_min_f32_e32 v17, 0x41f00000, v2
	v_mul_f32_e32 v17, 0x3fb8aa3b, v17
	v_min_f32_e32 v61, 0x41f00000, v3
	v_exp_f32_e32 v17, v17
	v_mul_f32_e32 v61, 0x3fb8aa3b, v61
	v_exp_f32_e32 v61, v61
	v_cmp_lt_f32_e32 vcc, s5, v3
	v_add_f32_e32 v17, 1.0, v17
	v_log_f32_e32 v92, v17
	v_add_f32_e32 v17, 1.0, v61
	v_log_f32_e32 v93, v17
	s_nop 0
	v_pk_mul_f32 v[92:93], v[92:93], s[6:7] op_sel_hi:[1,0]
	s_nop 0
	v_cndmask_b32_e32 v3, v93, v3, vcc
	v_cmp_lt_f32_e32 vcc, s5, v2
	s_nop 1
	v_cndmask_b32_e32 v2, v92, v2, vcc
	v_pk_mul_f32 v[92:93], v[2:3], v[44:45] op_sel_hi:[0,1]
	v_exp_f32_e32 v92, v92
	v_exp_f32_e32 v93, v93
	v_pk_mul_f32 v[94:95], v[2:3], v[46:47] op_sel_hi:[0,1]
	v_exp_f32_e32 v94, v94
	v_exp_f32_e32 v95, v95
	v_mul_f32_e32 v62, v2, v1
	v_pk_mul_f32 v[80:81], v[80:81], v[92:93]
	v_pk_mul_f32 v[92:93], v[2:3], v[40:41] op_sel_hi:[0,1]
	s_waitcnt lgkmcnt(1)
	v_pk_fma_f32 v[80:81], v[62:63], v[68:69], v[80:81] op_sel_hi:[0,1,1]
	v_pk_mul_f32 v[68:69], v[98:99], v[94:95]
	v_exp_f32_e32 v92, v92
	v_exp_f32_e32 v93, v93
	v_pk_mul_f32 v[94:95], v[2:3], v[42:43] op_sel_hi:[0,1]
	v_exp_f32_e32 v94, v94
	v_exp_f32_e32 v95, v95
	v_pk_fma_f32 v[98:99], v[62:63], v[70:71], v[68:69] op_sel_hi:[0,1,1]
	v_pk_mul_f32 v[68:69], v[82:83], v[92:93]
	s_waitcnt lgkmcnt(0)
	v_pk_fma_f32 v[82:83], v[62:63], v[72:73], v[68:69] op_sel_hi:[0,1,1]
	v_pk_mul_f32 v[68:69], v[84:85], v[94:95]
	v_pk_mul_f32 v[72:73], v[2:3], v[36:37] op_sel_hi:[0,1]
	v_pk_fma_f32 v[84:85], v[62:63], v[74:75], v[68:69] op_sel_hi:[0,1,1]
	ds_read_b128 v[68:71], v67 offset:800
	v_exp_f32_e32 v92, v72
	v_exp_f32_e32 v93, v73
	v_pk_mul_f32 v[72:73], v[2:3], v[38:39] op_sel_hi:[0,1]
	v_exp_f32_e32 v94, v72
	v_exp_f32_e32 v95, v73
	v_pk_mul_f32 v[76:77], v[76:77], v[92:93]
	v_pk_mul_f32 v[92:93], v[2:3], v[32:33] op_sel_hi:[0,1]
	ds_read_b128 v[72:75], v67 offset:816
	s_waitcnt lgkmcnt(1)
	v_pk_fma_f32 v[76:77], v[62:63], v[68:69], v[76:77] op_sel_hi:[0,1,1]
	v_pk_mul_f32 v[68:69], v[96:97], v[94:95]
	v_exp_f32_e32 v92, v92
	v_exp_f32_e32 v93, v93
	v_pk_mul_f32 v[94:95], v[2:3], v[34:35] op_sel_hi:[0,1]
	v_exp_f32_e32 v94, v94
	v_exp_f32_e32 v95, v95
	v_pk_fma_f32 v[96:97], v[62:63], v[70:71], v[68:69] op_sel_hi:[0,1,1]
	v_pk_mul_f32 v[68:69], v[86:87], v[92:93]
	s_waitcnt lgkmcnt(0)
	v_pk_fma_f32 v[86:87], v[62:63], v[72:73], v[68:69] op_sel_hi:[0,1,1]
	v_pk_mul_f32 v[68:69], v[78:79], v[94:95]
	s_nop 0
	v_pk_fma_f32 v[78:79], v[62:63], v[74:75], v[68:69] op_sel_hi:[0,1,1]
	s_or_b32 s8, s2, 1
	s_ashr_i32 s9, s8, 31
	s_lshl_b64 s[8:9], s[8:9], 15
	v_mov_b32_e32 v92, v3
	v_cvt_f32_f16_sdwa v17, v63 dst_sel:DWORD dst_unused:UNUSED_PAD src0_sel:WORD_1
	v_lshl_add_u64 v[62:63], v[64:65], 0, s[8:9]
	v_mov_b32_e32 v1, v60
	v_pk_mul_f32 v[72:73], v[92:93], v[44:45] op_sel_hi:[0,1]
	global_store_dwordx4 v[62:63], v[0:3], off
	ds_read_b128 v[68:71], v67 offset:896
	v_exp_f32_e32 v94, v72
	v_exp_f32_e32 v95, v73
	v_pk_mul_f32 v[72:73], v[92:93], v[46:47] op_sel_hi:[0,1]
	v_exp_f32_e32 v100, v72
	v_exp_f32_e32 v101, v73
	v_mul_f32_e32 v1, 0x3c800000, v17
	v_mul_f32_e32 v62, v3, v1
	v_pk_mul_f32 v[80:81], v[80:81], v[94:95]
	v_pk_mul_f32 v[94:95], v[92:93], v[40:41] op_sel_hi:[0,1]
	ds_read_b128 v[72:75], v67 offset:912
	s_waitcnt lgkmcnt(1)
	v_pk_fma_f32 v[80:81], v[62:63], v[68:69], v[80:81] op_sel_hi:[0,1,1]
	v_pk_mul_f32 v[68:69], v[98:99], v[100:101]
	v_exp_f32_e32 v94, v94
	v_exp_f32_e32 v95, v95
	v_pk_mul_f32 v[98:99], v[92:93], v[42:43] op_sel_hi:[0,1]
	v_exp_f32_e32 v98, v98
	v_exp_f32_e32 v99, v99
	v_pk_fma_f32 v[100:101], v[62:63], v[70:71], v[68:69] op_sel_hi:[0,1,1]
	v_pk_mul_f32 v[68:69], v[82:83], v[94:95]
	s_waitcnt lgkmcnt(0)
	v_pk_fma_f32 v[82:83], v[62:63], v[72:73], v[68:69] op_sel_hi:[0,1,1]
	v_pk_mul_f32 v[68:69], v[84:85], v[98:99]
	s_nop 0
	v_pk_fma_f32 v[84:85], v[62:63], v[74:75], v[68:69] op_sel_hi:[0,1,1]
	ds_read_b128 v[68:71], v67 offset:928
	ds_read_b128 v[72:75], v67 offset:944
	v_pk_mul_f32 v[94:95], v[92:93], v[36:37] op_sel_hi:[0,1]
	v_exp_f32_e32 v94, v94
	v_exp_f32_e32 v95, v95
	v_pk_mul_f32 v[98:99], v[92:93], v[38:39] op_sel_hi:[0,1]
	v_exp_f32_e32 v98, v98
	v_exp_f32_e32 v99, v99
	v_pk_mul_f32 v[76:77], v[76:77], v[94:95]
	v_pk_mul_f32 v[94:95], v[92:93], v[32:33] op_sel_hi:[0,1]
	v_exp_f32_e32 v94, v94
	v_exp_f32_e32 v95, v95
	v_pk_mul_f32 v[92:93], v[92:93], v[34:35] op_sel_hi:[0,1]
	v_exp_f32_e32 v92, v92
	v_exp_f32_e32 v93, v93
	s_waitcnt lgkmcnt(1)
	v_pk_fma_f32 v[76:77], v[62:63], v[68:69], v[76:77] op_sel_hi:[0,1,1]
	v_pk_mul_f32 v[68:69], v[96:97], v[98:99]
	s_waitcnt vmcnt(5)
	v_cvt_f32_f16_e32 v1, v56
	v_pk_fma_f32 v[96:97], v[62:63], v[70:71], v[68:69] op_sel_hi:[0,1,1]
	v_pk_mul_f32 v[68:69], v[86:87], v[94:95]
	v_mul_f32_e32 v1, 0x3c800000, v1
	s_waitcnt lgkmcnt(0)
	v_pk_fma_f32 v[86:87], v[62:63], v[72:73], v[68:69] op_sel_hi:[0,1,1]
	v_pk_mul_f32 v[68:69], v[78:79], v[92:93]
	s_nop 0
	v_pk_fma_f32 v[78:79], v[62:63], v[74:75], v[68:69] op_sel_hi:[0,1,1]
	ds_read_b128 v[68:71], v67 offset:1024
	ds_read_b128 v[72:75], v67 offset:1040
	v_pk_fma_f32 v[20:21], v[20:21], s[4:5], v[90:91] op_sel_hi:[1,0,0]
	s_nop 0
	v_min_f32_e32 v17, 0x41f00000, v20
	v_mul_f32_e32 v17, 0x3fb8aa3b, v17
	v_min_f32_e32 v61, 0x41f00000, v21
	v_exp_f32_e32 v17, v17
	v_mul_f32_e32 v61, 0x3fb8aa3b, v61
	v_exp_f32_e32 v61, v61
	v_cmp_lt_f32_e32 vcc, s5, v20
	v_add_f32_e32 v17, 1.0, v17
	v_log_f32_e32 v62, v17
	v_add_f32_e32 v17, 1.0, v61
	v_log_f32_e32 v63, v17
	s_nop 0
	v_pk_mul_f32 v[62:63], v[62:63], s[6:7] op_sel_hi:[1,0]
	s_nop 0
	v_cndmask_b32_e32 v20, v62, v20, vcc
	v_pk_mul_f32 v[92:93], v[20:21], v[44:45] op_sel_hi:[0,1]
	v_exp_f32_e32 v92, v92
	v_exp_f32_e32 v93, v93
	v_pk_mul_f32 v[94:95], v[20:21], v[46:47] op_sel_hi:[0,1]
	v_exp_f32_e32 v94, v94
	v_exp_f32_e32 v95, v95
	v_mul_f32_e32 v98, v20, v1
	v_pk_mul_f32 v[80:81], v[80:81], v[92:93]
	v_pk_mul_f32 v[92:93], v[20:21], v[40:41] op_sel_hi:[0,1]
	s_waitcnt lgkmcnt(1)
	v_pk_fma_f32 v[80:81], v[98:99], v[68:69], v[80:81] op_sel_hi:[0,1,1]
	v_pk_mul_f32 v[68:69], v[100:101], v[94:95]
	v_exp_f32_e32 v92, v92
	v_exp_f32_e32 v93, v93
	v_pk_mul_f32 v[94:95], v[20:21], v[42:43] op_sel_hi:[0,1]
	v_exp_f32_e32 v94, v94
	v_exp_f32_e32 v95, v95
	v_pk_fma_f32 v[100:101], v[98:99], v[70:71], v[68:69] op_sel_hi:[0,1,1]
	v_pk_mul_f32 v[68:69], v[82:83], v[92:93]
	v_cmp_lt_f32_e32 vcc, s5, v21
	s_waitcnt lgkmcnt(0)
	v_pk_fma_f32 v[82:83], v[98:99], v[72:73], v[68:69] op_sel_hi:[0,1,1]
	v_pk_mul_f32 v[68:69], v[84:85], v[94:95]
	v_cndmask_b32_e32 v62, v63, v21, vcc
	v_pk_fma_f32 v[84:85], v[98:99], v[74:75], v[68:69] op_sel_hi:[0,1,1]
	ds_read_b128 v[68:71], v67 offset:1056
	ds_read_b128 v[72:75], v67 offset:1072
	v_pk_mul_f32 v[92:93], v[20:21], v[36:37] op_sel_hi:[0,1]
	v_exp_f32_e32 v92, v92
	v_exp_f32_e32 v93, v93
	v_pk_mul_f32 v[94:95], v[20:21], v[38:39] op_sel_hi:[0,1]
	v_exp_f32_e32 v94, v94
	v_exp_f32_e32 v95, v95
	v_pk_mul_f32 v[76:77], v[76:77], v[92:93]
	v_cvt_f32_f16_sdwa v1, v56 dst_sel:DWORD dst_unused:UNUSED_PAD src0_sel:WORD_1
	s_waitcnt lgkmcnt(1)
	v_pk_fma_f32 v[76:77], v[98:99], v[68:69], v[76:77] op_sel_hi:[0,1,1]
	v_pk_mul_f32 v[68:69], v[96:97], v[94:95]
	v_mul_f32_e32 v1, 0x3c800000, v1
	v_pk_fma_f32 v[92:93], v[98:99], v[70:71], v[68:69] op_sel_hi:[0,1,1]
	v_pk_mul_f32 v[68:69], v[20:21], v[32:33] op_sel_hi:[0,1]
	v_exp_f32_e32 v68, v68
	v_exp_f32_e32 v69, v69
	v_pk_mul_f32 v[70:71], v[20:21], v[34:35] op_sel_hi:[0,1]
	v_exp_f32_e32 v70, v70
	v_exp_f32_e32 v71, v71
	v_pk_mul_f32 v[68:69], v[86:87], v[68:69]
	v_mul_f32_e32 v56, v62, v1
	s_waitcnt lgkmcnt(0)
	v_pk_fma_f32 v[86:87], v[98:99], v[72:73], v[68:69] op_sel_hi:[0,1,1]
	v_pk_mul_f32 v[68:69], v[78:79], v[70:71]
	v_pk_mul_f32 v[72:73], v[62:63], v[44:45] op_sel_hi:[0,1]
	v_pk_fma_f32 v[78:79], v[98:99], v[74:75], v[68:69] op_sel_hi:[0,1,1]
	ds_read_b128 v[68:71], v67 offset:1152
	v_exp_f32_e32 v94, v72
	v_exp_f32_e32 v95, v73
	v_pk_mul_f32 v[72:73], v[62:63], v[46:47] op_sel_hi:[0,1]
	v_exp_f32_e32 v96, v72
	v_exp_f32_e32 v97, v73
	v_pk_mul_f32 v[80:81], v[80:81], v[94:95]
	v_pk_mul_f32 v[94:95], v[62:63], v[40:41] op_sel_hi:[0,1]
	ds_read_b128 v[72:75], v67 offset:1168
	s_waitcnt lgkmcnt(1)
	v_pk_fma_f32 v[80:81], v[56:57], v[68:69], v[80:81] op_sel_hi:[0,1,1]
	v_pk_mul_f32 v[68:69], v[100:101], v[96:97]
	v_exp_f32_e32 v94, v94
	v_exp_f32_e32 v95, v95
	v_pk_mul_f32 v[96:97], v[62:63], v[42:43] op_sel_hi:[0,1]
	v_exp_f32_e32 v96, v96
	v_exp_f32_e32 v97, v97
	v_pk_fma_f32 v[98:99], v[56:57], v[70:71], v[68:69] op_sel_hi:[0,1,1]
	v_pk_mul_f32 v[68:69], v[82:83], v[94:95]
	s_waitcnt lgkmcnt(0)
	v_pk_fma_f32 v[82:83], v[56:57], v[72:73], v[68:69] op_sel_hi:[0,1,1]
	v_pk_mul_f32 v[68:69], v[84:85], v[96:97]
	s_nop 0
	v_pk_fma_f32 v[84:85], v[56:57], v[74:75], v[68:69] op_sel_hi:[0,1,1]
	ds_read_b128 v[68:71], v67 offset:1184
	ds_read_b128 v[72:75], v67 offset:1200
	v_pk_mul_f32 v[94:95], v[62:63], v[36:37] op_sel_hi:[0,1]
	v_exp_f32_e32 v94, v94
	v_exp_f32_e32 v95, v95
	v_pk_mul_f32 v[96:97], v[62:63], v[38:39] op_sel_hi:[0,1]
	v_exp_f32_e32 v96, v96
	v_exp_f32_e32 v97, v97
	v_pk_mul_f32 v[76:77], v[76:77], v[94:95]
	v_pk_mul_f32 v[94:95], v[62:63], v[34:35] op_sel_hi:[0,1]
	s_waitcnt lgkmcnt(1)
	v_pk_fma_f32 v[76:77], v[56:57], v[68:69], v[76:77] op_sel_hi:[0,1,1]
	v_pk_mul_f32 v[68:69], v[92:93], v[96:97]
	v_pk_mul_f32 v[92:93], v[62:63], v[32:33] op_sel_hi:[0,1]
	v_exp_f32_e32 v92, v92
	v_exp_f32_e32 v93, v93
	v_exp_f32_e32 v94, v94
	v_exp_f32_e32 v95, v95
	v_pk_fma_f32 v[96:97], v[56:57], v[70:71], v[68:69] op_sel_hi:[0,1,1]
	v_pk_mul_f32 v[68:69], v[86:87], v[92:93]
	v_cvt_f32_f16_e32 v1, v57
	s_waitcnt lgkmcnt(0)
	v_pk_fma_f32 v[86:87], v[56:57], v[72:73], v[68:69] op_sel_hi:[0,1,1]
	v_pk_mul_f32 v[68:69], v[78:79], v[94:95]
	v_mul_f32_e32 v1, 0x3c800000, v1
	v_pk_fma_f32 v[78:79], v[56:57], v[74:75], v[68:69] op_sel_hi:[0,1,1]
	ds_read_b128 v[68:71], v67 offset:1280
	ds_read_b128 v[72:75], v67 offset:1296
	v_pk_fma_f32 v[22:23], v[22:23], s[4:5], v[90:91] op_sel_hi:[1,0,0]
	s_nop 0
	v_min_f32_e32 v17, 0x41f00000, v22
	v_mul_f32_e32 v17, 0x3fb8aa3b, v17
	v_min_f32_e32 v21, 0x41f00000, v23
	v_exp_f32_e32 v17, v17
	v_mul_f32_e32 v21, 0x3fb8aa3b, v21
	v_exp_f32_e32 v21, v21
	v_cmp_lt_f32_e32 vcc, s5, v23
	v_add_f32_e32 v17, 1.0, v17
	v_log_f32_e32 v92, v17
	v_add_f32_e32 v17, 1.0, v21
	v_log_f32_e32 v93, v17
	s_nop 0
	v_pk_mul_f32 v[92:93], v[92:93], s[6:7] op_sel_hi:[1,0]
	s_nop 0
	v_cndmask_b32_e32 v23, v93, v23, vcc
	v_cmp_lt_f32_e32 vcc, s5, v22
	s_nop 1
	v_cndmask_b32_e32 v22, v92, v22, vcc
	v_pk_mul_f32 v[92:93], v[22:23], v[44:45] op_sel_hi:[0,1]
	v_exp_f32_e32 v92, v92
	v_exp_f32_e32 v93, v93
	v_pk_mul_f32 v[94:95], v[22:23], v[46:47] op_sel_hi:[0,1]
	v_exp_f32_e32 v94, v94
	v_exp_f32_e32 v95, v95
	v_mul_f32_e32 v56, v22, v1
	v_pk_mul_f32 v[80:81], v[80:81], v[92:93]
	v_pk_mul_f32 v[92:93], v[22:23], v[40:41] op_sel_hi:[0,1]
	s_waitcnt lgkmcnt(1)
	v_pk_fma_f32 v[80:81], v[56:57], v[68:69], v[80:81] op_sel_hi:[0,1,1]
	v_pk_mul_f32 v[68:69], v[98:99], v[94:95]
	v_exp_f32_e32 v92, v92
	v_exp_f32_e32 v93, v93
	v_pk_mul_f32 v[94:95], v[22:23], v[42:43] op_sel_hi:[0,1]
	v_exp_f32_e32 v94, v94
	v_exp_f32_e32 v95, v95
	v_pk_fma_f32 v[98:99], v[56:57], v[70:71], v[68:69] op_sel_hi:[0,1,1]
	v_pk_mul_f32 v[68:69], v[82:83], v[92:93]
	s_waitcnt lgkmcnt(0)
	v_pk_fma_f32 v[82:83], v[56:57], v[72:73], v[68:69] op_sel_hi:[0,1,1]
	v_pk_mul_f32 v[68:69], v[84:85], v[94:95]
	v_pk_mul_f32 v[72:73], v[22:23], v[36:37] op_sel_hi:[0,1]
	v_pk_fma_f32 v[84:85], v[56:57], v[74:75], v[68:69] op_sel_hi:[0,1,1]
	ds_read_b128 v[68:71], v67 offset:1312
	v_exp_f32_e32 v92, v72
	v_exp_f32_e32 v93, v73
	v_pk_mul_f32 v[72:73], v[22:23], v[38:39] op_sel_hi:[0,1]
	v_exp_f32_e32 v94, v72
	v_exp_f32_e32 v95, v73
	v_pk_mul_f32 v[76:77], v[76:77], v[92:93]
	v_pk_mul_f32 v[92:93], v[22:23], v[32:33] op_sel_hi:[0,1]
	ds_read_b128 v[72:75], v67 offset:1328
	s_waitcnt lgkmcnt(1)
	v_pk_fma_f32 v[76:77], v[56:57], v[68:69], v[76:77] op_sel_hi:[0,1,1]
	v_pk_mul_f32 v[68:69], v[96:97], v[94:95]
	v_exp_f32_e32 v92, v92
	v_exp_f32_e32 v93, v93
	v_pk_mul_f32 v[94:95], v[22:23], v[34:35] op_sel_hi:[0,1]
	v_exp_f32_e32 v94, v94
	v_exp_f32_e32 v95, v95
	v_pk_fma_f32 v[96:97], v[56:57], v[70:71], v[68:69] op_sel_hi:[0,1,1]
	v_pk_mul_f32 v[68:69], v[86:87], v[92:93]
	s_waitcnt lgkmcnt(0)
	v_pk_fma_f32 v[86:87], v[56:57], v[72:73], v[68:69] op_sel_hi:[0,1,1]
	v_pk_mul_f32 v[68:69], v[78:79], v[94:95]
	s_nop 0
	v_pk_fma_f32 v[78:79], v[56:57], v[74:75], v[68:69] op_sel_hi:[0,1,1]
	s_or_b32 s8, s2, 2
	s_ashr_i32 s9, s8, 31
	s_lshl_b64 s[8:9], s[8:9], 15
	v_mov_b32_e32 v92, v23
	v_cvt_f32_f16_sdwa v1, v57 dst_sel:DWORD dst_unused:UNUSED_PAD src0_sel:WORD_1
	v_lshl_add_u64 v[56:57], v[64:65], 0, s[8:9]
	v_mov_b32_e32 v21, v62
	v_pk_mul_f32 v[72:73], v[92:93], v[44:45] op_sel_hi:[0,1]
	global_store_dwordx4 v[56:57], v[20:23], off
	ds_read_b128 v[68:71], v67 offset:1408
	v_exp_f32_e32 v94, v72
	v_exp_f32_e32 v95, v73
	v_pk_mul_f32 v[72:73], v[92:93], v[46:47] op_sel_hi:[0,1]
	v_exp_f32_e32 v100, v72
	v_exp_f32_e32 v101, v73
	v_mul_f32_e32 v1, 0x3c800000, v1
	v_mul_f32_e32 v56, v23, v1
	v_pk_mul_f32 v[80:81], v[80:81], v[94:95]
	v_pk_mul_f32 v[94:95], v[92:93], v[40:41] op_sel_hi:[0,1]
	ds_read_b128 v[72:75], v67 offset:1424
	s_waitcnt lgkmcnt(1)
	v_pk_fma_f32 v[80:81], v[56:57], v[68:69], v[80:81] op_sel_hi:[0,1,1]
	v_pk_mul_f32 v[68:69], v[98:99], v[100:101]
	v_exp_f32_e32 v94, v94
	v_exp_f32_e32 v95, v95
	v_pk_mul_f32 v[98:99], v[92:93], v[42:43] op_sel_hi:[0,1]
	v_exp_f32_e32 v98, v98
	v_exp_f32_e32 v99, v99
	v_pk_fma_f32 v[100:101], v[56:57], v[70:71], v[68:69] op_sel_hi:[0,1,1]
	v_pk_mul_f32 v[68:69], v[82:83], v[94:95]
	s_waitcnt lgkmcnt(0)
	v_pk_fma_f32 v[82:83], v[56:57], v[72:73], v[68:69] op_sel_hi:[0,1,1]
	v_pk_mul_f32 v[68:69], v[84:85], v[98:99]
	s_nop 0
	v_pk_fma_f32 v[84:85], v[56:57], v[74:75], v[68:69] op_sel_hi:[0,1,1]
	ds_read_b128 v[68:71], v67 offset:1440
	ds_read_b128 v[72:75], v67 offset:1456
	v_pk_mul_f32 v[94:95], v[92:93], v[36:37] op_sel_hi:[0,1]
	v_exp_f32_e32 v94, v94
	v_exp_f32_e32 v95, v95
	v_pk_mul_f32 v[98:99], v[92:93], v[38:39] op_sel_hi:[0,1]
	v_exp_f32_e32 v98, v98
	v_exp_f32_e32 v99, v99
	v_pk_mul_f32 v[76:77], v[76:77], v[94:95]
	v_pk_mul_f32 v[94:95], v[92:93], v[32:33] op_sel_hi:[0,1]
	v_exp_f32_e32 v94, v94
	v_exp_f32_e32 v95, v95
	v_pk_mul_f32 v[92:93], v[92:93], v[34:35] op_sel_hi:[0,1]
	v_exp_f32_e32 v92, v92
	v_exp_f32_e32 v93, v93
	s_waitcnt lgkmcnt(1)
	v_pk_fma_f32 v[76:77], v[56:57], v[68:69], v[76:77] op_sel_hi:[0,1,1]
	v_pk_mul_f32 v[68:69], v[96:97], v[98:99]
	v_cvt_f32_f16_e32 v1, v58
	v_pk_fma_f32 v[96:97], v[56:57], v[70:71], v[68:69] op_sel_hi:[0,1,1]
	v_pk_mul_f32 v[68:69], v[86:87], v[94:95]
	v_mul_f32_e32 v1, 0x3c800000, v1
	s_waitcnt lgkmcnt(0)
	v_pk_fma_f32 v[86:87], v[56:57], v[72:73], v[68:69] op_sel_hi:[0,1,1]
	v_pk_mul_f32 v[68:69], v[78:79], v[92:93]
	s_nop 0
	v_pk_fma_f32 v[78:79], v[56:57], v[74:75], v[68:69] op_sel_hi:[0,1,1]
	ds_read_b128 v[68:71], v67 offset:1536
	ds_read_b128 v[72:75], v67 offset:1552
	v_pk_fma_f32 v[4:5], v[4:5], s[4:5], v[90:91] op_sel_hi:[1,0,0]
	s_nop 0
	v_min_f32_e32 v17, 0x41f00000, v4
	v_mul_f32_e32 v17, 0x3fb8aa3b, v17
	v_min_f32_e32 v21, 0x41f00000, v5
	v_exp_f32_e32 v17, v17
	v_mul_f32_e32 v21, 0x3fb8aa3b, v21
	v_exp_f32_e32 v21, v21
	v_cmp_lt_f32_e32 vcc, s5, v4
	v_add_f32_e32 v17, 1.0, v17
	v_log_f32_e32 v56, v17
	v_add_f32_e32 v17, 1.0, v21
	v_log_f32_e32 v57, v17
	s_nop 0
	v_pk_mul_f32 v[56:57], v[56:57], s[6:7] op_sel_hi:[1,0]
	s_nop 0
	v_cndmask_b32_e32 v4, v56, v4, vcc
	v_pk_mul_f32 v[92:93], v[4:5], v[44:45] op_sel_hi:[0,1]
	v_exp_f32_e32 v92, v92
	v_exp_f32_e32 v93, v93
	v_pk_mul_f32 v[94:95], v[4:5], v[46:47] op_sel_hi:[0,1]
	v_exp_f32_e32 v94, v94
	v_exp_f32_e32 v95, v95
	v_mul_f32_e32 v98, v4, v1
	v_pk_mul_f32 v[80:81], v[80:81], v[92:93]
	v_pk_mul_f32 v[92:93], v[4:5], v[40:41] op_sel_hi:[0,1]
	s_waitcnt lgkmcnt(1)
	v_pk_fma_f32 v[80:81], v[98:99], v[68:69], v[80:81] op_sel_hi:[0,1,1]
	v_pk_mul_f32 v[68:69], v[100:101], v[94:95]
	v_exp_f32_e32 v92, v92
	v_exp_f32_e32 v93, v93
	v_pk_mul_f32 v[94:95], v[4:5], v[42:43] op_sel_hi:[0,1]
	v_exp_f32_e32 v94, v94
	v_exp_f32_e32 v95, v95
	v_pk_fma_f32 v[100:101], v[98:99], v[70:71], v[68:69] op_sel_hi:[0,1,1]
	v_pk_mul_f32 v[68:69], v[82:83], v[92:93]
	v_cmp_lt_f32_e32 vcc, s5, v5
	s_waitcnt lgkmcnt(0)
	v_pk_fma_f32 v[82:83], v[98:99], v[72:73], v[68:69] op_sel_hi:[0,1,1]
	v_pk_mul_f32 v[68:69], v[84:85], v[94:95]
	v_cndmask_b32_e32 v56, v57, v5, vcc
	v_pk_fma_f32 v[84:85], v[98:99], v[74:75], v[68:69] op_sel_hi:[0,1,1]
	ds_read_b128 v[68:71], v67 offset:1568
	ds_read_b128 v[72:75], v67 offset:1584
	v_pk_mul_f32 v[92:93], v[4:5], v[36:37] op_sel_hi:[0,1]
	v_exp_f32_e32 v92, v92
	v_exp_f32_e32 v93, v93
	v_pk_mul_f32 v[94:95], v[4:5], v[38:39] op_sel_hi:[0,1]
	v_exp_f32_e32 v94, v94
	v_exp_f32_e32 v95, v95
	v_pk_mul_f32 v[76:77], v[76:77], v[92:93]
	v_cvt_f32_f16_sdwa v1, v58 dst_sel:DWORD dst_unused:UNUSED_PAD src0_sel:WORD_1
	s_waitcnt lgkmcnt(1)
	v_pk_fma_f32 v[76:77], v[98:99], v[68:69], v[76:77] op_sel_hi:[0,1,1]
	v_pk_mul_f32 v[68:69], v[96:97], v[94:95]
	v_mul_f32_e32 v1, 0x3c800000, v1
	v_pk_fma_f32 v[92:93], v[98:99], v[70:71], v[68:69] op_sel_hi:[0,1,1]
	v_pk_mul_f32 v[68:69], v[4:5], v[32:33] op_sel_hi:[0,1]
	v_exp_f32_e32 v68, v68
	v_exp_f32_e32 v69, v69
	v_pk_mul_f32 v[70:71], v[4:5], v[34:35] op_sel_hi:[0,1]
	v_exp_f32_e32 v70, v70
	v_exp_f32_e32 v71, v71
	v_pk_mul_f32 v[68:69], v[86:87], v[68:69]
	v_mul_f32_e32 v58, v56, v1
	s_waitcnt lgkmcnt(0)
	v_pk_fma_f32 v[86:87], v[98:99], v[72:73], v[68:69] op_sel_hi:[0,1,1]
	v_pk_mul_f32 v[68:69], v[78:79], v[70:71]
	v_pk_mul_f32 v[72:73], v[56:57], v[44:45] op_sel_hi:[0,1]
	v_pk_fma_f32 v[78:79], v[98:99], v[74:75], v[68:69] op_sel_hi:[0,1,1]
	ds_read_b128 v[68:71], v67 offset:1664
	v_exp_f32_e32 v94, v72
	v_exp_f32_e32 v95, v73
	v_pk_mul_f32 v[72:73], v[56:57], v[46:47] op_sel_hi:[0,1]
	v_exp_f32_e32 v96, v72
	v_exp_f32_e32 v97, v73
	v_pk_mul_f32 v[80:81], v[80:81], v[94:95]
	v_pk_mul_f32 v[94:95], v[56:57], v[40:41] op_sel_hi:[0,1]
	ds_read_b128 v[72:75], v67 offset:1680
	s_waitcnt lgkmcnt(1)
	v_pk_fma_f32 v[80:81], v[58:59], v[68:69], v[80:81] op_sel_hi:[0,1,1]
	v_pk_mul_f32 v[68:69], v[100:101], v[96:97]
	v_exp_f32_e32 v94, v94
	v_exp_f32_e32 v95, v95
	v_pk_mul_f32 v[96:97], v[56:57], v[42:43] op_sel_hi:[0,1]
	v_exp_f32_e32 v96, v96
	v_exp_f32_e32 v97, v97
	v_pk_fma_f32 v[98:99], v[58:59], v[70:71], v[68:69] op_sel_hi:[0,1,1]
	v_pk_mul_f32 v[68:69], v[82:83], v[94:95]
	s_waitcnt lgkmcnt(0)
	v_pk_fma_f32 v[82:83], v[58:59], v[72:73], v[68:69] op_sel_hi:[0,1,1]
	v_pk_mul_f32 v[68:69], v[84:85], v[96:97]
	s_nop 0
	v_pk_fma_f32 v[84:85], v[58:59], v[74:75], v[68:69] op_sel_hi:[0,1,1]
	ds_read_b128 v[68:71], v67 offset:1696
	ds_read_b128 v[72:75], v67 offset:1712
	v_pk_mul_f32 v[94:95], v[56:57], v[36:37] op_sel_hi:[0,1]
	v_exp_f32_e32 v94, v94
	v_exp_f32_e32 v95, v95
	v_pk_mul_f32 v[96:97], v[56:57], v[38:39] op_sel_hi:[0,1]
	v_exp_f32_e32 v96, v96
	v_exp_f32_e32 v97, v97
	v_pk_mul_f32 v[76:77], v[76:77], v[94:95]
	v_pk_mul_f32 v[94:95], v[56:57], v[34:35] op_sel_hi:[0,1]
	s_waitcnt lgkmcnt(1)
	v_pk_fma_f32 v[76:77], v[58:59], v[68:69], v[76:77] op_sel_hi:[0,1,1]
	v_pk_mul_f32 v[68:69], v[92:93], v[96:97]
	v_pk_mul_f32 v[92:93], v[56:57], v[32:33] op_sel_hi:[0,1]
	v_exp_f32_e32 v92, v92
	v_exp_f32_e32 v93, v93
	v_exp_f32_e32 v94, v94
	v_exp_f32_e32 v95, v95
	v_pk_fma_f32 v[96:97], v[58:59], v[70:71], v[68:69] op_sel_hi:[0,1,1]
	v_pk_mul_f32 v[68:69], v[86:87], v[92:93]
	v_cvt_f32_f16_e32 v1, v59
	s_waitcnt lgkmcnt(0)
	v_pk_fma_f32 v[86:87], v[58:59], v[72:73], v[68:69] op_sel_hi:[0,1,1]
	v_pk_mul_f32 v[68:69], v[78:79], v[94:95]
	v_mul_f32_e32 v1, 0x3c800000, v1
	v_pk_fma_f32 v[78:79], v[58:59], v[74:75], v[68:69] op_sel_hi:[0,1,1]
	ds_read_b128 v[68:71], v67 offset:1792
	ds_read_b128 v[72:75], v67 offset:1808
	v_pk_fma_f32 v[6:7], v[6:7], s[4:5], v[90:91] op_sel_hi:[1,0,0]
	s_nop 0
	v_min_f32_e32 v5, 0x41f00000, v6
	v_mul_f32_e32 v5, 0x3fb8aa3b, v5
	v_min_f32_e32 v17, 0x41f00000, v7
	v_exp_f32_e32 v5, v5
	v_mul_f32_e32 v17, 0x3fb8aa3b, v17
	v_exp_f32_e32 v17, v17
	v_cmp_lt_f32_e32 vcc, s5, v7
	v_add_f32_e32 v5, 1.0, v5
	v_log_f32_e32 v92, v5
	v_add_f32_e32 v5, 1.0, v17
	v_log_f32_e32 v93, v5
	s_nop 0
	v_pk_mul_f32 v[92:93], v[92:93], s[6:7] op_sel_hi:[1,0]
	s_nop 0
	v_cndmask_b32_e32 v7, v93, v7, vcc
	v_cmp_lt_f32_e32 vcc, s5, v6
	s_nop 1
	v_cndmask_b32_e32 v6, v92, v6, vcc
	v_pk_mul_f32 v[92:93], v[6:7], v[44:45] op_sel_hi:[0,1]
	v_exp_f32_e32 v92, v92
	v_exp_f32_e32 v93, v93
	v_pk_mul_f32 v[94:95], v[6:7], v[46:47] op_sel_hi:[0,1]
	v_exp_f32_e32 v94, v94
	v_exp_f32_e32 v95, v95
	v_mul_f32_e32 v58, v6, v1
	v_pk_mul_f32 v[80:81], v[80:81], v[92:93]
	v_pk_mul_f32 v[92:93], v[6:7], v[40:41] op_sel_hi:[0,1]
	s_waitcnt lgkmcnt(1)
	v_pk_fma_f32 v[80:81], v[58:59], v[68:69], v[80:81] op_sel_hi:[0,1,1]
	v_pk_mul_f32 v[68:69], v[98:99], v[94:95]
	v_exp_f32_e32 v92, v92
	v_exp_f32_e32 v93, v93
	v_pk_mul_f32 v[94:95], v[6:7], v[42:43] op_sel_hi:[0,1]
	v_exp_f32_e32 v94, v94
	v_exp_f32_e32 v95, v95
	v_pk_fma_f32 v[98:99], v[58:59], v[70:71], v[68:69] op_sel_hi:[0,1,1]
	v_pk_mul_f32 v[68:69], v[82:83], v[92:93]
	s_waitcnt lgkmcnt(0)
	v_pk_fma_f32 v[82:83], v[58:59], v[72:73], v[68:69] op_sel_hi:[0,1,1]
	v_pk_mul_f32 v[68:69], v[84:85], v[94:95]
	v_pk_mul_f32 v[72:73], v[6:7], v[36:37] op_sel_hi:[0,1]
	v_pk_fma_f32 v[84:85], v[58:59], v[74:75], v[68:69] op_sel_hi:[0,1,1]
	ds_read_b128 v[68:71], v67 offset:1824
	v_exp_f32_e32 v92, v72
	v_exp_f32_e32 v93, v73
	v_pk_mul_f32 v[72:73], v[6:7], v[38:39] op_sel_hi:[0,1]
	v_exp_f32_e32 v94, v72
	v_exp_f32_e32 v95, v73
	v_pk_mul_f32 v[76:77], v[76:77], v[92:93]
	v_pk_mul_f32 v[92:93], v[6:7], v[32:33] op_sel_hi:[0,1]
	ds_read_b128 v[72:75], v67 offset:1840
	s_waitcnt lgkmcnt(1)
	v_pk_fma_f32 v[76:77], v[58:59], v[68:69], v[76:77] op_sel_hi:[0,1,1]
	v_pk_mul_f32 v[68:69], v[96:97], v[94:95]
	v_exp_f32_e32 v92, v92
	v_exp_f32_e32 v93, v93
	v_pk_mul_f32 v[94:95], v[6:7], v[34:35] op_sel_hi:[0,1]
	v_exp_f32_e32 v94, v94
	v_exp_f32_e32 v95, v95
	v_pk_fma_f32 v[96:97], v[58:59], v[70:71], v[68:69] op_sel_hi:[0,1,1]
	v_pk_mul_f32 v[68:69], v[86:87], v[92:93]
	s_waitcnt lgkmcnt(0)
	v_pk_fma_f32 v[86:87], v[58:59], v[72:73], v[68:69] op_sel_hi:[0,1,1]
	v_pk_mul_f32 v[68:69], v[78:79], v[94:95]
	s_nop 0
	v_pk_fma_f32 v[78:79], v[58:59], v[74:75], v[68:69] op_sel_hi:[0,1,1]
	s_or_b32 s8, s2, 3
	s_ashr_i32 s9, s8, 31
	s_lshl_b64 s[8:9], s[8:9], 15
	v_mov_b32_e32 v92, v7
	v_cvt_f32_f16_sdwa v1, v59 dst_sel:DWORD dst_unused:UNUSED_PAD src0_sel:WORD_1
	v_lshl_add_u64 v[58:59], v[64:65], 0, s[8:9]
	v_mov_b32_e32 v5, v56
	v_pk_mul_f32 v[72:73], v[92:93], v[44:45] op_sel_hi:[0,1]
	global_store_dwordx4 v[58:59], v[4:7], off
	ds_read_b128 v[68:71], v67 offset:1920
	v_exp_f32_e32 v94, v72
	v_exp_f32_e32 v95, v73
	v_pk_mul_f32 v[72:73], v[92:93], v[46:47] op_sel_hi:[0,1]
	v_exp_f32_e32 v100, v72
	v_exp_f32_e32 v101, v73
	v_mul_f32_e32 v1, 0x3c800000, v1
	v_mul_f32_e32 v58, v7, v1
	v_pk_mul_f32 v[80:81], v[80:81], v[94:95]
	v_pk_mul_f32 v[94:95], v[92:93], v[40:41] op_sel_hi:[0,1]
	ds_read_b128 v[72:75], v67 offset:1936
	s_waitcnt lgkmcnt(1)
	v_pk_fma_f32 v[80:81], v[58:59], v[68:69], v[80:81] op_sel_hi:[0,1,1]
	v_pk_mul_f32 v[68:69], v[98:99], v[100:101]
	v_exp_f32_e32 v94, v94
	v_exp_f32_e32 v95, v95
	v_pk_mul_f32 v[98:99], v[92:93], v[42:43] op_sel_hi:[0,1]
	v_exp_f32_e32 v98, v98
	v_exp_f32_e32 v99, v99
	v_pk_fma_f32 v[100:101], v[58:59], v[70:71], v[68:69] op_sel_hi:[0,1,1]
	v_pk_mul_f32 v[68:69], v[82:83], v[94:95]
	s_waitcnt lgkmcnt(0)
	v_pk_fma_f32 v[82:83], v[58:59], v[72:73], v[68:69] op_sel_hi:[0,1,1]
	v_pk_mul_f32 v[68:69], v[84:85], v[98:99]
	s_nop 0
	v_pk_fma_f32 v[84:85], v[58:59], v[74:75], v[68:69] op_sel_hi:[0,1,1]
	ds_read_b128 v[68:71], v67 offset:1952
	ds_read_b128 v[72:75], v67 offset:1968
	v_pk_mul_f32 v[94:95], v[92:93], v[36:37] op_sel_hi:[0,1]
	v_exp_f32_e32 v94, v94
	v_exp_f32_e32 v95, v95
	v_pk_mul_f32 v[98:99], v[92:93], v[38:39] op_sel_hi:[0,1]
	v_exp_f32_e32 v98, v98
	v_exp_f32_e32 v99, v99
	v_pk_mul_f32 v[76:77], v[76:77], v[94:95]
	v_pk_mul_f32 v[94:95], v[92:93], v[32:33] op_sel_hi:[0,1]
	v_exp_f32_e32 v94, v94
	v_exp_f32_e32 v95, v95
	v_pk_mul_f32 v[92:93], v[92:93], v[34:35] op_sel_hi:[0,1]
	v_exp_f32_e32 v92, v92
	v_exp_f32_e32 v93, v93
	s_waitcnt lgkmcnt(1)
	v_pk_fma_f32 v[76:77], v[58:59], v[68:69], v[76:77] op_sel_hi:[0,1,1]
	v_pk_mul_f32 v[68:69], v[96:97], v[98:99]
	s_waitcnt vmcnt(6)
	v_cvt_f32_f16_e32 v1, v52
	v_pk_fma_f32 v[96:97], v[58:59], v[70:71], v[68:69] op_sel_hi:[0,1,1]
	v_pk_mul_f32 v[68:69], v[86:87], v[94:95]
	v_mul_f32_e32 v1, 0x3c800000, v1
	s_waitcnt lgkmcnt(0)
	v_pk_fma_f32 v[86:87], v[58:59], v[72:73], v[68:69] op_sel_hi:[0,1,1]
	v_pk_mul_f32 v[68:69], v[78:79], v[92:93]
	s_nop 0
	v_pk_fma_f32 v[78:79], v[58:59], v[74:75], v[68:69] op_sel_hi:[0,1,1]
	ds_read_b128 v[68:71], v67 offset:2048
	ds_read_b128 v[72:75], v67 offset:2064
	v_pk_fma_f32 v[24:25], v[24:25], s[4:5], v[90:91] op_sel_hi:[1,0,0]
	s_nop 0
	v_min_f32_e32 v5, 0x41f00000, v24
	v_mul_f32_e32 v5, 0x3fb8aa3b, v5
	v_min_f32_e32 v17, 0x41f00000, v25
	v_exp_f32_e32 v5, v5
	v_mul_f32_e32 v17, 0x3fb8aa3b, v17
	v_exp_f32_e32 v17, v17
	v_cmp_lt_f32_e32 vcc, s5, v24
	v_add_f32_e32 v5, 1.0, v5
	v_log_f32_e32 v58, v5
	v_add_f32_e32 v5, 1.0, v17
	v_log_f32_e32 v59, v5
	s_nop 0
	v_pk_mul_f32 v[58:59], v[58:59], s[6:7] op_sel_hi:[1,0]
	s_nop 0
	v_cndmask_b32_e32 v24, v58, v24, vcc
	v_pk_mul_f32 v[92:93], v[24:25], v[44:45] op_sel_hi:[0,1]
	v_exp_f32_e32 v92, v92
	v_exp_f32_e32 v93, v93
	v_pk_mul_f32 v[94:95], v[24:25], v[46:47] op_sel_hi:[0,1]
	v_exp_f32_e32 v94, v94
	v_exp_f32_e32 v95, v95
	v_mul_f32_e32 v98, v24, v1
	v_pk_mul_f32 v[80:81], v[80:81], v[92:93]
	v_pk_mul_f32 v[92:93], v[24:25], v[40:41] op_sel_hi:[0,1]
	s_waitcnt lgkmcnt(1)
	v_pk_fma_f32 v[80:81], v[98:99], v[68:69], v[80:81] op_sel_hi:[0,1,1]
	v_pk_mul_f32 v[68:69], v[100:101], v[94:95]
	v_exp_f32_e32 v92, v92
	v_exp_f32_e32 v93, v93
	v_pk_mul_f32 v[94:95], v[24:25], v[42:43] op_sel_hi:[0,1]
	v_exp_f32_e32 v94, v94
	v_exp_f32_e32 v95, v95
	v_pk_fma_f32 v[100:101], v[98:99], v[70:71], v[68:69] op_sel_hi:[0,1,1]
	v_pk_mul_f32 v[68:69], v[82:83], v[92:93]
	v_cmp_lt_f32_e32 vcc, s5, v25
	s_waitcnt lgkmcnt(0)
	v_pk_fma_f32 v[82:83], v[98:99], v[72:73], v[68:69] op_sel_hi:[0,1,1]
	v_pk_mul_f32 v[68:69], v[84:85], v[94:95]
	v_cndmask_b32_e32 v58, v59, v25, vcc
	v_pk_fma_f32 v[84:85], v[98:99], v[74:75], v[68:69] op_sel_hi:[0,1,1]
	ds_read_b128 v[68:71], v67 offset:2080
	ds_read_b128 v[72:75], v67 offset:2096
	v_pk_mul_f32 v[92:93], v[24:25], v[36:37] op_sel_hi:[0,1]
	v_exp_f32_e32 v92, v92
	v_exp_f32_e32 v93, v93
	v_pk_mul_f32 v[94:95], v[24:25], v[38:39] op_sel_hi:[0,1]
	v_exp_f32_e32 v94, v94
	v_exp_f32_e32 v95, v95
	v_pk_mul_f32 v[76:77], v[76:77], v[92:93]
	v_cvt_f32_f16_sdwa v1, v52 dst_sel:DWORD dst_unused:UNUSED_PAD src0_sel:WORD_1
	s_waitcnt lgkmcnt(1)
	v_pk_fma_f32 v[76:77], v[98:99], v[68:69], v[76:77] op_sel_hi:[0,1,1]
	v_pk_mul_f32 v[68:69], v[96:97], v[94:95]
	v_mul_f32_e32 v1, 0x3c800000, v1
	v_pk_fma_f32 v[92:93], v[98:99], v[70:71], v[68:69] op_sel_hi:[0,1,1]
	v_pk_mul_f32 v[68:69], v[24:25], v[32:33] op_sel_hi:[0,1]
	v_exp_f32_e32 v68, v68
	v_exp_f32_e32 v69, v69
	v_pk_mul_f32 v[70:71], v[24:25], v[34:35] op_sel_hi:[0,1]
	v_exp_f32_e32 v70, v70
	v_exp_f32_e32 v71, v71
	v_pk_mul_f32 v[68:69], v[86:87], v[68:69]
	v_mul_f32_e32 v52, v58, v1
	s_waitcnt lgkmcnt(0)
	v_pk_fma_f32 v[86:87], v[98:99], v[72:73], v[68:69] op_sel_hi:[0,1,1]
	v_pk_mul_f32 v[68:69], v[78:79], v[70:71]
	v_pk_mul_f32 v[72:73], v[58:59], v[44:45] op_sel_hi:[0,1]
	v_pk_fma_f32 v[78:79], v[98:99], v[74:75], v[68:69] op_sel_hi:[0,1,1]
	ds_read_b128 v[68:71], v67 offset:2176
	v_exp_f32_e32 v94, v72
	v_exp_f32_e32 v95, v73
	v_pk_mul_f32 v[72:73], v[58:59], v[46:47] op_sel_hi:[0,1]
	v_exp_f32_e32 v96, v72
	v_exp_f32_e32 v97, v73
	v_pk_mul_f32 v[80:81], v[80:81], v[94:95]
	v_pk_mul_f32 v[94:95], v[58:59], v[40:41] op_sel_hi:[0,1]
	ds_read_b128 v[72:75], v67 offset:2192
	s_waitcnt lgkmcnt(1)
	v_pk_fma_f32 v[80:81], v[52:53], v[68:69], v[80:81] op_sel_hi:[0,1,1]
	v_pk_mul_f32 v[68:69], v[100:101], v[96:97]
	v_exp_f32_e32 v94, v94
	v_exp_f32_e32 v95, v95
	v_pk_mul_f32 v[96:97], v[58:59], v[42:43] op_sel_hi:[0,1]
	v_exp_f32_e32 v96, v96
	v_exp_f32_e32 v97, v97
	v_pk_fma_f32 v[98:99], v[52:53], v[70:71], v[68:69] op_sel_hi:[0,1,1]
	v_pk_mul_f32 v[68:69], v[82:83], v[94:95]
	s_waitcnt lgkmcnt(0)
	v_pk_fma_f32 v[82:83], v[52:53], v[72:73], v[68:69] op_sel_hi:[0,1,1]
	v_pk_mul_f32 v[68:69], v[84:85], v[96:97]
	s_nop 0
	v_pk_fma_f32 v[84:85], v[52:53], v[74:75], v[68:69] op_sel_hi:[0,1,1]
	ds_read_b128 v[68:71], v67 offset:2208
	ds_read_b128 v[72:75], v67 offset:2224
	v_pk_mul_f32 v[94:95], v[58:59], v[36:37] op_sel_hi:[0,1]
	v_exp_f32_e32 v94, v94
	v_exp_f32_e32 v95, v95
	v_pk_mul_f32 v[96:97], v[58:59], v[38:39] op_sel_hi:[0,1]
	v_exp_f32_e32 v96, v96
	v_exp_f32_e32 v97, v97
	v_pk_mul_f32 v[76:77], v[76:77], v[94:95]
	v_pk_mul_f32 v[94:95], v[58:59], v[34:35] op_sel_hi:[0,1]
	s_waitcnt lgkmcnt(1)
	v_pk_fma_f32 v[76:77], v[52:53], v[68:69], v[76:77] op_sel_hi:[0,1,1]
	v_pk_mul_f32 v[68:69], v[92:93], v[96:97]
	v_pk_mul_f32 v[92:93], v[58:59], v[32:33] op_sel_hi:[0,1]
	v_exp_f32_e32 v92, v92
	v_exp_f32_e32 v93, v93
	v_exp_f32_e32 v94, v94
	v_exp_f32_e32 v95, v95
	v_pk_fma_f32 v[96:97], v[52:53], v[70:71], v[68:69] op_sel_hi:[0,1,1]
	v_pk_mul_f32 v[68:69], v[86:87], v[92:93]
	v_cvt_f32_f16_e32 v1, v53
	s_waitcnt lgkmcnt(0)
	v_pk_fma_f32 v[86:87], v[52:53], v[72:73], v[68:69] op_sel_hi:[0,1,1]
	v_pk_mul_f32 v[68:69], v[78:79], v[94:95]
	v_mul_f32_e32 v1, 0x3c800000, v1
	v_pk_fma_f32 v[78:79], v[52:53], v[74:75], v[68:69] op_sel_hi:[0,1,1]
	ds_read_b128 v[68:71], v67 offset:2304
	ds_read_b128 v[72:75], v67 offset:2320
	v_pk_fma_f32 v[26:27], v[26:27], s[4:5], v[90:91] op_sel_hi:[1,0,0]
	s_nop 0
	v_min_f32_e32 v5, 0x41f00000, v26
	v_mul_f32_e32 v5, 0x3fb8aa3b, v5
	v_min_f32_e32 v17, 0x41f00000, v27
	v_exp_f32_e32 v5, v5
	v_mul_f32_e32 v17, 0x3fb8aa3b, v17
	v_exp_f32_e32 v17, v17
	v_cmp_lt_f32_e32 vcc, s5, v27
	v_add_f32_e32 v5, 1.0, v5
	v_log_f32_e32 v92, v5
	v_add_f32_e32 v5, 1.0, v17
	v_log_f32_e32 v93, v5
	s_nop 0
	v_pk_mul_f32 v[92:93], v[92:93], s[6:7] op_sel_hi:[1,0]
	s_nop 0
	v_cndmask_b32_e32 v27, v93, v27, vcc
	v_cmp_lt_f32_e32 vcc, s5, v26
	s_nop 1
	v_cndmask_b32_e32 v26, v92, v26, vcc
	v_pk_mul_f32 v[92:93], v[26:27], v[44:45] op_sel_hi:[0,1]
	v_exp_f32_e32 v92, v92
	v_exp_f32_e32 v93, v93
	v_pk_mul_f32 v[94:95], v[26:27], v[46:47] op_sel_hi:[0,1]
	v_exp_f32_e32 v94, v94
	v_exp_f32_e32 v95, v95
	v_mul_f32_e32 v52, v26, v1
	v_pk_mul_f32 v[80:81], v[80:81], v[92:93]
	v_pk_mul_f32 v[92:93], v[26:27], v[40:41] op_sel_hi:[0,1]
	s_waitcnt lgkmcnt(1)
	v_pk_fma_f32 v[80:81], v[52:53], v[68:69], v[80:81] op_sel_hi:[0,1,1]
	v_pk_mul_f32 v[68:69], v[98:99], v[94:95]
	v_exp_f32_e32 v92, v92
	v_exp_f32_e32 v93, v93
	v_pk_mul_f32 v[94:95], v[26:27], v[42:43] op_sel_hi:[0,1]
	v_exp_f32_e32 v94, v94
	v_exp_f32_e32 v95, v95
	v_pk_fma_f32 v[98:99], v[52:53], v[70:71], v[68:69] op_sel_hi:[0,1,1]
	v_pk_mul_f32 v[68:69], v[82:83], v[92:93]
	s_waitcnt lgkmcnt(0)
	v_pk_fma_f32 v[82:83], v[52:53], v[72:73], v[68:69] op_sel_hi:[0,1,1]
	v_pk_mul_f32 v[68:69], v[84:85], v[94:95]
	v_pk_mul_f32 v[72:73], v[26:27], v[36:37] op_sel_hi:[0,1]
	v_pk_fma_f32 v[84:85], v[52:53], v[74:75], v[68:69] op_sel_hi:[0,1,1]
	ds_read_b128 v[68:71], v67 offset:2336
	v_exp_f32_e32 v92, v72
	v_exp_f32_e32 v93, v73
	v_pk_mul_f32 v[72:73], v[26:27], v[38:39] op_sel_hi:[0,1]
	v_exp_f32_e32 v94, v72
	v_exp_f32_e32 v95, v73
	v_pk_mul_f32 v[76:77], v[76:77], v[92:93]
	v_pk_mul_f32 v[92:93], v[26:27], v[32:33] op_sel_hi:[0,1]
	ds_read_b128 v[72:75], v67 offset:2352
	s_waitcnt lgkmcnt(1)
	v_pk_fma_f32 v[76:77], v[52:53], v[68:69], v[76:77] op_sel_hi:[0,1,1]
	v_pk_mul_f32 v[68:69], v[96:97], v[94:95]
	v_exp_f32_e32 v92, v92
	v_exp_f32_e32 v93, v93
	v_pk_mul_f32 v[94:95], v[26:27], v[34:35] op_sel_hi:[0,1]
	v_exp_f32_e32 v94, v94
	v_exp_f32_e32 v95, v95
	v_pk_fma_f32 v[96:97], v[52:53], v[70:71], v[68:69] op_sel_hi:[0,1,1]
	v_pk_mul_f32 v[68:69], v[86:87], v[92:93]
	s_waitcnt lgkmcnt(0)
	v_pk_fma_f32 v[86:87], v[52:53], v[72:73], v[68:69] op_sel_hi:[0,1,1]
	v_pk_mul_f32 v[68:69], v[78:79], v[94:95]
	s_nop 0
	v_pk_fma_f32 v[78:79], v[52:53], v[74:75], v[68:69] op_sel_hi:[0,1,1]
	s_or_b32 s8, s2, 4
	s_ashr_i32 s9, s8, 31
	s_lshl_b64 s[8:9], s[8:9], 15
	v_mov_b32_e32 v92, v27
	v_cvt_f32_f16_sdwa v1, v53 dst_sel:DWORD dst_unused:UNUSED_PAD src0_sel:WORD_1
	v_lshl_add_u64 v[52:53], v[64:65], 0, s[8:9]
	v_mov_b32_e32 v25, v58
	v_pk_mul_f32 v[72:73], v[92:93], v[44:45] op_sel_hi:[0,1]
	global_store_dwordx4 v[52:53], v[24:27], off
	ds_read_b128 v[68:71], v67 offset:2432
	v_exp_f32_e32 v94, v72
	v_exp_f32_e32 v95, v73
	v_pk_mul_f32 v[72:73], v[92:93], v[46:47] op_sel_hi:[0,1]
	v_exp_f32_e32 v100, v72
	v_exp_f32_e32 v101, v73
	v_mul_f32_e32 v1, 0x3c800000, v1
	v_mul_f32_e32 v52, v27, v1
	v_pk_mul_f32 v[80:81], v[80:81], v[94:95]
	v_pk_mul_f32 v[94:95], v[92:93], v[40:41] op_sel_hi:[0,1]
	ds_read_b128 v[72:75], v67 offset:2448
	s_waitcnt lgkmcnt(1)
	v_pk_fma_f32 v[80:81], v[52:53], v[68:69], v[80:81] op_sel_hi:[0,1,1]
	v_pk_mul_f32 v[68:69], v[98:99], v[100:101]
	v_exp_f32_e32 v94, v94
	v_exp_f32_e32 v95, v95
	v_pk_mul_f32 v[98:99], v[92:93], v[42:43] op_sel_hi:[0,1]
	v_exp_f32_e32 v98, v98
	v_exp_f32_e32 v99, v99
	v_pk_fma_f32 v[100:101], v[52:53], v[70:71], v[68:69] op_sel_hi:[0,1,1]
	v_pk_mul_f32 v[68:69], v[82:83], v[94:95]
	s_waitcnt lgkmcnt(0)
	v_pk_fma_f32 v[82:83], v[52:53], v[72:73], v[68:69] op_sel_hi:[0,1,1]
	v_pk_mul_f32 v[68:69], v[84:85], v[98:99]
	s_nop 0
	v_pk_fma_f32 v[84:85], v[52:53], v[74:75], v[68:69] op_sel_hi:[0,1,1]
	ds_read_b128 v[68:71], v67 offset:2464
	ds_read_b128 v[72:75], v67 offset:2480
	v_pk_mul_f32 v[94:95], v[92:93], v[36:37] op_sel_hi:[0,1]
	v_exp_f32_e32 v94, v94
	v_exp_f32_e32 v95, v95
	v_pk_mul_f32 v[98:99], v[92:93], v[38:39] op_sel_hi:[0,1]
	v_exp_f32_e32 v98, v98
	v_exp_f32_e32 v99, v99
	v_pk_mul_f32 v[76:77], v[76:77], v[94:95]
	v_pk_mul_f32 v[94:95], v[92:93], v[32:33] op_sel_hi:[0,1]
	v_exp_f32_e32 v94, v94
	v_exp_f32_e32 v95, v95
	v_pk_mul_f32 v[92:93], v[92:93], v[34:35] op_sel_hi:[0,1]
	v_exp_f32_e32 v92, v92
	v_exp_f32_e32 v93, v93
	s_waitcnt lgkmcnt(1)
	v_pk_fma_f32 v[76:77], v[52:53], v[68:69], v[76:77] op_sel_hi:[0,1,1]
	v_pk_mul_f32 v[68:69], v[96:97], v[98:99]
	v_cvt_f32_f16_e32 v1, v54
	v_pk_fma_f32 v[96:97], v[52:53], v[70:71], v[68:69] op_sel_hi:[0,1,1]
	v_pk_mul_f32 v[68:69], v[86:87], v[94:95]
	v_mul_f32_e32 v1, 0x3c800000, v1
	s_waitcnt lgkmcnt(0)
	v_pk_fma_f32 v[86:87], v[52:53], v[72:73], v[68:69] op_sel_hi:[0,1,1]
	v_pk_mul_f32 v[68:69], v[78:79], v[92:93]
	s_nop 0
	v_pk_fma_f32 v[78:79], v[52:53], v[74:75], v[68:69] op_sel_hi:[0,1,1]
	ds_read_b128 v[68:71], v67 offset:2560
	ds_read_b128 v[72:75], v67 offset:2576
	v_pk_fma_f32 v[8:9], v[8:9], s[4:5], v[90:91] op_sel_hi:[1,0,0]
	s_nop 0
	v_min_f32_e32 v5, 0x41f00000, v8
	v_mul_f32_e32 v5, 0x3fb8aa3b, v5
	v_min_f32_e32 v17, 0x41f00000, v9
	v_exp_f32_e32 v5, v5
	v_mul_f32_e32 v17, 0x3fb8aa3b, v17
	v_exp_f32_e32 v17, v17
	v_cmp_lt_f32_e32 vcc, s5, v8
	v_add_f32_e32 v5, 1.0, v5
	v_log_f32_e32 v52, v5
	v_add_f32_e32 v5, 1.0, v17
	v_log_f32_e32 v53, v5
	s_nop 0
	v_pk_mul_f32 v[52:53], v[52:53], s[6:7] op_sel_hi:[1,0]
	s_nop 0
	v_cndmask_b32_e32 v8, v52, v8, vcc
	v_pk_mul_f32 v[92:93], v[8:9], v[44:45] op_sel_hi:[0,1]
	v_exp_f32_e32 v92, v92
	v_exp_f32_e32 v93, v93
	v_pk_mul_f32 v[94:95], v[8:9], v[46:47] op_sel_hi:[0,1]
	v_exp_f32_e32 v94, v94
	v_exp_f32_e32 v95, v95
	v_mul_f32_e32 v98, v8, v1
	v_pk_mul_f32 v[80:81], v[80:81], v[92:93]
	v_pk_mul_f32 v[92:93], v[8:9], v[40:41] op_sel_hi:[0,1]
	s_waitcnt lgkmcnt(1)
	v_pk_fma_f32 v[80:81], v[98:99], v[68:69], v[80:81] op_sel_hi:[0,1,1]
	v_pk_mul_f32 v[68:69], v[100:101], v[94:95]
	v_exp_f32_e32 v92, v92
	v_exp_f32_e32 v93, v93
	v_pk_mul_f32 v[94:95], v[8:9], v[42:43] op_sel_hi:[0,1]
	v_exp_f32_e32 v94, v94
	v_exp_f32_e32 v95, v95
	v_pk_fma_f32 v[100:101], v[98:99], v[70:71], v[68:69] op_sel_hi:[0,1,1]
	v_pk_mul_f32 v[68:69], v[82:83], v[92:93]
	v_cmp_lt_f32_e32 vcc, s5, v9
	s_waitcnt lgkmcnt(0)
	v_pk_fma_f32 v[82:83], v[98:99], v[72:73], v[68:69] op_sel_hi:[0,1,1]
	v_pk_mul_f32 v[68:69], v[84:85], v[94:95]
	v_cndmask_b32_e32 v52, v53, v9, vcc
	v_pk_fma_f32 v[84:85], v[98:99], v[74:75], v[68:69] op_sel_hi:[0,1,1]
	ds_read_b128 v[68:71], v67 offset:2592
	ds_read_b128 v[72:75], v67 offset:2608
	v_pk_mul_f32 v[92:93], v[8:9], v[36:37] op_sel_hi:[0,1]
	v_exp_f32_e32 v92, v92
	v_exp_f32_e32 v93, v93
	v_pk_mul_f32 v[94:95], v[8:9], v[38:39] op_sel_hi:[0,1]
	v_exp_f32_e32 v94, v94
	v_exp_f32_e32 v95, v95
	v_pk_mul_f32 v[76:77], v[76:77], v[92:93]
	v_cvt_f32_f16_sdwa v1, v54 dst_sel:DWORD dst_unused:UNUSED_PAD src0_sel:WORD_1
	s_waitcnt lgkmcnt(1)
	v_pk_fma_f32 v[76:77], v[98:99], v[68:69], v[76:77] op_sel_hi:[0,1,1]
	v_pk_mul_f32 v[68:69], v[96:97], v[94:95]
	v_mul_f32_e32 v1, 0x3c800000, v1
	v_pk_fma_f32 v[92:93], v[98:99], v[70:71], v[68:69] op_sel_hi:[0,1,1]
	v_pk_mul_f32 v[68:69], v[8:9], v[32:33] op_sel_hi:[0,1]
	v_exp_f32_e32 v68, v68
	v_exp_f32_e32 v69, v69
	v_pk_mul_f32 v[70:71], v[8:9], v[34:35] op_sel_hi:[0,1]
	v_exp_f32_e32 v70, v70
	v_exp_f32_e32 v71, v71
	v_pk_mul_f32 v[68:69], v[86:87], v[68:69]
	v_mul_f32_e32 v54, v52, v1
	s_waitcnt lgkmcnt(0)
	v_pk_fma_f32 v[86:87], v[98:99], v[72:73], v[68:69] op_sel_hi:[0,1,1]
	v_pk_mul_f32 v[68:69], v[78:79], v[70:71]
	v_pk_mul_f32 v[72:73], v[52:53], v[44:45] op_sel_hi:[0,1]
	v_pk_fma_f32 v[78:79], v[98:99], v[74:75], v[68:69] op_sel_hi:[0,1,1]
	ds_read_b128 v[68:71], v67 offset:2688
	v_exp_f32_e32 v94, v72
	v_exp_f32_e32 v95, v73
	v_pk_mul_f32 v[72:73], v[52:53], v[46:47] op_sel_hi:[0,1]
	v_exp_f32_e32 v96, v72
	v_exp_f32_e32 v97, v73
	v_pk_mul_f32 v[80:81], v[80:81], v[94:95]
	v_pk_mul_f32 v[94:95], v[52:53], v[40:41] op_sel_hi:[0,1]
	ds_read_b128 v[72:75], v67 offset:2704
	s_waitcnt lgkmcnt(1)
	v_pk_fma_f32 v[80:81], v[54:55], v[68:69], v[80:81] op_sel_hi:[0,1,1]
	v_pk_mul_f32 v[68:69], v[100:101], v[96:97]
	v_exp_f32_e32 v94, v94
	v_exp_f32_e32 v95, v95
	v_pk_mul_f32 v[96:97], v[52:53], v[42:43] op_sel_hi:[0,1]
	v_exp_f32_e32 v96, v96
	v_exp_f32_e32 v97, v97
	v_pk_fma_f32 v[98:99], v[54:55], v[70:71], v[68:69] op_sel_hi:[0,1,1]
	v_pk_mul_f32 v[68:69], v[82:83], v[94:95]
	s_waitcnt lgkmcnt(0)
	v_pk_fma_f32 v[82:83], v[54:55], v[72:73], v[68:69] op_sel_hi:[0,1,1]
	v_pk_mul_f32 v[68:69], v[84:85], v[96:97]
	s_nop 0
	v_pk_fma_f32 v[84:85], v[54:55], v[74:75], v[68:69] op_sel_hi:[0,1,1]
	ds_read_b128 v[68:71], v67 offset:2720
	ds_read_b128 v[72:75], v67 offset:2736
	v_pk_mul_f32 v[94:95], v[52:53], v[36:37] op_sel_hi:[0,1]
	v_exp_f32_e32 v94, v94
	v_exp_f32_e32 v95, v95
	v_pk_mul_f32 v[96:97], v[52:53], v[38:39] op_sel_hi:[0,1]
	v_exp_f32_e32 v96, v96
	v_exp_f32_e32 v97, v97
	v_pk_mul_f32 v[76:77], v[76:77], v[94:95]
	v_pk_mul_f32 v[94:95], v[52:53], v[34:35] op_sel_hi:[0,1]
	s_waitcnt lgkmcnt(1)
	v_pk_fma_f32 v[76:77], v[54:55], v[68:69], v[76:77] op_sel_hi:[0,1,1]
	v_pk_mul_f32 v[68:69], v[92:93], v[96:97]
	v_pk_mul_f32 v[92:93], v[52:53], v[32:33] op_sel_hi:[0,1]
	v_exp_f32_e32 v92, v92
	v_exp_f32_e32 v93, v93
	v_exp_f32_e32 v94, v94
	v_exp_f32_e32 v95, v95
	v_pk_fma_f32 v[96:97], v[54:55], v[70:71], v[68:69] op_sel_hi:[0,1,1]
	v_pk_mul_f32 v[68:69], v[86:87], v[92:93]
	v_cvt_f32_f16_e32 v1, v55
	s_waitcnt lgkmcnt(0)
	v_pk_fma_f32 v[86:87], v[54:55], v[72:73], v[68:69] op_sel_hi:[0,1,1]
	v_pk_mul_f32 v[68:69], v[78:79], v[94:95]
	v_mul_f32_e32 v1, 0x3c800000, v1
	v_pk_fma_f32 v[78:79], v[54:55], v[74:75], v[68:69] op_sel_hi:[0,1,1]
	ds_read_b128 v[68:71], v67 offset:2816
	ds_read_b128 v[72:75], v67 offset:2832
	v_pk_fma_f32 v[10:11], v[10:11], s[4:5], v[90:91] op_sel_hi:[1,0,0]
	s_nop 0
	v_min_f32_e32 v5, 0x41f00000, v10
	v_mul_f32_e32 v5, 0x3fb8aa3b, v5
	v_min_f32_e32 v9, 0x41f00000, v11
	v_exp_f32_e32 v5, v5
	v_mul_f32_e32 v9, 0x3fb8aa3b, v9
	v_exp_f32_e32 v9, v9
	v_cmp_lt_f32_e32 vcc, s5, v11
	v_add_f32_e32 v5, 1.0, v5
	v_log_f32_e32 v92, v5
	v_add_f32_e32 v5, 1.0, v9
	v_log_f32_e32 v93, v5
	s_nop 0
	v_pk_mul_f32 v[92:93], v[92:93], s[6:7] op_sel_hi:[1,0]
	s_nop 0
	v_cndmask_b32_e32 v11, v93, v11, vcc
	v_cmp_lt_f32_e32 vcc, s5, v10
	s_nop 1
	v_cndmask_b32_e32 v10, v92, v10, vcc
	v_pk_mul_f32 v[92:93], v[10:11], v[44:45] op_sel_hi:[0,1]
	v_exp_f32_e32 v92, v92
	v_exp_f32_e32 v93, v93
	v_pk_mul_f32 v[94:95], v[10:11], v[46:47] op_sel_hi:[0,1]
	v_exp_f32_e32 v94, v94
	v_exp_f32_e32 v95, v95
	v_mul_f32_e32 v54, v10, v1
	v_pk_mul_f32 v[80:81], v[80:81], v[92:93]
	v_pk_mul_f32 v[92:93], v[10:11], v[40:41] op_sel_hi:[0,1]
	s_waitcnt lgkmcnt(1)
	v_pk_fma_f32 v[80:81], v[54:55], v[68:69], v[80:81] op_sel_hi:[0,1,1]
	v_pk_mul_f32 v[68:69], v[98:99], v[94:95]
	v_exp_f32_e32 v92, v92
	v_exp_f32_e32 v93, v93
	v_pk_mul_f32 v[94:95], v[10:11], v[42:43] op_sel_hi:[0,1]
	v_exp_f32_e32 v94, v94
	v_exp_f32_e32 v95, v95
	v_pk_fma_f32 v[98:99], v[54:55], v[70:71], v[68:69] op_sel_hi:[0,1,1]
	v_pk_mul_f32 v[68:69], v[82:83], v[92:93]
	s_waitcnt lgkmcnt(0)
	v_pk_fma_f32 v[82:83], v[54:55], v[72:73], v[68:69] op_sel_hi:[0,1,1]
	v_pk_mul_f32 v[68:69], v[84:85], v[94:95]
	v_pk_mul_f32 v[72:73], v[10:11], v[36:37] op_sel_hi:[0,1]
	v_pk_fma_f32 v[84:85], v[54:55], v[74:75], v[68:69] op_sel_hi:[0,1,1]
	ds_read_b128 v[68:71], v67 offset:2848
	v_exp_f32_e32 v92, v72
	v_exp_f32_e32 v93, v73
	v_pk_mul_f32 v[72:73], v[10:11], v[38:39] op_sel_hi:[0,1]
	v_exp_f32_e32 v94, v72
	v_exp_f32_e32 v95, v73
	v_pk_mul_f32 v[76:77], v[76:77], v[92:93]
	v_pk_mul_f32 v[92:93], v[10:11], v[32:33] op_sel_hi:[0,1]
	ds_read_b128 v[72:75], v67 offset:2864
	s_waitcnt lgkmcnt(1)
	v_pk_fma_f32 v[76:77], v[54:55], v[68:69], v[76:77] op_sel_hi:[0,1,1]
	v_pk_mul_f32 v[68:69], v[96:97], v[94:95]
	v_exp_f32_e32 v92, v92
	v_exp_f32_e32 v93, v93
	v_pk_mul_f32 v[94:95], v[10:11], v[34:35] op_sel_hi:[0,1]
	v_exp_f32_e32 v94, v94
	v_exp_f32_e32 v95, v95
	v_pk_fma_f32 v[96:97], v[54:55], v[70:71], v[68:69] op_sel_hi:[0,1,1]
	v_pk_mul_f32 v[68:69], v[86:87], v[92:93]
	s_waitcnt lgkmcnt(0)
	v_pk_fma_f32 v[86:87], v[54:55], v[72:73], v[68:69] op_sel_hi:[0,1,1]
	v_pk_mul_f32 v[68:69], v[78:79], v[94:95]
	s_nop 0
	v_pk_fma_f32 v[78:79], v[54:55], v[74:75], v[68:69] op_sel_hi:[0,1,1]
	s_or_b32 s8, s2, 5
	s_ashr_i32 s9, s8, 31
	s_lshl_b64 s[8:9], s[8:9], 15
	v_mov_b32_e32 v92, v11
	v_cvt_f32_f16_sdwa v1, v55 dst_sel:DWORD dst_unused:UNUSED_PAD src0_sel:WORD_1
	v_lshl_add_u64 v[54:55], v[64:65], 0, s[8:9]
	v_mov_b32_e32 v9, v52
	v_pk_mul_f32 v[72:73], v[92:93], v[44:45] op_sel_hi:[0,1]
	global_store_dwordx4 v[54:55], v[8:11], off
	ds_read_b128 v[68:71], v67 offset:2944
	v_exp_f32_e32 v94, v72
	v_exp_f32_e32 v95, v73
	v_pk_mul_f32 v[72:73], v[92:93], v[46:47] op_sel_hi:[0,1]
	v_exp_f32_e32 v100, v72
	v_exp_f32_e32 v101, v73
	v_mul_f32_e32 v1, 0x3c800000, v1
	v_mul_f32_e32 v54, v11, v1
	v_pk_mul_f32 v[80:81], v[80:81], v[94:95]
	v_pk_mul_f32 v[94:95], v[92:93], v[40:41] op_sel_hi:[0,1]
	ds_read_b128 v[72:75], v67 offset:2960
	s_waitcnt lgkmcnt(1)
	v_pk_fma_f32 v[80:81], v[54:55], v[68:69], v[80:81] op_sel_hi:[0,1,1]
	v_pk_mul_f32 v[68:69], v[98:99], v[100:101]
	v_exp_f32_e32 v94, v94
	v_exp_f32_e32 v95, v95
	v_pk_mul_f32 v[98:99], v[92:93], v[42:43] op_sel_hi:[0,1]
	v_exp_f32_e32 v98, v98
	v_exp_f32_e32 v99, v99
	v_pk_fma_f32 v[100:101], v[54:55], v[70:71], v[68:69] op_sel_hi:[0,1,1]
	v_pk_mul_f32 v[68:69], v[82:83], v[94:95]
	s_waitcnt lgkmcnt(0)
	v_pk_fma_f32 v[82:83], v[54:55], v[72:73], v[68:69] op_sel_hi:[0,1,1]
	v_pk_mul_f32 v[68:69], v[84:85], v[98:99]
	s_nop 0
	v_pk_fma_f32 v[84:85], v[54:55], v[74:75], v[68:69] op_sel_hi:[0,1,1]
	ds_read_b128 v[68:71], v67 offset:2976
	ds_read_b128 v[72:75], v67 offset:2992
	v_pk_mul_f32 v[94:95], v[92:93], v[36:37] op_sel_hi:[0,1]
	v_exp_f32_e32 v94, v94
	v_exp_f32_e32 v95, v95
	v_pk_mul_f32 v[98:99], v[92:93], v[38:39] op_sel_hi:[0,1]
	v_exp_f32_e32 v98, v98
	v_exp_f32_e32 v99, v99
	v_pk_mul_f32 v[76:77], v[76:77], v[94:95]
	v_pk_mul_f32 v[94:95], v[92:93], v[32:33] op_sel_hi:[0,1]
	v_exp_f32_e32 v94, v94
	v_exp_f32_e32 v95, v95
	v_pk_mul_f32 v[92:93], v[92:93], v[34:35] op_sel_hi:[0,1]
	v_exp_f32_e32 v92, v92
	v_exp_f32_e32 v93, v93
	s_waitcnt lgkmcnt(1)
	v_pk_fma_f32 v[76:77], v[54:55], v[68:69], v[76:77] op_sel_hi:[0,1,1]
	v_pk_mul_f32 v[68:69], v[96:97], v[98:99]
	s_waitcnt vmcnt(7)
	v_cvt_f32_f16_e32 v1, v48
	v_pk_fma_f32 v[96:97], v[54:55], v[70:71], v[68:69] op_sel_hi:[0,1,1]
	v_pk_mul_f32 v[68:69], v[86:87], v[94:95]
	v_mul_f32_e32 v1, 0x3c800000, v1
	s_waitcnt lgkmcnt(0)
	v_pk_fma_f32 v[86:87], v[54:55], v[72:73], v[68:69] op_sel_hi:[0,1,1]
	v_pk_mul_f32 v[68:69], v[78:79], v[92:93]
	s_nop 0
	v_pk_fma_f32 v[78:79], v[54:55], v[74:75], v[68:69] op_sel_hi:[0,1,1]
	ds_read_b128 v[68:71], v67 offset:3072
	ds_read_b128 v[72:75], v67 offset:3088
	v_pk_fma_f32 v[28:29], v[28:29], s[4:5], v[90:91] op_sel_hi:[1,0,0]
	s_nop 0
	v_min_f32_e32 v5, 0x41f00000, v28
	v_mul_f32_e32 v5, 0x3fb8aa3b, v5
	v_min_f32_e32 v9, 0x41f00000, v29
	v_exp_f32_e32 v5, v5
	v_mul_f32_e32 v9, 0x3fb8aa3b, v9
	v_exp_f32_e32 v9, v9
	v_cmp_lt_f32_e32 vcc, s5, v28
	v_add_f32_e32 v5, 1.0, v5
	v_log_f32_e32 v54, v5
	v_add_f32_e32 v5, 1.0, v9
	v_log_f32_e32 v55, v5
	s_nop 0
	v_pk_mul_f32 v[54:55], v[54:55], s[6:7] op_sel_hi:[1,0]
	s_nop 0
	v_cndmask_b32_e32 v28, v54, v28, vcc
	v_pk_mul_f32 v[92:93], v[28:29], v[44:45] op_sel_hi:[0,1]
	v_exp_f32_e32 v92, v92
	v_exp_f32_e32 v93, v93
	v_pk_mul_f32 v[94:95], v[28:29], v[46:47] op_sel_hi:[0,1]
	v_exp_f32_e32 v94, v94
	v_exp_f32_e32 v95, v95
	v_mul_f32_e32 v98, v28, v1
	v_pk_mul_f32 v[80:81], v[80:81], v[92:93]
	v_pk_mul_f32 v[92:93], v[28:29], v[40:41] op_sel_hi:[0,1]
	s_waitcnt lgkmcnt(1)
	v_pk_fma_f32 v[80:81], v[98:99], v[68:69], v[80:81] op_sel_hi:[0,1,1]
	v_pk_mul_f32 v[68:69], v[100:101], v[94:95]
	v_exp_f32_e32 v92, v92
	v_exp_f32_e32 v93, v93
	v_pk_mul_f32 v[94:95], v[28:29], v[42:43] op_sel_hi:[0,1]
	v_exp_f32_e32 v94, v94
	v_exp_f32_e32 v95, v95
	v_pk_fma_f32 v[100:101], v[98:99], v[70:71], v[68:69] op_sel_hi:[0,1,1]
	v_pk_mul_f32 v[68:69], v[82:83], v[92:93]
	v_cmp_lt_f32_e32 vcc, s5, v29
	s_waitcnt lgkmcnt(0)
	v_pk_fma_f32 v[82:83], v[98:99], v[72:73], v[68:69] op_sel_hi:[0,1,1]
	v_pk_mul_f32 v[68:69], v[84:85], v[94:95]
	v_cndmask_b32_e32 v54, v55, v29, vcc
	v_pk_fma_f32 v[84:85], v[98:99], v[74:75], v[68:69] op_sel_hi:[0,1,1]
	ds_read_b128 v[68:71], v67 offset:3104
	ds_read_b128 v[72:75], v67 offset:3120
	v_pk_mul_f32 v[92:93], v[28:29], v[36:37] op_sel_hi:[0,1]
	v_exp_f32_e32 v92, v92
	v_exp_f32_e32 v93, v93
	v_pk_mul_f32 v[94:95], v[28:29], v[38:39] op_sel_hi:[0,1]
	v_exp_f32_e32 v94, v94
	v_exp_f32_e32 v95, v95
	v_pk_mul_f32 v[76:77], v[76:77], v[92:93]
	v_cvt_f32_f16_sdwa v1, v48 dst_sel:DWORD dst_unused:UNUSED_PAD src0_sel:WORD_1
	s_waitcnt lgkmcnt(1)
	v_pk_fma_f32 v[76:77], v[98:99], v[68:69], v[76:77] op_sel_hi:[0,1,1]
	v_pk_mul_f32 v[68:69], v[96:97], v[94:95]
	v_mul_f32_e32 v1, 0x3c800000, v1
	v_pk_fma_f32 v[92:93], v[98:99], v[70:71], v[68:69] op_sel_hi:[0,1,1]
	v_pk_mul_f32 v[68:69], v[28:29], v[32:33] op_sel_hi:[0,1]
	v_exp_f32_e32 v68, v68
	v_exp_f32_e32 v69, v69
	v_pk_mul_f32 v[70:71], v[28:29], v[34:35] op_sel_hi:[0,1]
	v_exp_f32_e32 v70, v70
	v_exp_f32_e32 v71, v71
	v_pk_mul_f32 v[68:69], v[86:87], v[68:69]
	v_mul_f32_e32 v48, v54, v1
	s_waitcnt lgkmcnt(0)
	v_pk_fma_f32 v[86:87], v[98:99], v[72:73], v[68:69] op_sel_hi:[0,1,1]
	v_pk_mul_f32 v[68:69], v[78:79], v[70:71]
	v_pk_mul_f32 v[72:73], v[54:55], v[44:45] op_sel_hi:[0,1]
	v_pk_fma_f32 v[78:79], v[98:99], v[74:75], v[68:69] op_sel_hi:[0,1,1]
	ds_read_b128 v[68:71], v67 offset:3200
	v_exp_f32_e32 v94, v72
	v_exp_f32_e32 v95, v73
	v_pk_mul_f32 v[72:73], v[54:55], v[46:47] op_sel_hi:[0,1]
	v_exp_f32_e32 v96, v72
	v_exp_f32_e32 v97, v73
	v_pk_mul_f32 v[80:81], v[80:81], v[94:95]
	v_pk_mul_f32 v[94:95], v[54:55], v[40:41] op_sel_hi:[0,1]
	ds_read_b128 v[72:75], v67 offset:3216
	s_waitcnt lgkmcnt(1)
	v_pk_fma_f32 v[80:81], v[48:49], v[68:69], v[80:81] op_sel_hi:[0,1,1]
	v_pk_mul_f32 v[68:69], v[100:101], v[96:97]
	v_exp_f32_e32 v94, v94
	v_exp_f32_e32 v95, v95
	v_pk_mul_f32 v[96:97], v[54:55], v[42:43] op_sel_hi:[0,1]
	v_exp_f32_e32 v96, v96
	v_exp_f32_e32 v97, v97
	v_pk_fma_f32 v[98:99], v[48:49], v[70:71], v[68:69] op_sel_hi:[0,1,1]
	v_pk_mul_f32 v[68:69], v[82:83], v[94:95]
	s_waitcnt lgkmcnt(0)
	v_pk_fma_f32 v[82:83], v[48:49], v[72:73], v[68:69] op_sel_hi:[0,1,1]
	v_pk_mul_f32 v[68:69], v[84:85], v[96:97]
	s_nop 0
	v_pk_fma_f32 v[84:85], v[48:49], v[74:75], v[68:69] op_sel_hi:[0,1,1]
	ds_read_b128 v[68:71], v67 offset:3232
	ds_read_b128 v[72:75], v67 offset:3248
	v_pk_mul_f32 v[94:95], v[54:55], v[36:37] op_sel_hi:[0,1]
	v_exp_f32_e32 v94, v94
	v_exp_f32_e32 v95, v95
	v_pk_mul_f32 v[96:97], v[54:55], v[38:39] op_sel_hi:[0,1]
	v_exp_f32_e32 v96, v96
	v_exp_f32_e32 v97, v97
	v_pk_mul_f32 v[76:77], v[76:77], v[94:95]
	v_pk_mul_f32 v[94:95], v[54:55], v[34:35] op_sel_hi:[0,1]
	s_waitcnt lgkmcnt(1)
	v_pk_fma_f32 v[76:77], v[48:49], v[68:69], v[76:77] op_sel_hi:[0,1,1]
	v_pk_mul_f32 v[68:69], v[92:93], v[96:97]
	v_pk_mul_f32 v[92:93], v[54:55], v[32:33] op_sel_hi:[0,1]
	v_exp_f32_e32 v92, v92
	v_exp_f32_e32 v93, v93
	v_exp_f32_e32 v94, v94
	v_exp_f32_e32 v95, v95
	v_pk_fma_f32 v[96:97], v[48:49], v[70:71], v[68:69] op_sel_hi:[0,1,1]
	v_pk_mul_f32 v[68:69], v[86:87], v[92:93]
	v_cvt_f32_f16_e32 v1, v49
	s_waitcnt lgkmcnt(0)
	v_pk_fma_f32 v[86:87], v[48:49], v[72:73], v[68:69] op_sel_hi:[0,1,1]
	v_pk_mul_f32 v[68:69], v[78:79], v[94:95]
	v_mul_f32_e32 v1, 0x3c800000, v1
	v_pk_fma_f32 v[78:79], v[48:49], v[74:75], v[68:69] op_sel_hi:[0,1,1]
	ds_read_b128 v[68:71], v67 offset:3328
	ds_read_b128 v[72:75], v67 offset:3344
	v_pk_fma_f32 v[30:31], v[30:31], s[4:5], v[90:91] op_sel_hi:[1,0,0]
	s_nop 0
	v_min_f32_e32 v5, 0x41f00000, v30
	v_mul_f32_e32 v5, 0x3fb8aa3b, v5
	v_min_f32_e32 v9, 0x41f00000, v31
	v_exp_f32_e32 v5, v5
	v_mul_f32_e32 v9, 0x3fb8aa3b, v9
	v_exp_f32_e32 v9, v9
	v_cmp_lt_f32_e32 vcc, s5, v31
	v_add_f32_e32 v5, 1.0, v5
	v_log_f32_e32 v92, v5
	v_add_f32_e32 v5, 1.0, v9
	v_log_f32_e32 v93, v5
	s_nop 0
	v_pk_mul_f32 v[92:93], v[92:93], s[6:7] op_sel_hi:[1,0]
	s_nop 0
	v_cndmask_b32_e32 v31, v93, v31, vcc
	v_cmp_lt_f32_e32 vcc, s5, v30
	s_nop 1
	v_cndmask_b32_e32 v30, v92, v30, vcc
	v_pk_mul_f32 v[92:93], v[30:31], v[44:45] op_sel_hi:[0,1]
	v_exp_f32_e32 v92, v92
	v_exp_f32_e32 v93, v93
	v_pk_mul_f32 v[94:95], v[30:31], v[46:47] op_sel_hi:[0,1]
	v_exp_f32_e32 v94, v94
	v_exp_f32_e32 v95, v95
	v_mul_f32_e32 v48, v30, v1
	v_pk_mul_f32 v[80:81], v[80:81], v[92:93]
	v_pk_mul_f32 v[92:93], v[30:31], v[40:41] op_sel_hi:[0,1]
	s_waitcnt lgkmcnt(1)
	v_pk_fma_f32 v[80:81], v[48:49], v[68:69], v[80:81] op_sel_hi:[0,1,1]
	v_pk_mul_f32 v[68:69], v[98:99], v[94:95]
	v_exp_f32_e32 v92, v92
	v_exp_f32_e32 v93, v93
	v_pk_mul_f32 v[94:95], v[30:31], v[42:43] op_sel_hi:[0,1]
	v_exp_f32_e32 v94, v94
	v_exp_f32_e32 v95, v95
	v_pk_fma_f32 v[98:99], v[48:49], v[70:71], v[68:69] op_sel_hi:[0,1,1]
	v_pk_mul_f32 v[68:69], v[82:83], v[92:93]
	s_waitcnt lgkmcnt(0)
	v_pk_fma_f32 v[82:83], v[48:49], v[72:73], v[68:69] op_sel_hi:[0,1,1]
	v_pk_mul_f32 v[68:69], v[84:85], v[94:95]
	v_pk_mul_f32 v[72:73], v[30:31], v[36:37] op_sel_hi:[0,1]
	v_pk_fma_f32 v[84:85], v[48:49], v[74:75], v[68:69] op_sel_hi:[0,1,1]
	ds_read_b128 v[68:71], v67 offset:3360
	v_exp_f32_e32 v92, v72
	v_exp_f32_e32 v93, v73
	v_pk_mul_f32 v[72:73], v[30:31], v[38:39] op_sel_hi:[0,1]
	v_exp_f32_e32 v94, v72
	v_exp_f32_e32 v95, v73
	v_pk_mul_f32 v[76:77], v[76:77], v[92:93]
	v_pk_mul_f32 v[92:93], v[30:31], v[32:33] op_sel_hi:[0,1]
	ds_read_b128 v[72:75], v67 offset:3376
	s_waitcnt lgkmcnt(1)
	v_pk_fma_f32 v[76:77], v[48:49], v[68:69], v[76:77] op_sel_hi:[0,1,1]
	v_pk_mul_f32 v[68:69], v[96:97], v[94:95]
	v_exp_f32_e32 v92, v92
	v_exp_f32_e32 v93, v93
	v_pk_mul_f32 v[94:95], v[30:31], v[34:35] op_sel_hi:[0,1]
	v_exp_f32_e32 v94, v94
	v_exp_f32_e32 v95, v95
	v_pk_fma_f32 v[96:97], v[48:49], v[70:71], v[68:69] op_sel_hi:[0,1,1]
	v_pk_mul_f32 v[68:69], v[86:87], v[92:93]
	s_waitcnt lgkmcnt(0)
	v_pk_fma_f32 v[86:87], v[48:49], v[72:73], v[68:69] op_sel_hi:[0,1,1]
	v_pk_mul_f32 v[68:69], v[78:79], v[94:95]
	s_nop 0
	v_pk_fma_f32 v[78:79], v[48:49], v[74:75], v[68:69] op_sel_hi:[0,1,1]
	s_or_b32 s8, s2, 6
	s_ashr_i32 s9, s8, 31
	s_lshl_b64 s[8:9], s[8:9], 15
	v_mov_b32_e32 v92, v31
	v_cvt_f32_f16_sdwa v1, v49 dst_sel:DWORD dst_unused:UNUSED_PAD src0_sel:WORD_1
	v_lshl_add_u64 v[48:49], v[64:65], 0, s[8:9]
	v_mov_b32_e32 v29, v54
	v_pk_mul_f32 v[72:73], v[92:93], v[44:45] op_sel_hi:[0,1]
	global_store_dwordx4 v[48:49], v[28:31], off
	ds_read_b128 v[68:71], v67 offset:3456
	v_exp_f32_e32 v94, v72
	v_exp_f32_e32 v95, v73
	v_pk_mul_f32 v[72:73], v[92:93], v[46:47] op_sel_hi:[0,1]
	v_exp_f32_e32 v100, v72
	v_exp_f32_e32 v101, v73
	v_mul_f32_e32 v1, 0x3c800000, v1
	v_mul_f32_e32 v48, v31, v1
	v_pk_mul_f32 v[80:81], v[80:81], v[94:95]
	v_pk_mul_f32 v[94:95], v[92:93], v[40:41] op_sel_hi:[0,1]
	ds_read_b128 v[72:75], v67 offset:3472
	s_waitcnt lgkmcnt(1)
	v_pk_fma_f32 v[80:81], v[48:49], v[68:69], v[80:81] op_sel_hi:[0,1,1]
	v_pk_mul_f32 v[68:69], v[98:99], v[100:101]
	v_exp_f32_e32 v94, v94
	v_exp_f32_e32 v95, v95
	v_pk_mul_f32 v[98:99], v[92:93], v[42:43] op_sel_hi:[0,1]
	v_exp_f32_e32 v98, v98
	v_exp_f32_e32 v99, v99
	v_pk_fma_f32 v[100:101], v[48:49], v[70:71], v[68:69] op_sel_hi:[0,1,1]
	v_pk_mul_f32 v[68:69], v[82:83], v[94:95]
	s_waitcnt lgkmcnt(0)
	v_pk_fma_f32 v[82:83], v[48:49], v[72:73], v[68:69] op_sel_hi:[0,1,1]
	v_pk_mul_f32 v[68:69], v[84:85], v[98:99]
	s_nop 0
	v_pk_fma_f32 v[84:85], v[48:49], v[74:75], v[68:69] op_sel_hi:[0,1,1]
	ds_read_b128 v[68:71], v67 offset:3488
	ds_read_b128 v[72:75], v67 offset:3504
	v_pk_mul_f32 v[94:95], v[92:93], v[36:37] op_sel_hi:[0,1]
	v_exp_f32_e32 v94, v94
	v_exp_f32_e32 v95, v95
	v_pk_mul_f32 v[98:99], v[92:93], v[38:39] op_sel_hi:[0,1]
	v_exp_f32_e32 v98, v98
	v_exp_f32_e32 v99, v99
	v_pk_mul_f32 v[76:77], v[76:77], v[94:95]
	v_pk_mul_f32 v[94:95], v[92:93], v[32:33] op_sel_hi:[0,1]
	v_exp_f32_e32 v94, v94
	v_exp_f32_e32 v95, v95
	v_pk_mul_f32 v[92:93], v[92:93], v[34:35] op_sel_hi:[0,1]
	v_exp_f32_e32 v92, v92
	v_exp_f32_e32 v93, v93
	s_waitcnt lgkmcnt(1)
	v_pk_fma_f32 v[76:77], v[48:49], v[68:69], v[76:77] op_sel_hi:[0,1,1]
	v_pk_mul_f32 v[68:69], v[96:97], v[98:99]
	v_cvt_f32_f16_e32 v1, v50
	v_pk_fma_f32 v[96:97], v[48:49], v[70:71], v[68:69] op_sel_hi:[0,1,1]
	v_pk_mul_f32 v[68:69], v[86:87], v[94:95]
	v_mul_f32_e32 v1, 0x3c800000, v1
	s_waitcnt lgkmcnt(0)
	v_pk_fma_f32 v[86:87], v[48:49], v[72:73], v[68:69] op_sel_hi:[0,1,1]
	v_pk_mul_f32 v[68:69], v[78:79], v[92:93]
	s_nop 0
	v_pk_fma_f32 v[78:79], v[48:49], v[74:75], v[68:69] op_sel_hi:[0,1,1]
	ds_read_b128 v[68:71], v67 offset:3584
	ds_read_b128 v[72:75], v67 offset:3600
	v_pk_fma_f32 v[12:13], v[12:13], s[4:5], v[90:91] op_sel_hi:[1,0,0]
	s_nop 0
	v_min_f32_e32 v5, 0x41f00000, v12
	v_mul_f32_e32 v5, 0x3fb8aa3b, v5
	v_min_f32_e32 v9, 0x41f00000, v13
	v_exp_f32_e32 v5, v5
	v_mul_f32_e32 v9, 0x3fb8aa3b, v9
	v_exp_f32_e32 v9, v9
	v_cmp_lt_f32_e32 vcc, s5, v12
	v_add_f32_e32 v5, 1.0, v5
	v_log_f32_e32 v48, v5
	v_add_f32_e32 v5, 1.0, v9
	v_log_f32_e32 v49, v5
	s_nop 0
	v_pk_mul_f32 v[48:49], v[48:49], s[6:7] op_sel_hi:[1,0]
	s_nop 0
	v_cndmask_b32_e32 v12, v48, v12, vcc
	v_pk_mul_f32 v[92:93], v[12:13], v[44:45] op_sel_hi:[0,1]
	v_exp_f32_e32 v92, v92
	v_exp_f32_e32 v93, v93
	v_pk_mul_f32 v[94:95], v[12:13], v[46:47] op_sel_hi:[0,1]
	v_exp_f32_e32 v94, v94
	v_exp_f32_e32 v95, v95
	v_mul_f32_e32 v98, v12, v1
	v_pk_mul_f32 v[80:81], v[80:81], v[92:93]
	v_pk_mul_f32 v[92:93], v[12:13], v[40:41] op_sel_hi:[0,1]
	s_waitcnt lgkmcnt(1)
	v_pk_fma_f32 v[80:81], v[98:99], v[68:69], v[80:81] op_sel_hi:[0,1,1]
	v_pk_mul_f32 v[68:69], v[100:101], v[94:95]
	v_exp_f32_e32 v92, v92
	v_exp_f32_e32 v93, v93
	v_pk_mul_f32 v[94:95], v[12:13], v[42:43] op_sel_hi:[0,1]
	v_exp_f32_e32 v94, v94
	v_exp_f32_e32 v95, v95
	v_pk_fma_f32 v[100:101], v[98:99], v[70:71], v[68:69] op_sel_hi:[0,1,1]
	v_pk_mul_f32 v[68:69], v[82:83], v[92:93]
	v_cmp_lt_f32_e32 vcc, s5, v13
	s_waitcnt lgkmcnt(0)
	v_pk_fma_f32 v[82:83], v[98:99], v[72:73], v[68:69] op_sel_hi:[0,1,1]
	v_pk_mul_f32 v[68:69], v[84:85], v[94:95]
	v_cndmask_b32_e32 v48, v49, v13, vcc
	v_pk_fma_f32 v[84:85], v[98:99], v[74:75], v[68:69] op_sel_hi:[0,1,1]
	ds_read_b128 v[68:71], v67 offset:3616
	ds_read_b128 v[72:75], v67 offset:3632
	v_pk_mul_f32 v[92:93], v[12:13], v[36:37] op_sel_hi:[0,1]
	v_exp_f32_e32 v92, v92
	v_exp_f32_e32 v93, v93
	v_pk_mul_f32 v[94:95], v[12:13], v[38:39] op_sel_hi:[0,1]
	v_exp_f32_e32 v94, v94
	v_exp_f32_e32 v95, v95
	v_pk_mul_f32 v[76:77], v[76:77], v[92:93]
	v_cvt_f32_f16_sdwa v1, v50 dst_sel:DWORD dst_unused:UNUSED_PAD src0_sel:WORD_1
	s_waitcnt lgkmcnt(1)
	v_pk_fma_f32 v[92:93], v[98:99], v[68:69], v[76:77] op_sel_hi:[0,1,1]
	v_pk_mul_f32 v[68:69], v[96:97], v[94:95]
	v_mul_f32_e32 v1, 0x3c800000, v1
	v_pk_fma_f32 v[94:95], v[98:99], v[70:71], v[68:69] op_sel_hi:[0,1,1]
	v_pk_mul_f32 v[68:69], v[12:13], v[32:33] op_sel_hi:[0,1]
	v_exp_f32_e32 v68, v68
	v_exp_f32_e32 v69, v69
	v_pk_mul_f32 v[70:71], v[12:13], v[34:35] op_sel_hi:[0,1]
	v_exp_f32_e32 v70, v70
	v_exp_f32_e32 v71, v71
	v_pk_mul_f32 v[68:69], v[86:87], v[68:69]
	v_mul_f32_e32 v50, v48, v1
	s_waitcnt lgkmcnt(0)
	v_pk_fma_f32 v[86:87], v[98:99], v[72:73], v[68:69] op_sel_hi:[0,1,1]
	v_pk_mul_f32 v[68:69], v[78:79], v[70:71]
	v_pk_mul_f32 v[72:73], v[48:49], v[44:45] op_sel_hi:[0,1]
	v_pk_fma_f32 v[96:97], v[98:99], v[74:75], v[68:69] op_sel_hi:[0,1,1]
	ds_read_b128 v[68:71], v67 offset:3712
	v_exp_f32_e32 v76, v72
	v_exp_f32_e32 v77, v73
	v_pk_mul_f32 v[72:73], v[48:49], v[46:47] op_sel_hi:[0,1]
	v_exp_f32_e32 v78, v72
	v_exp_f32_e32 v79, v73
	v_pk_mul_f32 v[76:77], v[80:81], v[76:77]
	ds_read_b128 v[72:75], v67 offset:3728
	s_waitcnt lgkmcnt(1)
	v_pk_fma_f32 v[80:81], v[50:51], v[68:69], v[76:77] op_sel_hi:[0,1,1]
	v_pk_mul_f32 v[76:77], v[48:49], v[40:41] op_sel_hi:[0,1]
	v_pk_mul_f32 v[68:69], v[100:101], v[78:79]
	v_exp_f32_e32 v76, v76
	v_exp_f32_e32 v77, v77
	v_pk_mul_f32 v[78:79], v[48:49], v[42:43] op_sel_hi:[0,1]
	v_exp_f32_e32 v78, v78
	v_exp_f32_e32 v79, v79
	v_pk_fma_f32 v[98:99], v[50:51], v[70:71], v[68:69] op_sel_hi:[0,1,1]
	v_pk_mul_f32 v[68:69], v[82:83], v[76:77]
	s_waitcnt lgkmcnt(0)
	v_pk_fma_f32 v[100:101], v[50:51], v[72:73], v[68:69] op_sel_hi:[0,1,1]
	v_pk_mul_f32 v[68:69], v[84:85], v[78:79]
	s_nop 0
	v_pk_fma_f32 v[102:103], v[50:51], v[74:75], v[68:69] op_sel_hi:[0,1,1]
	ds_read_b128 v[70:73], v67 offset:3744
	ds_read_b128 v[76:79], v67 offset:3760
	v_pk_mul_f32 v[68:69], v[48:49], v[36:37] op_sel_hi:[0,1]
	v_exp_f32_e32 v68, v68
	v_exp_f32_e32 v69, v69
	v_pk_mul_f32 v[74:75], v[48:49], v[38:39] op_sel_hi:[0,1]
	v_exp_f32_e32 v74, v74
	v_exp_f32_e32 v75, v75
	v_pk_mul_f32 v[68:69], v[92:93], v[68:69]
	v_cvt_f32_f16_e32 v1, v51
	s_waitcnt lgkmcnt(1)
	v_pk_fma_f32 v[70:71], v[50:51], v[70:71], v[68:69] op_sel_hi:[0,1,1]
	v_pk_mul_f32 v[68:69], v[94:95], v[74:75]
	v_pk_mul_f32 v[74:75], v[48:49], v[32:33] op_sel_hi:[0,1]
	v_exp_f32_e32 v82, v74
	v_exp_f32_e32 v83, v75
	v_pk_mul_f32 v[74:75], v[48:49], v[34:35] op_sel_hi:[0,1]
	v_exp_f32_e32 v84, v74
	v_exp_f32_e32 v85, v75
	v_pk_fma_f32 v[74:75], v[50:51], v[72:73], v[68:69] op_sel_hi:[0,1,1]
	v_pk_mul_f32 v[68:69], v[86:87], v[82:83]
	v_mul_f32_e32 v1, 0x3c800000, v1
	s_waitcnt lgkmcnt(0)
	v_pk_fma_f32 v[72:73], v[50:51], v[76:77], v[68:69] op_sel_hi:[0,1,1]
	v_pk_mul_f32 v[68:69], v[96:97], v[84:85]
	s_nop 0
	v_pk_fma_f32 v[68:69], v[50:51], v[78:79], v[68:69] op_sel_hi:[0,1,1]
	ds_read_b128 v[76:79], v67 offset:3840
	ds_read_b128 v[84:87], v67 offset:3856
	v_pk_fma_f32 v[14:15], v[14:15], s[4:5], v[90:91] op_sel_hi:[1,0,0]
	s_nop 0
	v_min_f32_e32 v5, 0x41f00000, v14
	v_mul_f32_e32 v5, 0x3fb8aa3b, v5
	v_min_f32_e32 v9, 0x41f00000, v15
	v_exp_f32_e32 v5, v5
	v_mul_f32_e32 v9, 0x3fb8aa3b, v9
	v_exp_f32_e32 v9, v9
	v_cmp_lt_f32_e32 vcc, s5, v15
	v_add_f32_e32 v5, 1.0, v5
	v_log_f32_e32 v82, v5
	v_add_f32_e32 v5, 1.0, v9
	v_log_f32_e32 v83, v5
	s_nop 0
	v_pk_mul_f32 v[82:83], v[82:83], s[6:7] op_sel_hi:[1,0]
	s_nop 0
	v_cndmask_b32_e32 v15, v83, v15, vcc
	v_cmp_lt_f32_e32 vcc, s5, v14
	s_nop 1
	v_cndmask_b32_e32 v14, v82, v14, vcc
	v_pk_mul_f32 v[82:83], v[14:15], v[44:45] op_sel_hi:[0,1]
	v_exp_f32_e32 v82, v82
	v_exp_f32_e32 v83, v83
	v_pk_mul_f32 v[90:91], v[14:15], v[46:47] op_sel_hi:[0,1]
	v_exp_f32_e32 v90, v90
	v_exp_f32_e32 v91, v91
	v_mul_f32_e32 v50, v14, v1
	v_pk_mul_f32 v[80:81], v[80:81], v[82:83]
	v_pk_mul_f32 v[82:83], v[14:15], v[40:41] op_sel_hi:[0,1]
	s_waitcnt lgkmcnt(1)
	v_pk_fma_f32 v[80:81], v[50:51], v[76:77], v[80:81] op_sel_hi:[0,1,1]
	v_pk_mul_f32 v[76:77], v[98:99], v[90:91]
	v_exp_f32_e32 v90, v82
	v_exp_f32_e32 v91, v83
	v_pk_mul_f32 v[82:83], v[14:15], v[42:43] op_sel_hi:[0,1]
	v_exp_f32_e32 v92, v82
	v_exp_f32_e32 v93, v83
	v_pk_fma_f32 v[82:83], v[50:51], v[78:79], v[76:77] op_sel_hi:[0,1,1]
	v_pk_mul_f32 v[76:77], v[100:101], v[90:91]
	s_waitcnt lgkmcnt(0)
	v_pk_fma_f32 v[78:79], v[50:51], v[84:85], v[76:77] op_sel_hi:[0,1,1]
	v_pk_mul_f32 v[76:77], v[102:103], v[92:93]
	s_nop 0
	v_pk_fma_f32 v[76:77], v[50:51], v[86:87], v[76:77] op_sel_hi:[0,1,1]
	ds_read_b128 v[84:87], v67 offset:3872
	ds_read_b128 v[90:93], v67 offset:3888
	v_add_f32_e32 v1, 0, v16
	v_add_f32_e32 v1, v1, v66
	v_add_f32_e32 v1, v1, v18
	v_add_f32_e32 v1, v1, v19
	v_add_f32_e32 v0, v1, v0
	v_add_f32_e32 v0, v0, v60
	v_add_f32_e32 v0, v0, v2
	v_add_f32_e32 v0, v0, v3
	v_add_f32_e32 v0, v0, v20
	v_add_f32_e32 v0, v0, v62
	v_add_f32_e32 v0, v0, v22
	v_add_f32_e32 v0, v0, v23
	v_add_f32_e32 v0, v0, v4
	v_add_f32_e32 v0, v0, v56
	v_add_f32_e32 v0, v0, v6
	v_add_f32_e32 v0, v0, v7
	v_add_f32_e32 v0, v0, v24
	v_add_f32_e32 v0, v0, v58
	v_add_f32_e32 v0, v0, v26
	v_add_f32_e32 v0, v0, v27
	v_add_f32_e32 v0, v0, v8
	s_or_b32 s2, s2, 7
	v_add_f32_e32 v0, v0, v52
	s_ashr_i32 s3, s2, 31
	v_add_f32_e32 v0, v0, v10
	s_lshl_b64 s[2:3], s[2:3], 15
	v_add_f32_e32 v2, v0, v11
	v_lshl_add_u64 v[0:1], v[64:65], 0, s[2:3]
	v_mov_b32_e32 v13, v48
	global_store_dwordx4 v[0:1], v[12:15], off
	v_add_f32_e32 v0, v2, v28
	v_add_f32_e32 v0, v0, v54
	v_add_f32_e32 v0, v0, v30
	v_add_f32_e32 v0, v0, v31
	v_add_f32_e32 v0, v0, v12
	v_add_f32_e32 v4, v0, v48
	v_pk_mul_f32 v[0:1], v[14:15], v[36:37] op_sel_hi:[0,1]
	v_exp_f32_e32 v0, v0
	v_exp_f32_e32 v1, v1
	v_pk_mul_f32 v[2:3], v[14:15], v[38:39] op_sel_hi:[0,1]
	v_exp_f32_e32 v2, v2
	v_exp_f32_e32 v3, v3
	v_pk_mul_f32 v[0:1], v[70:71], v[0:1]
	v_add_f32_e32 v48, v4, v14
	s_waitcnt lgkmcnt(1)
	v_pk_fma_f32 v[8:9], v[50:51], v[84:85], v[0:1] op_sel_hi:[0,1,1]
	v_pk_mul_f32 v[0:1], v[74:75], v[2:3]
	v_pk_mul_f32 v[2:3], v[14:15], v[34:35] op_sel_hi:[0,1]
	v_pk_fma_f32 v[10:11], v[50:51], v[86:87], v[0:1] op_sel_hi:[0,1,1]
	v_pk_mul_f32 v[0:1], v[14:15], v[32:33] op_sel_hi:[0,1]
	v_exp_f32_e32 v0, v0
	v_exp_f32_e32 v1, v1
	v_exp_f32_e32 v2, v2
	v_exp_f32_e32 v3, v3
	v_cvt_f32_f16_sdwa v4, v51 dst_sel:DWORD dst_unused:UNUSED_PAD src0_sel:WORD_1
	v_pk_mul_f32 v[0:1], v[72:73], v[0:1]
	v_mov_b32_e32 v18, v15
	s_waitcnt lgkmcnt(0)
	v_pk_fma_f32 v[12:13], v[50:51], v[90:91], v[0:1] op_sel_hi:[0,1,1]
	v_pk_mul_f32 v[0:1], v[68:69], v[2:3]
	v_pk_mul_f32 v[24:25], v[18:19], v[42:43] op_sel_hi:[0,1]
	v_pk_fma_f32 v[16:17], v[50:51], v[92:93], v[0:1] op_sel_hi:[0,1,1]
	v_mul_f32_e32 v0, 0x3c800000, v4
	v_pk_mul_f32 v[4:5], v[18:19], v[44:45] op_sel_hi:[0,1]
	v_mul_f32_e32 v14, v15, v0
	ds_read_b128 v[0:3], v67 offset:3968
	v_exp_f32_e32 v20, v4
	v_exp_f32_e32 v21, v5
	v_pk_mul_f32 v[4:5], v[18:19], v[46:47] op_sel_hi:[0,1]
	v_exp_f32_e32 v22, v4
	v_exp_f32_e32 v23, v5
	v_pk_mul_f32 v[20:21], v[80:81], v[20:21]
	ds_read_b128 v[4:7], v67 offset:3984
	s_waitcnt lgkmcnt(1)
	v_pk_fma_f32 v[20:21], v[14:15], v[0:1], v[20:21] op_sel_hi:[0,1,1]
	v_pk_mul_f32 v[0:1], v[82:83], v[22:23]
	v_pk_mul_f32 v[22:23], v[18:19], v[40:41] op_sel_hi:[0,1]
	v_exp_f32_e32 v22, v22
	v_exp_f32_e32 v23, v23
	v_exp_f32_e32 v24, v24
	v_exp_f32_e32 v25, v25
	v_pk_fma_f32 v[26:27], v[14:15], v[2:3], v[0:1] op_sel_hi:[0,1,1]
	v_pk_mul_f32 v[0:1], v[78:79], v[22:23]
	s_waitcnt lgkmcnt(0)
	v_pk_fma_f32 v[22:23], v[14:15], v[4:5], v[0:1] op_sel_hi:[0,1,1]
	v_pk_mul_f32 v[0:1], v[76:77], v[24:25]
	s_nop 0
	v_pk_fma_f32 v[24:25], v[14:15], v[6:7], v[0:1] op_sel_hi:[0,1,1]
	v_pk_mul_f32 v[4:5], v[18:19], v[36:37] op_sel_hi:[0,1]
	ds_read_b128 v[0:3], v67 offset:4000
	v_exp_f32_e32 v28, v4
	v_exp_f32_e32 v29, v5
	v_pk_mul_f32 v[4:5], v[18:19], v[38:39] op_sel_hi:[0,1]
	v_exp_f32_e32 v30, v4
	v_exp_f32_e32 v31, v5
	v_pk_mul_f32 v[8:9], v[8:9], v[28:29]
	ds_read_b128 v[4:7], v67 offset:4016
	s_waitcnt lgkmcnt(1)
	v_pk_fma_f32 v[0:1], v[14:15], v[0:1], v[8:9] op_sel_hi:[0,1,1]
	v_pk_mul_f32 v[8:9], v[10:11], v[30:31]
	v_pk_mul_f32 v[10:11], v[18:19], v[32:33] op_sel_hi:[0,1]
	v_exp_f32_e32 v10, v10
	v_exp_f32_e32 v11, v11
	v_pk_mul_f32 v[18:19], v[18:19], v[34:35] op_sel_hi:[0,1]
	v_exp_f32_e32 v18, v18
	v_exp_f32_e32 v19, v19
	v_pk_fma_f32 v[2:3], v[14:15], v[2:3], v[8:9] op_sel_hi:[0,1,1]
	v_pk_mul_f32 v[8:9], v[12:13], v[10:11]
	s_waitcnt lgkmcnt(0)
	v_pk_fma_f32 v[4:5], v[14:15], v[4:5], v[8:9] op_sel_hi:[0,1,1]
	v_pk_mul_f32 v[8:9], v[16:17], v[18:19]
	s_nop 0
	v_pk_fma_f32 v[6:7], v[14:15], v[6:7], v[8:9] op_sel_hi:[0,1,1]
	s_lshl_b64 s[2:3], s[0:1], 16
	s_add_u32 s2, s12, s2
	s_addc_u32 s3, s13, s3
	v_mul_f32_e32 v10, 0x43800000, v20
	v_mul_f32_e32 v11, 0x43800000, v21
	v_lshl_add_u64 v[8:9], s[2:3], 0, v[88:89]
	v_cvt_pk_f16_f32 v10, v10, v11
	global_store_dword v[8:9], v10, off
	v_mul_f32_e32 v10, 0x43800000, v26
	v_mul_f32_e32 v11, 0x43800000, v27
	s_movk_i32 s2, 0x2000
	v_cvt_pk_f16_f32 v12, v10, v11
	v_add_co_u32_e32 v10, vcc, s2, v8
	s_movk_i32 s2, 0x4000
	s_nop 0
	v_addc_co_u32_e32 v11, vcc, 0, v9, vcc
	global_store_dword v[10:11], v12, off
	v_mul_f32_e32 v10, 0x43800000, v22
	v_mul_f32_e32 v11, 0x43800000, v23
	v_cvt_pk_f16_f32 v12, v10, v11
	v_add_co_u32_e32 v10, vcc, s2, v8
	s_movk_i32 s2, 0x6000
	s_nop 0
	v_addc_co_u32_e32 v11, vcc, 0, v9, vcc
	global_store_dword v[10:11], v12, off
	v_mul_f32_e32 v10, 0x43800000, v24
	v_mul_f32_e32 v11, 0x43800000, v25
	v_cvt_pk_f16_f32 v12, v10, v11
	v_add_co_u32_e32 v10, vcc, s2, v8
	v_mul_f32_e32 v0, 0x43800000, v0
	s_nop 0
	v_addc_co_u32_e32 v11, vcc, 0, v9, vcc
	v_mul_f32_e32 v1, 0x43800000, v1
	s_mov_b32 s2, 0x8000
	global_store_dword v[10:11], v12, off
	v_cvt_pk_f16_f32 v10, v0, v1
	v_add_co_u32_e32 v0, vcc, s2, v8
	s_mov_b32 s2, 0xa000
	s_nop 0
	v_addc_co_u32_e32 v1, vcc, 0, v9, vcc
	global_store_dword v[0:1], v10, off
	v_mul_f32_e32 v0, 0x43800000, v2
	v_mul_f32_e32 v1, 0x43800000, v3
	v_cvt_pk_f16_f32 v2, v0, v1
	v_add_co_u32_e32 v0, vcc, s2, v8
	s_mov_b32 s2, 0xc000
	s_nop 0
	v_addc_co_u32_e32 v1, vcc, 0, v9, vcc
	global_store_dword v[0:1], v2, off
	v_mul_f32_e32 v0, 0x43800000, v4
	v_mul_f32_e32 v1, 0x43800000, v5
	v_cvt_pk_f16_f32 v2, v0, v1
	v_add_co_u32_e32 v0, vcc, s2, v8
	s_mov_b32 s2, 0xe000
	s_nop 0
	v_addc_co_u32_e32 v1, vcc, 0, v9, vcc
	global_store_dword v[0:1], v2, off
	v_mul_f32_e32 v0, 0x43800000, v6
	v_mul_f32_e32 v1, 0x43800000, v7
	s_lshl_b64 s[0:1], s[0:1], 13
	v_cvt_pk_f16_f32 v2, v0, v1
	v_add_co_u32_e32 v0, vcc, s2, v8
	s_add_u32 s0, s14, s0
	s_nop 0
	v_addc_co_u32_e32 v1, vcc, 0, v9, vcc
	s_addc_u32 s1, s15, s1
	global_store_dword v[0:1], v2, off
	v_add_f32_e32 v2, v48, v15
	v_lshl_add_u64 v[0:1], s[0:1], 0, v[88:89]
	global_store_dword v[0:1], v2, off
	s_endpgm
	.p2alignl 8, 3212836864

_Z10scan_pass2PKDF16_PKfS2_S0_S2_S0_PDF16_S2_:
	s_load_dwordx8 s[16:23], s[0:1], 0x0
	s_lshl_b32 s5, s4, 11
	s_lshl_b32 s6, s3, 5
	s_add_i32 s6, s5, s6
	s_ashr_i32 s7, s6, 31
	s_lshl_b32 s2, s2, 8
	s_lshl_b64 s[8:9], s[6:7], 7
	s_waitcnt lgkmcnt(0)
	s_add_u32 s8, s18, s8
	s_addc_u32 s9, s19, s9
	v_lshlrev_b32_e32 v38, 4, v0
	global_load_dwordx4 v[16:19], v38, s[8:9]
	s_load_dwordx8 s[8:15], s[0:1], 0x20
	s_lshl_b32 s0, s4, 6
	s_add_i32 s0, s0, s3
	v_and_b32_e32 v1, 0xc0, v0
	v_and_b32_e32 v0, 63, v0
	s_ashr_i32 s1, s0, 31
	v_or3_b32 v40, s2, v1, v0
	s_lshl_b64 s[0:1], s[0:1], 16
	v_ashrrev_i32_e32 v41, 31, v40
	s_add_u32 s2, s22, s0
	v_lshlrev_b64 v[0:1], 6, v[40:41]
	v_lshlrev_b64 v[20:21], 2, v[40:41]
	s_addc_u32 s3, s23, s1
	s_movk_i32 s7, 0x2000
	v_lshl_add_u64 v[22:23], s[20:21], 0, v[0:1]
	s_waitcnt lgkmcnt(0)
	v_lshl_add_u64 v[26:27], s[8:9], 0, v[20:21]
	v_lshl_add_u64 v[20:21], s[2:3], 0, v[20:21]
	global_load_dwordx4 v[0:3], v[22:23], off offset:48
	global_load_dwordx4 v[4:7], v[22:23], off offset:32
	global_load_dwordx4 v[8:11], v[22:23], off offset:16
	global_load_dwordx4 v[12:15], v[22:23], off
	global_load_dword v72, v[26:27], off
	v_add_co_u32_e32 v22, vcc, s7, v20
	s_movk_i32 s5, 0x4000
	s_nop 0
	v_addc_co_u32_e32 v23, vcc, 0, v21, vcc
	v_add_co_u32_e32 v26, vcc, s5, v20
	s_movk_i32 s18, 0x6000
	s_nop 0
	v_addc_co_u32_e32 v27, vcc, 0, v21, vcc
	v_add_co_u32_e32 v28, vcc, s18, v20
	s_mov_b32 s19, 0x8000
	s_nop 0
	v_addc_co_u32_e32 v29, vcc, 0, v21, vcc
	s_ashr_i32 s0, s6, 2
	v_add_co_u32_e32 v30, vcc, s19, v20
	s_mov_b32 s24, 0xa000
	s_ashr_i32 s1, s0, 31
	v_addc_co_u32_e32 v31, vcc, 0, v21, vcc
	v_add_co_u32_e32 v32, vcc, s24, v20
	s_lshl_b64 s[8:9], s[0:1], 15
	s_mov_b32 s25, 0xc000
	v_addc_co_u32_e32 v33, vcc, 0, v21, vcc
	s_add_u32 s2, s14, s8
	v_add_co_u32_e32 v34, vcc, s25, v20
	s_addc_u32 s3, s15, s9
	s_or_b32 s18, s0, 1
	s_mov_b32 s26, 0xe000
	v_addc_co_u32_e32 v35, vcc, 0, v21, vcc
	s_ashr_i32 s19, s18, 31
	v_lshlrev_b64 v[24:25], 4, v[40:41]
	v_add_co_u32_e32 v36, vcc, s26, v20
	s_lshl_b64 s[18:19], s[18:19], 15
	s_nop 0
	v_addc_co_u32_e32 v37, vcc, 0, v21, vcc
	global_load_dword v57, v[20:21], off
	global_load_dword v58, v[22:23], off
	global_load_dword v59, v[26:27], off
	global_load_dword v61, v[28:29], off
	global_load_dword v63, v[30:31], off
	global_load_dword v64, v[32:33], off
	global_load_dword v65, v[34:35], off
	global_load_dword v66, v[36:37], off
	v_lshl_add_u64 v[26:27], s[2:3], 0, v[24:25]
	s_add_u32 s2, s14, s18
	s_addc_u32 s3, s15, s19
	v_lshl_add_u64 v[46:47], s[14:15], 0, v[24:25]
	v_lshl_add_u64 v[44:45], s[16:17], 0, v[24:25]
	s_mov_b32 s4, 0x3b800000
	v_mov_b32_e32 v73, 0
	s_waitcnt vmcnt(13)
	ds_write_b128 v38, v[16:19]
	v_lshl_add_u64 v[16:17], s[2:3], 0, v[24:25]
	s_ashr_i32 s2, s6, 3
	s_ashr_i32 s3, s2, 31
	s_lshl_b64 s[20:21], s[2:3], 15
	s_add_u32 s20, s16, s20
	s_addc_u32 s21, s17, s21
	global_load_dwordx4 v[36:39], v[26:27], off
	global_load_dwordx4 v[20:23], v[16:17], off
	v_lshl_add_u64 v[16:17], s[20:21], 0, v[24:25]
	global_load_dwordx4 v[28:31], v[16:17], off
	s_add_u32 s8, s10, s8
	v_lshlrev_b64 v[18:19], 3, v[40:41]
	s_addc_u32 s9, s11, s9
	v_lshl_add_u64 v[26:27], s[8:9], 0, v[18:19]
	s_add_u32 s8, s10, s18
	s_addc_u32 s9, s11, s19
	v_lshl_add_u64 v[32:33], s[8:9], 0, v[18:19]
	v_add_co_u32_e32 v26, vcc, s5, v26
	v_lshl_add_u64 v[42:43], s[10:11], 0, v[18:19]
	s_or_b32 s8, s0, 2
	s_or_b32 s10, s0, 3
	v_addc_co_u32_e32 v27, vcc, 0, v27, vcc
	s_ashr_i32 s9, s8, 31
	s_ashr_i32 s11, s10, 31
	v_add_co_u32_e32 v16, vcc, s5, v32
	s_lshl_b64 s[8:9], s[8:9], 15
	s_lshl_b64 s[10:11], s[10:11], 15
	v_addc_co_u32_e32 v17, vcc, 0, v33, vcc
	global_load_dwordx2 v[54:55], v[26:27], off
	global_load_dwordx2 v[50:51], v[16:17], off
	v_lshl_add_u64 v[24:25], v[46:47], 0, s[8:9]
	v_lshl_add_u64 v[26:27], v[46:47], 0, s[10:11]
	s_waitcnt lgkmcnt(0)
	s_barrier
	global_load_dwordx4 v[32:35], v[24:25], off
	global_load_dwordx4 v[16:19], v[26:27], off
	v_lshl_add_u64 v[26:27], v[42:43], 0, s[8:9]
	s_or_b32 s14, s2, 1
	v_add_co_u32_e32 v52, vcc, s5, v26
	s_ashr_i32 s15, s14, 31
	v_lshl_add_u64 v[48:49], v[42:43], 0, s[10:11]
	v_addc_co_u32_e32 v53, vcc, 0, v27, vcc
	s_lshl_b64 s[14:15], s[14:15], 15
	v_add_co_u32_e32 v48, vcc, s5, v48
	v_lshl_add_u64 v[24:25], v[44:45], 0, s[14:15]
	s_nop 0
	v_addc_co_u32_e32 v49, vcc, 0, v49, vcc
	global_load_dwordx4 v[24:27], v[24:25], off
	s_nop 0
	global_load_dwordx2 v[52:53], v[52:53], off
	s_nop 0
	global_load_dwordx2 v[48:49], v[48:49], off
	s_waitcnt vmcnt(17)
	v_cvt_f32_f16_e32 v56, v57
	v_cvt_f32_f16_sdwa v57, v57 dst_sel:DWORD dst_unused:UNUSED_PAD src0_sel:WORD_1
	v_lshl_add_u32 v40, s6, 11, v40
	s_waitcnt vmcnt(14)
	v_cvt_f32_f16_e32 v60, v61
	v_cvt_f32_f16_sdwa v61, v61 dst_sel:DWORD dst_unused:UNUSED_PAD src0_sel:WORD_1
	v_pk_mul_f32 v[74:75], v[56:57], s[4:5] op_sel_hi:[1,0]
	v_cvt_f32_f16_e32 v56, v58
	v_cvt_f32_f16_sdwa v57, v58 dst_sel:DWORD dst_unused:UNUSED_PAD src0_sel:WORD_1
	v_cvt_f32_f16_e32 v58, v59
	v_cvt_f32_f16_sdwa v59, v59 dst_sel:DWORD dst_unused:UNUSED_PAD src0_sel:WORD_1
	s_waitcnt vmcnt(13)
	v_cvt_f32_f16_e32 v62, v63
	v_cvt_f32_f16_sdwa v63, v63 dst_sel:DWORD dst_unused:UNUSED_PAD src0_sel:WORD_1
	v_pk_mul_f32 v[76:77], v[56:57], s[4:5] op_sel_hi:[1,0]
	v_pk_mul_f32 v[78:79], v[58:59], s[4:5] op_sel_hi:[1,0]
	v_pk_mul_f32 v[80:81], v[60:61], s[4:5] op_sel_hi:[1,0]
	s_waitcnt vmcnt(12)
	v_cvt_f32_f16_e32 v56, v64
	v_cvt_f32_f16_sdwa v57, v64 dst_sel:DWORD dst_unused:UNUSED_PAD src0_sel:WORD_1
	s_waitcnt vmcnt(11)
	v_cvt_f32_f16_e32 v58, v65
	v_cvt_f32_f16_sdwa v59, v65 dst_sel:DWORD dst_unused:UNUSED_PAD src0_sel:WORD_1
	s_waitcnt vmcnt(10)
	v_cvt_f32_f16_e32 v60, v66
	v_cvt_f32_f16_sdwa v61, v66 dst_sel:DWORD dst_unused:UNUSED_PAD src0_sel:WORD_1
	v_pk_mul_f32 v[82:83], v[62:63], s[4:5] op_sel_hi:[1,0]
	v_pk_mul_f32 v[84:85], v[56:57], s[4:5] op_sel_hi:[1,0]
	v_pk_mul_f32 v[86:87], v[58:59], s[4:5] op_sel_hi:[1,0]
	v_pk_mul_f32 v[88:89], v[60:61], s[4:5] op_sel_hi:[1,0]
	s_waitcnt vmcnt(9)
	v_pk_mul_f32 v[92:93], v[36:37], v[12:13] op_sel_hi:[0,1]
	v_exp_f32_e32 v92, v92
	v_exp_f32_e32 v93, v93
	s_waitcnt vmcnt(7)
	v_cvt_f32_f16_e32 v41, v28
	v_pk_mul_f32 v[94:95], v[36:37], v[14:15] op_sel_hi:[0,1]
	v_exp_f32_e32 v94, v94
	v_exp_f32_e32 v95, v95
	ds_read_b128 v[56:59], v73
	ds_read_b128 v[60:63], v73 offset:16
	ds_read_b128 v[64:67], v73 offset:64
	ds_read_b128 v[68:71], v73 offset:80
	v_mul_f32_e32 v91, 0x3c800000, v41
	v_mul_f32_e32 v90, v91, v36
	v_pk_mul_f32 v[74:75], v[74:75], v[92:93]
	v_mov_b32_e32 v41, 0
	s_waitcnt lgkmcnt(3)
	v_pk_fma_f32 v[56:57], v[90:91], v[56:57], v[74:75] op_sel_hi:[0,1,1]
	v_pk_mul_f32 v[74:75], v[76:77], v[94:95]
	s_waitcnt lgkmcnt(1)
	v_pk_fma_f32 v[64:65], v[64:65], v[56:57], 0 op_sel_hi:[1,1,0]
	v_pk_fma_f32 v[58:59], v[90:91], v[58:59], v[74:75] op_sel_hi:[0,1,1]
	v_pk_fma_f32 v[64:65], v[66:67], v[58:59], v[64:65]
	v_pk_mul_f32 v[66:67], v[36:37], v[8:9] op_sel_hi:[0,1]
	v_exp_f32_e32 v66, v66
	v_exp_f32_e32 v67, v67
	v_pk_mul_f32 v[74:75], v[36:37], v[10:11] op_sel_hi:[0,1]
	v_exp_f32_e32 v74, v74
	v_exp_f32_e32 v75, v75
	v_pk_mul_f32 v[66:67], v[78:79], v[66:67]
	s_nop 0
	v_pk_fma_f32 v[60:61], v[90:91], v[60:61], v[66:67] op_sel_hi:[0,1,1]
	v_pk_mul_f32 v[66:67], v[80:81], v[74:75]
	s_waitcnt lgkmcnt(0)
	v_pk_fma_f32 v[64:65], v[68:69], v[60:61], v[64:65]
	v_pk_fma_f32 v[62:63], v[90:91], v[62:63], v[66:67] op_sel_hi:[0,1,1]
	v_pk_fma_f32 v[92:93], v[70:71], v[62:63], v[64:65]
	v_pk_mul_f32 v[94:95], v[36:37], v[4:5] op_sel_hi:[0,1]
	v_exp_f32_e32 v94, v94
	v_exp_f32_e32 v95, v95
	v_pk_mul_f32 v[96:97], v[36:37], v[6:7] op_sel_hi:[0,1]
	v_exp_f32_e32 v96, v96
	v_exp_f32_e32 v97, v97
	ds_read_b128 v[64:67], v73 offset:32
	ds_read_b128 v[68:71], v73 offset:48
	ds_read_b128 v[74:77], v73 offset:96
	ds_read_b128 v[78:81], v73 offset:112
	v_pk_mul_f32 v[82:83], v[82:83], v[94:95]
	s_waitcnt lgkmcnt(3)
	v_pk_fma_f32 v[64:65], v[90:91], v[64:65], v[82:83] op_sel_hi:[0,1,1]
	v_pk_mul_f32 v[82:83], v[84:85], v[96:97]
	s_waitcnt lgkmcnt(1)
	v_pk_fma_f32 v[74:75], v[74:75], v[64:65], v[92:93]
	v_pk_fma_f32 v[66:67], v[90:91], v[66:67], v[82:83] op_sel_hi:[0,1,1]
	v_pk_fma_f32 v[74:75], v[76:77], v[66:67], v[74:75]
	v_pk_mul_f32 v[76:77], v[36:37], v[0:1] op_sel_hi:[0,1]
	v_exp_f32_e32 v76, v76
	v_exp_f32_e32 v77, v77
	v_pk_mul_f32 v[82:83], v[36:37], v[2:3] op_sel_hi:[0,1]
	v_exp_f32_e32 v82, v82
	v_exp_f32_e32 v83, v83
	v_pk_mul_f32 v[76:77], v[86:87], v[76:77]
	s_nop 0
	v_pk_fma_f32 v[68:69], v[90:91], v[68:69], v[76:77] op_sel_hi:[0,1,1]
	v_pk_mul_f32 v[76:77], v[88:89], v[82:83]
	s_waitcnt lgkmcnt(0)
	v_pk_fma_f32 v[74:75], v[78:79], v[68:69], v[74:75]
	v_pk_fma_f32 v[70:71], v[90:91], v[70:71], v[76:77] op_sel_hi:[0,1,1]
	v_pk_fma_f32 v[74:75], v[80:81], v[70:71], v[74:75]
	s_waitcnt vmcnt(6)
	v_cvt_f32_f16_e32 v76, v54
	v_add_f32_e32 v74, v74, v75
	v_fmac_f32_e32 v74, v72, v91
	s_mov_b32 s1, 0x43800000
	v_mul_f32_e32 v74, v74, v76
	v_cvt_f32_f16_sdwa v28, v28 dst_sel:DWORD dst_unused:UNUSED_PAD src0_sel:WORD_1
	v_pk_mul_f32 v[90:91], v[36:37], v[12:13] op_sel:[1,0]
	v_pk_mul_f32 v[92:93], v[36:37], v[14:15] op_sel:[1,0]
	v_fma_mixlo_f16 v76, v74, s1, 0
	v_lshl_add_u64 v[74:75], v[40:41], 1, s[12:13]
	v_add_u32_e32 v40, 0x800, v40
	v_exp_f32_e32 v90, v90
	v_exp_f32_e32 v91, v91
	v_exp_f32_e32 v92, v92
	v_exp_f32_e32 v93, v93
	global_store_short v[74:75], v76, off
	ds_read_b128 v[74:77], v73 offset:128
	ds_read_b128 v[78:81], v73 offset:144
	ds_read_b128 v[82:85], v73 offset:192
	ds_read_b128 v[86:89], v73 offset:208
	v_mul_f32_e32 v96, 0x3c800000, v28
	v_mul_f32_e32 v28, v96, v37
	v_pk_mul_f32 v[56:57], v[56:57], v[90:91]
	v_pk_mul_f32 v[58:59], v[58:59], v[92:93]
	s_waitcnt lgkmcnt(3)
	v_pk_fma_f32 v[56:57], v[28:29], v[74:75], v[56:57] op_sel_hi:[0,1,1]
	v_pk_fma_f32 v[58:59], v[28:29], v[76:77], v[58:59] op_sel_hi:[0,1,1]
	v_pk_mul_f32 v[76:77], v[36:37], v[8:9] op_sel:[1,0]
	s_waitcnt lgkmcnt(1)
	v_pk_fma_f32 v[74:75], v[82:83], v[56:57], 0 op_sel_hi:[1,1,0]
	v_exp_f32_e32 v76, v76
	v_exp_f32_e32 v77, v77
	v_pk_mul_f32 v[82:83], v[36:37], v[10:11] op_sel:[1,0]
	v_pk_fma_f32 v[74:75], v[84:85], v[58:59], v[74:75]
	v_exp_f32_e32 v82, v82
	v_exp_f32_e32 v83, v83
	v_pk_mul_f32 v[60:61], v[60:61], v[76:77]
	v_pk_mul_f32 v[62:63], v[62:63], v[82:83]
	v_pk_fma_f32 v[60:61], v[28:29], v[78:79], v[60:61] op_sel_hi:[0,1,1]
	s_waitcnt lgkmcnt(0)
	v_pk_fma_f32 v[74:75], v[86:87], v[60:61], v[74:75]
	v_pk_fma_f32 v[62:63], v[28:29], v[80:81], v[62:63] op_sel_hi:[0,1,1]
	v_pk_fma_f32 v[90:91], v[88:89], v[62:63], v[74:75]
	v_pk_mul_f32 v[94:95], v[36:37], v[6:7] op_sel:[1,0]
	ds_read_b128 v[74:77], v73 offset:160
	ds_read_b128 v[78:81], v73 offset:176
	ds_read_b128 v[82:85], v73 offset:224
	ds_read_b128 v[86:89], v73 offset:240
	v_exp_f32_e32 v94, v94
	v_exp_f32_e32 v95, v95
	v_pk_mul_f32 v[92:93], v[36:37], v[4:5] op_sel:[1,0]
	v_pk_mul_f32 v[66:67], v[66:67], v[94:95]
	v_exp_f32_e32 v92, v92
	v_exp_f32_e32 v93, v93
	s_waitcnt lgkmcnt(3)
	v_pk_fma_f32 v[66:67], v[28:29], v[76:77], v[66:67] op_sel_hi:[0,1,1]
	v_pk_mul_f32 v[76:77], v[36:37], v[0:1] op_sel:[1,0]
	v_pk_mul_f32 v[36:37], v[36:37], v[2:3] op_sel:[1,0]
	v_exp_f32_e32 v76, v76
	v_exp_f32_e32 v77, v77
	v_exp_f32_e32 v36, v36
	v_exp_f32_e32 v37, v37
	v_pk_mul_f32 v[64:65], v[64:65], v[92:93]
	v_pk_mul_f32 v[68:69], v[68:69], v[76:77]
	v_pk_fma_f32 v[64:65], v[28:29], v[74:75], v[64:65] op_sel_hi:[0,1,1]
	s_waitcnt lgkmcnt(1)
	v_pk_fma_f32 v[74:75], v[82:83], v[64:65], v[90:91]
	v_pk_fma_f32 v[68:69], v[28:29], v[78:79], v[68:69] op_sel_hi:[0,1,1]
	v_pk_fma_f32 v[74:75], v[84:85], v[66:67], v[74:75]
	v_pk_mul_f32 v[36:37], v[70:71], v[36:37]
	s_waitcnt lgkmcnt(0)
	v_pk_fma_f32 v[74:75], v[86:87], v[68:69], v[74:75]
	v_pk_fma_f32 v[70:71], v[28:29], v[80:81], v[36:37] op_sel_hi:[0,1,1]
	v_pk_fma_f32 v[36:37], v[88:89], v[70:71], v[74:75]
	v_cvt_f32_f16_sdwa v28, v54 dst_sel:DWORD dst_unused:UNUSED_PAD src0_sel:WORD_1
	v_add_f32_e32 v54, v36, v37
	v_fmac_f32_e32 v54, v72, v96
	v_lshl_add_u64 v[36:37], v[40:41], 1, s[12:13]
	v_mul_f32_e32 v28, v54, v28
	v_fma_mixlo_f16 v28, v28, s1, 0
	v_cvt_f32_f16_e32 v54, v29
	global_store_short v[36:37], v28, off
	v_pk_mul_f32 v[36:37], v[38:39], v[12:13] op_sel_hi:[0,1]
	v_pk_mul_f32 v[90:91], v[38:39], v[14:15] op_sel_hi:[0,1]
	v_exp_f32_e32 v36, v36
	v_exp_f32_e32 v37, v37
	v_exp_f32_e32 v90, v90
	v_exp_f32_e32 v91, v91
	v_add_u32_e32 v40, 0x800, v40
	v_mul_f32_e32 v54, 0x3c800000, v54
	ds_read_b128 v[74:77], v73 offset:256
	ds_read_b128 v[78:81], v73 offset:272
	ds_read_b128 v[82:85], v73 offset:320
	ds_read_b128 v[86:89], v73 offset:336
	v_mul_f32_e32 v28, v54, v38
	v_pk_mul_f32 v[36:37], v[56:57], v[36:37]
	v_pk_mul_f32 v[56:57], v[58:59], v[90:91]
	v_pk_mul_f32 v[58:59], v[38:39], v[8:9] op_sel_hi:[0,1]
	s_waitcnt lgkmcnt(3)
	v_pk_fma_f32 v[56:57], v[28:29], v[76:77], v[56:57] op_sel_hi:[0,1,1]
	v_exp_f32_e32 v58, v58
	v_exp_f32_e32 v59, v59
	v_pk_mul_f32 v[76:77], v[38:39], v[10:11] op_sel_hi:[0,1]
	v_exp_f32_e32 v76, v76
	v_exp_f32_e32 v77, v77
	v_pk_fma_f32 v[36:37], v[28:29], v[74:75], v[36:37] op_sel_hi:[0,1,1]
	s_waitcnt lgkmcnt(1)
	v_pk_fma_f32 v[74:75], v[82:83], v[36:37], 0 op_sel_hi:[1,1,0]
	v_pk_mul_f32 v[58:59], v[60:61], v[58:59]
	v_pk_fma_f32 v[74:75], v[84:85], v[56:57], v[74:75]
	v_pk_fma_f32 v[58:59], v[28:29], v[78:79], v[58:59] op_sel_hi:[0,1,1]
	v_pk_mul_f32 v[60:61], v[62:63], v[76:77]
	s_waitcnt lgkmcnt(0)
	v_pk_fma_f32 v[74:75], v[86:87], v[58:59], v[74:75]
	v_pk_fma_f32 v[60:61], v[28:29], v[80:81], v[60:61] op_sel_hi:[0,1,1]
	v_pk_fma_f32 v[90:91], v[88:89], v[60:61], v[74:75]
	v_pk_mul_f32 v[62:63], v[38:39], v[4:5] op_sel_hi:[0,1]
	v_pk_mul_f32 v[92:93], v[38:39], v[6:7] op_sel_hi:[0,1]
	v_exp_f32_e32 v62, v62
	v_exp_f32_e32 v63, v63
	v_exp_f32_e32 v92, v92
	v_exp_f32_e32 v93, v93
	ds_read_b128 v[74:77], v73 offset:288
	ds_read_b128 v[78:81], v73 offset:304
	ds_read_b128 v[82:85], v73 offset:352
	ds_read_b128 v[86:89], v73 offset:368
	v_pk_mul_f32 v[62:63], v[64:65], v[62:63]
	v_pk_mul_f32 v[64:65], v[66:67], v[92:93]
	v_pk_mul_f32 v[66:67], v[38:39], v[0:1] op_sel_hi:[0,1]
	s_waitcnt lgkmcnt(3)
	v_pk_fma_f32 v[64:65], v[28:29], v[76:77], v[64:65] op_sel_hi:[0,1,1]
	v_exp_f32_e32 v66, v66
	v_exp_f32_e32 v67, v67
	v_pk_mul_f32 v[76:77], v[38:39], v[2:3] op_sel_hi:[0,1]
	v_exp_f32_e32 v76, v76
	v_exp_f32_e32 v77, v77
	v_pk_fma_f32 v[62:63], v[28:29], v[74:75], v[62:63] op_sel_hi:[0,1,1]
	s_waitcnt lgkmcnt(1)
	v_pk_fma_f32 v[74:75], v[82:83], v[62:63], v[90:91]
	v_pk_mul_f32 v[66:67], v[68:69], v[66:67]
	v_pk_fma_f32 v[74:75], v[84:85], v[64:65], v[74:75]
	v_pk_fma_f32 v[66:67], v[28:29], v[78:79], v[66:67] op_sel_hi:[0,1,1]
	v_pk_mul_f32 v[68:69], v[70:71], v[76:77]
	s_waitcnt lgkmcnt(0)
	v_pk_fma_f32 v[74:75], v[86:87], v[66:67], v[74:75]
	v_pk_fma_f32 v[68:69], v[28:29], v[80:81], v[68:69] op_sel_hi:[0,1,1]
	v_pk_fma_f32 v[70:71], v[88:89], v[68:69], v[74:75]
	v_cvt_f32_f16_e32 v28, v55
	v_add_f32_e32 v38, v70, v71
	v_fmac_f32_e32 v38, v72, v54
	v_cvt_f32_f16_sdwa v29, v29 dst_sel:DWORD dst_unused:UNUSED_PAD src0_sel:WORD_1
	v_mul_f32_e32 v28, v38, v28
	v_lshl_add_u64 v[70:71], v[40:41], 1, s[12:13]
	v_fma_mixlo_f16 v28, v28, s1, 0
	global_store_short v[70:71], v28, off
	v_mov_b32_e32 v70, v39
	v_mul_f32_e32 v92, 0x3c800000, v29
	v_pk_mul_f32 v[28:29], v[70:71], v[12:13] op_sel_hi:[0,1]
	v_add_u32_e32 v40, 0x800, v40
	v_mul_f32_e32 v54, v92, v39
	v_exp_f32_e32 v28, v28
	v_exp_f32_e32 v29, v29
	v_pk_mul_f32 v[38:39], v[70:71], v[14:15] op_sel_hi:[0,1]
	v_exp_f32_e32 v38, v38
	v_exp_f32_e32 v39, v39
	ds_read_b128 v[74:77], v73 offset:384
	ds_read_b128 v[78:81], v73 offset:400
	ds_read_b128 v[82:85], v73 offset:448
	ds_read_b128 v[86:89], v73 offset:464
	v_pk_mul_f32 v[28:29], v[36:37], v[28:29]
	v_pk_mul_f32 v[36:37], v[56:57], v[38:39]
	s_waitcnt lgkmcnt(3)
	v_pk_fma_f32 v[28:29], v[54:55], v[74:75], v[28:29] op_sel_hi:[0,1,1]
	v_pk_mul_f32 v[38:39], v[70:71], v[8:9] op_sel_hi:[0,1]
	s_waitcnt lgkmcnt(1)
	v_pk_fma_f32 v[74:75], v[82:83], v[28:29], 0 op_sel_hi:[1,1,0]
	v_pk_fma_f32 v[36:37], v[54:55], v[76:77], v[36:37] op_sel_hi:[0,1,1]
	v_exp_f32_e32 v38, v38
	v_exp_f32_e32 v39, v39
	v_pk_fma_f32 v[56:57], v[84:85], v[36:37], v[74:75]
	v_pk_mul_f32 v[74:75], v[70:71], v[10:11] op_sel_hi:[0,1]
	v_exp_f32_e32 v74, v74
	v_exp_f32_e32 v75, v75
	v_pk_mul_f32 v[38:39], v[58:59], v[38:39]
	s_nop 0
	v_pk_fma_f32 v[38:39], v[54:55], v[78:79], v[38:39] op_sel_hi:[0,1,1]
	s_waitcnt lgkmcnt(0)
	v_pk_fma_f32 v[58:59], v[86:87], v[38:39], v[56:57]
	v_pk_mul_f32 v[56:57], v[60:61], v[74:75]
	s_nop 0
	v_pk_fma_f32 v[56:57], v[54:55], v[80:81], v[56:57] op_sel_hi:[0,1,1]
	v_pk_fma_f32 v[86:87], v[88:89], v[56:57], v[58:59]
	v_pk_mul_f32 v[88:89], v[70:71], v[4:5] op_sel_hi:[0,1]
	v_exp_f32_e32 v88, v88
	v_exp_f32_e32 v89, v89
	v_pk_mul_f32 v[90:91], v[70:71], v[6:7] op_sel_hi:[0,1]
	v_exp_f32_e32 v90, v90
	v_exp_f32_e32 v91, v91
	ds_read_b128 v[58:61], v73 offset:416
	ds_read_b128 v[74:77], v73 offset:432
	ds_read_b128 v[78:81], v73 offset:480
	ds_read_b128 v[82:85], v73 offset:496
	v_pk_mul_f32 v[62:63], v[62:63], v[88:89]
	v_pk_mul_f32 v[64:65], v[64:65], v[90:91]
	s_waitcnt lgkmcnt(3)
	v_pk_fma_f32 v[58:59], v[54:55], v[58:59], v[62:63] op_sel_hi:[0,1,1]
	s_waitcnt lgkmcnt(1)
	v_pk_fma_f32 v[62:63], v[78:79], v[58:59], v[86:87]
	v_pk_fma_f32 v[60:61], v[54:55], v[60:61], v[64:65] op_sel_hi:[0,1,1]
	v_pk_fma_f32 v[64:65], v[80:81], v[60:61], v[62:63]
	v_pk_mul_f32 v[62:63], v[70:71], v[0:1] op_sel_hi:[0,1]
	v_exp_f32_e32 v62, v62
	v_exp_f32_e32 v63, v63
	v_pk_mul_f32 v[70:71], v[70:71], v[2:3] op_sel_hi:[0,1]
	v_exp_f32_e32 v70, v70
	v_exp_f32_e32 v71, v71
	v_pk_mul_f32 v[62:63], v[66:67], v[62:63]
	s_nop 0
	v_pk_fma_f32 v[62:63], v[54:55], v[74:75], v[62:63] op_sel_hi:[0,1,1]
	s_waitcnt lgkmcnt(0)
	v_pk_fma_f32 v[66:67], v[82:83], v[62:63], v[64:65]
	v_pk_mul_f32 v[64:65], v[68:69], v[70:71]
	s_nop 0
	v_pk_fma_f32 v[64:65], v[54:55], v[76:77], v[64:65] op_sel_hi:[0,1,1]
	v_pk_fma_f32 v[66:67], v[84:85], v[64:65], v[66:67]
	v_cvt_f32_f16_sdwa v68, v55 dst_sel:DWORD dst_unused:UNUSED_PAD src0_sel:WORD_1
	v_add_f32_e32 v66, v66, v67
	v_fmac_f32_e32 v66, v72, v92
	v_lshl_add_u64 v[54:55], v[40:41], 1, s[12:13]
	v_mul_f32_e32 v66, v66, v68
	v_fma_mixlo_f16 v66, v66, s1, 0
	v_cvt_f32_f16_e32 v67, v30
	global_store_short v[54:55], v66, off
	v_pk_mul_f32 v[54:55], v[20:21], v[12:13] op_sel_hi:[0,1]
	v_exp_f32_e32 v54, v54
	v_exp_f32_e32 v55, v55
	v_add_u32_e32 v40, 0x800, v40
	v_pk_mul_f32 v[86:87], v[20:21], v[14:15] op_sel_hi:[0,1]
	v_exp_f32_e32 v86, v86
	v_exp_f32_e32 v87, v87
	v_mul_f32_e32 v71, 0x3c800000, v67
	ds_read_b128 v[66:69], v73 offset:512
	ds_read_b128 v[74:77], v73 offset:528
	ds_read_b128 v[78:81], v73 offset:576
	ds_read_b128 v[82:85], v73 offset:592
	v_mul_f32_e32 v70, v71, v20
	v_pk_mul_f32 v[28:29], v[28:29], v[54:55]
	v_pk_mul_f32 v[36:37], v[36:37], v[86:87]
	s_waitcnt lgkmcnt(3)
	v_pk_fma_f32 v[28:29], v[70:71], v[66:67], v[28:29] op_sel_hi:[0,1,1]
	v_pk_mul_f32 v[66:67], v[20:21], v[8:9] op_sel_hi:[0,1]
	v_exp_f32_e32 v66, v66
	v_exp_f32_e32 v67, v67
	v_pk_fma_f32 v[36:37], v[70:71], v[68:69], v[36:37] op_sel_hi:[0,1,1]
	v_pk_mul_f32 v[68:69], v[20:21], v[10:11] op_sel_hi:[0,1]
	v_exp_f32_e32 v68, v68
	v_exp_f32_e32 v69, v69
	s_waitcnt lgkmcnt(1)
	v_pk_fma_f32 v[54:55], v[78:79], v[28:29], 0 op_sel_hi:[1,1,0]
	v_pk_mul_f32 v[38:39], v[38:39], v[66:67]
	v_pk_fma_f32 v[54:55], v[80:81], v[36:37], v[54:55]
	v_pk_fma_f32 v[38:39], v[70:71], v[74:75], v[38:39] op_sel_hi:[0,1,1]
	s_waitcnt lgkmcnt(0)
	v_pk_fma_f32 v[66:67], v[82:83], v[38:39], v[54:55]
	v_pk_mul_f32 v[54:55], v[56:57], v[68:69]
	s_nop 0
	v_pk_fma_f32 v[54:55], v[70:71], v[76:77], v[54:55] op_sel_hi:[0,1,1]
	v_pk_fma_f32 v[86:87], v[84:85], v[54:55], v[66:67]
	v_pk_mul_f32 v[56:57], v[20:21], v[4:5] op_sel_hi:[0,1]
	v_pk_mul_f32 v[88:89], v[20:21], v[6:7] op_sel_hi:[0,1]
	v_exp_f32_e32 v56, v56
	v_exp_f32_e32 v57, v57
	v_exp_f32_e32 v88, v88
	v_exp_f32_e32 v89, v89
	ds_read_b128 v[66:69], v73 offset:544
	ds_read_b128 v[74:77], v73 offset:560
	ds_read_b128 v[78:81], v73 offset:608
	ds_read_b128 v[82:85], v73 offset:624
	v_pk_mul_f32 v[56:57], v[58:59], v[56:57]
	v_pk_mul_f32 v[58:59], v[60:61], v[88:89]
	v_pk_mul_f32 v[60:61], v[20:21], v[0:1] op_sel_hi:[0,1]
	s_waitcnt lgkmcnt(3)
	v_pk_fma_f32 v[58:59], v[70:71], v[68:69], v[58:59] op_sel_hi:[0,1,1]
	v_exp_f32_e32 v60, v60
	v_exp_f32_e32 v61, v61
	v_pk_mul_f32 v[68:69], v[20:21], v[2:3] op_sel_hi:[0,1]
	v_exp_f32_e32 v68, v68
	v_exp_f32_e32 v69, v69
	v_pk_fma_f32 v[56:57], v[70:71], v[66:67], v[56:57] op_sel_hi:[0,1,1]
	s_waitcnt lgkmcnt(1)
	v_pk_fma_f32 v[66:67], v[78:79], v[56:57], v[86:87]
	v_pk_mul_f32 v[60:61], v[62:63], v[60:61]
	v_pk_fma_f32 v[66:67], v[80:81], v[58:59], v[66:67]
	v_pk_fma_f32 v[60:61], v[70:71], v[74:75], v[60:61] op_sel_hi:[0,1,1]
	v_pk_mul_f32 v[62:63], v[64:65], v[68:69]
	s_waitcnt lgkmcnt(0)
	v_pk_fma_f32 v[66:67], v[82:83], v[60:61], v[66:67]
	v_pk_fma_f32 v[62:63], v[70:71], v[76:77], v[62:63] op_sel_hi:[0,1,1]
	v_pk_fma_f32 v[64:65], v[84:85], v[62:63], v[66:67]
	s_waitcnt vmcnt(9)
	v_cvt_f32_f16_e32 v66, v50
	v_add_f32_e32 v67, v64, v65
	v_fmac_f32_e32 v67, v72, v71
	v_cvt_f32_f16_sdwa v30, v30 dst_sel:DWORD dst_unused:UNUSED_PAD src0_sel:WORD_1
	v_mul_f32_e32 v66, v67, v66
	v_pk_mul_f32 v[82:83], v[20:21], v[12:13] op_sel:[1,0]
	v_pk_mul_f32 v[84:85], v[20:21], v[14:15] op_sel:[1,0]
	v_lshl_add_u64 v[64:65], v[40:41], 1, s[12:13]
	v_fma_mixlo_f16 v66, v66, s1, 0
	v_add_u32_e32 v40, 0x800, v40
	v_exp_f32_e32 v82, v82
	v_exp_f32_e32 v83, v83
	v_exp_f32_e32 v84, v84
	v_exp_f32_e32 v85, v85
	global_store_short v[64:65], v66, off
	ds_read_b128 v[64:67], v73 offset:640
	ds_read_b128 v[68:71], v73 offset:656
	ds_read_b128 v[74:77], v73 offset:704
	ds_read_b128 v[78:81], v73 offset:720
	v_mul_f32_e32 v88, 0x3c800000, v30
	v_mul_f32_e32 v30, v88, v21
	v_pk_mul_f32 v[28:29], v[28:29], v[82:83]
	v_pk_mul_f32 v[36:37], v[36:37], v[84:85]
	s_waitcnt lgkmcnt(3)
	v_pk_fma_f32 v[28:29], v[30:31], v[64:65], v[28:29] op_sel_hi:[0,1,1]
	v_pk_fma_f32 v[36:37], v[30:31], v[66:67], v[36:37] op_sel_hi:[0,1,1]
	v_pk_mul_f32 v[66:67], v[20:21], v[8:9] op_sel:[1,0]
	s_waitcnt lgkmcnt(1)
	v_pk_fma_f32 v[64:65], v[74:75], v[28:29], 0 op_sel_hi:[1,1,0]
	v_exp_f32_e32 v66, v66
	v_exp_f32_e32 v67, v67
	v_pk_mul_f32 v[74:75], v[20:21], v[10:11] op_sel:[1,0]
	v_pk_fma_f32 v[64:65], v[76:77], v[36:37], v[64:65]
	v_exp_f32_e32 v74, v74
	v_exp_f32_e32 v75, v75
	v_pk_mul_f32 v[38:39], v[38:39], v[66:67]
	v_pk_mul_f32 v[54:55], v[54:55], v[74:75]
	v_pk_fma_f32 v[38:39], v[30:31], v[68:69], v[38:39] op_sel_hi:[0,1,1]
	s_waitcnt lgkmcnt(0)
	v_pk_fma_f32 v[64:65], v[78:79], v[38:39], v[64:65]
	v_pk_fma_f32 v[54:55], v[30:31], v[70:71], v[54:55] op_sel_hi:[0,1,1]
	v_pk_fma_f32 v[82:83], v[80:81], v[54:55], v[64:65]
	v_pk_mul_f32 v[86:87], v[20:21], v[6:7] op_sel:[1,0]
	ds_read_b128 v[64:67], v73 offset:672
	ds_read_b128 v[68:71], v73 offset:688
	ds_read_b128 v[74:77], v73 offset:736
	ds_read_b128 v[78:81], v73 offset:752
	v_exp_f32_e32 v86, v86
	v_exp_f32_e32 v87, v87
	v_pk_mul_f32 v[84:85], v[20:21], v[4:5] op_sel:[1,0]
	v_pk_mul_f32 v[58:59], v[58:59], v[86:87]
	v_exp_f32_e32 v84, v84
	v_exp_f32_e32 v85, v85
	s_waitcnt lgkmcnt(3)
	v_pk_fma_f32 v[58:59], v[30:31], v[66:67], v[58:59] op_sel_hi:[0,1,1]
	v_pk_mul_f32 v[66:67], v[20:21], v[0:1] op_sel:[1,0]
	v_pk_mul_f32 v[20:21], v[20:21], v[2:3] op_sel:[1,0]
	v_exp_f32_e32 v66, v66
	v_exp_f32_e32 v67, v67
	v_exp_f32_e32 v20, v20
	v_exp_f32_e32 v21, v21
	v_pk_mul_f32 v[56:57], v[56:57], v[84:85]
	v_pk_mul_f32 v[60:61], v[60:61], v[66:67]
	v_pk_fma_f32 v[56:57], v[30:31], v[64:65], v[56:57] op_sel_hi:[0,1,1]
	s_waitcnt lgkmcnt(1)
	v_pk_fma_f32 v[64:65], v[74:75], v[56:57], v[82:83]
	v_pk_fma_f32 v[60:61], v[30:31], v[68:69], v[60:61] op_sel_hi:[0,1,1]
	v_pk_fma_f32 v[64:65], v[76:77], v[58:59], v[64:65]
	v_pk_mul_f32 v[20:21], v[62:63], v[20:21]
	s_waitcnt lgkmcnt(0)
	v_pk_fma_f32 v[64:65], v[78:79], v[60:61], v[64:65]
	v_pk_fma_f32 v[62:63], v[30:31], v[70:71], v[20:21] op_sel_hi:[0,1,1]
	v_pk_fma_f32 v[20:21], v[80:81], v[62:63], v[64:65]
	v_cvt_f32_f16_sdwa v30, v50 dst_sel:DWORD dst_unused:UNUSED_PAD src0_sel:WORD_1
	v_add_f32_e32 v50, v20, v21
	v_fmac_f32_e32 v50, v72, v88
	v_lshl_add_u64 v[20:21], v[40:41], 1, s[12:13]
	v_mul_f32_e32 v30, v50, v30
	v_fma_mixlo_f16 v30, v30, s1, 0
	v_cvt_f32_f16_e32 v50, v31
	global_store_short v[20:21], v30, off
	v_pk_mul_f32 v[20:21], v[22:23], v[12:13] op_sel_hi:[0,1]
	v_pk_mul_f32 v[82:83], v[22:23], v[14:15] op_sel_hi:[0,1]
	v_exp_f32_e32 v20, v20
	v_exp_f32_e32 v21, v21
	v_exp_f32_e32 v82, v82
	v_exp_f32_e32 v83, v83
	v_add_u32_e32 v40, 0x800, v40
	v_mul_f32_e32 v50, 0x3c800000, v50
	ds_read_b128 v[64:67], v73 offset:768
	ds_read_b128 v[68:71], v73 offset:784
	ds_read_b128 v[74:77], v73 offset:832
	ds_read_b128 v[78:81], v73 offset:848
	v_mul_f32_e32 v30, v50, v22
	v_pk_mul_f32 v[20:21], v[28:29], v[20:21]
	v_pk_mul_f32 v[28:29], v[36:37], v[82:83]
	v_pk_mul_f32 v[36:37], v[22:23], v[8:9] op_sel_hi:[0,1]
	s_waitcnt lgkmcnt(3)
	v_pk_fma_f32 v[28:29], v[30:31], v[66:67], v[28:29] op_sel_hi:[0,1,1]
	v_exp_f32_e32 v36, v36
	v_exp_f32_e32 v37, v37
	v_pk_mul_f32 v[66:67], v[22:23], v[10:11] op_sel_hi:[0,1]
	v_exp_f32_e32 v66, v66
	v_exp_f32_e32 v67, v67
	v_pk_fma_f32 v[20:21], v[30:31], v[64:65], v[20:21] op_sel_hi:[0,1,1]
	s_waitcnt lgkmcnt(1)
	v_pk_fma_f32 v[64:65], v[74:75], v[20:21], 0 op_sel_hi:[1,1,0]
	v_pk_mul_f32 v[36:37], v[38:39], v[36:37]
	v_pk_fma_f32 v[64:65], v[76:77], v[28:29], v[64:65]
	v_pk_fma_f32 v[36:37], v[30:31], v[68:69], v[36:37] op_sel_hi:[0,1,1]
	v_pk_mul_f32 v[38:39], v[54:55], v[66:67]
	s_waitcnt lgkmcnt(0)
	v_pk_fma_f32 v[64:65], v[78:79], v[36:37], v[64:65]
	v_pk_fma_f32 v[38:39], v[30:31], v[70:71], v[38:39] op_sel_hi:[0,1,1]
	v_pk_fma_f32 v[82:83], v[80:81], v[38:39], v[64:65]
	v_pk_mul_f32 v[84:85], v[22:23], v[6:7] op_sel_hi:[0,1]
	v_pk_mul_f32 v[54:55], v[22:23], v[4:5] op_sel_hi:[0,1]
	v_exp_f32_e32 v84, v84
	v_exp_f32_e32 v85, v85
	v_exp_f32_e32 v54, v54
	v_exp_f32_e32 v55, v55
	ds_read_b128 v[64:67], v73 offset:800
	ds_read_b128 v[68:71], v73 offset:816
	ds_read_b128 v[74:77], v73 offset:864
	ds_read_b128 v[78:81], v73 offset:880
	v_pk_mul_f32 v[58:59], v[58:59], v[84:85]
	v_pk_mul_f32 v[54:55], v[56:57], v[54:55]
	s_waitcnt lgkmcnt(3)
	v_pk_fma_f32 v[66:67], v[30:31], v[66:67], v[58:59] op_sel_hi:[0,1,1]
	v_pk_mul_f32 v[58:59], v[22:23], v[0:1] op_sel_hi:[0,1]
	v_pk_fma_f32 v[54:55], v[30:31], v[64:65], v[54:55] op_sel_hi:[0,1,1]
	v_exp_f32_e32 v58, v58
	v_exp_f32_e32 v59, v59
	v_pk_mul_f32 v[64:65], v[22:23], v[2:3] op_sel_hi:[0,1]
	v_exp_f32_e32 v64, v64
	v_exp_f32_e32 v65, v65
	s_waitcnt lgkmcnt(1)
	v_pk_fma_f32 v[56:57], v[74:75], v[54:55], v[82:83]
	v_pk_mul_f32 v[58:59], v[60:61], v[58:59]
	v_pk_fma_f32 v[56:57], v[76:77], v[66:67], v[56:57]
	v_pk_fma_f32 v[68:69], v[30:31], v[68:69], v[58:59] op_sel_hi:[0,1,1]
	v_pk_mul_f32 v[58:59], v[62:63], v[64:65]
	s_waitcnt lgkmcnt(0)
	v_pk_fma_f32 v[56:57], v[78:79], v[68:69], v[56:57]
	v_pk_fma_f32 v[70:71], v[30:31], v[70:71], v[58:59] op_sel_hi:[0,1,1]
	v_pk_fma_f32 v[56:57], v[80:81], v[70:71], v[56:57]
	v_cvt_f32_f16_e32 v22, v51
	v_add_f32_e32 v30, v56, v57
	v_fmac_f32_e32 v30, v72, v50
	v_lshl_add_u64 v[56:57], v[40:41], 1, s[12:13]
	v_mul_f32_e32 v22, v30, v22
	v_cvt_f32_f16_sdwa v30, v31 dst_sel:DWORD dst_unused:UNUSED_PAD src0_sel:WORD_1
	v_fma_mixlo_f16 v22, v22, s1, 0
	v_mov_b32_e32 v82, v23
	global_store_short v[56:57], v22, off
	v_mul_f32_e32 v83, 0x3c800000, v30
	v_mul_f32_e32 v50, v83, v23
	v_pk_mul_f32 v[22:23], v[82:83], v[12:13] op_sel_hi:[0,1]
	v_pk_mul_f32 v[30:31], v[82:83], v[14:15] op_sel_hi:[0,1]
	v_exp_f32_e32 v22, v22
	v_exp_f32_e32 v23, v23
	v_exp_f32_e32 v30, v30
	v_exp_f32_e32 v31, v31
	v_add_u32_e32 v40, 0x800, v40
	ds_read_b128 v[56:59], v73 offset:896
	ds_read_b128 v[60:63], v73 offset:912
	ds_read_b128 v[74:77], v73 offset:960
	ds_read_b128 v[78:81], v73 offset:976
	v_pk_mul_f32 v[20:21], v[20:21], v[22:23]
	v_pk_mul_f32 v[22:23], v[28:29], v[30:31]
	v_pk_mul_f32 v[28:29], v[82:83], v[10:11] op_sel_hi:[0,1]
	s_waitcnt lgkmcnt(3)
	v_pk_fma_f32 v[58:59], v[50:51], v[58:59], v[22:23] op_sel_hi:[0,1,1]
	v_pk_mul_f32 v[22:23], v[82:83], v[8:9] op_sel_hi:[0,1]
	v_exp_f32_e32 v22, v22
	v_exp_f32_e32 v23, v23
	v_exp_f32_e32 v28, v28
	v_exp_f32_e32 v29, v29
	v_pk_fma_f32 v[56:57], v[50:51], v[56:57], v[20:21] op_sel_hi:[0,1,1]
	s_waitcnt lgkmcnt(1)
	v_pk_fma_f32 v[20:21], v[74:75], v[56:57], 0 op_sel_hi:[1,1,0]
	v_pk_mul_f32 v[22:23], v[36:37], v[22:23]
	v_pk_fma_f32 v[20:21], v[76:77], v[58:59], v[20:21]
	v_pk_fma_f32 v[60:61], v[50:51], v[60:61], v[22:23] op_sel_hi:[0,1,1]
	v_pk_mul_f32 v[22:23], v[38:39], v[28:29]
	s_waitcnt lgkmcnt(0)
	v_pk_fma_f32 v[20:21], v[78:79], v[60:61], v[20:21]
	v_pk_fma_f32 v[62:63], v[50:51], v[62:63], v[22:23] op_sel_hi:[0,1,1]
	v_pk_fma_f32 v[78:79], v[80:81], v[62:63], v[20:21]
	v_pk_mul_f32 v[64:65], v[82:83], v[4:5] op_sel_hi:[0,1]
	v_exp_f32_e32 v64, v64
	v_exp_f32_e32 v65, v65
	v_pk_mul_f32 v[80:81], v[82:83], v[6:7] op_sel_hi:[0,1]
	ds_read_b128 v[20:23], v73 offset:928
	ds_read_b128 v[28:31], v73 offset:944
	ds_read_b128 v[36:39], v73 offset:992
	ds_read_b128 v[74:77], v73 offset:1008
	v_exp_f32_e32 v80, v80
	v_exp_f32_e32 v81, v81
	v_pk_mul_f32 v[54:55], v[54:55], v[64:65]
	s_waitcnt lgkmcnt(3)
	v_pk_fma_f32 v[64:65], v[50:51], v[20:21], v[54:55] op_sel_hi:[0,1,1]
	s_waitcnt lgkmcnt(1)
	v_pk_fma_f32 v[20:21], v[36:37], v[64:65], v[78:79]
	v_pk_mul_f32 v[36:37], v[66:67], v[80:81]
	s_nop 0
	v_pk_fma_f32 v[66:67], v[50:51], v[22:23], v[36:37] op_sel_hi:[0,1,1]
	v_pk_mul_f32 v[22:23], v[82:83], v[0:1] op_sel_hi:[0,1]
	v_exp_f32_e32 v22, v22
	v_exp_f32_e32 v23, v23
	v_pk_mul_f32 v[36:37], v[82:83], v[2:3] op_sel_hi:[0,1]
	v_exp_f32_e32 v36, v36
	v_exp_f32_e32 v37, v37
	v_pk_mul_f32 v[22:23], v[68:69], v[22:23]
	v_pk_fma_f32 v[20:21], v[38:39], v[66:67], v[20:21]
	v_pk_fma_f32 v[68:69], v[50:51], v[28:29], v[22:23] op_sel_hi:[0,1,1]
	v_pk_mul_f32 v[22:23], v[70:71], v[36:37]
	s_waitcnt lgkmcnt(0)
	v_pk_fma_f32 v[20:21], v[74:75], v[68:69], v[20:21]
	v_pk_fma_f32 v[70:71], v[50:51], v[30:31], v[22:23] op_sel_hi:[0,1,1]
	v_pk_fma_f32 v[20:21], v[76:77], v[70:71], v[20:21]
	s_or_b32 s6, s0, 4
	v_cvt_f32_f16_sdwa v22, v51 dst_sel:DWORD dst_unused:UNUSED_PAD src0_sel:WORD_1
	s_ashr_i32 s7, s6, 31
	s_lshl_b64 s[6:7], s[6:7], 15
	s_or_b32 s8, s0, 5
	v_add_f32_e32 v23, v20, v21
	s_ashr_i32 s9, s8, 31
	v_lshl_add_u64 v[30:31], v[42:43], 0, s[6:7]
	v_fmac_f32_e32 v23, v72, v83
	s_lshl_b64 s[8:9], s[8:9], 15
	s_or_b32 s10, s2, 2
	v_add_co_u32_e32 v54, vcc, s5, v30
	v_mul_f32_e32 v22, v23, v22
	s_ashr_i32 s11, s10, 31
	v_lshl_add_u64 v[50:51], v[42:43], 0, s[8:9]
	v_addc_co_u32_e32 v55, vcc, 0, v31, vcc
	v_lshl_add_u64 v[20:21], v[40:41], 1, s[12:13]
	v_fma_mixlo_f16 v22, v22, s1, 0
	s_lshl_b64 s[10:11], s[10:11], 15
	v_add_co_u32_e32 v50, vcc, s5, v50
	global_store_short v[20:21], v22, off
	v_add_u32_e32 v40, 0x800, v40
	v_lshl_add_u64 v[20:21], v[46:47], 0, s[6:7]
	v_lshl_add_u64 v[22:23], v[46:47], 0, s[8:9]
	v_lshl_add_u64 v[28:29], v[44:45], 0, s[10:11]
	v_addc_co_u32_e32 v51, vcc, 0, v51, vcc
	global_load_dwordx4 v[36:39], v[20:21], off
	s_nop 0
	global_load_dwordx4 v[20:23], v[22:23], off
	s_waitcnt vmcnt(12)
	v_cvt_f32_f16_e32 v74, v24
	global_load_dwordx4 v[28:31], v[28:29], off
	s_nop 0
	global_load_dwordx2 v[54:55], v[54:55], off
	s_nop 0
	global_load_dwordx2 v[50:51], v[50:51], off
	v_pk_mul_f32 v[92:93], v[32:33], v[12:13] op_sel_hi:[0,1]
	v_pk_mul_f32 v[94:95], v[32:33], v[14:15] op_sel_hi:[0,1]
	v_exp_f32_e32 v92, v92
	v_exp_f32_e32 v93, v93
	v_exp_f32_e32 v94, v94
	v_exp_f32_e32 v95, v95
	v_mul_f32_e32 v91, 0x3c800000, v74
	ds_read_b128 v[74:77], v73 offset:1024
	ds_read_b128 v[78:81], v73 offset:1040
	ds_read_b128 v[82:85], v73 offset:1088
	ds_read_b128 v[86:89], v73 offset:1104
	v_mul_f32_e32 v90, v91, v32
	v_pk_mul_f32 v[56:57], v[56:57], v[92:93]
	v_pk_mul_f32 v[58:59], v[58:59], v[94:95]
	s_waitcnt lgkmcnt(3)
	v_pk_fma_f32 v[56:57], v[90:91], v[74:75], v[56:57] op_sel_hi:[0,1,1]
	v_pk_fma_f32 v[58:59], v[90:91], v[76:77], v[58:59] op_sel_hi:[0,1,1]
	v_pk_mul_f32 v[76:77], v[32:33], v[8:9] op_sel_hi:[0,1]
	s_waitcnt lgkmcnt(1)
	v_pk_fma_f32 v[74:75], v[82:83], v[56:57], 0 op_sel_hi:[1,1,0]
	v_exp_f32_e32 v76, v76
	v_exp_f32_e32 v77, v77
	v_pk_mul_f32 v[82:83], v[32:33], v[10:11] op_sel_hi:[0,1]
	v_exp_f32_e32 v82, v82
	v_exp_f32_e32 v83, v83
	v_pk_mul_f32 v[60:61], v[60:61], v[76:77]
	v_pk_fma_f32 v[74:75], v[84:85], v[58:59], v[74:75]
	v_pk_fma_f32 v[60:61], v[90:91], v[78:79], v[60:61] op_sel_hi:[0,1,1]
	v_pk_mul_f32 v[62:63], v[62:63], v[82:83]
	s_waitcnt lgkmcnt(0)
	v_pk_fma_f32 v[74:75], v[86:87], v[60:61], v[74:75]
	v_pk_fma_f32 v[62:63], v[90:91], v[80:81], v[62:63] op_sel_hi:[0,1,1]
	v_pk_fma_f32 v[92:93], v[88:89], v[62:63], v[74:75]
	v_pk_mul_f32 v[94:95], v[32:33], v[4:5] op_sel_hi:[0,1]
	v_pk_mul_f32 v[96:97], v[32:33], v[6:7] op_sel_hi:[0,1]
	v_exp_f32_e32 v94, v94
	v_exp_f32_e32 v95, v95
	v_exp_f32_e32 v96, v96
	v_exp_f32_e32 v97, v97
	ds_read_b128 v[74:77], v73 offset:1056
	ds_read_b128 v[78:81], v73 offset:1072
	ds_read_b128 v[82:85], v73 offset:1120
	ds_read_b128 v[86:89], v73 offset:1136
	v_pk_mul_f32 v[64:65], v[64:65], v[94:95]
	v_pk_mul_f32 v[66:67], v[66:67], v[96:97]
	s_waitcnt lgkmcnt(3)
	v_pk_fma_f32 v[64:65], v[90:91], v[74:75], v[64:65] op_sel_hi:[0,1,1]
	v_pk_fma_f32 v[66:67], v[90:91], v[76:77], v[66:67] op_sel_hi:[0,1,1]
	v_pk_mul_f32 v[76:77], v[32:33], v[0:1] op_sel_hi:[0,1]
	s_waitcnt lgkmcnt(1)
	v_pk_fma_f32 v[74:75], v[82:83], v[64:65], v[92:93]
	v_exp_f32_e32 v76, v76
	v_exp_f32_e32 v77, v77
	v_pk_mul_f32 v[82:83], v[32:33], v[2:3] op_sel_hi:[0,1]
	v_exp_f32_e32 v82, v82
	v_exp_f32_e32 v83, v83
	v_pk_mul_f32 v[68:69], v[68:69], v[76:77]
	v_pk_fma_f32 v[74:75], v[84:85], v[66:67], v[74:75]
	v_pk_fma_f32 v[68:69], v[90:91], v[78:79], v[68:69] op_sel_hi:[0,1,1]
	v_pk_mul_f32 v[70:71], v[70:71], v[82:83]
	s_waitcnt lgkmcnt(0)
	v_pk_fma_f32 v[74:75], v[86:87], v[68:69], v[74:75]
	v_pk_fma_f32 v[70:71], v[90:91], v[80:81], v[70:71] op_sel_hi:[0,1,1]
	v_pk_fma_f32 v[74:75], v[88:89], v[70:71], v[74:75]
	s_waitcnt vmcnt(14)
	v_cvt_f32_f16_e32 v76, v52
	v_add_f32_e32 v77, v74, v75
	v_fmac_f32_e32 v77, v72, v91
	v_cvt_f32_f16_sdwa v24, v24 dst_sel:DWORD dst_unused:UNUSED_PAD src0_sel:WORD_1
	v_mul_f32_e32 v76, v77, v76
	v_pk_mul_f32 v[90:91], v[32:33], v[12:13] op_sel:[1,0]
	v_pk_mul_f32 v[92:93], v[32:33], v[14:15] op_sel:[1,0]
	v_lshl_add_u64 v[74:75], v[40:41], 1, s[12:13]
	v_fma_mixlo_f16 v76, v76, s1, 0
	v_add_u32_e32 v40, 0x800, v40
	v_exp_f32_e32 v90, v90
	v_exp_f32_e32 v91, v91
	v_exp_f32_e32 v92, v92
	v_exp_f32_e32 v93, v93
	global_store_short v[74:75], v76, off
	ds_read_b128 v[74:77], v73 offset:1152
	ds_read_b128 v[78:81], v73 offset:1168
	ds_read_b128 v[82:85], v73 offset:1216
	ds_read_b128 v[86:89], v73 offset:1232
	v_mul_f32_e32 v96, 0x3c800000, v24
	v_mul_f32_e32 v24, v96, v33
	v_pk_mul_f32 v[56:57], v[56:57], v[90:91]
	v_pk_mul_f32 v[58:59], v[58:59], v[92:93]
	s_waitcnt lgkmcnt(3)
	v_pk_fma_f32 v[56:57], v[24:25], v[74:75], v[56:57] op_sel_hi:[0,1,1]
	v_pk_fma_f32 v[58:59], v[24:25], v[76:77], v[58:59] op_sel_hi:[0,1,1]
	v_pk_mul_f32 v[76:77], v[32:33], v[8:9] op_sel:[1,0]
	s_waitcnt lgkmcnt(1)
	v_pk_fma_f32 v[74:75], v[82:83], v[56:57], 0 op_sel_hi:[1,1,0]
	v_exp_f32_e32 v76, v76
	v_exp_f32_e32 v77, v77
	v_pk_mul_f32 v[82:83], v[32:33], v[10:11] op_sel:[1,0]
	v_pk_fma_f32 v[74:75], v[84:85], v[58:59], v[74:75]
	v_exp_f32_e32 v82, v82
	v_exp_f32_e32 v83, v83
	v_pk_mul_f32 v[60:61], v[60:61], v[76:77]
	v_pk_mul_f32 v[62:63], v[62:63], v[82:83]
	v_pk_fma_f32 v[60:61], v[24:25], v[78:79], v[60:61] op_sel_hi:[0,1,1]
	s_waitcnt lgkmcnt(0)
	v_pk_fma_f32 v[74:75], v[86:87], v[60:61], v[74:75]
	v_pk_fma_f32 v[62:63], v[24:25], v[80:81], v[62:63] op_sel_hi:[0,1,1]
	v_pk_fma_f32 v[90:91], v[88:89], v[62:63], v[74:75]
	v_pk_mul_f32 v[94:95], v[32:33], v[6:7] op_sel:[1,0]
	ds_read_b128 v[74:77], v73 offset:1184
	ds_read_b128 v[78:81], v73 offset:1200
	ds_read_b128 v[82:85], v73 offset:1248
	ds_read_b128 v[86:89], v73 offset:1264
	v_exp_f32_e32 v94, v94
	v_exp_f32_e32 v95, v95
	v_pk_mul_f32 v[92:93], v[32:33], v[4:5] op_sel:[1,0]
	v_pk_mul_f32 v[66:67], v[66:67], v[94:95]
	v_exp_f32_e32 v92, v92
	v_exp_f32_e32 v93, v93
	s_waitcnt lgkmcnt(3)
	v_pk_fma_f32 v[66:67], v[24:25], v[76:77], v[66:67] op_sel_hi:[0,1,1]
	v_pk_mul_f32 v[76:77], v[32:33], v[0:1] op_sel:[1,0]
	v_pk_mul_f32 v[32:33], v[32:33], v[2:3] op_sel:[1,0]
	v_exp_f32_e32 v76, v76
	v_exp_f32_e32 v77, v77
	v_exp_f32_e32 v32, v32
	v_exp_f32_e32 v33, v33
	v_pk_mul_f32 v[64:65], v[64:65], v[92:93]
	v_pk_mul_f32 v[68:69], v[68:69], v[76:77]
	v_pk_fma_f32 v[64:65], v[24:25], v[74:75], v[64:65] op_sel_hi:[0,1,1]
	s_waitcnt lgkmcnt(1)
	v_pk_fma_f32 v[74:75], v[82:83], v[64:65], v[90:91]
	v_pk_fma_f32 v[68:69], v[24:25], v[78:79], v[68:69] op_sel_hi:[0,1,1]
	v_pk_fma_f32 v[74:75], v[84:85], v[66:67], v[74:75]
	v_pk_mul_f32 v[32:33], v[70:71], v[32:33]
	s_waitcnt lgkmcnt(0)
	v_pk_fma_f32 v[74:75], v[86:87], v[68:69], v[74:75]
	v_pk_fma_f32 v[70:71], v[24:25], v[80:81], v[32:33] op_sel_hi:[0,1,1]
	v_pk_fma_f32 v[32:33], v[88:89], v[70:71], v[74:75]
	v_cvt_f32_f16_sdwa v24, v52 dst_sel:DWORD dst_unused:UNUSED_PAD src0_sel:WORD_1
	v_add_f32_e32 v52, v32, v33
	v_fmac_f32_e32 v52, v72, v96
	v_lshl_add_u64 v[32:33], v[40:41], 1, s[12:13]
	v_mul_f32_e32 v24, v52, v24
	v_fma_mixlo_f16 v24, v24, s1, 0
	v_cvt_f32_f16_e32 v52, v25
	global_store_short v[32:33], v24, off
	v_pk_mul_f32 v[32:33], v[34:35], v[12:13] op_sel_hi:[0,1]
	v_pk_mul_f32 v[90:91], v[34:35], v[14:15] op_sel_hi:[0,1]
	v_exp_f32_e32 v32, v32
	v_exp_f32_e32 v33, v33
	v_exp_f32_e32 v90, v90
	v_exp_f32_e32 v91, v91
	v_add_u32_e32 v40, 0x800, v40
	v_mul_f32_e32 v52, 0x3c800000, v52
	ds_read_b128 v[74:77], v73 offset:1280
	ds_read_b128 v[78:81], v73 offset:1296
	ds_read_b128 v[82:85], v73 offset:1344
	ds_read_b128 v[86:89], v73 offset:1360
	v_mul_f32_e32 v24, v52, v34
	v_pk_mul_f32 v[32:33], v[56:57], v[32:33]
	v_pk_mul_f32 v[56:57], v[58:59], v[90:91]
	v_pk_mul_f32 v[58:59], v[34:35], v[8:9] op_sel_hi:[0,1]
	s_waitcnt lgkmcnt(3)
	v_pk_fma_f32 v[56:57], v[24:25], v[76:77], v[56:57] op_sel_hi:[0,1,1]
	v_exp_f32_e32 v58, v58
	v_exp_f32_e32 v59, v59
	v_pk_mul_f32 v[76:77], v[34:35], v[10:11] op_sel_hi:[0,1]
	v_exp_f32_e32 v76, v76
	v_exp_f32_e32 v77, v77
	v_pk_fma_f32 v[32:33], v[24:25], v[74:75], v[32:33] op_sel_hi:[0,1,1]
	s_waitcnt lgkmcnt(1)
	v_pk_fma_f32 v[74:75], v[82:83], v[32:33], 0 op_sel_hi:[1,1,0]
	v_pk_mul_f32 v[58:59], v[60:61], v[58:59]
	v_pk_fma_f32 v[74:75], v[84:85], v[56:57], v[74:75]
	v_pk_fma_f32 v[58:59], v[24:25], v[78:79], v[58:59] op_sel_hi:[0,1,1]
	v_pk_mul_f32 v[60:61], v[62:63], v[76:77]
	s_waitcnt lgkmcnt(0)
	v_pk_fma_f32 v[74:75], v[86:87], v[58:59], v[74:75]
	v_pk_fma_f32 v[60:61], v[24:25], v[80:81], v[60:61] op_sel_hi:[0,1,1]
	v_pk_fma_f32 v[90:91], v[88:89], v[60:61], v[74:75]
	v_pk_mul_f32 v[62:63], v[34:35], v[4:5] op_sel_hi:[0,1]
	v_pk_mul_f32 v[92:93], v[34:35], v[6:7] op_sel_hi:[0,1]
	v_exp_f32_e32 v62, v62
	v_exp_f32_e32 v63, v63
	v_exp_f32_e32 v92, v92
	v_exp_f32_e32 v93, v93
	ds_read_b128 v[74:77], v73 offset:1312
	ds_read_b128 v[78:81], v73 offset:1328
	ds_read_b128 v[82:85], v73 offset:1376
	ds_read_b128 v[86:89], v73 offset:1392
	v_pk_mul_f32 v[62:63], v[64:65], v[62:63]
	v_pk_mul_f32 v[64:65], v[66:67], v[92:93]
	v_pk_mul_f32 v[66:67], v[34:35], v[0:1] op_sel_hi:[0,1]
	s_waitcnt lgkmcnt(3)
	v_pk_fma_f32 v[64:65], v[24:25], v[76:77], v[64:65] op_sel_hi:[0,1,1]
	v_exp_f32_e32 v66, v66
	v_exp_f32_e32 v67, v67
	v_pk_mul_f32 v[76:77], v[34:35], v[2:3] op_sel_hi:[0,1]
	v_exp_f32_e32 v76, v76
	v_exp_f32_e32 v77, v77
	v_pk_fma_f32 v[62:63], v[24:25], v[74:75], v[62:63] op_sel_hi:[0,1,1]
	s_waitcnt lgkmcnt(1)
	v_pk_fma_f32 v[74:75], v[82:83], v[62:63], v[90:91]
	v_pk_mul_f32 v[66:67], v[68:69], v[66:67]
	v_pk_fma_f32 v[74:75], v[84:85], v[64:65], v[74:75]
	v_pk_fma_f32 v[66:67], v[24:25], v[78:79], v[66:67] op_sel_hi:[0,1,1]
	v_pk_mul_f32 v[68:69], v[70:71], v[76:77]
	s_waitcnt lgkmcnt(0)
	v_pk_fma_f32 v[74:75], v[86:87], v[66:67], v[74:75]
	v_pk_fma_f32 v[68:69], v[24:25], v[80:81], v[68:69] op_sel_hi:[0,1,1]
	v_pk_fma_f32 v[70:71], v[88:89], v[68:69], v[74:75]
	v_cvt_f32_f16_e32 v24, v53
	v_add_f32_e32 v34, v70, v71
	v_fmac_f32_e32 v34, v72, v52
	v_cvt_f32_f16_sdwa v25, v25 dst_sel:DWORD dst_unused:UNUSED_PAD src0_sel:WORD_1
	v_mul_f32_e32 v24, v34, v24
	v_lshl_add_u64 v[70:71], v[40:41], 1, s[12:13]
	v_fma_mixlo_f16 v24, v24, s1, 0
	global_store_short v[70:71], v24, off
	v_mov_b32_e32 v70, v35
	v_mul_f32_e32 v92, 0x3c800000, v25
	v_pk_mul_f32 v[24:25], v[70:71], v[12:13] op_sel_hi:[0,1]
	v_add_u32_e32 v40, 0x800, v40
	v_mul_f32_e32 v52, v92, v35
	v_exp_f32_e32 v24, v24
	v_exp_f32_e32 v25, v25
	v_pk_mul_f32 v[34:35], v[70:71], v[14:15] op_sel_hi:[0,1]
	v_exp_f32_e32 v34, v34
	v_exp_f32_e32 v35, v35
	ds_read_b128 v[74:77], v73 offset:1408
	ds_read_b128 v[78:81], v73 offset:1424
	ds_read_b128 v[82:85], v73 offset:1472
	ds_read_b128 v[86:89], v73 offset:1488
	v_pk_mul_f32 v[24:25], v[32:33], v[24:25]
	v_pk_mul_f32 v[32:33], v[56:57], v[34:35]
	s_waitcnt lgkmcnt(3)
	v_pk_fma_f32 v[24:25], v[52:53], v[74:75], v[24:25] op_sel_hi:[0,1,1]
	v_pk_mul_f32 v[34:35], v[70:71], v[8:9] op_sel_hi:[0,1]
	s_waitcnt lgkmcnt(1)
	v_pk_fma_f32 v[74:75], v[82:83], v[24:25], 0 op_sel_hi:[1,1,0]
	v_pk_fma_f32 v[32:33], v[52:53], v[76:77], v[32:33] op_sel_hi:[0,1,1]
	v_exp_f32_e32 v34, v34
	v_exp_f32_e32 v35, v35
	v_pk_fma_f32 v[56:57], v[84:85], v[32:33], v[74:75]
	v_pk_mul_f32 v[74:75], v[70:71], v[10:11] op_sel_hi:[0,1]
	v_exp_f32_e32 v74, v74
	v_exp_f32_e32 v75, v75
	v_pk_mul_f32 v[34:35], v[58:59], v[34:35]
	s_nop 0
	v_pk_fma_f32 v[34:35], v[52:53], v[78:79], v[34:35] op_sel_hi:[0,1,1]
	s_waitcnt lgkmcnt(0)
	v_pk_fma_f32 v[58:59], v[86:87], v[34:35], v[56:57]
	v_pk_mul_f32 v[56:57], v[60:61], v[74:75]
	s_nop 0
	v_pk_fma_f32 v[56:57], v[52:53], v[80:81], v[56:57] op_sel_hi:[0,1,1]
	v_pk_fma_f32 v[86:87], v[88:89], v[56:57], v[58:59]
	v_pk_mul_f32 v[88:89], v[70:71], v[4:5] op_sel_hi:[0,1]
	v_exp_f32_e32 v88, v88
	v_exp_f32_e32 v89, v89
	v_pk_mul_f32 v[90:91], v[70:71], v[6:7] op_sel_hi:[0,1]
	v_exp_f32_e32 v90, v90
	v_exp_f32_e32 v91, v91
	ds_read_b128 v[58:61], v73 offset:1440
	ds_read_b128 v[74:77], v73 offset:1456
	ds_read_b128 v[78:81], v73 offset:1504
	ds_read_b128 v[82:85], v73 offset:1520
	v_pk_mul_f32 v[62:63], v[62:63], v[88:89]
	v_pk_mul_f32 v[64:65], v[64:65], v[90:91]
	s_waitcnt lgkmcnt(3)
	v_pk_fma_f32 v[58:59], v[52:53], v[58:59], v[62:63] op_sel_hi:[0,1,1]
	s_waitcnt lgkmcnt(1)
	v_pk_fma_f32 v[62:63], v[78:79], v[58:59], v[86:87]
	v_pk_fma_f32 v[60:61], v[52:53], v[60:61], v[64:65] op_sel_hi:[0,1,1]
	v_pk_fma_f32 v[64:65], v[80:81], v[60:61], v[62:63]
	v_pk_mul_f32 v[62:63], v[70:71], v[0:1] op_sel_hi:[0,1]
	v_exp_f32_e32 v62, v62
	v_exp_f32_e32 v63, v63
	v_pk_mul_f32 v[70:71], v[70:71], v[2:3] op_sel_hi:[0,1]
	v_exp_f32_e32 v70, v70
	v_exp_f32_e32 v71, v71
	v_pk_mul_f32 v[62:63], v[66:67], v[62:63]
	s_nop 0
	v_pk_fma_f32 v[62:63], v[52:53], v[74:75], v[62:63] op_sel_hi:[0,1,1]
	s_waitcnt lgkmcnt(0)
	v_pk_fma_f32 v[66:67], v[82:83], v[62:63], v[64:65]
	v_pk_mul_f32 v[64:65], v[68:69], v[70:71]
	s_nop 0
	v_pk_fma_f32 v[64:65], v[52:53], v[76:77], v[64:65] op_sel_hi:[0,1,1]
	v_pk_fma_f32 v[66:67], v[84:85], v[64:65], v[66:67]
	v_cvt_f32_f16_sdwa v68, v53 dst_sel:DWORD dst_unused:UNUSED_PAD src0_sel:WORD_1
	v_add_f32_e32 v66, v66, v67
	v_fmac_f32_e32 v66, v72, v92
	v_lshl_add_u64 v[52:53], v[40:41], 1, s[12:13]
	v_mul_f32_e32 v66, v66, v68
	v_fma_mixlo_f16 v66, v66, s1, 0
	v_cvt_f32_f16_e32 v67, v26
	global_store_short v[52:53], v66, off
	v_pk_mul_f32 v[52:53], v[16:17], v[12:13] op_sel_hi:[0,1]
	v_exp_f32_e32 v52, v52
	v_exp_f32_e32 v53, v53
	v_add_u32_e32 v40, 0x800, v40
	v_pk_mul_f32 v[86:87], v[16:17], v[14:15] op_sel_hi:[0,1]
	v_exp_f32_e32 v86, v86
	v_exp_f32_e32 v87, v87
	v_mul_f32_e32 v71, 0x3c800000, v67
	ds_read_b128 v[66:69], v73 offset:1536
	ds_read_b128 v[74:77], v73 offset:1552
	ds_read_b128 v[78:81], v73 offset:1600
	ds_read_b128 v[82:85], v73 offset:1616
	v_mul_f32_e32 v70, v71, v16
	v_pk_mul_f32 v[24:25], v[24:25], v[52:53]
	v_pk_mul_f32 v[32:33], v[32:33], v[86:87]
	s_waitcnt lgkmcnt(3)
	v_pk_fma_f32 v[24:25], v[70:71], v[66:67], v[24:25] op_sel_hi:[0,1,1]
	v_pk_mul_f32 v[66:67], v[16:17], v[8:9] op_sel_hi:[0,1]
	v_exp_f32_e32 v66, v66
	v_exp_f32_e32 v67, v67
	v_pk_fma_f32 v[32:33], v[70:71], v[68:69], v[32:33] op_sel_hi:[0,1,1]
	v_pk_mul_f32 v[68:69], v[16:17], v[10:11] op_sel_hi:[0,1]
	v_exp_f32_e32 v68, v68
	v_exp_f32_e32 v69, v69
	s_waitcnt lgkmcnt(1)
	v_pk_fma_f32 v[52:53], v[78:79], v[24:25], 0 op_sel_hi:[1,1,0]
	v_pk_mul_f32 v[34:35], v[34:35], v[66:67]
	v_pk_fma_f32 v[52:53], v[80:81], v[32:33], v[52:53]
	v_pk_fma_f32 v[34:35], v[70:71], v[74:75], v[34:35] op_sel_hi:[0,1,1]
	s_waitcnt lgkmcnt(0)
	v_pk_fma_f32 v[66:67], v[82:83], v[34:35], v[52:53]
	v_pk_mul_f32 v[52:53], v[56:57], v[68:69]
	s_nop 0
	v_pk_fma_f32 v[52:53], v[70:71], v[76:77], v[52:53] op_sel_hi:[0,1,1]
	v_pk_fma_f32 v[86:87], v[84:85], v[52:53], v[66:67]
	v_pk_mul_f32 v[56:57], v[16:17], v[4:5] op_sel_hi:[0,1]
	v_pk_mul_f32 v[88:89], v[16:17], v[6:7] op_sel_hi:[0,1]
	v_exp_f32_e32 v56, v56
	v_exp_f32_e32 v57, v57
	v_exp_f32_e32 v88, v88
	v_exp_f32_e32 v89, v89
	ds_read_b128 v[66:69], v73 offset:1568
	ds_read_b128 v[74:77], v73 offset:1584
	ds_read_b128 v[78:81], v73 offset:1632
	ds_read_b128 v[82:85], v73 offset:1648
	v_pk_mul_f32 v[56:57], v[58:59], v[56:57]
	v_pk_mul_f32 v[58:59], v[60:61], v[88:89]
	v_pk_mul_f32 v[60:61], v[16:17], v[0:1] op_sel_hi:[0,1]
	s_waitcnt lgkmcnt(3)
	v_pk_fma_f32 v[58:59], v[70:71], v[68:69], v[58:59] op_sel_hi:[0,1,1]
	v_exp_f32_e32 v60, v60
	v_exp_f32_e32 v61, v61
	v_pk_mul_f32 v[68:69], v[16:17], v[2:3] op_sel_hi:[0,1]
	v_exp_f32_e32 v68, v68
	v_exp_f32_e32 v69, v69
	v_pk_fma_f32 v[56:57], v[70:71], v[66:67], v[56:57] op_sel_hi:[0,1,1]
	s_waitcnt lgkmcnt(1)
	v_pk_fma_f32 v[66:67], v[78:79], v[56:57], v[86:87]
	v_pk_mul_f32 v[60:61], v[62:63], v[60:61]
	v_pk_fma_f32 v[66:67], v[80:81], v[58:59], v[66:67]
	v_pk_fma_f32 v[60:61], v[70:71], v[74:75], v[60:61] op_sel_hi:[0,1,1]
	v_pk_mul_f32 v[62:63], v[64:65], v[68:69]
	s_waitcnt lgkmcnt(0)
	v_pk_fma_f32 v[66:67], v[82:83], v[60:61], v[66:67]
	v_pk_fma_f32 v[62:63], v[70:71], v[76:77], v[62:63] op_sel_hi:[0,1,1]
	v_pk_fma_f32 v[64:65], v[84:85], v[62:63], v[66:67]
	s_waitcnt vmcnt(17)
	v_cvt_f32_f16_e32 v66, v48
	v_add_f32_e32 v67, v64, v65
	v_fmac_f32_e32 v67, v72, v71
	v_cvt_f32_f16_sdwa v26, v26 dst_sel:DWORD dst_unused:UNUSED_PAD src0_sel:WORD_1
	v_mul_f32_e32 v66, v67, v66
	v_pk_mul_f32 v[82:83], v[16:17], v[12:13] op_sel:[1,0]
	v_pk_mul_f32 v[84:85], v[16:17], v[14:15] op_sel:[1,0]
	v_lshl_add_u64 v[64:65], v[40:41], 1, s[12:13]
	v_fma_mixlo_f16 v66, v66, s1, 0
	v_add_u32_e32 v40, 0x800, v40
	v_exp_f32_e32 v82, v82
	v_exp_f32_e32 v83, v83
	v_exp_f32_e32 v84, v84
	v_exp_f32_e32 v85, v85
	global_store_short v[64:65], v66, off
	ds_read_b128 v[64:67], v73 offset:1664
	ds_read_b128 v[68:71], v73 offset:1680
	ds_read_b128 v[74:77], v73 offset:1728
	ds_read_b128 v[78:81], v73 offset:1744
	v_mul_f32_e32 v88, 0x3c800000, v26
	v_mul_f32_e32 v26, v88, v17
	v_pk_mul_f32 v[24:25], v[24:25], v[82:83]
	v_pk_mul_f32 v[32:33], v[32:33], v[84:85]
	s_waitcnt lgkmcnt(3)
	v_pk_fma_f32 v[24:25], v[26:27], v[64:65], v[24:25] op_sel_hi:[0,1,1]
	v_pk_fma_f32 v[32:33], v[26:27], v[66:67], v[32:33] op_sel_hi:[0,1,1]
	v_pk_mul_f32 v[66:67], v[16:17], v[8:9] op_sel:[1,0]
	s_waitcnt lgkmcnt(1)
	v_pk_fma_f32 v[64:65], v[74:75], v[24:25], 0 op_sel_hi:[1,1,0]
	v_exp_f32_e32 v66, v66
	v_exp_f32_e32 v67, v67
	v_pk_mul_f32 v[74:75], v[16:17], v[10:11] op_sel:[1,0]
	v_pk_fma_f32 v[64:65], v[76:77], v[32:33], v[64:65]
	v_exp_f32_e32 v74, v74
	v_exp_f32_e32 v75, v75
	v_pk_mul_f32 v[34:35], v[34:35], v[66:67]
	v_pk_mul_f32 v[52:53], v[52:53], v[74:75]
	v_pk_fma_f32 v[34:35], v[26:27], v[68:69], v[34:35] op_sel_hi:[0,1,1]
	s_waitcnt lgkmcnt(0)
	v_pk_fma_f32 v[64:65], v[78:79], v[34:35], v[64:65]
	v_pk_fma_f32 v[52:53], v[26:27], v[70:71], v[52:53] op_sel_hi:[0,1,1]
	v_pk_fma_f32 v[82:83], v[80:81], v[52:53], v[64:65]
	v_pk_mul_f32 v[86:87], v[16:17], v[6:7] op_sel:[1,0]
	ds_read_b128 v[64:67], v73 offset:1696
	ds_read_b128 v[68:71], v73 offset:1712
	ds_read_b128 v[74:77], v73 offset:1760
	ds_read_b128 v[78:81], v73 offset:1776
	v_exp_f32_e32 v86, v86
	v_exp_f32_e32 v87, v87
	v_pk_mul_f32 v[84:85], v[16:17], v[4:5] op_sel:[1,0]
	v_pk_mul_f32 v[58:59], v[58:59], v[86:87]
	v_exp_f32_e32 v84, v84
	v_exp_f32_e32 v85, v85
	s_waitcnt lgkmcnt(3)
	v_pk_fma_f32 v[58:59], v[26:27], v[66:67], v[58:59] op_sel_hi:[0,1,1]
	v_pk_mul_f32 v[66:67], v[16:17], v[0:1] op_sel:[1,0]
	v_pk_mul_f32 v[16:17], v[16:17], v[2:3] op_sel:[1,0]
	v_exp_f32_e32 v66, v66
	v_exp_f32_e32 v67, v67
	v_exp_f32_e32 v16, v16
	v_exp_f32_e32 v17, v17
	v_pk_mul_f32 v[56:57], v[56:57], v[84:85]
	v_pk_mul_f32 v[60:61], v[60:61], v[66:67]
	v_pk_fma_f32 v[56:57], v[26:27], v[64:65], v[56:57] op_sel_hi:[0,1,1]
	s_waitcnt lgkmcnt(1)
	v_pk_fma_f32 v[64:65], v[74:75], v[56:57], v[82:83]
	v_pk_fma_f32 v[60:61], v[26:27], v[68:69], v[60:61] op_sel_hi:[0,1,1]
	v_pk_fma_f32 v[64:65], v[76:77], v[58:59], v[64:65]
	v_pk_mul_f32 v[16:17], v[62:63], v[16:17]
	s_waitcnt lgkmcnt(0)
	v_pk_fma_f32 v[64:65], v[78:79], v[60:61], v[64:65]
	v_pk_fma_f32 v[68:69], v[26:27], v[70:71], v[16:17] op_sel_hi:[0,1,1]
	v_pk_fma_f32 v[16:17], v[80:81], v[68:69], v[64:65]
	v_cvt_f32_f16_sdwa v26, v48 dst_sel:DWORD dst_unused:UNUSED_PAD src0_sel:WORD_1
	v_add_f32_e32 v48, v16, v17
	v_fmac_f32_e32 v48, v72, v88
	v_lshl_add_u64 v[16:17], v[40:41], 1, s[12:13]
	v_mul_f32_e32 v26, v48, v26
	v_fma_mixlo_f16 v26, v26, s1, 0
	v_cvt_f32_f16_e32 v48, v27
	global_store_short v[16:17], v26, off
	v_pk_mul_f32 v[16:17], v[18:19], v[12:13] op_sel_hi:[0,1]
	v_pk_mul_f32 v[66:67], v[18:19], v[14:15] op_sel_hi:[0,1]
	v_exp_f32_e32 v16, v16
	v_exp_f32_e32 v17, v17
	v_exp_f32_e32 v66, v66
	v_exp_f32_e32 v67, v67
	v_add_u32_e32 v40, 0x800, v40
	v_mul_f32_e32 v48, 0x3c800000, v48
	ds_read_b128 v[62:65], v73 offset:1792
	ds_read_b128 v[74:77], v73 offset:1808
	ds_read_b128 v[78:81], v73 offset:1856
	ds_read_b128 v[82:85], v73 offset:1872
	v_mul_f32_e32 v26, v48, v18
	v_pk_mul_f32 v[16:17], v[24:25], v[16:17]
	v_pk_mul_f32 v[24:25], v[32:33], v[66:67]
	v_pk_mul_f32 v[32:33], v[18:19], v[8:9] op_sel_hi:[0,1]
	s_waitcnt lgkmcnt(3)
	v_pk_fma_f32 v[24:25], v[26:27], v[64:65], v[24:25] op_sel_hi:[0,1,1]
	v_exp_f32_e32 v32, v32
	v_exp_f32_e32 v33, v33
	v_pk_mul_f32 v[64:65], v[18:19], v[10:11] op_sel_hi:[0,1]
	v_exp_f32_e32 v64, v64
	v_exp_f32_e32 v65, v65
	v_pk_fma_f32 v[16:17], v[26:27], v[62:63], v[16:17] op_sel_hi:[0,1,1]
	s_waitcnt lgkmcnt(1)
	v_pk_fma_f32 v[62:63], v[78:79], v[16:17], 0 op_sel_hi:[1,1,0]
	v_pk_mul_f32 v[32:33], v[34:35], v[32:33]
	v_pk_fma_f32 v[62:63], v[80:81], v[24:25], v[62:63]
	v_pk_fma_f32 v[32:33], v[26:27], v[74:75], v[32:33] op_sel_hi:[0,1,1]
	v_pk_mul_f32 v[34:35], v[52:53], v[64:65]
	s_waitcnt lgkmcnt(0)
	v_pk_fma_f32 v[62:63], v[82:83], v[32:33], v[62:63]
	v_pk_fma_f32 v[34:35], v[26:27], v[76:77], v[34:35] op_sel_hi:[0,1,1]
	v_pk_fma_f32 v[52:53], v[84:85], v[34:35], v[62:63]
	v_pk_mul_f32 v[66:67], v[18:19], v[4:5] op_sel_hi:[0,1]
	v_exp_f32_e32 v66, v66
	v_exp_f32_e32 v67, v67
	v_pk_mul_f32 v[70:71], v[18:19], v[6:7] op_sel_hi:[0,1]
	v_exp_f32_e32 v70, v70
	v_exp_f32_e32 v71, v71
	ds_read_b128 v[62:65], v73 offset:1824
	ds_read_b128 v[74:77], v73 offset:1840
	ds_read_b128 v[78:81], v73 offset:1888
	ds_read_b128 v[82:85], v73 offset:1904
	v_pk_mul_f32 v[56:57], v[56:57], v[66:67]
	s_waitcnt lgkmcnt(3)
	v_pk_fma_f32 v[62:63], v[26:27], v[62:63], v[56:57] op_sel_hi:[0,1,1]
	v_pk_mul_f32 v[56:57], v[58:59], v[70:71]
	v_pk_mul_f32 v[58:59], v[18:19], v[2:3] op_sel_hi:[0,1]
	v_pk_fma_f32 v[64:65], v[26:27], v[64:65], v[56:57] op_sel_hi:[0,1,1]
	v_pk_mul_f32 v[56:57], v[18:19], v[0:1] op_sel_hi:[0,1]
	v_exp_f32_e32 v56, v56
	v_exp_f32_e32 v57, v57
	v_exp_f32_e32 v58, v58
	v_exp_f32_e32 v59, v59
	s_waitcnt lgkmcnt(1)
	v_pk_fma_f32 v[52:53], v[78:79], v[62:63], v[52:53]
	v_pk_mul_f32 v[56:57], v[60:61], v[56:57]
	v_pk_fma_f32 v[52:53], v[80:81], v[64:65], v[52:53]
	v_pk_fma_f32 v[66:67], v[26:27], v[74:75], v[56:57] op_sel_hi:[0,1,1]
	v_pk_mul_f32 v[56:57], v[68:69], v[58:59]
	s_waitcnt lgkmcnt(0)
	v_pk_fma_f32 v[52:53], v[82:83], v[66:67], v[52:53]
	v_pk_fma_f32 v[68:69], v[26:27], v[76:77], v[56:57] op_sel_hi:[0,1,1]
	v_pk_fma_f32 v[52:53], v[84:85], v[68:69], v[52:53]
	v_cvt_f32_f16_e32 v18, v49
	v_add_f32_e32 v26, v52, v53
	v_fmac_f32_e32 v26, v72, v48
	v_lshl_add_u64 v[52:53], v[40:41], 1, s[12:13]
	v_mul_f32_e32 v18, v26, v18
	v_cvt_f32_f16_sdwa v26, v27 dst_sel:DWORD dst_unused:UNUSED_PAD src0_sel:WORD_1
	v_fma_mixlo_f16 v18, v18, s1, 0
	v_mov_b32_e32 v70, v19
	global_store_short v[52:53], v18, off
	v_mul_f32_e32 v71, 0x3c800000, v26
	v_mul_f32_e32 v48, v71, v19
	v_pk_mul_f32 v[18:19], v[70:71], v[12:13] op_sel_hi:[0,1]
	v_pk_mul_f32 v[26:27], v[70:71], v[14:15] op_sel_hi:[0,1]
	v_exp_f32_e32 v18, v18
	v_exp_f32_e32 v19, v19
	v_exp_f32_e32 v26, v26
	v_exp_f32_e32 v27, v27
	v_add_u32_e32 v40, 0x800, v40
	ds_read_b128 v[56:59], v73 offset:1920
	ds_read_b128 v[74:77], v73 offset:1936
	ds_read_b128 v[78:81], v73 offset:1984
	ds_read_b128 v[82:85], v73 offset:2000
	v_pk_mul_f32 v[16:17], v[16:17], v[18:19]
	v_pk_mul_f32 v[18:19], v[24:25], v[26:27]
	s_waitcnt lgkmcnt(3)
	v_pk_fma_f32 v[52:53], v[48:49], v[56:57], v[16:17] op_sel_hi:[0,1,1]
	v_pk_fma_f32 v[56:57], v[48:49], v[58:59], v[18:19] op_sel_hi:[0,1,1]
	v_pk_mul_f32 v[18:19], v[70:71], v[8:9] op_sel_hi:[0,1]
	v_exp_f32_e32 v18, v18
	v_exp_f32_e32 v19, v19
	v_pk_mul_f32 v[24:25], v[70:71], v[10:11] op_sel_hi:[0,1]
	v_exp_f32_e32 v24, v24
	v_exp_f32_e32 v25, v25
	s_waitcnt lgkmcnt(1)
	v_pk_fma_f32 v[16:17], v[78:79], v[52:53], 0 op_sel_hi:[1,1,0]
	v_pk_mul_f32 v[18:19], v[32:33], v[18:19]
	v_pk_fma_f32 v[16:17], v[80:81], v[56:57], v[16:17]
	v_pk_fma_f32 v[58:59], v[48:49], v[74:75], v[18:19] op_sel_hi:[0,1,1]
	v_pk_mul_f32 v[18:19], v[34:35], v[24:25]
	s_waitcnt lgkmcnt(0)
	v_pk_fma_f32 v[16:17], v[82:83], v[58:59], v[16:17]
	v_pk_fma_f32 v[60:61], v[48:49], v[76:77], v[18:19] op_sel_hi:[0,1,1]
	v_pk_fma_f32 v[78:79], v[84:85], v[60:61], v[16:17]
	v_pk_mul_f32 v[80:81], v[70:71], v[4:5] op_sel_hi:[0,1]
	v_exp_f32_e32 v80, v80
	v_exp_f32_e32 v81, v81
	v_pk_mul_f32 v[82:83], v[70:71], v[6:7] op_sel_hi:[0,1]
	ds_read_b128 v[16:19], v73 offset:1952
	ds_read_b128 v[24:27], v73 offset:1968
	ds_read_b128 v[32:35], v73 offset:2016
	ds_read_b128 v[74:77], v73 offset:2032
	v_exp_f32_e32 v82, v82
	v_exp_f32_e32 v83, v83
	v_pk_mul_f32 v[62:63], v[62:63], v[80:81]
	s_waitcnt lgkmcnt(3)
	v_pk_fma_f32 v[62:63], v[48:49], v[16:17], v[62:63] op_sel_hi:[0,1,1]
	s_waitcnt lgkmcnt(1)
	v_pk_fma_f32 v[16:17], v[32:33], v[62:63], v[78:79]
	v_pk_mul_f32 v[32:33], v[64:65], v[82:83]
	s_nop 0
	v_pk_fma_f32 v[64:65], v[48:49], v[18:19], v[32:33] op_sel_hi:[0,1,1]
	v_pk_mul_f32 v[18:19], v[70:71], v[0:1] op_sel_hi:[0,1]
	v_exp_f32_e32 v18, v18
	v_exp_f32_e32 v19, v19
	v_pk_mul_f32 v[32:33], v[70:71], v[2:3] op_sel_hi:[0,1]
	v_exp_f32_e32 v32, v32
	v_exp_f32_e32 v33, v33
	v_pk_mul_f32 v[18:19], v[66:67], v[18:19]
	v_pk_fma_f32 v[16:17], v[34:35], v[64:65], v[16:17]
	v_pk_fma_f32 v[66:67], v[48:49], v[24:25], v[18:19] op_sel_hi:[0,1,1]
	v_pk_mul_f32 v[18:19], v[68:69], v[32:33]
	s_waitcnt lgkmcnt(0)
	v_pk_fma_f32 v[16:17], v[74:75], v[66:67], v[16:17]
	v_pk_fma_f32 v[68:69], v[48:49], v[26:27], v[18:19] op_sel_hi:[0,1,1]
	v_pk_fma_f32 v[16:17], v[76:77], v[68:69], v[16:17]
	s_or_b32 s6, s0, 6
	v_cvt_f32_f16_sdwa v18, v49 dst_sel:DWORD dst_unused:UNUSED_PAD src0_sel:WORD_1
	s_ashr_i32 s7, s6, 31
	s_or_b32 s2, s2, 3
	s_lshl_b64 s[6:7], s[6:7], 15
	s_or_b32 s8, s0, 7
	s_ashr_i32 s3, s2, 31
	v_add_f32_e32 v19, v16, v17
	s_ashr_i32 s9, s8, 31
	s_lshl_b64 s[2:3], s[2:3], 15
	v_lshl_add_u64 v[26:27], v[42:43], 0, s[6:7]
	v_fmac_f32_e32 v19, v72, v71
	s_lshl_b64 s[8:9], s[8:9], 15
	v_lshl_add_u64 v[24:25], v[44:45], 0, s[2:3]
	v_add_co_u32_e32 v44, vcc, s5, v26
	v_mul_f32_e32 v18, v19, v18
	v_lshl_add_u64 v[42:43], v[42:43], 0, s[8:9]
	v_addc_co_u32_e32 v45, vcc, 0, v27, vcc
	v_lshl_add_u64 v[16:17], v[40:41], 1, s[12:13]
	v_fma_mixlo_f16 v18, v18, s1, 0
	v_add_co_u32_e32 v42, vcc, s5, v42
	global_store_short v[16:17], v18, off
	v_add_u32_e32 v40, 0x800, v40
	v_lshl_add_u64 v[16:17], v[46:47], 0, s[6:7]
	v_lshl_add_u64 v[18:19], v[46:47], 0, s[8:9]
	v_addc_co_u32_e32 v43, vcc, 0, v43, vcc
	global_load_dwordx4 v[32:35], v[16:17], off
	s_nop 0
	global_load_dwordx4 v[16:19], v[18:19], off
	s_waitcnt vmcnt(12)
	v_cvt_f32_f16_e32 v46, v28
	global_load_dwordx4 v[24:27], v[24:25], off
	s_nop 0
	global_load_dwordx2 v[44:45], v[44:45], off
	s_nop 0
	global_load_dwordx2 v[42:43], v[42:43], off
	v_pk_mul_f32 v[86:87], v[36:37], v[12:13] op_sel_hi:[0,1]
	v_exp_f32_e32 v86, v86
	v_exp_f32_e32 v87, v87
	v_pk_mul_f32 v[88:89], v[36:37], v[14:15] op_sel_hi:[0,1]
	v_exp_f32_e32 v88, v88
	v_exp_f32_e32 v89, v89
	v_mul_f32_e32 v71, 0x3c800000, v46
	ds_read_b128 v[46:49], v73 offset:2048
	ds_read_b128 v[74:77], v73 offset:2064
	ds_read_b128 v[78:81], v73 offset:2112
	ds_read_b128 v[82:85], v73 offset:2128
	v_mul_f32_e32 v70, v71, v36
	v_pk_mul_f32 v[52:53], v[52:53], v[86:87]
	v_pk_mul_f32 v[56:57], v[56:57], v[88:89]
	s_waitcnt lgkmcnt(3)
	v_pk_fma_f32 v[46:47], v[70:71], v[46:47], v[52:53] op_sel_hi:[0,1,1]
	s_waitcnt lgkmcnt(1)
	v_pk_fma_f32 v[52:53], v[78:79], v[46:47], 0 op_sel_hi:[1,1,0]
	v_pk_fma_f32 v[48:49], v[70:71], v[48:49], v[56:57] op_sel_hi:[0,1,1]
	v_pk_fma_f32 v[56:57], v[80:81], v[48:49], v[52:53]
	v_pk_mul_f32 v[52:53], v[36:37], v[8:9] op_sel_hi:[0,1]
	v_exp_f32_e32 v52, v52
	v_exp_f32_e32 v53, v53
	v_pk_mul_f32 v[78:79], v[36:37], v[10:11] op_sel_hi:[0,1]
	v_exp_f32_e32 v78, v78
	v_exp_f32_e32 v79, v79
	v_pk_mul_f32 v[52:53], v[58:59], v[52:53]
	s_nop 0
	v_pk_fma_f32 v[52:53], v[70:71], v[74:75], v[52:53] op_sel_hi:[0,1,1]
	s_waitcnt lgkmcnt(0)
	v_pk_fma_f32 v[58:59], v[82:83], v[52:53], v[56:57]
	v_pk_mul_f32 v[56:57], v[60:61], v[78:79]
	s_nop 0
	v_pk_fma_f32 v[56:57], v[70:71], v[76:77], v[56:57] op_sel_hi:[0,1,1]
	v_pk_fma_f32 v[86:87], v[84:85], v[56:57], v[58:59]
	v_pk_mul_f32 v[88:89], v[36:37], v[4:5] op_sel_hi:[0,1]
	v_exp_f32_e32 v88, v88
	v_exp_f32_e32 v89, v89
	v_pk_mul_f32 v[90:91], v[36:37], v[6:7] op_sel_hi:[0,1]
	v_exp_f32_e32 v90, v90
	v_exp_f32_e32 v91, v91
	ds_read_b128 v[58:61], v73 offset:2080
	ds_read_b128 v[74:77], v73 offset:2096
	ds_read_b128 v[78:81], v73 offset:2144
	ds_read_b128 v[82:85], v73 offset:2160
	v_pk_mul_f32 v[62:63], v[62:63], v[88:89]
	v_pk_mul_f32 v[64:65], v[64:65], v[90:91]
	s_waitcnt lgkmcnt(3)
	v_pk_fma_f32 v[58:59], v[70:71], v[58:59], v[62:63] op_sel_hi:[0,1,1]
	s_waitcnt lgkmcnt(1)
	v_pk_fma_f32 v[62:63], v[78:79], v[58:59], v[86:87]
	v_pk_fma_f32 v[60:61], v[70:71], v[60:61], v[64:65] op_sel_hi:[0,1,1]
	v_pk_fma_f32 v[64:65], v[80:81], v[60:61], v[62:63]
	v_pk_mul_f32 v[62:63], v[36:37], v[0:1] op_sel_hi:[0,1]
	v_exp_f32_e32 v62, v62
	v_exp_f32_e32 v63, v63
	v_pk_mul_f32 v[78:79], v[36:37], v[2:3] op_sel_hi:[0,1]
	v_exp_f32_e32 v78, v78
	v_exp_f32_e32 v79, v79
	v_pk_mul_f32 v[62:63], v[66:67], v[62:63]
	s_nop 0
	v_pk_fma_f32 v[62:63], v[70:71], v[74:75], v[62:63] op_sel_hi:[0,1,1]
	s_waitcnt lgkmcnt(0)
	v_pk_fma_f32 v[66:67], v[82:83], v[62:63], v[64:65]
	v_pk_mul_f32 v[64:65], v[68:69], v[78:79]
	s_nop 0
	v_pk_fma_f32 v[64:65], v[70:71], v[76:77], v[64:65] op_sel_hi:[0,1,1]
	v_pk_fma_f32 v[66:67], v[84:85], v[64:65], v[66:67]
	s_waitcnt vmcnt(14)
	v_cvt_f32_f16_e32 v68, v54
	v_add_f32_e32 v69, v66, v67
	v_fmac_f32_e32 v69, v72, v71
	v_cvt_f32_f16_sdwa v28, v28 dst_sel:DWORD dst_unused:UNUSED_PAD src0_sel:WORD_1
	v_pk_mul_f32 v[86:87], v[36:37], v[14:15] op_sel:[1,0]
	v_mul_f32_e32 v68, v69, v68
	v_exp_f32_e32 v86, v86
	v_exp_f32_e32 v87, v87
	v_lshl_add_u64 v[66:67], v[40:41], 1, s[12:13]
	v_fma_mixlo_f16 v68, v68, s1, 0
	v_add_u32_e32 v40, 0x800, v40
	v_pk_mul_f32 v[70:71], v[36:37], v[12:13] op_sel:[1,0]
	global_store_short v[66:67], v68, off
	v_exp_f32_e32 v70, v70
	v_exp_f32_e32 v71, v71
	v_mul_f32_e32 v90, 0x3c800000, v28
	ds_read_b128 v[66:69], v73 offset:2176
	ds_read_b128 v[74:77], v73 offset:2192
	ds_read_b128 v[78:81], v73 offset:2240
	ds_read_b128 v[82:85], v73 offset:2256
	v_mul_f32_e32 v28, v90, v37
	v_pk_mul_f32 v[48:49], v[48:49], v[86:87]
	v_pk_mul_f32 v[46:47], v[46:47], v[70:71]
	s_waitcnt lgkmcnt(3)
	v_pk_fma_f32 v[48:49], v[28:29], v[68:69], v[48:49] op_sel_hi:[0,1,1]
	v_pk_mul_f32 v[68:69], v[36:37], v[8:9] op_sel:[1,0]
	v_pk_mul_f32 v[70:71], v[36:37], v[10:11] op_sel:[1,0]
	v_exp_f32_e32 v68, v68
	v_exp_f32_e32 v69, v69
	v_exp_f32_e32 v70, v70
	v_exp_f32_e32 v71, v71
	v_pk_fma_f32 v[46:47], v[28:29], v[66:67], v[46:47] op_sel_hi:[0,1,1]
	s_waitcnt lgkmcnt(1)
	v_pk_fma_f32 v[66:67], v[78:79], v[46:47], 0 op_sel_hi:[1,1,0]
	v_pk_mul_f32 v[52:53], v[52:53], v[68:69]
	v_pk_fma_f32 v[66:67], v[80:81], v[48:49], v[66:67]
	v_pk_fma_f32 v[52:53], v[28:29], v[74:75], v[52:53] op_sel_hi:[0,1,1]
	v_pk_mul_f32 v[56:57], v[56:57], v[70:71]
	s_waitcnt lgkmcnt(0)
	v_pk_fma_f32 v[66:67], v[82:83], v[52:53], v[66:67]
	v_pk_fma_f32 v[56:57], v[28:29], v[76:77], v[56:57] op_sel_hi:[0,1,1]
	v_pk_fma_f32 v[70:71], v[84:85], v[56:57], v[66:67]
	v_pk_mul_f32 v[88:89], v[36:37], v[6:7] op_sel:[1,0]
	ds_read_b128 v[66:69], v73 offset:2208
	ds_read_b128 v[74:77], v73 offset:2224
	ds_read_b128 v[78:81], v73 offset:2272
	ds_read_b128 v[82:85], v73 offset:2288
	v_exp_f32_e32 v88, v88
	v_exp_f32_e32 v89, v89
	v_pk_mul_f32 v[86:87], v[36:37], v[4:5] op_sel:[1,0]
	v_pk_mul_f32 v[60:61], v[60:61], v[88:89]
	v_exp_f32_e32 v86, v86
	v_exp_f32_e32 v87, v87
	s_waitcnt lgkmcnt(3)
	v_pk_fma_f32 v[60:61], v[28:29], v[68:69], v[60:61] op_sel_hi:[0,1,1]
	v_pk_mul_f32 v[68:69], v[36:37], v[0:1] op_sel:[1,0]
	v_pk_mul_f32 v[36:37], v[36:37], v[2:3] op_sel:[1,0]
	v_exp_f32_e32 v68, v68
	v_exp_f32_e32 v69, v69
	v_exp_f32_e32 v36, v36
	v_exp_f32_e32 v37, v37
	v_pk_mul_f32 v[58:59], v[58:59], v[86:87]
	v_pk_mul_f32 v[62:63], v[62:63], v[68:69]
	v_pk_fma_f32 v[58:59], v[28:29], v[66:67], v[58:59] op_sel_hi:[0,1,1]
	s_waitcnt lgkmcnt(1)
	v_pk_fma_f32 v[66:67], v[78:79], v[58:59], v[70:71]
	v_pk_fma_f32 v[62:63], v[28:29], v[74:75], v[62:63] op_sel_hi:[0,1,1]
	v_pk_fma_f32 v[66:67], v[80:81], v[60:61], v[66:67]
	v_pk_mul_f32 v[36:37], v[64:65], v[36:37]
	s_waitcnt lgkmcnt(0)
	v_pk_fma_f32 v[66:67], v[82:83], v[62:63], v[66:67]
	v_pk_fma_f32 v[64:65], v[28:29], v[76:77], v[36:37] op_sel_hi:[0,1,1]
	v_pk_fma_f32 v[36:37], v[84:85], v[64:65], v[66:67]
	v_cvt_f32_f16_sdwa v28, v54 dst_sel:DWORD dst_unused:UNUSED_PAD src0_sel:WORD_1
	v_add_f32_e32 v54, v36, v37
	v_fmac_f32_e32 v54, v72, v90
	v_lshl_add_u64 v[36:37], v[40:41], 1, s[12:13]
	v_mul_f32_e32 v28, v54, v28
	v_fma_mixlo_f16 v28, v28, s1, 0
	v_cvt_f32_f16_e32 v54, v29
	global_store_short v[36:37], v28, off
	v_pk_mul_f32 v[36:37], v[38:39], v[12:13] op_sel_hi:[0,1]
	v_pk_mul_f32 v[70:71], v[38:39], v[14:15] op_sel_hi:[0,1]
	v_exp_f32_e32 v36, v36
	v_exp_f32_e32 v37, v37
	v_exp_f32_e32 v70, v70
	v_exp_f32_e32 v71, v71
	v_add_u32_e32 v40, 0x800, v40
	v_mul_f32_e32 v54, 0x3c800000, v54
	ds_read_b128 v[66:69], v73 offset:2304
	ds_read_b128 v[74:77], v73 offset:2320
	ds_read_b128 v[78:81], v73 offset:2368
	ds_read_b128 v[82:85], v73 offset:2384
	v_mul_f32_e32 v28, v54, v38
	v_pk_mul_f32 v[36:37], v[46:47], v[36:37]
	v_pk_mul_f32 v[46:47], v[48:49], v[70:71]
	v_pk_mul_f32 v[48:49], v[38:39], v[8:9] op_sel_hi:[0,1]
	s_waitcnt lgkmcnt(3)
	v_pk_fma_f32 v[46:47], v[28:29], v[68:69], v[46:47] op_sel_hi:[0,1,1]
	v_exp_f32_e32 v48, v48
	v_exp_f32_e32 v49, v49
	v_pk_mul_f32 v[68:69], v[38:39], v[10:11] op_sel_hi:[0,1]
	v_exp_f32_e32 v68, v68
	v_exp_f32_e32 v69, v69
	v_pk_fma_f32 v[36:37], v[28:29], v[66:67], v[36:37] op_sel_hi:[0,1,1]
	s_waitcnt lgkmcnt(1)
	v_pk_fma_f32 v[66:67], v[78:79], v[36:37], 0 op_sel_hi:[1,1,0]
	v_pk_mul_f32 v[48:49], v[52:53], v[48:49]
	v_pk_fma_f32 v[66:67], v[80:81], v[46:47], v[66:67]
	v_pk_fma_f32 v[48:49], v[28:29], v[74:75], v[48:49] op_sel_hi:[0,1,1]
	v_pk_mul_f32 v[52:53], v[56:57], v[68:69]
	s_waitcnt lgkmcnt(0)
	v_pk_fma_f32 v[66:67], v[82:83], v[48:49], v[66:67]
	v_pk_fma_f32 v[52:53], v[28:29], v[76:77], v[52:53] op_sel_hi:[0,1,1]
	v_pk_fma_f32 v[70:71], v[84:85], v[52:53], v[66:67]
	v_pk_mul_f32 v[56:57], v[38:39], v[4:5] op_sel_hi:[0,1]
	v_pk_mul_f32 v[86:87], v[38:39], v[6:7] op_sel_hi:[0,1]
	v_exp_f32_e32 v56, v56
	v_exp_f32_e32 v57, v57
	v_exp_f32_e32 v86, v86
	v_exp_f32_e32 v87, v87
	ds_read_b128 v[66:69], v73 offset:2336
	ds_read_b128 v[74:77], v73 offset:2352
	ds_read_b128 v[78:81], v73 offset:2400
	ds_read_b128 v[82:85], v73 offset:2416
	v_pk_mul_f32 v[56:57], v[58:59], v[56:57]
	v_pk_mul_f32 v[58:59], v[60:61], v[86:87]
	v_pk_mul_f32 v[60:61], v[38:39], v[0:1] op_sel_hi:[0,1]
	s_waitcnt lgkmcnt(3)
	v_pk_fma_f32 v[58:59], v[28:29], v[68:69], v[58:59] op_sel_hi:[0,1,1]
	v_exp_f32_e32 v60, v60
	v_exp_f32_e32 v61, v61
	v_pk_mul_f32 v[68:69], v[38:39], v[2:3] op_sel_hi:[0,1]
	v_exp_f32_e32 v68, v68
	v_exp_f32_e32 v69, v69
	v_pk_fma_f32 v[56:57], v[28:29], v[66:67], v[56:57] op_sel_hi:[0,1,1]
	s_waitcnt lgkmcnt(1)
	v_pk_fma_f32 v[66:67], v[78:79], v[56:57], v[70:71]
	v_pk_mul_f32 v[60:61], v[62:63], v[60:61]
	v_pk_fma_f32 v[66:67], v[80:81], v[58:59], v[66:67]
	v_pk_fma_f32 v[60:61], v[28:29], v[74:75], v[60:61] op_sel_hi:[0,1,1]
	v_pk_mul_f32 v[62:63], v[64:65], v[68:69]
	s_waitcnt lgkmcnt(0)
	v_pk_fma_f32 v[66:67], v[82:83], v[60:61], v[66:67]
	v_pk_fma_f32 v[62:63], v[28:29], v[76:77], v[62:63] op_sel_hi:[0,1,1]
	v_pk_fma_f32 v[64:65], v[84:85], v[62:63], v[66:67]
	v_cvt_f32_f16_e32 v28, v55
	v_cvt_f32_f16_sdwa v29, v29 dst_sel:DWORD dst_unused:UNUSED_PAD src0_sel:WORD_1
	v_add_f32_e32 v38, v64, v65
	v_fmac_f32_e32 v38, v72, v54
	v_mul_f32_e32 v28, v38, v28
	v_lshl_add_u64 v[64:65], v[40:41], 1, s[12:13]
	v_fma_mixlo_f16 v28, v28, s1, 0
	v_mul_f32_e32 v83, 0x3c800000, v29
	v_mov_b32_e32 v82, v39
	global_store_short v[64:65], v28, off
	v_pk_mul_f32 v[28:29], v[82:83], v[12:13] op_sel_hi:[0,1]
	v_add_u32_e32 v40, 0x800, v40
	v_mul_f32_e32 v54, v83, v39
	v_exp_f32_e32 v28, v28
	v_exp_f32_e32 v29, v29
	v_pk_mul_f32 v[38:39], v[82:83], v[14:15] op_sel_hi:[0,1]
	v_exp_f32_e32 v38, v38
	v_exp_f32_e32 v39, v39
	ds_read_b128 v[64:67], v73 offset:2432
	ds_read_b128 v[68:71], v73 offset:2448
	ds_read_b128 v[74:77], v73 offset:2496
	ds_read_b128 v[78:81], v73 offset:2512
	v_pk_mul_f32 v[28:29], v[36:37], v[28:29]
	v_pk_mul_f32 v[36:37], v[46:47], v[38:39]
	s_waitcnt lgkmcnt(3)
	v_pk_fma_f32 v[28:29], v[54:55], v[64:65], v[28:29] op_sel_hi:[0,1,1]
	v_pk_mul_f32 v[38:39], v[82:83], v[8:9] op_sel_hi:[0,1]
	s_waitcnt lgkmcnt(1)
	v_pk_fma_f32 v[64:65], v[74:75], v[28:29], 0 op_sel_hi:[1,1,0]
	v_pk_fma_f32 v[36:37], v[54:55], v[66:67], v[36:37] op_sel_hi:[0,1,1]
	v_exp_f32_e32 v38, v38
	v_exp_f32_e32 v39, v39
	v_pk_fma_f32 v[46:47], v[76:77], v[36:37], v[64:65]
	v_pk_mul_f32 v[64:65], v[82:83], v[10:11] op_sel_hi:[0,1]
	v_exp_f32_e32 v64, v64
	v_exp_f32_e32 v65, v65
	v_pk_mul_f32 v[38:39], v[48:49], v[38:39]
	s_nop 0
	v_pk_fma_f32 v[38:39], v[54:55], v[68:69], v[38:39] op_sel_hi:[0,1,1]
	s_waitcnt lgkmcnt(0)
	v_pk_fma_f32 v[48:49], v[78:79], v[38:39], v[46:47]
	v_pk_mul_f32 v[46:47], v[52:53], v[64:65]
	s_nop 0
	v_pk_fma_f32 v[46:47], v[54:55], v[70:71], v[46:47] op_sel_hi:[0,1,1]
	v_pk_fma_f32 v[52:53], v[80:81], v[46:47], v[48:49]
	v_pk_mul_f32 v[48:49], v[82:83], v[4:5] op_sel_hi:[0,1]
	v_exp_f32_e32 v48, v48
	v_exp_f32_e32 v49, v49
	v_pk_mul_f32 v[84:85], v[82:83], v[6:7] op_sel_hi:[0,1]
	ds_read_b128 v[64:67], v73 offset:2464
	ds_read_b128 v[68:71], v73 offset:2480
	ds_read_b128 v[74:77], v73 offset:2528
	ds_read_b128 v[78:81], v73 offset:2544
	v_exp_f32_e32 v84, v84
	v_exp_f32_e32 v85, v85
	v_pk_mul_f32 v[48:49], v[56:57], v[48:49]
	s_waitcnt lgkmcnt(3)
	v_pk_fma_f32 v[48:49], v[54:55], v[64:65], v[48:49] op_sel_hi:[0,1,1]
	s_waitcnt lgkmcnt(1)
	v_pk_fma_f32 v[56:57], v[74:75], v[48:49], v[52:53]
	v_pk_mul_f32 v[52:53], v[58:59], v[84:85]
	v_pk_mul_f32 v[64:65], v[82:83], v[2:3] op_sel_hi:[0,1]
	v_pk_fma_f32 v[52:53], v[54:55], v[66:67], v[52:53] op_sel_hi:[0,1,1]
	v_pk_fma_f32 v[58:59], v[76:77], v[52:53], v[56:57]
	v_pk_mul_f32 v[56:57], v[82:83], v[0:1] op_sel_hi:[0,1]
	v_exp_f32_e32 v56, v56
	v_exp_f32_e32 v57, v57
	v_exp_f32_e32 v64, v64
	v_exp_f32_e32 v65, v65
	v_pk_mul_f32 v[56:57], v[60:61], v[56:57]
	s_nop 0
	v_pk_fma_f32 v[56:57], v[54:55], v[68:69], v[56:57] op_sel_hi:[0,1,1]
	s_waitcnt lgkmcnt(0)
	v_pk_fma_f32 v[60:61], v[78:79], v[56:57], v[58:59]
	v_pk_mul_f32 v[58:59], v[62:63], v[64:65]
	s_nop 0
	v_pk_fma_f32 v[58:59], v[54:55], v[70:71], v[58:59] op_sel_hi:[0,1,1]
	v_pk_fma_f32 v[60:61], v[80:81], v[58:59], v[60:61]
	v_cvt_f32_f16_sdwa v62, v55 dst_sel:DWORD dst_unused:UNUSED_PAD src0_sel:WORD_1
	v_add_f32_e32 v60, v60, v61
	v_fmac_f32_e32 v60, v72, v83
	v_lshl_add_u64 v[54:55], v[40:41], 1, s[12:13]
	v_mul_f32_e32 v60, v60, v62
	v_fma_mixlo_f16 v60, v60, s1, 0
	v_cvt_f32_f16_e32 v61, v30
	global_store_short v[54:55], v60, off
	v_pk_mul_f32 v[54:55], v[20:21], v[12:13] op_sel_hi:[0,1]
	v_exp_f32_e32 v54, v54
	v_exp_f32_e32 v55, v55
	v_pk_mul_f32 v[80:81], v[20:21], v[14:15] op_sel_hi:[0,1]
	v_add_u32_e32 v40, 0x800, v40
	v_exp_f32_e32 v80, v80
	v_exp_f32_e32 v81, v81
	v_mul_f32_e32 v79, 0x3c800000, v61
	ds_read_b128 v[60:63], v73 offset:2560
	ds_read_b128 v[64:67], v73 offset:2576
	ds_read_b128 v[68:71], v73 offset:2624
	ds_read_b128 v[74:77], v73 offset:2640
	v_mul_f32_e32 v78, v79, v20
	v_pk_mul_f32 v[28:29], v[28:29], v[54:55]
	v_pk_mul_f32 v[36:37], v[36:37], v[80:81]
	s_waitcnt lgkmcnt(3)
	v_pk_fma_f32 v[28:29], v[78:79], v[60:61], v[28:29] op_sel_hi:[0,1,1]
	v_pk_mul_f32 v[60:61], v[20:21], v[8:9] op_sel_hi:[0,1]
	v_pk_fma_f32 v[36:37], v[78:79], v[62:63], v[36:37] op_sel_hi:[0,1,1]
	v_exp_f32_e32 v60, v60
	v_exp_f32_e32 v61, v61
	v_pk_mul_f32 v[62:63], v[20:21], v[10:11] op_sel_hi:[0,1]
	v_exp_f32_e32 v62, v62
	v_exp_f32_e32 v63, v63
	s_waitcnt lgkmcnt(1)
	v_pk_fma_f32 v[54:55], v[68:69], v[28:29], 0 op_sel_hi:[1,1,0]
	v_pk_mul_f32 v[38:39], v[38:39], v[60:61]
	v_pk_fma_f32 v[54:55], v[70:71], v[36:37], v[54:55]
	v_pk_fma_f32 v[38:39], v[78:79], v[64:65], v[38:39] op_sel_hi:[0,1,1]
	v_pk_mul_f32 v[46:47], v[46:47], v[62:63]
	s_waitcnt lgkmcnt(0)
	v_pk_fma_f32 v[54:55], v[74:75], v[38:39], v[54:55]
	v_pk_fma_f32 v[46:47], v[78:79], v[66:67], v[46:47] op_sel_hi:[0,1,1]
	v_pk_fma_f32 v[54:55], v[76:77], v[46:47], v[54:55]
	v_pk_mul_f32 v[80:81], v[20:21], v[4:5] op_sel_hi:[0,1]
	v_exp_f32_e32 v80, v80
	v_exp_f32_e32 v81, v81
	v_pk_mul_f32 v[82:83], v[20:21], v[6:7] op_sel_hi:[0,1]
	v_exp_f32_e32 v82, v82
	v_exp_f32_e32 v83, v83
	ds_read_b128 v[60:63], v73 offset:2592
	ds_read_b128 v[64:67], v73 offset:2608
	ds_read_b128 v[68:71], v73 offset:2656
	ds_read_b128 v[74:77], v73 offset:2672
	v_pk_mul_f32 v[48:49], v[48:49], v[80:81]
	v_pk_mul_f32 v[52:53], v[52:53], v[82:83]
	s_waitcnt lgkmcnt(3)
	v_pk_fma_f32 v[48:49], v[78:79], v[60:61], v[48:49] op_sel_hi:[0,1,1]
	s_waitcnt lgkmcnt(1)
	v_pk_fma_f32 v[54:55], v[68:69], v[48:49], v[54:55]
	v_pk_fma_f32 v[52:53], v[78:79], v[62:63], v[52:53] op_sel_hi:[0,1,1]
	v_pk_fma_f32 v[60:61], v[70:71], v[52:53], v[54:55]
	v_pk_mul_f32 v[54:55], v[20:21], v[0:1] op_sel_hi:[0,1]
	v_exp_f32_e32 v54, v54
	v_exp_f32_e32 v55, v55
	v_pk_mul_f32 v[62:63], v[20:21], v[2:3] op_sel_hi:[0,1]
	v_exp_f32_e32 v62, v62
	v_exp_f32_e32 v63, v63
	v_pk_mul_f32 v[54:55], v[56:57], v[54:55]
	v_pk_mul_f32 v[56:57], v[58:59], v[62:63]
	v_pk_fma_f32 v[54:55], v[78:79], v[64:65], v[54:55] op_sel_hi:[0,1,1]
	s_waitcnt lgkmcnt(0)
	v_pk_fma_f32 v[60:61], v[74:75], v[54:55], v[60:61]
	v_pk_fma_f32 v[56:57], v[78:79], v[66:67], v[56:57] op_sel_hi:[0,1,1]
	v_pk_fma_f32 v[58:59], v[76:77], v[56:57], v[60:61]
	s_waitcnt vmcnt(17)
	v_cvt_f32_f16_e32 v60, v50
	v_add_f32_e32 v61, v58, v59
	v_fmac_f32_e32 v61, v72, v79
	v_cvt_f32_f16_sdwa v30, v30 dst_sel:DWORD dst_unused:UNUSED_PAD src0_sel:WORD_1
	v_mul_f32_e32 v60, v61, v60
	v_pk_mul_f32 v[70:71], v[20:21], v[12:13] op_sel:[1,0]
	v_pk_mul_f32 v[78:79], v[20:21], v[14:15] op_sel:[1,0]
	v_lshl_add_u64 v[58:59], v[40:41], 1, s[12:13]
	v_fma_mixlo_f16 v60, v60, s1, 0
	v_add_u32_e32 v40, 0x800, v40
	v_exp_f32_e32 v70, v70
	v_exp_f32_e32 v71, v71
	v_exp_f32_e32 v78, v78
	v_exp_f32_e32 v79, v79
	global_store_short v[58:59], v60, off
	ds_read_b128 v[58:61], v73 offset:2688
	ds_read_b128 v[62:65], v73 offset:2704
	ds_read_b128 v[66:69], v73 offset:2752
	ds_read_b128 v[74:77], v73 offset:2768
	v_mul_f32_e32 v82, 0x3c800000, v30
	v_mul_f32_e32 v30, v82, v21
	v_pk_mul_f32 v[28:29], v[28:29], v[70:71]
	v_pk_mul_f32 v[36:37], v[36:37], v[78:79]
	s_waitcnt lgkmcnt(3)
	v_pk_fma_f32 v[28:29], v[30:31], v[58:59], v[28:29] op_sel_hi:[0,1,1]
	v_pk_fma_f32 v[36:37], v[30:31], v[60:61], v[36:37] op_sel_hi:[0,1,1]
	v_pk_mul_f32 v[60:61], v[20:21], v[8:9] op_sel:[1,0]
	s_waitcnt lgkmcnt(1)
	v_pk_fma_f32 v[58:59], v[66:67], v[28:29], 0 op_sel_hi:[1,1,0]
	v_exp_f32_e32 v60, v60
	v_exp_f32_e32 v61, v61
	v_pk_mul_f32 v[66:67], v[20:21], v[10:11] op_sel:[1,0]
	v_pk_fma_f32 v[58:59], v[68:69], v[36:37], v[58:59]
	v_exp_f32_e32 v66, v66
	v_exp_f32_e32 v67, v67
	v_pk_mul_f32 v[38:39], v[38:39], v[60:61]
	v_pk_mul_f32 v[46:47], v[46:47], v[66:67]
	v_pk_fma_f32 v[38:39], v[30:31], v[62:63], v[38:39] op_sel_hi:[0,1,1]
	s_waitcnt lgkmcnt(0)
	v_pk_fma_f32 v[58:59], v[74:75], v[38:39], v[58:59]
	v_pk_fma_f32 v[46:47], v[30:31], v[64:65], v[46:47] op_sel_hi:[0,1,1]
	v_pk_fma_f32 v[70:71], v[76:77], v[46:47], v[58:59]
	v_pk_mul_f32 v[80:81], v[20:21], v[6:7] op_sel:[1,0]
	ds_read_b128 v[58:61], v73 offset:2720
	ds_read_b128 v[62:65], v73 offset:2736
	ds_read_b128 v[66:69], v73 offset:2784
	ds_read_b128 v[74:77], v73 offset:2800
	v_exp_f32_e32 v80, v80
	v_exp_f32_e32 v81, v81
	v_pk_mul_f32 v[78:79], v[20:21], v[4:5] op_sel:[1,0]
	v_pk_mul_f32 v[52:53], v[52:53], v[80:81]
	v_exp_f32_e32 v78, v78
	v_exp_f32_e32 v79, v79
	s_waitcnt lgkmcnt(3)
	v_pk_fma_f32 v[52:53], v[30:31], v[60:61], v[52:53] op_sel_hi:[0,1,1]
	v_pk_mul_f32 v[60:61], v[20:21], v[0:1] op_sel:[1,0]
	v_pk_mul_f32 v[20:21], v[20:21], v[2:3] op_sel:[1,0]
	v_exp_f32_e32 v60, v60
	v_exp_f32_e32 v61, v61
	v_exp_f32_e32 v20, v20
	v_exp_f32_e32 v21, v21
	v_pk_mul_f32 v[48:49], v[48:49], v[78:79]
	v_pk_mul_f32 v[54:55], v[54:55], v[60:61]
	v_pk_fma_f32 v[48:49], v[30:31], v[58:59], v[48:49] op_sel_hi:[0,1,1]
	s_waitcnt lgkmcnt(1)
	v_pk_fma_f32 v[58:59], v[66:67], v[48:49], v[70:71]
	v_pk_fma_f32 v[54:55], v[30:31], v[62:63], v[54:55] op_sel_hi:[0,1,1]
	v_pk_fma_f32 v[58:59], v[68:69], v[52:53], v[58:59]
	v_pk_mul_f32 v[20:21], v[56:57], v[20:21]
	s_waitcnt lgkmcnt(0)
	v_pk_fma_f32 v[58:59], v[74:75], v[54:55], v[58:59]
	v_pk_fma_f32 v[56:57], v[30:31], v[64:65], v[20:21] op_sel_hi:[0,1,1]
	v_pk_fma_f32 v[20:21], v[76:77], v[56:57], v[58:59]
	v_cvt_f32_f16_sdwa v30, v50 dst_sel:DWORD dst_unused:UNUSED_PAD src0_sel:WORD_1
	v_add_f32_e32 v50, v20, v21
	v_fmac_f32_e32 v50, v72, v82
	v_lshl_add_u64 v[20:21], v[40:41], 1, s[12:13]
	v_mul_f32_e32 v30, v50, v30
	v_fma_mixlo_f16 v30, v30, s1, 0
	v_cvt_f32_f16_e32 v50, v31
	global_store_short v[20:21], v30, off
	v_pk_mul_f32 v[20:21], v[22:23], v[12:13] op_sel_hi:[0,1]
	v_pk_mul_f32 v[70:71], v[22:23], v[14:15] op_sel_hi:[0,1]
	v_exp_f32_e32 v20, v20
	v_exp_f32_e32 v21, v21
	v_exp_f32_e32 v70, v70
	v_exp_f32_e32 v71, v71
	v_add_u32_e32 v40, 0x800, v40
	v_mul_f32_e32 v50, 0x3c800000, v50
	ds_read_b128 v[58:61], v73 offset:2816
	ds_read_b128 v[62:65], v73 offset:2832
	ds_read_b128 v[66:69], v73 offset:2880
	ds_read_b128 v[74:77], v73 offset:2896
	v_mul_f32_e32 v30, v50, v22
	v_pk_mul_f32 v[20:21], v[28:29], v[20:21]
	v_pk_mul_f32 v[28:29], v[36:37], v[70:71]
	v_pk_mul_f32 v[36:37], v[22:23], v[8:9] op_sel_hi:[0,1]
	s_waitcnt lgkmcnt(3)
	v_pk_fma_f32 v[28:29], v[30:31], v[60:61], v[28:29] op_sel_hi:[0,1,1]
	v_exp_f32_e32 v36, v36
	v_exp_f32_e32 v37, v37
	v_pk_mul_f32 v[60:61], v[22:23], v[10:11] op_sel_hi:[0,1]
	v_exp_f32_e32 v60, v60
	v_exp_f32_e32 v61, v61
	v_pk_fma_f32 v[20:21], v[30:31], v[58:59], v[20:21] op_sel_hi:[0,1,1]
	s_waitcnt lgkmcnt(1)
	v_pk_fma_f32 v[58:59], v[66:67], v[20:21], 0 op_sel_hi:[1,1,0]
	v_pk_mul_f32 v[36:37], v[38:39], v[36:37]
	v_pk_fma_f32 v[58:59], v[68:69], v[28:29], v[58:59]
	v_pk_fma_f32 v[36:37], v[30:31], v[62:63], v[36:37] op_sel_hi:[0,1,1]
	v_pk_mul_f32 v[38:39], v[46:47], v[60:61]
	s_waitcnt lgkmcnt(0)
	v_pk_fma_f32 v[58:59], v[74:75], v[36:37], v[58:59]
	v_pk_fma_f32 v[38:39], v[30:31], v[64:65], v[38:39] op_sel_hi:[0,1,1]
	v_pk_fma_f32 v[70:71], v[76:77], v[38:39], v[58:59]
	v_pk_mul_f32 v[46:47], v[22:23], v[4:5] op_sel_hi:[0,1]
	v_pk_mul_f32 v[78:79], v[22:23], v[6:7] op_sel_hi:[0,1]
	v_exp_f32_e32 v46, v46
	v_exp_f32_e32 v47, v47
	v_exp_f32_e32 v78, v78
	v_exp_f32_e32 v79, v79
	ds_read_b128 v[58:61], v73 offset:2848
	ds_read_b128 v[62:65], v73 offset:2864
	ds_read_b128 v[66:69], v73 offset:2912
	ds_read_b128 v[74:77], v73 offset:2928
	v_pk_mul_f32 v[46:47], v[48:49], v[46:47]
	v_pk_mul_f32 v[48:49], v[52:53], v[78:79]
	v_pk_mul_f32 v[52:53], v[22:23], v[0:1] op_sel_hi:[0,1]
	s_waitcnt lgkmcnt(3)
	v_pk_fma_f32 v[48:49], v[30:31], v[60:61], v[48:49] op_sel_hi:[0,1,1]
	v_exp_f32_e32 v52, v52
	v_exp_f32_e32 v53, v53
	v_pk_mul_f32 v[60:61], v[22:23], v[2:3] op_sel_hi:[0,1]
	v_exp_f32_e32 v60, v60
	v_exp_f32_e32 v61, v61
	v_pk_fma_f32 v[46:47], v[30:31], v[58:59], v[46:47] op_sel_hi:[0,1,1]
	s_waitcnt lgkmcnt(1)
	v_pk_fma_f32 v[58:59], v[66:67], v[46:47], v[70:71]
	v_pk_mul_f32 v[52:53], v[54:55], v[52:53]
	v_pk_fma_f32 v[58:59], v[68:69], v[48:49], v[58:59]
	v_pk_fma_f32 v[52:53], v[30:31], v[62:63], v[52:53] op_sel_hi:[0,1,1]
	v_pk_mul_f32 v[54:55], v[56:57], v[60:61]
	s_waitcnt lgkmcnt(0)
	v_pk_fma_f32 v[58:59], v[74:75], v[52:53], v[58:59]
	v_pk_fma_f32 v[54:55], v[30:31], v[64:65], v[54:55] op_sel_hi:[0,1,1]
	v_pk_fma_f32 v[56:57], v[76:77], v[54:55], v[58:59]
	v_cvt_f32_f16_e32 v22, v51
	v_add_f32_e32 v30, v56, v57
	v_fmac_f32_e32 v30, v72, v50
	v_lshl_add_u64 v[56:57], v[40:41], 1, s[12:13]
	v_mul_f32_e32 v22, v30, v22
	v_cvt_f32_f16_sdwa v30, v31 dst_sel:DWORD dst_unused:UNUSED_PAD src0_sel:WORD_1
	v_fma_mixlo_f16 v22, v22, s1, 0
	v_mov_b32_e32 v74, v23
	global_store_short v[56:57], v22, off
	v_mul_f32_e32 v75, 0x3c800000, v30
	v_mul_f32_e32 v50, v75, v23
	v_pk_mul_f32 v[22:23], v[74:75], v[12:13] op_sel_hi:[0,1]
	v_add_u32_e32 v40, 0x800, v40
	v_exp_f32_e32 v22, v22
	v_exp_f32_e32 v23, v23
	v_pk_mul_f32 v[30:31], v[74:75], v[14:15] op_sel_hi:[0,1]
	v_exp_f32_e32 v30, v30
	v_exp_f32_e32 v31, v31
	ds_read_b128 v[56:59], v73 offset:2944
	ds_read_b128 v[60:63], v73 offset:2960
	ds_read_b128 v[64:67], v73 offset:3008
	ds_read_b128 v[68:71], v73 offset:3024
	v_pk_mul_f32 v[20:21], v[20:21], v[22:23]
	v_pk_mul_f32 v[22:23], v[28:29], v[30:31]
	s_waitcnt lgkmcnt(3)
	v_pk_fma_f32 v[20:21], v[50:51], v[56:57], v[20:21] op_sel_hi:[0,1,1]
	v_pk_mul_f32 v[28:29], v[74:75], v[8:9] op_sel_hi:[0,1]
	s_waitcnt lgkmcnt(1)
	v_pk_fma_f32 v[56:57], v[64:65], v[20:21], 0 op_sel_hi:[1,1,0]
	v_pk_fma_f32 v[22:23], v[50:51], v[58:59], v[22:23] op_sel_hi:[0,1,1]
	v_exp_f32_e32 v28, v28
	v_exp_f32_e32 v29, v29
	v_pk_fma_f32 v[30:31], v[66:67], v[22:23], v[56:57]
	v_pk_mul_f32 v[56:57], v[74:75], v[10:11] op_sel_hi:[0,1]
	v_exp_f32_e32 v56, v56
	v_exp_f32_e32 v57, v57
	v_pk_mul_f32 v[28:29], v[36:37], v[28:29]
	s_nop 0
	v_pk_fma_f32 v[28:29], v[50:51], v[60:61], v[28:29] op_sel_hi:[0,1,1]
	s_waitcnt lgkmcnt(0)
	v_pk_fma_f32 v[36:37], v[68:69], v[28:29], v[30:31]
	v_pk_mul_f32 v[30:31], v[38:39], v[56:57]
	s_nop 0
	v_pk_fma_f32 v[30:31], v[50:51], v[62:63], v[30:31] op_sel_hi:[0,1,1]
	v_pk_fma_f32 v[68:69], v[70:71], v[30:31], v[36:37]
	v_pk_mul_f32 v[70:71], v[74:75], v[4:5] op_sel_hi:[0,1]
	v_exp_f32_e32 v70, v70
	v_exp_f32_e32 v71, v71
	v_pk_mul_f32 v[76:77], v[74:75], v[6:7] op_sel_hi:[0,1]
	v_exp_f32_e32 v76, v76
	v_exp_f32_e32 v77, v77
	ds_read_b128 v[36:39], v73 offset:2976
	ds_read_b128 v[56:59], v73 offset:2992
	ds_read_b128 v[60:63], v73 offset:3040
	ds_read_b128 v[64:67], v73 offset:3056
	v_pk_mul_f32 v[46:47], v[46:47], v[70:71]
	v_pk_mul_f32 v[48:49], v[48:49], v[76:77]
	s_waitcnt lgkmcnt(3)
	v_pk_fma_f32 v[36:37], v[50:51], v[36:37], v[46:47] op_sel_hi:[0,1,1]
	s_waitcnt lgkmcnt(1)
	v_pk_fma_f32 v[46:47], v[60:61], v[36:37], v[68:69]
	v_pk_fma_f32 v[38:39], v[50:51], v[38:39], v[48:49] op_sel_hi:[0,1,1]
	v_pk_fma_f32 v[48:49], v[62:63], v[38:39], v[46:47]
	v_pk_mul_f32 v[46:47], v[74:75], v[0:1] op_sel_hi:[0,1]
	v_exp_f32_e32 v46, v46
	v_exp_f32_e32 v47, v47
	v_pk_mul_f32 v[60:61], v[74:75], v[2:3] op_sel_hi:[0,1]
	v_exp_f32_e32 v60, v60
	v_exp_f32_e32 v61, v61
	v_pk_mul_f32 v[46:47], v[52:53], v[46:47]
	s_nop 0
	v_pk_fma_f32 v[46:47], v[50:51], v[56:57], v[46:47] op_sel_hi:[0,1,1]
	s_waitcnt lgkmcnt(0)
	v_pk_fma_f32 v[52:53], v[64:65], v[46:47], v[48:49]
	v_pk_mul_f32 v[48:49], v[54:55], v[60:61]
	s_nop 0
	v_pk_fma_f32 v[48:49], v[50:51], v[58:59], v[48:49] op_sel_hi:[0,1,1]
	v_pk_fma_f32 v[52:53], v[66:67], v[48:49], v[52:53]
	v_cvt_f32_f16_sdwa v54, v51 dst_sel:DWORD dst_unused:UNUSED_PAD src0_sel:WORD_1
	v_add_f32_e32 v52, v52, v53
	v_fmac_f32_e32 v52, v72, v75
	s_waitcnt vmcnt(9)
	v_cvt_f32_f16_e32 v53, v24
	v_mul_f32_e32 v52, v52, v54
	v_pk_mul_f32 v[68:69], v[32:33], v[12:13] op_sel_hi:[0,1]
	v_pk_mul_f32 v[70:71], v[32:33], v[14:15] op_sel_hi:[0,1]
	v_lshl_add_u64 v[50:51], v[40:41], 1, s[12:13]
	v_fma_mixlo_f16 v52, v52, s1, 0
	v_add_u32_e32 v40, 0x800, v40
	v_exp_f32_e32 v68, v68
	v_exp_f32_e32 v69, v69
	v_exp_f32_e32 v70, v70
	v_exp_f32_e32 v71, v71
	global_store_short v[50:51], v52, off
	v_mul_f32_e32 v67, 0x3c800000, v53
	ds_read_b128 v[50:53], v73 offset:3072
	ds_read_b128 v[54:57], v73 offset:3088
	ds_read_b128 v[58:61], v73 offset:3136
	ds_read_b128 v[62:65], v73 offset:3152
	v_mul_f32_e32 v66, v67, v32
	v_pk_mul_f32 v[20:21], v[20:21], v[68:69]
	v_pk_mul_f32 v[22:23], v[22:23], v[70:71]
	s_waitcnt lgkmcnt(3)
	v_pk_fma_f32 v[20:21], v[66:67], v[50:51], v[20:21] op_sel_hi:[0,1,1]
	v_pk_fma_f32 v[22:23], v[66:67], v[52:53], v[22:23] op_sel_hi:[0,1,1]
	v_pk_mul_f32 v[52:53], v[32:33], v[8:9] op_sel_hi:[0,1]
	s_waitcnt lgkmcnt(1)
	v_pk_fma_f32 v[50:51], v[58:59], v[20:21], 0 op_sel_hi:[1,1,0]
	v_exp_f32_e32 v52, v52
	v_exp_f32_e32 v53, v53
	v_pk_mul_f32 v[58:59], v[32:33], v[10:11] op_sel_hi:[0,1]
	v_exp_f32_e32 v58, v58
	v_exp_f32_e32 v59, v59
	v_pk_mul_f32 v[28:29], v[28:29], v[52:53]
	v_pk_fma_f32 v[50:51], v[60:61], v[22:23], v[50:51]
	v_pk_fma_f32 v[28:29], v[66:67], v[54:55], v[28:29] op_sel_hi:[0,1,1]
	v_pk_mul_f32 v[30:31], v[30:31], v[58:59]
	s_waitcnt lgkmcnt(0)
	v_pk_fma_f32 v[50:51], v[62:63], v[28:29], v[50:51]
	v_pk_fma_f32 v[30:31], v[66:67], v[56:57], v[30:31] op_sel_hi:[0,1,1]
	v_pk_fma_f32 v[68:69], v[64:65], v[30:31], v[50:51]
	v_pk_mul_f32 v[70:71], v[32:33], v[4:5] op_sel_hi:[0,1]
	v_pk_mul_f32 v[74:75], v[32:33], v[6:7] op_sel_hi:[0,1]
	v_exp_f32_e32 v70, v70
	v_exp_f32_e32 v71, v71
	v_exp_f32_e32 v74, v74
	v_exp_f32_e32 v75, v75
	ds_read_b128 v[50:53], v73 offset:3104
	ds_read_b128 v[54:57], v73 offset:3120
	ds_read_b128 v[58:61], v73 offset:3168
	ds_read_b128 v[62:65], v73 offset:3184
	v_pk_mul_f32 v[36:37], v[36:37], v[70:71]
	v_pk_mul_f32 v[38:39], v[38:39], v[74:75]
	s_waitcnt lgkmcnt(3)
	v_pk_fma_f32 v[36:37], v[66:67], v[50:51], v[36:37] op_sel_hi:[0,1,1]
	v_pk_fma_f32 v[38:39], v[66:67], v[52:53], v[38:39] op_sel_hi:[0,1,1]
	v_pk_mul_f32 v[52:53], v[32:33], v[0:1] op_sel_hi:[0,1]
	s_waitcnt lgkmcnt(1)
	v_pk_fma_f32 v[50:51], v[58:59], v[36:37], v[68:69]
	v_exp_f32_e32 v52, v52
	v_exp_f32_e32 v53, v53
	v_pk_mul_f32 v[58:59], v[32:33], v[2:3] op_sel_hi:[0,1]
	v_exp_f32_e32 v58, v58
	v_exp_f32_e32 v59, v59
	v_pk_mul_f32 v[46:47], v[46:47], v[52:53]
	v_pk_fma_f32 v[50:51], v[60:61], v[38:39], v[50:51]
	v_pk_fma_f32 v[46:47], v[66:67], v[54:55], v[46:47] op_sel_hi:[0,1,1]
	v_pk_mul_f32 v[48:49], v[48:49], v[58:59]
	s_waitcnt lgkmcnt(0)
	v_pk_fma_f32 v[50:51], v[62:63], v[46:47], v[50:51]
	v_pk_fma_f32 v[48:49], v[66:67], v[56:57], v[48:49] op_sel_hi:[0,1,1]
	v_pk_fma_f32 v[50:51], v[64:65], v[48:49], v[50:51]
	s_waitcnt vmcnt(9)
	v_cvt_f32_f16_e32 v52, v44
	v_add_f32_e32 v53, v50, v51
	v_fmac_f32_e32 v53, v72, v67
	v_cvt_f32_f16_sdwa v24, v24 dst_sel:DWORD dst_unused:UNUSED_PAD src0_sel:WORD_1
	v_mul_f32_e32 v52, v53, v52
	v_pk_mul_f32 v[66:67], v[32:33], v[12:13] op_sel:[1,0]
	v_pk_mul_f32 v[68:69], v[32:33], v[14:15] op_sel:[1,0]
	v_lshl_add_u64 v[50:51], v[40:41], 1, s[12:13]
	v_fma_mixlo_f16 v52, v52, s1, 0
	v_add_u32_e32 v40, 0x800, v40
	v_exp_f32_e32 v66, v66
	v_exp_f32_e32 v67, v67
	v_exp_f32_e32 v68, v68
	v_exp_f32_e32 v69, v69
	global_store_short v[50:51], v52, off
	ds_read_b128 v[50:53], v73 offset:3200
	ds_read_b128 v[54:57], v73 offset:3216
	ds_read_b128 v[58:61], v73 offset:3264
	ds_read_b128 v[62:65], v73 offset:3280
	v_mul_f32_e32 v74, 0x3c800000, v24
	v_mul_f32_e32 v24, v74, v33
	v_pk_mul_f32 v[20:21], v[20:21], v[66:67]
	v_pk_mul_f32 v[22:23], v[22:23], v[68:69]
	s_waitcnt lgkmcnt(3)
	v_pk_fma_f32 v[20:21], v[24:25], v[50:51], v[20:21] op_sel_hi:[0,1,1]
	v_pk_fma_f32 v[22:23], v[24:25], v[52:53], v[22:23] op_sel_hi:[0,1,1]
	v_pk_mul_f32 v[52:53], v[32:33], v[8:9] op_sel:[1,0]
	s_waitcnt lgkmcnt(1)
	v_pk_fma_f32 v[50:51], v[58:59], v[20:21], 0 op_sel_hi:[1,1,0]
	v_exp_f32_e32 v52, v52
	v_exp_f32_e32 v53, v53
	v_pk_mul_f32 v[58:59], v[32:33], v[10:11] op_sel:[1,0]
	v_pk_fma_f32 v[50:51], v[60:61], v[22:23], v[50:51]
	v_exp_f32_e32 v58, v58
	v_exp_f32_e32 v59, v59
	v_pk_mul_f32 v[28:29], v[28:29], v[52:53]
	v_pk_mul_f32 v[30:31], v[30:31], v[58:59]
	v_pk_fma_f32 v[28:29], v[24:25], v[54:55], v[28:29] op_sel_hi:[0,1,1]
	s_waitcnt lgkmcnt(0)
	v_pk_fma_f32 v[50:51], v[62:63], v[28:29], v[50:51]
	v_pk_fma_f32 v[30:31], v[24:25], v[56:57], v[30:31] op_sel_hi:[0,1,1]
	v_pk_fma_f32 v[66:67], v[64:65], v[30:31], v[50:51]
	v_pk_mul_f32 v[70:71], v[32:33], v[6:7] op_sel:[1,0]
	ds_read_b128 v[50:53], v73 offset:3232
	ds_read_b128 v[54:57], v73 offset:3248
	ds_read_b128 v[58:61], v73 offset:3296
	ds_read_b128 v[62:65], v73 offset:3312
	v_exp_f32_e32 v70, v70
	v_exp_f32_e32 v71, v71
	v_pk_mul_f32 v[68:69], v[32:33], v[4:5] op_sel:[1,0]
	v_pk_mul_f32 v[38:39], v[38:39], v[70:71]
	v_exp_f32_e32 v68, v68
	v_exp_f32_e32 v69, v69
	s_waitcnt lgkmcnt(3)
	v_pk_fma_f32 v[38:39], v[24:25], v[52:53], v[38:39] op_sel_hi:[0,1,1]
	v_pk_mul_f32 v[52:53], v[32:33], v[0:1] op_sel:[1,0]
	v_pk_mul_f32 v[32:33], v[32:33], v[2:3] op_sel:[1,0]
	v_exp_f32_e32 v52, v52
	v_exp_f32_e32 v53, v53
	v_exp_f32_e32 v32, v32
	v_exp_f32_e32 v33, v33
	v_pk_mul_f32 v[36:37], v[36:37], v[68:69]
	v_pk_mul_f32 v[46:47], v[46:47], v[52:53]
	v_pk_fma_f32 v[36:37], v[24:25], v[50:51], v[36:37] op_sel_hi:[0,1,1]
	s_waitcnt lgkmcnt(1)
	v_pk_fma_f32 v[50:51], v[58:59], v[36:37], v[66:67]
	v_pk_fma_f32 v[46:47], v[24:25], v[54:55], v[46:47] op_sel_hi:[0,1,1]
	v_pk_fma_f32 v[50:51], v[60:61], v[38:39], v[50:51]
	v_pk_mul_f32 v[32:33], v[48:49], v[32:33]
	s_waitcnt lgkmcnt(0)
	v_pk_fma_f32 v[50:51], v[62:63], v[46:47], v[50:51]
	v_pk_fma_f32 v[48:49], v[24:25], v[56:57], v[32:33] op_sel_hi:[0,1,1]
	v_pk_fma_f32 v[32:33], v[64:65], v[48:49], v[50:51]
	v_cvt_f32_f16_sdwa v24, v44 dst_sel:DWORD dst_unused:UNUSED_PAD src0_sel:WORD_1
	v_add_f32_e32 v44, v32, v33
	v_fmac_f32_e32 v44, v72, v74
	v_lshl_add_u64 v[32:33], v[40:41], 1, s[12:13]
	v_mul_f32_e32 v24, v44, v24
	v_fma_mixlo_f16 v24, v24, s1, 0
	v_cvt_f32_f16_e32 v44, v25
	global_store_short v[32:33], v24, off
	v_pk_mul_f32 v[32:33], v[34:35], v[12:13] op_sel_hi:[0,1]
	v_exp_f32_e32 v32, v32
	v_exp_f32_e32 v33, v33
	v_pk_mul_f32 v[66:67], v[34:35], v[14:15] op_sel_hi:[0,1]
	v_add_u32_e32 v40, 0x800, v40
	v_exp_f32_e32 v66, v66
	v_exp_f32_e32 v67, v67
	v_mul_f32_e32 v44, 0x3c800000, v44
	ds_read_b128 v[50:53], v73 offset:3328
	ds_read_b128 v[54:57], v73 offset:3344
	ds_read_b128 v[58:61], v73 offset:3392
	ds_read_b128 v[62:65], v73 offset:3408
	v_mul_f32_e32 v24, v44, v34
	v_pk_mul_f32 v[20:21], v[20:21], v[32:33]
	v_pk_mul_f32 v[22:23], v[22:23], v[66:67]
	s_waitcnt lgkmcnt(3)
	v_pk_fma_f32 v[20:21], v[24:25], v[50:51], v[20:21] op_sel_hi:[0,1,1]
	v_pk_mul_f32 v[50:51], v[34:35], v[8:9] op_sel_hi:[0,1]
	v_pk_fma_f32 v[22:23], v[24:25], v[52:53], v[22:23] op_sel_hi:[0,1,1]
	v_exp_f32_e32 v50, v50
	v_exp_f32_e32 v51, v51
	v_pk_mul_f32 v[52:53], v[34:35], v[10:11] op_sel_hi:[0,1]
	v_exp_f32_e32 v52, v52
	v_exp_f32_e32 v53, v53
	s_waitcnt lgkmcnt(1)
	v_pk_fma_f32 v[32:33], v[58:59], v[20:21], 0 op_sel_hi:[1,1,0]
	v_pk_mul_f32 v[28:29], v[28:29], v[50:51]
	v_pk_fma_f32 v[32:33], v[60:61], v[22:23], v[32:33]
	v_pk_fma_f32 v[28:29], v[24:25], v[54:55], v[28:29] op_sel_hi:[0,1,1]
	v_pk_mul_f32 v[30:31], v[30:31], v[52:53]
	s_waitcnt lgkmcnt(0)
	v_pk_fma_f32 v[32:33], v[62:63], v[28:29], v[32:33]
	v_pk_fma_f32 v[30:31], v[24:25], v[56:57], v[30:31] op_sel_hi:[0,1,1]
	v_pk_fma_f32 v[66:67], v[64:65], v[30:31], v[32:33]
	v_pk_mul_f32 v[32:33], v[34:35], v[4:5] op_sel_hi:[0,1]
	v_pk_mul_f32 v[68:69], v[34:35], v[6:7] op_sel_hi:[0,1]
	v_exp_f32_e32 v32, v32
	v_exp_f32_e32 v33, v33
	v_exp_f32_e32 v68, v68
	v_exp_f32_e32 v69, v69
	ds_read_b128 v[50:53], v73 offset:3360
	ds_read_b128 v[54:57], v73 offset:3376
	ds_read_b128 v[58:61], v73 offset:3424
	ds_read_b128 v[62:65], v73 offset:3440
	v_pk_mul_f32 v[32:33], v[36:37], v[32:33]
	v_pk_mul_f32 v[36:37], v[38:39], v[68:69]
	v_pk_mul_f32 v[38:39], v[34:35], v[0:1] op_sel_hi:[0,1]
	s_waitcnt lgkmcnt(3)
	v_pk_fma_f32 v[36:37], v[24:25], v[52:53], v[36:37] op_sel_hi:[0,1,1]
	v_exp_f32_e32 v38, v38
	v_exp_f32_e32 v39, v39
	v_pk_mul_f32 v[52:53], v[34:35], v[2:3] op_sel_hi:[0,1]
	v_exp_f32_e32 v52, v52
	v_exp_f32_e32 v53, v53
	v_pk_fma_f32 v[32:33], v[24:25], v[50:51], v[32:33] op_sel_hi:[0,1,1]
	s_waitcnt lgkmcnt(1)
	v_pk_fma_f32 v[50:51], v[58:59], v[32:33], v[66:67]
	v_pk_mul_f32 v[38:39], v[46:47], v[38:39]
	v_pk_fma_f32 v[50:51], v[60:61], v[36:37], v[50:51]
	v_pk_fma_f32 v[38:39], v[24:25], v[54:55], v[38:39] op_sel_hi:[0,1,1]
	v_pk_mul_f32 v[46:47], v[48:49], v[52:53]
	s_waitcnt lgkmcnt(0)
	v_pk_fma_f32 v[50:51], v[62:63], v[38:39], v[50:51]
	v_pk_fma_f32 v[46:47], v[24:25], v[56:57], v[46:47] op_sel_hi:[0,1,1]
	v_pk_fma_f32 v[48:49], v[64:65], v[46:47], v[50:51]
	v_cvt_f32_f16_e32 v24, v45
	v_add_f32_e32 v34, v48, v49
	v_cvt_f32_f16_sdwa v25, v25 dst_sel:DWORD dst_unused:UNUSED_PAD src0_sel:WORD_1
	v_fmac_f32_e32 v34, v72, v44
	v_mul_f32_e32 v24, v34, v24
	v_lshl_add_u64 v[48:49], v[40:41], 1, s[12:13]
	v_fma_mixlo_f16 v24, v24, s1, 0
	v_mov_b32_e32 v34, v35
	global_store_short v[48:49], v24, off
	v_mul_f32_e32 v68, 0x3c800000, v25
	v_pk_mul_f32 v[24:25], v[34:35], v[12:13] op_sel_hi:[0,1]
	v_add_u32_e32 v40, 0x800, v40
	v_exp_f32_e32 v24, v24
	v_exp_f32_e32 v25, v25
	v_pk_mul_f32 v[64:65], v[34:35], v[14:15] op_sel_hi:[0,1]
	v_exp_f32_e32 v64, v64
	v_exp_f32_e32 v65, v65
	ds_read_b128 v[48:51], v73 offset:3456
	ds_read_b128 v[52:55], v73 offset:3472
	ds_read_b128 v[56:59], v73 offset:3520
	ds_read_b128 v[60:63], v73 offset:3536
	v_mul_f32_e32 v44, v68, v35
	v_pk_mul_f32 v[20:21], v[20:21], v[24:25]
	v_pk_mul_f32 v[22:23], v[22:23], v[64:65]
	s_waitcnt lgkmcnt(3)
	v_pk_fma_f32 v[20:21], v[44:45], v[48:49], v[20:21] op_sel_hi:[0,1,1]
	s_waitcnt lgkmcnt(1)
	v_pk_fma_f32 v[24:25], v[56:57], v[20:21], 0 op_sel_hi:[1,1,0]
	v_pk_fma_f32 v[22:23], v[44:45], v[50:51], v[22:23] op_sel_hi:[0,1,1]
	v_pk_fma_f32 v[48:49], v[58:59], v[22:23], v[24:25]
	v_pk_mul_f32 v[24:25], v[34:35], v[8:9] op_sel_hi:[0,1]
	v_exp_f32_e32 v24, v24
	v_exp_f32_e32 v25, v25
	v_pk_mul_f32 v[50:51], v[34:35], v[10:11] op_sel_hi:[0,1]
	v_exp_f32_e32 v50, v50
	v_exp_f32_e32 v51, v51
	v_pk_mul_f32 v[24:25], v[28:29], v[24:25]
	v_pk_mul_f32 v[28:29], v[30:31], v[50:51]
	v_pk_fma_f32 v[24:25], v[44:45], v[52:53], v[24:25] op_sel_hi:[0,1,1]
	s_waitcnt lgkmcnt(0)
	v_pk_fma_f32 v[48:49], v[60:61], v[24:25], v[48:49]
	v_pk_fma_f32 v[28:29], v[44:45], v[54:55], v[28:29] op_sel_hi:[0,1,1]
	v_pk_fma_f32 v[64:65], v[62:63], v[28:29], v[48:49]
	v_pk_mul_f32 v[30:31], v[34:35], v[4:5] op_sel_hi:[0,1]
	v_exp_f32_e32 v30, v30
	v_exp_f32_e32 v31, v31
	v_pk_mul_f32 v[66:67], v[34:35], v[6:7] op_sel_hi:[0,1]
	v_exp_f32_e32 v66, v66
	v_exp_f32_e32 v67, v67
	ds_read_b128 v[48:51], v73 offset:3488
	ds_read_b128 v[52:55], v73 offset:3504
	ds_read_b128 v[56:59], v73 offset:3552
	ds_read_b128 v[60:63], v73 offset:3568
	v_pk_mul_f32 v[30:31], v[32:33], v[30:31]
	v_pk_mul_f32 v[32:33], v[36:37], v[66:67]
	s_waitcnt lgkmcnt(3)
	v_pk_fma_f32 v[30:31], v[44:45], v[48:49], v[30:31] op_sel_hi:[0,1,1]
	s_waitcnt lgkmcnt(1)
	v_pk_fma_f32 v[48:49], v[56:57], v[30:31], v[64:65]
	v_pk_fma_f32 v[32:33], v[44:45], v[50:51], v[32:33] op_sel_hi:[0,1,1]
	v_pk_fma_f32 v[36:37], v[58:59], v[32:33], v[48:49]
	v_pk_mul_f32 v[48:49], v[34:35], v[0:1] op_sel_hi:[0,1]
	v_exp_f32_e32 v48, v48
	v_exp_f32_e32 v49, v49
	v_pk_mul_f32 v[34:35], v[34:35], v[2:3] op_sel_hi:[0,1]
	v_exp_f32_e32 v50, v34
	v_exp_f32_e32 v51, v35
	v_pk_mul_f32 v[34:35], v[38:39], v[48:49]
	s_nop 0
	v_pk_fma_f32 v[34:35], v[44:45], v[52:53], v[34:35] op_sel_hi:[0,1,1]
	s_waitcnt lgkmcnt(0)
	v_pk_fma_f32 v[38:39], v[60:61], v[34:35], v[36:37]
	v_pk_mul_f32 v[36:37], v[46:47], v[50:51]
	s_nop 0
	v_pk_fma_f32 v[36:37], v[44:45], v[54:55], v[36:37] op_sel_hi:[0,1,1]
	v_pk_fma_f32 v[38:39], v[62:63], v[36:37], v[38:39]
	v_cvt_f32_f16_sdwa v44, v45 dst_sel:DWORD dst_unused:UNUSED_PAD src0_sel:WORD_1
	v_add_f32_e32 v45, v38, v39
	v_fmac_f32_e32 v45, v72, v68
	v_pk_mul_f32 v[60:61], v[16:17], v[12:13] op_sel_hi:[0,1]
	v_mul_f32_e32 v44, v45, v44
	v_cvt_f32_f16_e32 v45, v26
	v_pk_mul_f32 v[62:63], v[16:17], v[14:15] op_sel_hi:[0,1]
	v_lshl_add_u64 v[38:39], v[40:41], 1, s[12:13]
	v_fma_mixlo_f16 v44, v44, s1, 0
	v_add_u32_e32 v40, 0x800, v40
	v_exp_f32_e32 v60, v60
	v_exp_f32_e32 v61, v61
	v_exp_f32_e32 v62, v62
	v_exp_f32_e32 v63, v63
	global_store_short v[38:39], v44, off
	v_mul_f32_e32 v66, 0x3c800000, v45
	ds_read_b128 v[44:47], v73 offset:3584
	ds_read_b128 v[48:51], v73 offset:3600
	ds_read_b128 v[52:55], v73 offset:3648
	ds_read_b128 v[56:59], v73 offset:3664
	v_mul_f32_e32 v38, v66, v16
	v_pk_mul_f32 v[20:21], v[20:21], v[60:61]
	v_pk_mul_f32 v[22:23], v[22:23], v[62:63]
	s_waitcnt lgkmcnt(3)
	v_pk_fma_f32 v[20:21], v[38:39], v[44:45], v[20:21] op_sel_hi:[0,1,1]
	v_pk_fma_f32 v[22:23], v[38:39], v[46:47], v[22:23] op_sel_hi:[0,1,1]
	v_pk_mul_f32 v[46:47], v[16:17], v[8:9] op_sel_hi:[0,1]
	s_waitcnt lgkmcnt(1)
	v_pk_fma_f32 v[44:45], v[52:53], v[20:21], 0 op_sel_hi:[1,1,0]
	v_exp_f32_e32 v46, v46
	v_exp_f32_e32 v47, v47
	v_pk_mul_f32 v[52:53], v[16:17], v[10:11] op_sel_hi:[0,1]
	v_exp_f32_e32 v52, v52
	v_exp_f32_e32 v53, v53
	v_pk_mul_f32 v[24:25], v[24:25], v[46:47]
	v_pk_fma_f32 v[44:45], v[54:55], v[22:23], v[44:45]
	v_pk_fma_f32 v[24:25], v[38:39], v[48:49], v[24:25] op_sel_hi:[0,1,1]
	v_pk_mul_f32 v[28:29], v[28:29], v[52:53]
	s_waitcnt lgkmcnt(0)
	v_pk_fma_f32 v[44:45], v[56:57], v[24:25], v[44:45]
	v_pk_fma_f32 v[28:29], v[38:39], v[50:51], v[28:29] op_sel_hi:[0,1,1]
	v_pk_fma_f32 v[60:61], v[58:59], v[28:29], v[44:45]
	v_pk_mul_f32 v[62:63], v[16:17], v[4:5] op_sel_hi:[0,1]
	v_pk_mul_f32 v[64:65], v[16:17], v[6:7] op_sel_hi:[0,1]
	v_exp_f32_e32 v62, v62
	v_exp_f32_e32 v63, v63
	v_exp_f32_e32 v64, v64
	v_exp_f32_e32 v65, v65
	ds_read_b128 v[44:47], v73 offset:3616
	ds_read_b128 v[48:51], v73 offset:3632
	ds_read_b128 v[52:55], v73 offset:3680
	ds_read_b128 v[56:59], v73 offset:3696
	v_pk_mul_f32 v[30:31], v[30:31], v[62:63]
	v_pk_mul_f32 v[32:33], v[32:33], v[64:65]
	s_waitcnt lgkmcnt(3)
	v_pk_fma_f32 v[30:31], v[38:39], v[44:45], v[30:31] op_sel_hi:[0,1,1]
	v_pk_fma_f32 v[32:33], v[38:39], v[46:47], v[32:33] op_sel_hi:[0,1,1]
	v_pk_mul_f32 v[46:47], v[16:17], v[0:1] op_sel_hi:[0,1]
	s_waitcnt lgkmcnt(1)
	v_pk_fma_f32 v[44:45], v[52:53], v[30:31], v[60:61]
	v_exp_f32_e32 v46, v46
	v_exp_f32_e32 v47, v47
	v_pk_mul_f32 v[52:53], v[16:17], v[2:3] op_sel_hi:[0,1]
	v_exp_f32_e32 v52, v52
	v_exp_f32_e32 v53, v53
	v_pk_mul_f32 v[34:35], v[34:35], v[46:47]
	v_pk_fma_f32 v[44:45], v[54:55], v[32:33], v[44:45]
	v_pk_fma_f32 v[34:35], v[38:39], v[48:49], v[34:35] op_sel_hi:[0,1,1]
	v_pk_mul_f32 v[36:37], v[36:37], v[52:53]
	s_waitcnt lgkmcnt(0)
	v_pk_fma_f32 v[44:45], v[56:57], v[34:35], v[44:45]
	v_pk_fma_f32 v[36:37], v[38:39], v[50:51], v[36:37] op_sel_hi:[0,1,1]
	v_pk_fma_f32 v[38:39], v[58:59], v[36:37], v[44:45]
	s_waitcnt vmcnt(12)
	v_cvt_f32_f16_e32 v44, v42
	v_add_f32_e32 v45, v38, v39
	v_fmac_f32_e32 v45, v72, v66
	v_lshl_add_u64 v[38:39], v[40:41], 1, s[12:13]
	v_mul_f32_e32 v44, v45, v44
	v_fma_mixlo_f16 v44, v44, s1, 0
	v_cvt_f32_f16_sdwa v26, v26 dst_sel:DWORD dst_unused:UNUSED_PAD src0_sel:WORD_1
	global_store_short v[38:39], v44, off
	v_pk_mul_f32 v[38:39], v[16:17], v[12:13] op_sel:[1,0]
	v_pk_mul_f32 v[60:61], v[16:17], v[14:15] op_sel:[1,0]
	v_exp_f32_e32 v38, v38
	v_exp_f32_e32 v39, v39
	v_add_u32_e32 v40, 0x800, v40
	v_exp_f32_e32 v60, v60
	v_exp_f32_e32 v61, v61
	v_mul_f32_e32 v64, 0x3c800000, v26
	ds_read_b128 v[44:47], v73 offset:3712
	ds_read_b128 v[48:51], v73 offset:3728
	ds_read_b128 v[52:55], v73 offset:3776
	ds_read_b128 v[56:59], v73 offset:3792
	v_mul_f32_e32 v26, v64, v17
	v_pk_mul_f32 v[20:21], v[20:21], v[38:39]
	v_pk_mul_f32 v[22:23], v[22:23], v[60:61]
	s_waitcnt lgkmcnt(3)
	v_pk_fma_f32 v[20:21], v[26:27], v[44:45], v[20:21] op_sel_hi:[0,1,1]
	v_pk_mul_f32 v[44:45], v[16:17], v[8:9] op_sel:[1,0]
	v_pk_fma_f32 v[22:23], v[26:27], v[46:47], v[22:23] op_sel_hi:[0,1,1]
	v_exp_f32_e32 v44, v44
	v_exp_f32_e32 v45, v45
	v_pk_mul_f32 v[46:47], v[16:17], v[10:11] op_sel:[1,0]
	s_waitcnt lgkmcnt(1)
	v_pk_fma_f32 v[38:39], v[52:53], v[20:21], 0 op_sel_hi:[1,1,0]
	v_exp_f32_e32 v46, v46
	v_exp_f32_e32 v47, v47
	v_pk_mul_f32 v[24:25], v[24:25], v[44:45]
	v_pk_fma_f32 v[38:39], v[54:55], v[22:23], v[38:39]
	v_pk_fma_f32 v[24:25], v[26:27], v[48:49], v[24:25] op_sel_hi:[0,1,1]
	v_pk_mul_f32 v[28:29], v[28:29], v[46:47]
	s_waitcnt lgkmcnt(0)
	v_pk_fma_f32 v[38:39], v[56:57], v[24:25], v[38:39]
	v_pk_fma_f32 v[28:29], v[26:27], v[50:51], v[28:29] op_sel_hi:[0,1,1]
	v_pk_fma_f32 v[38:39], v[58:59], v[28:29], v[38:39]
	v_pk_mul_f32 v[60:61], v[16:17], v[4:5] op_sel:[1,0]
	ds_read_b128 v[44:47], v73 offset:3744
	ds_read_b128 v[48:51], v73 offset:3760
	ds_read_b128 v[52:55], v73 offset:3808
	ds_read_b128 v[56:59], v73 offset:3824
	v_exp_f32_e32 v60, v60
	v_exp_f32_e32 v61, v61
	v_pk_mul_f32 v[62:63], v[16:17], v[6:7] op_sel:[1,0]
	v_pk_mul_f32 v[30:31], v[30:31], v[60:61]
	v_exp_f32_e32 v62, v62
	v_exp_f32_e32 v63, v63
	s_waitcnt lgkmcnt(3)
	v_pk_fma_f32 v[30:31], v[26:27], v[44:45], v[30:31] op_sel_hi:[0,1,1]
	v_pk_mul_f32 v[44:45], v[16:17], v[0:1] op_sel:[1,0]
	v_pk_mul_f32 v[16:17], v[16:17], v[2:3] op_sel:[1,0]
	v_exp_f32_e32 v44, v44
	v_exp_f32_e32 v45, v45
	v_exp_f32_e32 v16, v16
	v_exp_f32_e32 v17, v17
	v_pk_mul_f32 v[32:33], v[32:33], v[62:63]
	s_waitcnt lgkmcnt(1)
	v_pk_fma_f32 v[38:39], v[52:53], v[30:31], v[38:39]
	v_pk_fma_f32 v[32:33], v[26:27], v[46:47], v[32:33] op_sel_hi:[0,1,1]
	v_pk_mul_f32 v[34:35], v[34:35], v[44:45]
	v_pk_fma_f32 v[38:39], v[54:55], v[32:33], v[38:39]
	v_pk_fma_f32 v[34:35], v[26:27], v[48:49], v[34:35] op_sel_hi:[0,1,1]
	v_pk_mul_f32 v[16:17], v[36:37], v[16:17]
	s_waitcnt lgkmcnt(0)
	v_pk_fma_f32 v[38:39], v[56:57], v[34:35], v[38:39]
	v_pk_fma_f32 v[36:37], v[26:27], v[50:51], v[16:17] op_sel_hi:[0,1,1]
	v_pk_fma_f32 v[16:17], v[58:59], v[36:37], v[38:39]
	v_cvt_f32_f16_sdwa v26, v42 dst_sel:DWORD dst_unused:UNUSED_PAD src0_sel:WORD_1
	v_add_f32_e32 v38, v16, v17
	v_fmac_f32_e32 v38, v72, v64
	v_lshl_add_u64 v[16:17], v[40:41], 1, s[12:13]
	v_mul_f32_e32 v26, v38, v26
	v_cvt_f32_f16_e32 v38, v27
	v_fma_mixlo_f16 v26, v26, s1, 0
	global_store_short v[16:17], v26, off
	v_pk_mul_f32 v[16:17], v[18:19], v[12:13] op_sel_hi:[0,1]
	v_add_u32_e32 v40, 0x800, v40
	v_mul_f32_e32 v42, 0x3c800000, v38
	v_exp_f32_e32 v16, v16
	v_exp_f32_e32 v17, v17
	v_pk_mul_f32 v[38:39], v[18:19], v[14:15] op_sel_hi:[0,1]
	v_exp_f32_e32 v38, v38
	v_exp_f32_e32 v39, v39
	ds_read_b128 v[44:47], v73 offset:3840
	ds_read_b128 v[48:51], v73 offset:3856
	ds_read_b128 v[52:55], v73 offset:3904
	ds_read_b128 v[56:59], v73 offset:3920
	v_mul_f32_e32 v26, v42, v18
	v_pk_mul_f32 v[16:17], v[20:21], v[16:17]
	v_pk_mul_f32 v[20:21], v[22:23], v[38:39]
	s_waitcnt lgkmcnt(3)
	v_pk_fma_f32 v[16:17], v[26:27], v[44:45], v[16:17] op_sel_hi:[0,1,1]
	s_waitcnt lgkmcnt(1)
	v_pk_fma_f32 v[44:45], v[52:53], v[16:17], 0 op_sel_hi:[1,1,0]
	v_pk_fma_f32 v[20:21], v[26:27], v[46:47], v[20:21] op_sel_hi:[0,1,1]
	v_pk_mul_f32 v[22:23], v[18:19], v[8:9] op_sel_hi:[0,1]
	v_pk_fma_f32 v[38:39], v[54:55], v[20:21], v[44:45]
	v_exp_f32_e32 v22, v22
	v_exp_f32_e32 v23, v23
	v_pk_mul_f32 v[44:45], v[18:19], v[10:11] op_sel_hi:[0,1]
	v_exp_f32_e32 v44, v44
	v_exp_f32_e32 v45, v45
	v_pk_mul_f32 v[22:23], v[24:25], v[22:23]
	v_pk_mul_f32 v[24:25], v[28:29], v[44:45]
	v_pk_fma_f32 v[22:23], v[26:27], v[48:49], v[22:23] op_sel_hi:[0,1,1]
	s_waitcnt lgkmcnt(0)
	v_pk_fma_f32 v[38:39], v[56:57], v[22:23], v[38:39]
	v_pk_fma_f32 v[24:25], v[26:27], v[50:51], v[24:25] op_sel_hi:[0,1,1]
	v_pk_fma_f32 v[38:39], v[58:59], v[24:25], v[38:39]
	v_pk_mul_f32 v[28:29], v[18:19], v[4:5] op_sel_hi:[0,1]
	v_pk_mul_f32 v[60:61], v[18:19], v[6:7] op_sel_hi:[0,1]
	v_exp_f32_e32 v28, v28
	v_exp_f32_e32 v29, v29
	v_exp_f32_e32 v60, v60
	v_exp_f32_e32 v61, v61
	ds_read_b128 v[44:47], v73 offset:3872
	ds_read_b128 v[48:51], v73 offset:3888
	ds_read_b128 v[52:55], v73 offset:3936
	ds_read_b128 v[56:59], v73 offset:3952
	v_pk_mul_f32 v[28:29], v[30:31], v[28:29]
	v_pk_mul_f32 v[30:31], v[32:33], v[60:61]
	v_pk_mul_f32 v[32:33], v[18:19], v[0:1] op_sel_hi:[0,1]
	s_waitcnt lgkmcnt(3)
	v_pk_fma_f32 v[28:29], v[26:27], v[44:45], v[28:29] op_sel_hi:[0,1,1]
	v_exp_f32_e32 v32, v32
	v_exp_f32_e32 v33, v33
	v_pk_mul_f32 v[44:45], v[18:19], v[2:3] op_sel_hi:[0,1]
	v_exp_f32_e32 v44, v44
	v_exp_f32_e32 v45, v45
	s_waitcnt lgkmcnt(1)
	v_pk_fma_f32 v[38:39], v[52:53], v[28:29], v[38:39]
	v_pk_fma_f32 v[30:31], v[26:27], v[46:47], v[30:31] op_sel_hi:[0,1,1]
	v_pk_mul_f32 v[32:33], v[34:35], v[32:33]
	v_pk_fma_f32 v[38:39], v[54:55], v[30:31], v[38:39]
	v_pk_fma_f32 v[32:33], v[26:27], v[48:49], v[32:33] op_sel_hi:[0,1,1]
	v_pk_mul_f32 v[34:35], v[36:37], v[44:45]
	s_waitcnt lgkmcnt(0)
	v_pk_fma_f32 v[38:39], v[56:57], v[32:33], v[38:39]
	v_pk_fma_f32 v[34:35], v[26:27], v[50:51], v[34:35] op_sel_hi:[0,1,1]
	v_pk_fma_f32 v[36:37], v[58:59], v[34:35], v[38:39]
	v_cvt_f32_f16_e32 v18, v43
	v_add_f32_e32 v26, v36, v37
	v_fmac_f32_e32 v26, v72, v42
	v_mov_b32_e32 v42, v19
	v_mul_f32_e32 v18, v26, v18
	v_cvt_f32_f16_sdwa v26, v27 dst_sel:DWORD dst_unused:UNUSED_PAD src0_sel:WORD_1
	v_pk_mul_f32 v[12:13], v[42:43], v[12:13] op_sel_hi:[0,1]
	v_lshl_add_u64 v[36:37], v[40:41], 1, s[12:13]
	v_fma_mixlo_f16 v18, v18, s1, 0
	v_add_u32_e32 v40, 0x800, v40
	v_exp_f32_e32 v12, v12
	v_exp_f32_e32 v13, v13
	v_pk_mul_f32 v[14:15], v[42:43], v[14:15] op_sel_hi:[0,1]
	global_store_short v[36:37], v18, off
	v_exp_f32_e32 v14, v14
	v_exp_f32_e32 v15, v15
	v_pk_mul_f32 v[8:9], v[42:43], v[8:9] op_sel_hi:[0,1]
	ds_read_b128 v[36:39], v73 offset:3968
	ds_read_b128 v[44:47], v73 offset:3984
	ds_read_b128 v[48:51], v73 offset:4032
	ds_read_b128 v[52:55], v73 offset:4048
	v_exp_f32_e32 v8, v8
	v_exp_f32_e32 v9, v9
	v_pk_mul_f32 v[10:11], v[42:43], v[10:11] op_sel_hi:[0,1]
	v_mul_f32_e32 v27, 0x3c800000, v26
	v_exp_f32_e32 v10, v10
	v_exp_f32_e32 v11, v11
	v_mul_f32_e32 v26, v27, v19
	v_pk_mul_f32 v[12:13], v[16:17], v[12:13]
	v_pk_mul_f32 v[14:15], v[20:21], v[14:15]
	s_waitcnt lgkmcnt(3)
	v_pk_fma_f32 v[12:13], v[26:27], v[36:37], v[12:13] op_sel_hi:[0,1,1]
	s_waitcnt lgkmcnt(1)
	v_pk_fma_f32 v[16:17], v[48:49], v[12:13], 0 op_sel_hi:[1,1,0]
	v_pk_fma_f32 v[14:15], v[26:27], v[38:39], v[14:15] op_sel_hi:[0,1,1]
	v_pk_mul_f32 v[8:9], v[22:23], v[8:9]
	v_pk_fma_f32 v[16:17], v[50:51], v[14:15], v[16:17]
	v_pk_fma_f32 v[8:9], v[26:27], v[44:45], v[8:9] op_sel_hi:[0,1,1]
	v_pk_mul_f32 v[10:11], v[24:25], v[10:11]
	s_waitcnt lgkmcnt(0)
	v_pk_fma_f32 v[16:17], v[52:53], v[8:9], v[16:17]
	v_pk_fma_f32 v[10:11], v[26:27], v[46:47], v[10:11] op_sel_hi:[0,1,1]
	v_pk_fma_f32 v[24:25], v[54:55], v[10:11], v[16:17]
	v_pk_mul_f32 v[4:5], v[42:43], v[4:5] op_sel_hi:[0,1]
	v_exp_f32_e32 v4, v4
	v_exp_f32_e32 v5, v5
	v_pk_mul_f32 v[6:7], v[42:43], v[6:7] op_sel_hi:[0,1]
	v_exp_f32_e32 v6, v6
	v_exp_f32_e32 v7, v7
	v_pk_mul_f32 v[0:1], v[42:43], v[0:1] op_sel_hi:[0,1]
	ds_read_b128 v[8:11], v73 offset:4000
	ds_read_b128 v[12:15], v73 offset:4016
	ds_read_b128 v[16:19], v73 offset:4064
	ds_read_b128 v[20:23], v73 offset:4080
	v_exp_f32_e32 v0, v0
	v_exp_f32_e32 v1, v1
	v_pk_mul_f32 v[2:3], v[42:43], v[2:3] op_sel_hi:[0,1]
	v_exp_f32_e32 v2, v2
	v_exp_f32_e32 v3, v3
	v_pk_mul_f32 v[4:5], v[28:29], v[4:5]
	v_pk_mul_f32 v[6:7], v[30:31], v[6:7]
	s_waitcnt lgkmcnt(3)
	v_pk_fma_f32 v[4:5], v[26:27], v[8:9], v[4:5] op_sel_hi:[0,1,1]
	s_waitcnt lgkmcnt(1)
	v_pk_fma_f32 v[4:5], v[16:17], v[4:5], v[24:25]
	v_pk_fma_f32 v[6:7], v[26:27], v[10:11], v[6:7] op_sel_hi:[0,1,1]
	v_pk_mul_f32 v[0:1], v[32:33], v[0:1]
	v_pk_fma_f32 v[4:5], v[18:19], v[6:7], v[4:5]
	v_pk_fma_f32 v[0:1], v[26:27], v[12:13], v[0:1] op_sel_hi:[0,1,1]
	v_pk_mul_f32 v[2:3], v[34:35], v[2:3]
	s_waitcnt lgkmcnt(0)
	v_pk_fma_f32 v[0:1], v[20:21], v[0:1], v[4:5]
	v_pk_fma_f32 v[2:3], v[26:27], v[14:15], v[2:3] op_sel_hi:[0,1,1]
	v_pk_fma_f32 v[0:1], v[22:23], v[2:3], v[0:1]
	v_cvt_f32_f16_sdwa v2, v43 dst_sel:DWORD dst_unused:UNUSED_PAD src0_sel:WORD_1
	v_add_f32_e32 v3, v0, v1
	v_fmac_f32_e32 v3, v72, v27
	v_lshl_add_u64 v[0:1], v[40:41], 1, s[12:13]
	v_mul_f32_e32 v2, v3, v2
	v_fma_mixlo_f16 v2, v2, s1, 0
	global_store_short v[0:1], v2, off
	v_add_u32_e32 v0, 0x800, v40
	s_endpgm
	.p2alignl 8, 3212836864

.LBB4_10:
	s_or_b64 exec, exec, s[4:5]
	s_load_dwordx2 s[0:1], s[0:1], 0x18
	v_pk_add_f32 v[36:37], v[0:1], 0 op_sel_hi:[1,0]
	s_mov_b32 s4, 0x43800000
	v_pk_mul_f32 v[36:37], v[36:37], s[4:5] op_sel_hi:[1,0]
	s_waitcnt lgkmcnt(0)
	v_lshl_add_u64 v[4:5], s[0:1], 0, v[4:5]
	v_lshl_add_u64 v[4:5], v[4:5], 0, s[2:3]
	v_cvt_pk_f16_f32 v36, v36, v37
	v_lshl_add_u64 v[4:5], v[4:5], 0, v[2:3]
	global_store_dword v[4:5], v36, off
	v_pk_add_f32 v[4:5], v[24:25], v[48:49]
	s_nop 0
	v_pk_mul_f32 v[4:5], v[4:5], s[4:5] op_sel_hi:[1,0]
	s_nop 0
	v_cvt_pk_f16_f32 v24, v4, v5
	v_lshl_add_u64 v[4:5], s[0:1], 0, v[6:7]
	v_lshl_add_u64 v[4:5], v[4:5], 0, s[2:3]
	v_lshl_add_u64 v[4:5], v[4:5], 0, v[2:3]
	global_store_dword v[4:5], v24, off
	v_pk_fma_f32 v[4:5], v[0:1], v[22:23], v[20:21]
	s_nop 0
	v_pk_mul_f32 v[4:5], v[4:5], s[4:5] op_sel_hi:[1,0]
	s_nop 0
	v_cvt_pk_f16_f32 v6, v4, v5
	v_lshl_add_u64 v[4:5], s[0:1], 0, v[8:9]
	v_lshl_add_u64 v[4:5], v[4:5], 0, s[2:3]
	v_lshl_add_u64 v[4:5], v[4:5], 0, v[2:3]
	global_store_dword v[4:5], v6, off
	v_pk_fma_f32 v[4:5], v[0:1], v[32:33], v[30:31]
	s_nop 0
	v_pk_mul_f32 v[4:5], v[4:5], s[4:5] op_sel_hi:[1,0]
	s_nop 0
	v_cvt_pk_f16_f32 v6, v4, v5
	v_lshl_add_u64 v[4:5], s[0:1], 0, v[10:11]
	v_lshl_add_u64 v[4:5], v[4:5], 0, s[2:3]
	v_lshl_add_u64 v[4:5], v[4:5], 0, v[2:3]
	global_store_dword v[4:5], v6, off
	v_pk_fma_f32 v[4:5], v[0:1], v[28:29], v[26:27]
	s_nop 0
	v_pk_mul_f32 v[4:5], v[4:5], s[4:5] op_sel_hi:[1,0]
	s_nop 0
	v_cvt_pk_f16_f32 v6, v4, v5
	v_lshl_add_u64 v[4:5], s[0:1], 0, v[12:13]
	v_lshl_add_u64 v[4:5], v[4:5], 0, s[2:3]
	v_lshl_add_u64 v[4:5], v[4:5], 0, v[2:3]
	global_store_dword v[4:5], v6, off
	v_pk_fma_f32 v[4:5], v[0:1], v[42:43], v[40:41]
	s_nop 0
	v_pk_mul_f32 v[4:5], v[4:5], s[4:5] op_sel_hi:[1,0]
	s_nop 0
	v_cvt_pk_f16_f32 v6, v4, v5
	v_lshl_add_u64 v[4:5], s[0:1], 0, v[14:15]
	v_lshl_add_u64 v[4:5], v[4:5], 0, s[2:3]
	v_lshl_add_u64 v[4:5], v[4:5], 0, v[2:3]
	global_store_dword v[4:5], v6, off
	v_pk_fma_f32 v[4:5], v[0:1], v[38:39], v[34:35]
	v_pk_fma_f32 v[0:1], v[0:1], v[46:47], v[44:45]
	v_pk_mul_f32 v[4:5], v[4:5], s[4:5] op_sel_hi:[1,0]
	v_pk_mul_f32 v[0:1], v[0:1], s[4:5] op_sel_hi:[1,0]
	v_cvt_pk_f16_f32 v6, v4, v5
	v_lshl_add_u64 v[4:5], s[0:1], 0, v[16:17]
	v_lshl_add_u64 v[4:5], v[4:5], 0, s[2:3]
	v_lshl_add_u64 v[4:5], v[4:5], 0, v[2:3]
	global_store_dword v[4:5], v6, off
	v_cvt_pk_f16_f32 v4, v0, v1
	v_lshl_add_u64 v[0:1], s[0:1], 0, v[18:19]
	v_lshl_add_u64 v[0:1], v[0:1], 0, s[2:3]
	v_lshl_add_u64 v[0:1], v[0:1], 0, v[2:3]
	global_store_dword v[0:1], v4, off
	s_endpgm
	.p2alignl 8, 3212836864

.LBB5_10:
	s_or_b64 exec, exec, s[4:5]
	s_load_dword s0, s[0:1], 0x20
	v_and_b32_e32 v0, 12, v154
	v_or3_b32 v132, v0, v138, s28
	v_ashrrev_i32_e32 v130, 2, v132
	v_lshlrev_b32_e32 v0, 5, v1
	v_ashrrev_i32_e32 v131, 31, v130
	v_or3_b32 v134, s29, v0, v152
	v_lshlrev_b64 v[0:1], 15, v[130:131]
	v_lshl_add_u64 v[136:137], s[2:3], 0, v[0:1]
	s_waitcnt lgkmcnt(0)
	v_pk_mul_f32 v[0:1], s[0:1], v[128:129] op_sel_hi:[0,1]
	v_ashrrev_i32_e32 v135, 31, v134
	v_pk_mul_f32 v[126:127], s[0:1], v[126:127] op_sel_hi:[0,1]
	v_cvt_pk_f16_f32 v129, v0, v1
	v_lshlrev_b64 v[0:1], 3, v[134:135]
	v_cvt_pk_f16_f32 v128, v126, v127
	v_lshl_add_u64 v[126:127], v[136:137], 0, v[0:1]
	global_store_dwordx2 v[126:127], v[128:129], off
	v_or_b32_e32 v126, 16, v134
	v_pk_mul_f32 v[120:121], s[0:1], v[120:121] op_sel_hi:[0,1]
	v_pk_mul_f32 v[118:119], s[0:1], v[118:119] op_sel_hi:[0,1]
	v_ashrrev_i32_e32 v127, 31, v126
	v_cvt_pk_f16_f32 v121, v120, v121
	v_cvt_pk_f16_f32 v120, v118, v119
	v_lshlrev_b64 v[118:119], 3, v[126:127]
	v_lshl_add_u64 v[126:127], v[136:137], 0, v[118:119]
	v_pk_mul_f32 v[122:123], s[0:1], v[122:123] op_sel_hi:[0,1]
	global_store_dwordx2 v[126:127], v[120:121], off
	v_mul_f32_e32 v121, 0xbfb8aa3b, v122
	v_pk_mul_f32 v[124:125], s[0:1], v[124:125] op_sel_hi:[0,1]
	v_exp_f32_e32 v121, v121
	v_mul_f32_e32 v126, 0xbfb8aa3b, v123
	v_mul_f32_e32 v127, 0xbfb8aa3b, v124
	v_exp_f32_e32 v126, v126
	v_exp_f32_e32 v127, v127
	v_mul_f32_e32 v128, 0xbfb8aa3b, v125
	v_exp_f32_e32 v128, v128
	v_add_f32_e32 v121, 1.0, v121
	v_rcp_f32_e32 v121, v121
	v_add_f32_e32 v126, 1.0, v126
	v_add_f32_e32 v127, 1.0, v127
	v_rcp_f32_e32 v126, v126
	v_rcp_f32_e32 v127, v127
	v_add_f32_e32 v128, 1.0, v128
	v_rcp_f32_e32 v128, v128
	v_fma_mixlo_f16 v121, v122, v121, 0
	v_pk_mov_b32 v[122:123], v[122:123], v[124:125] op_sel:[1,0]
	v_add_u32_e32 v120, 0x800, v134
	v_pk_mul_f32 v[122:123], v[122:123], v[126:127]
	v_pk_mul_f32 v[114:115], s[0:1], v[114:115] op_sel_hi:[0,1]
	v_cvt_pk_f16_f32 v123, v122, v123
	v_pack_b32_f16 v122, v121, v123
	v_fma_mixlo_f16 v121, v125, v128, 0
	v_alignbit_b32 v123, v121, v123, 16
	v_ashrrev_i32_e32 v121, 31, v120
	v_lshlrev_b64 v[120:121], 3, v[120:121]
	v_lshl_add_u64 v[124:125], v[136:137], 0, v[120:121]
	global_store_dwordx2 v[124:125], v[122:123], off
	v_mul_f32_e32 v123, 0xbfb8aa3b, v114
	v_pk_mul_f32 v[116:117], s[0:1], v[116:117] op_sel_hi:[0,1]
	v_exp_f32_e32 v123, v123
	v_mul_f32_e32 v124, 0xbfb8aa3b, v115
	v_mul_f32_e32 v125, 0xbfb8aa3b, v116
	v_exp_f32_e32 v124, v124
	v_exp_f32_e32 v125, v125
	v_mul_f32_e32 v126, 0xbfb8aa3b, v117
	v_exp_f32_e32 v126, v126
	v_add_f32_e32 v123, 1.0, v123
	v_rcp_f32_e32 v123, v123
	v_add_f32_e32 v124, 1.0, v124
	v_add_f32_e32 v125, 1.0, v125
	v_rcp_f32_e32 v124, v124
	v_rcp_f32_e32 v125, v125
	v_add_f32_e32 v126, 1.0, v126
	v_rcp_f32_e32 v126, v126
	v_fma_mixlo_f16 v123, v114, v123, 0
	v_pk_mov_b32 v[114:115], v[114:115], v[116:117] op_sel:[1,0]
	v_add_u32_e32 v122, 0x810, v134
	v_pk_mul_f32 v[114:115], v[114:115], v[124:125]
	v_pk_mul_f32 v[104:105], s[0:1], v[104:105] op_sel_hi:[0,1]
	v_cvt_pk_f16_f32 v114, v114, v115
	v_pack_b32_f16 v116, v123, v114
	v_fma_mixlo_f16 v115, v117, v126, 0
	v_ashrrev_i32_e32 v123, 31, v122
	v_alignbit_b32 v117, v115, v114, 16
	v_lshlrev_b64 v[114:115], 3, v[122:123]
	v_lshl_add_u64 v[122:123], v[136:137], 0, v[114:115]
	global_store_dwordx2 v[122:123], v[116:117], off
	v_or_b32_e32 v116, 4, v130
	v_ashrrev_i32_e32 v117, 31, v116
	v_lshlrev_b64 v[116:117], 15, v[116:117]
	v_lshl_add_u64 v[116:117], s[2:3], 0, v[116:117]
	v_pk_mul_f32 v[102:103], s[0:1], v[102:103] op_sel_hi:[0,1]
	v_cvt_pk_f16_f32 v105, v104, v105
	v_cvt_pk_f16_f32 v104, v102, v103
	v_lshl_add_u64 v[102:103], v[116:117], 0, v[118:119]
	global_store_dwordx2 v[102:103], v[104:105], off
	v_pk_mul_f32 v[102:103], s[0:1], v[106:107] op_sel_hi:[0,1]
	v_mul_f32_e32 v104, 0xbfb8aa3b, v102
	v_exp_f32_e32 v106, v104
	v_mul_f32_e32 v104, 0xbfb8aa3b, v103
	v_exp_f32_e32 v107, v104
	v_pk_mul_f32 v[104:105], s[0:1], v[108:109] op_sel_hi:[0,1]
	v_add_f32_e32 v106, 1.0, v106
	v_rcp_f32_e32 v108, v106
	v_add_f32_e32 v106, 1.0, v107
	v_mul_f32_e32 v107, 0xbfb8aa3b, v104
	v_exp_f32_e32 v107, v107
	v_mul_f32_e32 v109, 0xbfb8aa3b, v105
	v_exp_f32_e32 v109, v109
	v_rcp_f32_e32 v106, v106
	v_add_f32_e32 v107, 1.0, v107
	v_rcp_f32_e32 v107, v107
	v_add_f32_e32 v109, 1.0, v109
	v_rcp_f32_e32 v109, v109
	v_fma_mixlo_f16 v108, v102, v108, 0
	v_pk_mov_b32 v[102:103], v[102:103], v[104:105] op_sel:[1,0]
	v_pk_mul_f32 v[98:99], s[0:1], v[98:99] op_sel_hi:[0,1]
	v_pk_mul_f32 v[102:103], v[102:103], v[106:107]
	v_fma_mixlo_f16 v104, v105, v109, 0
	v_cvt_pk_f16_f32 v103, v102, v103
	v_pack_b32_f16 v102, v108, v103
	v_alignbit_b32 v103, v104, v103, 16
	v_lshl_add_u64 v[104:105], v[116:117], 0, v[120:121]
	global_store_dwordx2 v[104:105], v[102:103], off
	v_mul_f32_e32 v102, 0xbfb8aa3b, v98
	v_exp_f32_e32 v102, v102
	v_mul_f32_e32 v103, 0xbfb8aa3b, v99
	v_exp_f32_e32 v103, v103
	v_pk_mul_f32 v[100:101], s[0:1], v[100:101] op_sel_hi:[0,1]
	v_add_f32_e32 v102, 1.0, v102
	v_rcp_f32_e32 v104, v102
	v_add_f32_e32 v102, 1.0, v103
	v_mul_f32_e32 v103, 0xbfb8aa3b, v100
	v_exp_f32_e32 v103, v103
	v_mul_f32_e32 v105, 0xbfb8aa3b, v101
	v_exp_f32_e32 v105, v105
	v_rcp_f32_e32 v102, v102
	v_add_f32_e32 v103, 1.0, v103
	v_rcp_f32_e32 v103, v103
	v_add_f32_e32 v105, 1.0, v105
	v_rcp_f32_e32 v105, v105
	v_fma_mixlo_f16 v104, v98, v104, 0
	v_pk_mov_b32 v[98:99], v[98:99], v[100:101] op_sel:[1,0]
	v_pk_mul_f32 v[88:89], s[0:1], v[88:89] op_sel_hi:[0,1]
	v_pk_mul_f32 v[98:99], v[98:99], v[102:103]
	v_fma_mixlo_f16 v100, v101, v105, 0
	v_cvt_pk_f16_f32 v99, v98, v99
	v_pack_b32_f16 v98, v104, v99
	v_alignbit_b32 v99, v100, v99, 16
	v_lshl_add_u64 v[100:101], v[116:117], 0, v[114:115]
	global_store_dwordx2 v[100:101], v[98:99], off
	v_or_b32_e32 v98, 8, v130
	v_ashrrev_i32_e32 v99, 31, v98
	v_lshlrev_b64 v[98:99], 15, v[98:99]
	v_lshl_add_u64 v[98:99], s[2:3], 0, v[98:99]
	v_pk_mul_f32 v[86:87], s[0:1], v[86:87] op_sel_hi:[0,1]
	v_cvt_pk_f16_f32 v89, v88, v89
	v_cvt_pk_f16_f32 v88, v86, v87
	v_lshl_add_u64 v[86:87], v[98:99], 0, v[118:119]
	global_store_dwordx2 v[86:87], v[88:89], off
	v_pk_mul_f32 v[86:87], s[0:1], v[90:91] op_sel_hi:[0,1]
	v_mul_f32_e32 v88, 0xbfb8aa3b, v86
	v_exp_f32_e32 v90, v88
	v_mul_f32_e32 v88, 0xbfb8aa3b, v87
	v_exp_f32_e32 v91, v88
	v_pk_mul_f32 v[88:89], s[0:1], v[92:93] op_sel_hi:[0,1]
	v_add_f32_e32 v90, 1.0, v90
	v_rcp_f32_e32 v92, v90
	v_add_f32_e32 v90, 1.0, v91
	v_mul_f32_e32 v91, 0xbfb8aa3b, v88
	v_exp_f32_e32 v91, v91
	v_mul_f32_e32 v93, 0xbfb8aa3b, v89
	v_exp_f32_e32 v93, v93
	v_rcp_f32_e32 v90, v90
	v_add_f32_e32 v91, 1.0, v91
	v_rcp_f32_e32 v91, v91
	v_add_f32_e32 v93, 1.0, v93
	v_rcp_f32_e32 v93, v93
	v_fma_mixlo_f16 v92, v86, v92, 0
	v_pk_mov_b32 v[86:87], v[86:87], v[88:89] op_sel:[1,0]
	v_pk_mul_f32 v[112:113], s[0:1], v[112:113] op_sel_hi:[0,1]
	v_pk_mul_f32 v[86:87], v[86:87], v[90:91]
	v_pk_mul_f32 v[110:111], s[0:1], v[110:111] op_sel_hi:[0,1]
	v_cvt_pk_f16_f32 v87, v86, v87
	v_fma_mixlo_f16 v88, v89, v93, 0
	v_cvt_pk_f16_f32 v113, v112, v113
	v_cvt_pk_f16_f32 v112, v110, v111
	v_lshl_add_u64 v[110:111], v[116:117], 0, v[0:1]
	v_pack_b32_f16 v86, v92, v87
	v_alignbit_b32 v87, v88, v87, 16
	v_lshl_add_u64 v[88:89], v[98:99], 0, v[120:121]
	v_pk_mul_f32 v[82:83], s[0:1], v[82:83] op_sel_hi:[0,1]
	global_store_dwordx2 v[110:111], v[112:113], off
	global_store_dwordx2 v[88:89], v[86:87], off
	v_mul_f32_e32 v86, 0xbfb8aa3b, v82
	v_exp_f32_e32 v86, v86
	v_mul_f32_e32 v87, 0xbfb8aa3b, v83
	v_exp_f32_e32 v87, v87
	v_pk_mul_f32 v[84:85], s[0:1], v[84:85] op_sel_hi:[0,1]
	v_add_f32_e32 v86, 1.0, v86
	v_rcp_f32_e32 v88, v86
	v_add_f32_e32 v86, 1.0, v87
	v_mul_f32_e32 v87, 0xbfb8aa3b, v84
	v_exp_f32_e32 v87, v87
	v_mul_f32_e32 v89, 0xbfb8aa3b, v85
	v_exp_f32_e32 v89, v89
	v_rcp_f32_e32 v86, v86
	v_add_f32_e32 v87, 1.0, v87
	v_rcp_f32_e32 v87, v87
	v_add_f32_e32 v89, 1.0, v89
	v_rcp_f32_e32 v89, v89
	v_fma_mixlo_f16 v88, v82, v88, 0
	v_pk_mov_b32 v[82:83], v[82:83], v[84:85] op_sel:[1,0]
	v_pk_mul_f32 v[72:73], s[0:1], v[72:73] op_sel_hi:[0,1]
	v_pk_mul_f32 v[82:83], v[82:83], v[86:87]
	v_fma_mixlo_f16 v84, v85, v89, 0
	v_cvt_pk_f16_f32 v83, v82, v83
	v_pack_b32_f16 v82, v88, v83
	v_alignbit_b32 v83, v84, v83, 16
	v_lshl_add_u64 v[84:85], v[98:99], 0, v[114:115]
	global_store_dwordx2 v[84:85], v[82:83], off
	v_or_b32_e32 v82, 12, v130
	v_ashrrev_i32_e32 v83, 31, v82
	v_lshlrev_b64 v[82:83], 15, v[82:83]
	v_lshl_add_u64 v[82:83], s[2:3], 0, v[82:83]
	v_pk_mul_f32 v[70:71], s[0:1], v[70:71] op_sel_hi:[0,1]
	v_cvt_pk_f16_f32 v73, v72, v73
	v_cvt_pk_f16_f32 v72, v70, v71
	v_lshl_add_u64 v[70:71], v[82:83], 0, v[118:119]
	global_store_dwordx2 v[70:71], v[72:73], off
	v_pk_mul_f32 v[70:71], s[0:1], v[74:75] op_sel_hi:[0,1]
	v_mul_f32_e32 v72, 0xbfb8aa3b, v70
	v_exp_f32_e32 v74, v72
	v_mul_f32_e32 v72, 0xbfb8aa3b, v71
	v_exp_f32_e32 v75, v72
	v_pk_mul_f32 v[72:73], s[0:1], v[76:77] op_sel_hi:[0,1]
	v_add_f32_e32 v74, 1.0, v74
	v_rcp_f32_e32 v76, v74
	v_add_f32_e32 v74, 1.0, v75
	v_mul_f32_e32 v75, 0xbfb8aa3b, v72
	v_exp_f32_e32 v75, v75
	v_mul_f32_e32 v77, 0xbfb8aa3b, v73
	v_exp_f32_e32 v77, v77
	v_rcp_f32_e32 v74, v74
	v_add_f32_e32 v75, 1.0, v75
	v_rcp_f32_e32 v75, v75
	v_add_f32_e32 v77, 1.0, v77
	v_rcp_f32_e32 v77, v77
	v_fma_mixlo_f16 v76, v70, v76, 0
	v_pk_mov_b32 v[70:71], v[70:71], v[72:73] op_sel:[1,0]
	v_pk_mul_f32 v[96:97], s[0:1], v[96:97] op_sel_hi:[0,1]
	v_pk_mul_f32 v[70:71], v[70:71], v[74:75]
	v_pk_mul_f32 v[94:95], s[0:1], v[94:95] op_sel_hi:[0,1]
	v_cvt_pk_f16_f32 v71, v70, v71
	v_fma_mixlo_f16 v72, v73, v77, 0
	v_cvt_pk_f16_f32 v97, v96, v97
	v_cvt_pk_f16_f32 v96, v94, v95
	v_lshl_add_u64 v[94:95], v[98:99], 0, v[0:1]
	v_pack_b32_f16 v70, v76, v71
	v_alignbit_b32 v71, v72, v71, 16
	v_lshl_add_u64 v[72:73], v[82:83], 0, v[120:121]
	v_pk_mul_f32 v[66:67], s[0:1], v[66:67] op_sel_hi:[0,1]
	global_store_dwordx2 v[94:95], v[96:97], off
	global_store_dwordx2 v[72:73], v[70:71], off
	v_mul_f32_e32 v70, 0xbfb8aa3b, v66
	v_exp_f32_e32 v70, v70
	v_mul_f32_e32 v71, 0xbfb8aa3b, v67
	v_exp_f32_e32 v71, v71
	v_pk_mul_f32 v[68:69], s[0:1], v[68:69] op_sel_hi:[0,1]
	v_add_f32_e32 v70, 1.0, v70
	v_rcp_f32_e32 v72, v70
	v_add_f32_e32 v70, 1.0, v71
	v_mul_f32_e32 v71, 0xbfb8aa3b, v68
	v_exp_f32_e32 v71, v71
	v_mul_f32_e32 v73, 0xbfb8aa3b, v69
	v_exp_f32_e32 v73, v73
	v_rcp_f32_e32 v70, v70
	v_add_f32_e32 v71, 1.0, v71
	v_rcp_f32_e32 v71, v71
	v_add_f32_e32 v73, 1.0, v73
	v_rcp_f32_e32 v73, v73
	v_fma_mixlo_f16 v72, v66, v72, 0
	v_pk_mov_b32 v[66:67], v[66:67], v[68:69] op_sel:[1,0]
	v_pk_mul_f32 v[60:61], s[0:1], v[60:61] op_sel_hi:[0,1]
	v_pk_mul_f32 v[66:67], v[66:67], v[70:71]
	v_fma_mixlo_f16 v68, v69, v73, 0
	v_cvt_pk_f16_f32 v67, v66, v67
	v_pack_b32_f16 v66, v72, v67
	v_alignbit_b32 v67, v68, v67, 16
	v_lshl_add_u64 v[68:69], v[82:83], 0, v[114:115]
	global_store_dwordx2 v[68:69], v[66:67], off
	v_add_u32_e32 v66, 0x80, v132
	v_ashrrev_i32_e32 v66, 2, v66
	v_ashrrev_i32_e32 v67, 31, v66
	v_lshlrev_b64 v[66:67], 15, v[66:67]
	v_lshl_add_u64 v[66:67], s[2:3], 0, v[66:67]
	v_pk_mul_f32 v[58:59], s[0:1], v[58:59] op_sel_hi:[0,1]
	v_cvt_pk_f16_f32 v61, v60, v61
	v_cvt_pk_f16_f32 v60, v58, v59
	v_lshl_add_u64 v[58:59], v[66:67], 0, v[118:119]
	v_pk_mul_f32 v[54:55], s[0:1], v[54:55] op_sel_hi:[0,1]
	global_store_dwordx2 v[58:59], v[60:61], off
	v_mul_f32_e32 v58, 0xbfb8aa3b, v54
	v_exp_f32_e32 v58, v58
	v_mul_f32_e32 v59, 0xbfb8aa3b, v55
	v_exp_f32_e32 v59, v59
	v_pk_mul_f32 v[56:57], s[0:1], v[56:57] op_sel_hi:[0,1]
	v_add_f32_e32 v58, 1.0, v58
	v_rcp_f32_e32 v60, v58
	v_add_f32_e32 v58, 1.0, v59
	v_mul_f32_e32 v59, 0xbfb8aa3b, v56
	v_exp_f32_e32 v59, v59
	v_mul_f32_e32 v61, 0xbfb8aa3b, v57
	v_exp_f32_e32 v61, v61
	v_rcp_f32_e32 v58, v58
	v_add_f32_e32 v59, 1.0, v59
	v_rcp_f32_e32 v59, v59
	v_add_f32_e32 v61, 1.0, v61
	v_rcp_f32_e32 v61, v61
	v_fma_mixlo_f16 v60, v54, v60, 0
	v_pk_mov_b32 v[54:55], v[54:55], v[56:57] op_sel:[1,0]
	v_pk_mul_f32 v[80:81], s[0:1], v[80:81] op_sel_hi:[0,1]
	v_pk_mul_f32 v[54:55], v[54:55], v[58:59]
	v_pk_mul_f32 v[78:79], s[0:1], v[78:79] op_sel_hi:[0,1]
	v_cvt_pk_f16_f32 v55, v54, v55
	v_fma_mixlo_f16 v56, v57, v61, 0
	v_cvt_pk_f16_f32 v81, v80, v81
	v_cvt_pk_f16_f32 v80, v78, v79
	v_lshl_add_u64 v[78:79], v[82:83], 0, v[0:1]
	v_pack_b32_f16 v54, v60, v55
	v_alignbit_b32 v55, v56, v55, 16
	v_lshl_add_u64 v[56:57], v[66:67], 0, v[120:121]
	v_pk_mul_f32 v[50:51], s[0:1], v[50:51] op_sel_hi:[0,1]
	global_store_dwordx2 v[78:79], v[80:81], off
	global_store_dwordx2 v[56:57], v[54:55], off
	v_mul_f32_e32 v54, 0xbfb8aa3b, v50
	v_exp_f32_e32 v54, v54
	v_mul_f32_e32 v55, 0xbfb8aa3b, v51
	v_exp_f32_e32 v55, v55
	v_pk_mul_f32 v[52:53], s[0:1], v[52:53] op_sel_hi:[0,1]
	v_add_f32_e32 v54, 1.0, v54
	v_rcp_f32_e32 v56, v54
	v_add_f32_e32 v54, 1.0, v55
	v_mul_f32_e32 v55, 0xbfb8aa3b, v52
	v_exp_f32_e32 v55, v55
	v_mul_f32_e32 v57, 0xbfb8aa3b, v53
	v_exp_f32_e32 v57, v57
	v_rcp_f32_e32 v54, v54
	v_add_f32_e32 v55, 1.0, v55
	v_rcp_f32_e32 v55, v55
	v_add_f32_e32 v57, 1.0, v57
	v_rcp_f32_e32 v57, v57
	v_fma_mixlo_f16 v56, v50, v56, 0
	v_pk_mov_b32 v[50:51], v[50:51], v[52:53] op_sel:[1,0]
	v_pk_mul_f32 v[44:45], s[0:1], v[44:45] op_sel_hi:[0,1]
	v_pk_mul_f32 v[50:51], v[50:51], v[54:55]
	v_fma_mixlo_f16 v52, v53, v57, 0
	v_cvt_pk_f16_f32 v51, v50, v51
	v_pack_b32_f16 v50, v56, v51
	v_alignbit_b32 v51, v52, v51, 16
	v_lshl_add_u64 v[52:53], v[66:67], 0, v[114:115]
	global_store_dwordx2 v[52:53], v[50:51], off
	v_add_u32_e32 v50, 0x90, v132
	v_ashrrev_i32_e32 v50, 2, v50
	v_ashrrev_i32_e32 v51, 31, v50
	v_lshlrev_b64 v[50:51], 15, v[50:51]
	v_lshl_add_u64 v[50:51], s[2:3], 0, v[50:51]
	v_pk_mul_f32 v[42:43], s[0:1], v[42:43] op_sel_hi:[0,1]
	v_cvt_pk_f16_f32 v45, v44, v45
	v_cvt_pk_f16_f32 v44, v42, v43
	v_lshl_add_u64 v[42:43], v[50:51], 0, v[118:119]
	v_pk_mul_f32 v[38:39], s[0:1], v[38:39] op_sel_hi:[0,1]
	global_store_dwordx2 v[42:43], v[44:45], off
	v_mul_f32_e32 v42, 0xbfb8aa3b, v38
	v_exp_f32_e32 v42, v42
	v_mul_f32_e32 v43, 0xbfb8aa3b, v39
	v_exp_f32_e32 v43, v43
	v_pk_mul_f32 v[40:41], s[0:1], v[40:41] op_sel_hi:[0,1]
	v_add_f32_e32 v42, 1.0, v42
	v_rcp_f32_e32 v44, v42
	v_add_f32_e32 v42, 1.0, v43
	v_mul_f32_e32 v43, 0xbfb8aa3b, v40
	v_exp_f32_e32 v43, v43
	v_mul_f32_e32 v45, 0xbfb8aa3b, v41
	v_exp_f32_e32 v45, v45
	v_rcp_f32_e32 v42, v42
	v_add_f32_e32 v43, 1.0, v43
	v_rcp_f32_e32 v43, v43
	v_add_f32_e32 v45, 1.0, v45
	v_rcp_f32_e32 v45, v45
	v_fma_mixlo_f16 v44, v38, v44, 0
	v_pk_mov_b32 v[38:39], v[38:39], v[40:41] op_sel:[1,0]
	v_pk_mul_f32 v[64:65], s[0:1], v[64:65] op_sel_hi:[0,1]
	v_pk_mul_f32 v[38:39], v[38:39], v[42:43]
	v_pk_mul_f32 v[62:63], s[0:1], v[62:63] op_sel_hi:[0,1]
	v_cvt_pk_f16_f32 v39, v38, v39
	v_fma_mixlo_f16 v40, v41, v45, 0
	v_cvt_pk_f16_f32 v65, v64, v65
	v_cvt_pk_f16_f32 v64, v62, v63
	v_lshl_add_u64 v[62:63], v[66:67], 0, v[0:1]
	v_pack_b32_f16 v38, v44, v39
	v_alignbit_b32 v39, v40, v39, 16
	v_lshl_add_u64 v[40:41], v[50:51], 0, v[120:121]
	v_pk_mul_f32 v[34:35], s[0:1], v[34:35] op_sel_hi:[0,1]
	global_store_dwordx2 v[62:63], v[64:65], off
	global_store_dwordx2 v[40:41], v[38:39], off
	v_mul_f32_e32 v38, 0xbfb8aa3b, v34
	v_exp_f32_e32 v38, v38
	v_mul_f32_e32 v39, 0xbfb8aa3b, v35
	v_exp_f32_e32 v39, v39
	v_pk_mul_f32 v[36:37], s[0:1], v[36:37] op_sel_hi:[0,1]
	v_add_f32_e32 v38, 1.0, v38
	v_rcp_f32_e32 v40, v38
	v_add_f32_e32 v38, 1.0, v39
	v_mul_f32_e32 v39, 0xbfb8aa3b, v36
	v_exp_f32_e32 v39, v39
	v_mul_f32_e32 v41, 0xbfb8aa3b, v37
	v_exp_f32_e32 v41, v41
	v_rcp_f32_e32 v38, v38
	v_add_f32_e32 v39, 1.0, v39
	v_rcp_f32_e32 v39, v39
	v_add_f32_e32 v41, 1.0, v41
	v_rcp_f32_e32 v41, v41
	v_fma_mixlo_f16 v40, v34, v40, 0
	v_pk_mov_b32 v[34:35], v[34:35], v[36:37] op_sel:[1,0]
	v_pk_mul_f32 v[28:29], s[0:1], v[28:29] op_sel_hi:[0,1]
	v_pk_mul_f32 v[34:35], v[34:35], v[38:39]
	v_fma_mixlo_f16 v36, v37, v41, 0
	v_cvt_pk_f16_f32 v35, v34, v35
	v_pack_b32_f16 v34, v40, v35
	v_alignbit_b32 v35, v36, v35, 16
	v_lshl_add_u64 v[36:37], v[50:51], 0, v[114:115]
	global_store_dwordx2 v[36:37], v[34:35], off
	v_add_u32_e32 v34, 0xa0, v132
	v_ashrrev_i32_e32 v34, 2, v34
	v_ashrrev_i32_e32 v35, 31, v34
	v_lshlrev_b64 v[34:35], 15, v[34:35]
	v_lshl_add_u64 v[34:35], s[2:3], 0, v[34:35]
	v_pk_mul_f32 v[26:27], s[0:1], v[26:27] op_sel_hi:[0,1]
	v_cvt_pk_f16_f32 v29, v28, v29
	v_cvt_pk_f16_f32 v28, v26, v27
	v_lshl_add_u64 v[26:27], v[34:35], 0, v[118:119]
	v_pk_mul_f32 v[22:23], s[0:1], v[22:23] op_sel_hi:[0,1]
	global_store_dwordx2 v[26:27], v[28:29], off
	v_mul_f32_e32 v26, 0xbfb8aa3b, v22
	v_exp_f32_e32 v26, v26
	v_mul_f32_e32 v27, 0xbfb8aa3b, v23
	v_exp_f32_e32 v27, v27
	v_pk_mul_f32 v[24:25], s[0:1], v[24:25] op_sel_hi:[0,1]
	v_add_f32_e32 v26, 1.0, v26
	v_rcp_f32_e32 v28, v26
	v_add_f32_e32 v26, 1.0, v27
	v_mul_f32_e32 v27, 0xbfb8aa3b, v24
	v_exp_f32_e32 v27, v27
	v_mul_f32_e32 v29, 0xbfb8aa3b, v25
	v_exp_f32_e32 v29, v29
	v_rcp_f32_e32 v26, v26
	v_add_f32_e32 v27, 1.0, v27
	v_rcp_f32_e32 v27, v27
	v_add_f32_e32 v29, 1.0, v29
	v_rcp_f32_e32 v29, v29
	v_fma_mixlo_f16 v28, v22, v28, 0
	v_pk_mov_b32 v[22:23], v[22:23], v[24:25] op_sel:[1,0]
	v_pk_mul_f32 v[48:49], s[0:1], v[48:49] op_sel_hi:[0,1]
	v_pk_mul_f32 v[22:23], v[22:23], v[26:27]
	v_pk_mul_f32 v[46:47], s[0:1], v[46:47] op_sel_hi:[0,1]
	v_cvt_pk_f16_f32 v23, v22, v23
	v_fma_mixlo_f16 v24, v25, v29, 0
	v_cvt_pk_f16_f32 v49, v48, v49
	v_cvt_pk_f16_f32 v48, v46, v47
	v_lshl_add_u64 v[46:47], v[50:51], 0, v[0:1]
	v_pack_b32_f16 v22, v28, v23
	v_alignbit_b32 v23, v24, v23, 16
	v_lshl_add_u64 v[24:25], v[34:35], 0, v[120:121]
	v_pk_mul_f32 v[18:19], s[0:1], v[18:19] op_sel_hi:[0,1]
	global_store_dwordx2 v[46:47], v[48:49], off
	global_store_dwordx2 v[24:25], v[22:23], off
	v_mul_f32_e32 v22, 0xbfb8aa3b, v18
	v_exp_f32_e32 v22, v22
	v_mul_f32_e32 v23, 0xbfb8aa3b, v19
	v_exp_f32_e32 v23, v23
	v_pk_mul_f32 v[20:21], s[0:1], v[20:21] op_sel_hi:[0,1]
	v_add_f32_e32 v22, 1.0, v22
	v_rcp_f32_e32 v24, v22
	v_add_f32_e32 v22, 1.0, v23
	v_mul_f32_e32 v23, 0xbfb8aa3b, v20
	v_exp_f32_e32 v23, v23
	v_mul_f32_e32 v25, 0xbfb8aa3b, v21
	v_exp_f32_e32 v25, v25
	v_rcp_f32_e32 v22, v22
	v_add_f32_e32 v23, 1.0, v23
	v_rcp_f32_e32 v23, v23
	v_add_f32_e32 v25, 1.0, v25
	v_rcp_f32_e32 v25, v25
	v_fma_mixlo_f16 v24, v18, v24, 0
	v_pk_mov_b32 v[18:19], v[18:19], v[20:21] op_sel:[1,0]
	v_pk_mul_f32 v[32:33], s[0:1], v[32:33] op_sel_hi:[0,1]
	v_pk_mul_f32 v[18:19], v[18:19], v[22:23]
	v_fma_mixlo_f16 v20, v21, v25, 0
	v_cvt_pk_f16_f32 v19, v18, v19
	v_pack_b32_f16 v18, v24, v19
	v_alignbit_b32 v19, v20, v19, 16
	v_lshl_add_u64 v[20:21], v[34:35], 0, v[114:115]
	global_store_dwordx2 v[20:21], v[18:19], off
	v_add_u32_e32 v18, 0xb0, v132
	v_ashrrev_i32_e32 v18, 2, v18
	v_ashrrev_i32_e32 v19, 31, v18
	v_lshlrev_b64 v[18:19], 15, v[18:19]
	v_pk_mul_f32 v[30:31], s[0:1], v[30:31] op_sel_hi:[0,1]
	v_lshl_add_u64 v[18:19], s[2:3], 0, v[18:19]
	v_pk_mul_f32 v[16:17], s[0:1], v[16:17] op_sel_hi:[0,1]
	v_pk_mul_f32 v[14:15], s[0:1], v[14:15] op_sel_hi:[0,1]
	v_cvt_pk_f16_f32 v33, v32, v33
	v_cvt_pk_f16_f32 v32, v30, v31
	v_lshl_add_u64 v[30:31], v[34:35], 0, v[0:1]
	v_cvt_pk_f16_f32 v17, v16, v17
	v_cvt_pk_f16_f32 v16, v14, v15
	v_lshl_add_u64 v[0:1], v[18:19], 0, v[0:1]
	global_store_dwordx2 v[0:1], v[16:17], off
	v_pk_mul_f32 v[0:1], s[0:1], v[12:13] op_sel_hi:[0,1]
	v_pk_mul_f32 v[10:11], s[0:1], v[10:11] op_sel_hi:[0,1]
	v_cvt_pk_f16_f32 v1, v0, v1
	v_cvt_pk_f16_f32 v0, v10, v11
	v_lshl_add_u64 v[10:11], v[18:19], 0, v[118:119]
	global_store_dwordx2 v[10:11], v[0:1], off
	v_pk_mul_f32 v[0:1], s[0:1], v[6:7] op_sel_hi:[0,1]
	v_mul_f32_e32 v6, 0xbfb8aa3b, v0
	v_exp_f32_e32 v10, v6
	v_mul_f32_e32 v6, 0xbfb8aa3b, v1
	v_exp_f32_e32 v11, v6
	v_pk_mul_f32 v[6:7], s[0:1], v[8:9] op_sel_hi:[0,1]
	v_add_f32_e32 v8, 1.0, v10
	v_mul_f32_e32 v9, 0xbfb8aa3b, v6
	v_rcp_f32_e32 v10, v8
	v_add_f32_e32 v8, 1.0, v11
	v_exp_f32_e32 v9, v9
	v_mul_f32_e32 v11, 0xbfb8aa3b, v7
	v_exp_f32_e32 v11, v11
	v_rcp_f32_e32 v8, v8
	v_add_f32_e32 v9, 1.0, v9
	v_rcp_f32_e32 v9, v9
	v_add_f32_e32 v11, 1.0, v11
	v_rcp_f32_e32 v11, v11
	v_fma_mixlo_f16 v10, v0, v10, 0
	v_pk_mov_b32 v[0:1], v[0:1], v[6:7] op_sel:[1,0]
	global_store_dwordx2 v[30:31], v[32:33], off
	v_pk_mul_f32 v[0:1], v[0:1], v[8:9]
	v_fma_mixlo_f16 v6, v7, v11, 0
	v_cvt_pk_f16_f32 v1, v0, v1
	v_pack_b32_f16 v0, v10, v1
	v_alignbit_b32 v1, v6, v1, 16
	v_lshl_add_u64 v[6:7], v[18:19], 0, v[120:121]
	global_store_dwordx2 v[6:7], v[0:1], off
	v_pk_mul_f32 v[0:1], s[0:1], v[2:3] op_sel_hi:[0,1]
	v_mul_f32_e32 v2, 0xbfb8aa3b, v0
	v_exp_f32_e32 v6, v2
	v_mul_f32_e32 v2, 0xbfb8aa3b, v1
	v_exp_f32_e32 v7, v2
	v_pk_mul_f32 v[2:3], s[0:1], v[4:5] op_sel_hi:[0,1]
	v_add_f32_e32 v4, 1.0, v6
	v_mul_f32_e32 v5, 0xbfb8aa3b, v2
	v_rcp_f32_e32 v6, v4
	v_add_f32_e32 v4, 1.0, v7
	v_exp_f32_e32 v5, v5
	v_mul_f32_e32 v7, 0xbfb8aa3b, v3
	v_exp_f32_e32 v7, v7
	v_rcp_f32_e32 v4, v4
	v_add_f32_e32 v5, 1.0, v5
	v_rcp_f32_e32 v5, v5
	v_add_f32_e32 v7, 1.0, v7
	v_rcp_f32_e32 v7, v7
	v_fma_mixlo_f16 v6, v0, v6, 0
	v_pk_mov_b32 v[0:1], v[0:1], v[2:3] op_sel:[1,0]
	v_fma_mixlo_f16 v2, v3, v7, 0
	v_pk_mul_f32 v[0:1], v[0:1], v[4:5]
	s_nop 0
	v_cvt_pk_f16_f32 v1, v0, v1
	v_pack_b32_f16 v0, v6, v1
	v_alignbit_b32 v1, v2, v1, 16
	v_lshl_add_u64 v[2:3], v[18:19], 0, v[114:115]
	global_store_dwordx2 v[2:3], v[0:1], off
	s_endpgm
	.p2alignl 8, 3212836864

_Z11gemm_8phaseILi2ELi16ELi4ELi512ELi2048ELi1024ELi4EEvPKDF16_S1_PvS2_fPj:
	s_and_b32 s3, s2, 7
	s_lshr_b32 s4, s2, 3
	s_and_b32 s9, s4, 3
	s_lshl_b32 s3, s3, 2
	s_add_i32 s3, s3, s9
	s_lshl_b32 s33, s3, 7
	s_lshr_b32 s4, s4, 2
	s_lshl_b32 s8, s4, 7
	v_lshrrev_b32_e32 v3, 3, v0
	v_and_b32_e32 v4, 48, v3
	v_bfe_u32 v5, v0, 2, 4
	v_and_b32_e32 v2, 32, v0
	v_or_b32_e32 v10, v4, v5
	v_lshlrev_b32_e32 v1, 4, v0
	s_load_dwordx4 s[4:7], s[0:1], 0x0
	v_bitop3_b32 v6, v1, v2, 48 bitop3:0x6c
	v_or_b32_e32 v2, s8, v10
	v_ashrrev_i32_e32 v3, 31, v2
	v_mov_b32_e32 v131, 0
	v_lshlrev_b64 v[8:9], 12, v[2:3]
	v_or_b32_e32 v2, s33, v10
	v_mov_b32_e32 v3, v131
	v_and_b32_e32 v7, 64, v0
	v_lshlrev_b64 v[2:3], 12, v[2:3]
	s_add_i32 s22, 0, 0x10000
	v_or_b32_e32 v130, v6, v7
	s_waitcnt lgkmcnt(0)
	v_lshl_add_u64 v[2:3], s[4:5], 0, v[2:3]
	v_add_u32_e32 v145, s22, v1
	s_mov_b32 s21, 0
	v_lshl_add_u64 v[2:3], v[2:3], 0, v[130:131]
	s_mov_b32 s20, 0
	v_readfirstlane_b32 s10, v145
	v_add_u32_e32 v146, 0x2000, v145
	v_lshl_add_u64 v[8:9], s[6:7], 0, v[8:9]
	v_lshl_add_u64 v[2:3], v[2:3], 0, s[20:21]
	s_mov_b32 m0, s10
	s_mov_b64 s[10:11], 0x40000
	v_readfirstlane_b32 s12, v146
	v_lshl_add_u64 v[8:9], v[8:9], 0, v[130:131]
	v_add_u32_e32 v142, 0, v1
	global_load_lds_dwordx4 v[2:3], off
	v_lshl_add_u64 v[10:11], v[2:3], 0, s[10:11]
	s_mov_b32 m0, s12
	v_lshl_add_u64 v[132:133], v[8:9], 0, s[20:21]
	v_readfirstlane_b32 s12, v142
	v_add_u32_e32 v147, 0x2000, v142
	s_add_i32 s21, 0, 0x14000
	global_load_lds_dwordx4 v[10:11], off
	s_mov_b32 m0, s12
	v_lshl_add_u64 v[8:9], v[132:133], 0, s[10:11]
	v_readfirstlane_b32 s10, v147
	v_add_u32_e32 v150, s21, v1
	global_load_lds_dwordx4 v[132:133], off
	s_mov_b32 m0, s10
	s_mov_b64 s[10:11], 0x800
	v_readfirstlane_b32 s12, v150
	v_add_u32_e32 v152, 0x2000, v150
	global_load_lds_dwordx4 v[8:9], off
	v_lshl_add_u64 v[8:9], v[2:3], 0, s[10:11]
	s_mov_b32 m0, s12
	s_mov_b64 s[12:13], 0x40800
	v_readfirstlane_b32 s16, v152
	global_load_lds_dwordx4 v[8:9], off
	v_lshl_add_u64 v[8:9], v[2:3], 0, s[12:13]
	s_mov_b32 m0, s16
	v_add_u32_e32 v153, 0x4000, v142
	global_load_lds_dwordx4 v[8:9], off
	v_lshl_add_u64 v[8:9], v[132:133], 0, s[10:11]
	v_readfirstlane_b32 s10, v153
	v_add_u32_e32 v154, 0x6000, v142
	s_mov_b32 m0, s10
	v_readfirstlane_b32 s10, v154
	global_load_lds_dwordx4 v[8:9], off
	v_lshl_add_u64 v[8:9], v[132:133], 0, s[12:13]
	s_mov_b32 m0, s10
	global_load_lds_dwordx4 v[8:9], off
	v_lshrrev_b32_e32 v8, 8, v0
	v_cmp_eq_u32_e32 vcc, 1, v8
	s_and_saveexec_b64 s[10:11], vcc
	s_cbranch_execz .LBB7_2
	s_barrier
.LBB7_2:
	s_or_b64 exec, exec, s[10:11]
	s_add_i32 s23, 0, 0x18000
	v_add_u32_e32 v155, s23, v1
	s_mov_b64 s[16:17], 0x80
	v_readfirstlane_b32 s18, v155
	v_add_u32_e32 v156, 0x2000, v155
	v_lshl_add_u64 v[10:11], v[2:3], 0, s[16:17]
	s_mov_b32 m0, s18
	s_mov_b64 s[18:19], 0x40080
	v_readfirstlane_b32 s24, v156
	s_waitcnt vmcnt(4)
	s_barrier
	global_load_lds_dwordx4 v[10:11], off
	v_lshl_add_u64 v[10:11], v[2:3], 0, s[18:19]
	s_mov_b32 m0, s24
	v_add_u32_e32 v157, 0x8000, v142
	global_load_lds_dwordx4 v[10:11], off
	v_lshl_add_u64 v[10:11], v[132:133], 0, s[16:17]
	v_readfirstlane_b32 s16, v157
	v_add_u32_e32 v158, 0xa000, v142
	s_add_i32 s24, 0, 0x1c000
	s_mov_b32 m0, s16
	v_readfirstlane_b32 s16, v158
	v_add_u32_e32 v159, s24, v1
	global_load_lds_dwordx4 v[10:11], off
	v_lshl_add_u64 v[10:11], v[132:133], 0, s[18:19]
	s_mov_b32 m0, s16
	s_mov_b64 s[16:17], 0x880
	v_readfirstlane_b32 s18, v159
	v_add_u32_e32 v161, 0x2000, v159
	global_load_lds_dwordx4 v[10:11], off
	v_lshl_add_u64 v[10:11], v[2:3], 0, s[16:17]
	s_mov_b32 m0, s18
	s_mov_b64 s[18:19], 0x40880
	v_readfirstlane_b32 s25, v161
	global_load_lds_dwordx4 v[10:11], off
	v_lshl_add_u64 v[2:3], v[2:3], 0, s[18:19]
	s_mov_b32 m0, s25
	v_lshlrev_b32_e32 v10, 2, v0
	global_load_lds_dwordx4 v[2:3], off
	v_lshlrev_b32_e32 v3, 6, v0
	v_and_b32_e32 v2, 48, v0
	v_and_b32_e32 v3, 0x3c0, v3
	v_and_b32_e32 v10, 32, v10
	v_bitop3_b32 v2, v3, v10, v2 bitop3:0x36
	v_add_u32_e32 v10, s22, v2
	v_add_u32_e32 v11, s21, v2
	v_add_u32_e32 v12, s23, v2
	v_add_u32_e32 v13, s24, v2
	v_add_u32_e32 v14, 0, v2
	v_add3_u32 v2, s33, v4, v5
	v_mov_b32_e32 v3, v131
	s_add_u32 s4, s4, s20
	v_lshlrev_b64 v[2:3], 12, v[2:3]
	s_addc_u32 s5, s5, 0
	v_lshl_add_u64 v[134:135], s[4:5], 0, v[2:3]
	v_add3_u32 v2, s8, v4, v5
	s_load_dwordx2 s[10:11], s[0:1], 0x10
	v_bfe_u32 v143, v0, 6, 2
	s_waitcnt vmcnt(6)
	v_lshlrev_b32_e32 v148, 6, v8
	v_lshlrev_b32_e32 v8, 13, v8
	v_ashrrev_i32_e32 v3, 31, v2
	s_add_u32 s4, s6, s20
	v_lshlrev_b32_e32 v9, 12, v143
	v_or_b32_e32 v15, 0x800, v8
	v_or_b32_e32 v16, 0x1000, v8
	v_or_b32_e32 v17, 0x1800, v8
	v_lshlrev_b64 v[2:3], 12, v[2:3]
	s_addc_u32 s5, s7, 0
	v_add_u32_e32 v130, v6, v7
	v_lshl_add_u64 v[136:137], s[4:5], 0, v[2:3]
	s_mov_b32 s3, -2
	v_add_u32_e32 v162, v10, v9
	v_add_u32_e32 v141, v14, v8
	v_add_u32_e32 v140, v14, v15
	v_add_u32_e32 v139, v14, v16
	v_add_u32_e32 v138, v14, v17
	v_add_u32_e32 v160, v11, v9
	s_mov_b64 s[4:5], 0x100
	s_mov_b64 s[6:7], 0x40100
	s_mov_b64 s[20:21], 0x900
	s_mov_b64 s[22:23], 0x40900
	v_add_u32_e32 v151, v12, v9
	v_add_u32_e32 v144, v13, v9
	s_mov_b64 s[24:25], 0x180
	s_mov_b64 s[26:27], 0x40180
	s_mov_b64 s[28:29], 0x980
	s_mov_b64 s[30:31], 0x40980
	v_mov_b32_e32 v2, v131
	v_mov_b32_e32 v3, v131
	v_mov_b32_e32 v4, v131
	v_mov_b32_e32 v5, v131
	v_mov_b32_e32 v6, v131
	v_mov_b32_e32 v7, v131
	v_mov_b32_e32 v8, v131
	v_mov_b32_e32 v9, v131
	v_mov_b32_e32 v10, v131
	v_mov_b32_e32 v11, v131
	v_mov_b32_e32 v12, v131
	v_mov_b32_e32 v13, v131
	v_mov_b32_e32 v14, v131
	v_mov_b32_e32 v15, v131
	v_mov_b32_e32 v16, v131
	v_mov_b32_e32 v17, v131
	v_mov_b32_e32 v18, v131
	v_mov_b32_e32 v19, v131
	v_mov_b32_e32 v20, v131
	v_mov_b32_e32 v21, v131
	v_mov_b32_e32 v22, v131
	v_mov_b32_e32 v23, v131
	v_mov_b32_e32 v24, v131
	v_mov_b32_e32 v25, v131
	v_mov_b32_e32 v26, v131
	v_mov_b32_e32 v27, v131
	v_mov_b32_e32 v28, v131
	v_mov_b32_e32 v29, v131
	v_mov_b32_e32 v30, v131
	v_mov_b32_e32 v31, v131
	v_mov_b32_e32 v32, v131
	v_mov_b32_e32 v33, v131
	v_mov_b32_e32 v34, v131
	v_mov_b32_e32 v35, v131
	v_mov_b32_e32 v36, v131
	v_mov_b32_e32 v37, v131
	v_mov_b32_e32 v38, v131
	v_mov_b32_e32 v39, v131
	v_mov_b32_e32 v40, v131
	v_mov_b32_e32 v41, v131
	v_mov_b32_e32 v42, v131
	v_mov_b32_e32 v43, v131
	v_mov_b32_e32 v44, v131
	v_mov_b32_e32 v45, v131
	v_mov_b32_e32 v46, v131
	v_mov_b32_e32 v47, v131
	v_mov_b32_e32 v48, v131
	v_mov_b32_e32 v49, v131
	v_mov_b32_e32 v50, v131
	v_mov_b32_e32 v51, v131
	v_mov_b32_e32 v52, v131
	v_mov_b32_e32 v53, v131
	v_mov_b32_e32 v54, v131
	v_mov_b32_e32 v55, v131
	v_mov_b32_e32 v56, v131
	v_mov_b32_e32 v57, v131
	v_mov_b32_e32 v58, v131
	v_mov_b32_e32 v59, v131
	v_mov_b32_e32 v60, v131
	v_mov_b32_e32 v61, v131
	v_mov_b32_e32 v62, v131
	v_mov_b32_e32 v63, v131
	v_mov_b32_e32 v64, v131
	v_mov_b32_e32 v65, v131
	v_mov_b32_e32 v66, v131
	v_mov_b32_e32 v67, v131
	v_mov_b32_e32 v68, v131
	v_mov_b32_e32 v69, v131
	v_mov_b32_e32 v70, v131
	v_mov_b32_e32 v71, v131
	v_mov_b32_e32 v72, v131
	v_mov_b32_e32 v73, v131
	v_mov_b32_e32 v74, v131
	v_mov_b32_e32 v75, v131
	v_mov_b32_e32 v76, v131
	v_mov_b32_e32 v77, v131
	v_mov_b32_e32 v78, v131
	v_mov_b32_e32 v79, v131
	v_mov_b32_e32 v80, v131
	v_mov_b32_e32 v81, v131
	v_mov_b32_e32 v82, v131
	v_mov_b32_e32 v83, v131
	v_mov_b32_e32 v84, v131
	v_mov_b32_e32 v85, v131
	v_mov_b32_e32 v86, v131
	v_mov_b32_e32 v87, v131
	v_mov_b32_e32 v88, v131
	v_mov_b32_e32 v89, v131
	v_mov_b32_e32 v90, v131
	v_mov_b32_e32 v91, v131
	v_mov_b32_e32 v92, v131
	v_mov_b32_e32 v93, v131
	v_mov_b32_e32 v94, v131
	v_mov_b32_e32 v95, v131
	v_mov_b32_e32 v96, v131
	v_mov_b32_e32 v97, v131
	v_mov_b32_e32 v98, v131
	v_mov_b32_e32 v99, v131
	v_mov_b32_e32 v100, v131
	v_mov_b32_e32 v101, v131
	v_mov_b32_e32 v102, v131
	v_mov_b32_e32 v103, v131
	v_mov_b32_e32 v104, v131
	v_mov_b32_e32 v105, v131
	v_mov_b32_e32 v106, v131
	v_mov_b32_e32 v107, v131
	v_mov_b32_e32 v108, v131
	v_mov_b32_e32 v109, v131
	v_mov_b32_e32 v110, v131
	v_mov_b32_e32 v111, v131
	v_mov_b32_e32 v112, v131
	v_mov_b32_e32 v113, v131
	v_mov_b32_e32 v114, v131
	v_mov_b32_e32 v115, v131
	v_mov_b32_e32 v116, v131
	v_mov_b32_e32 v117, v131
	v_mov_b32_e32 v118, v131
	v_mov_b32_e32 v119, v131
	v_mov_b32_e32 v120, v131
	v_mov_b32_e32 v121, v131
	v_mov_b32_e32 v122, v131
	v_mov_b32_e32 v123, v131
	v_mov_b32_e32 v124, v131
	v_mov_b32_e32 v125, v131
	v_mov_b32_e32 v126, v131
	v_mov_b32_e32 v127, v131
	v_mov_b32_e32 v128, v131
	v_mov_b32_e32 v129, v131
	v_and_b32_e32 v149, 15, v0
	v_add_u32_e32 v163, 0xc000, v142
	v_add_u32_e32 v164, 0xe000, v142
	s_barrier
.LBB7_3:
	ds_read_b128 v[166:169], v162
	ds_read_b128 v[170:173], v162 offset:1024
	ds_read_b128 v[174:177], v162 offset:2048
	ds_read_b128 v[178:181], v162 offset:3072
	v_lshl_add_u64 v[230:231], v[136:137], 0, v[130:131]
	v_readfirstlane_b32 s9, v163
	v_lshl_add_u64 v[182:183], v[230:231], 0, s[16:17]
	s_mov_b32 m0, s9
	v_readfirstlane_b32 s9, v164
	global_load_lds_dwordx4 v[182:183], off
	v_lshl_add_u64 v[182:183], v[230:231], 0, s[18:19]
	s_mov_b32 m0, s9
	s_nop 0
	global_load_lds_dwordx4 v[182:183], off
	ds_read_b128 v[182:185], v141
	ds_read_b128 v[186:189], v141 offset:1024
	ds_read_b128 v[190:193], v140
	ds_read_b128 v[194:197], v140 offset:1024
	ds_read_b128 v[198:201], v139
	ds_read_b128 v[202:205], v139 offset:1024
	ds_read_b128 v[206:209], v138
	ds_read_b128 v[210:213], v138 offset:1024
	s_waitcnt lgkmcnt(8)
	s_barrier
	s_waitcnt lgkmcnt(0)
	s_setprio 1
	s_waitcnt lgkmcnt(0)
	v_mfma_f32_16x16x32_f16 v[126:129], v[182:185], v[166:169], v[126:129]
	v_mfma_f32_16x16x32_f16 v[122:125], v[182:185], v[174:177], v[122:125]
	v_mfma_f32_16x16x32_f16 v[118:121], v[190:193], v[166:169], v[118:121]
	v_mfma_f32_16x16x32_f16 v[114:117], v[190:193], v[174:177], v[114:117]
	v_mfma_f32_16x16x32_f16 v[110:113], v[198:201], v[166:169], v[110:113]
	v_mfma_f32_16x16x32_f16 v[106:109], v[198:201], v[174:177], v[106:109]
	v_mfma_f32_16x16x32_f16 v[102:105], v[206:209], v[166:169], v[102:105]
	v_mfma_f32_16x16x32_f16 v[98:101], v[206:209], v[174:177], v[98:101]
	v_mfma_f32_16x16x32_f16 v[126:129], v[186:189], v[170:173], v[126:129]
	v_mfma_f32_16x16x32_f16 v[122:125], v[186:189], v[178:181], v[122:125]
	v_mfma_f32_16x16x32_f16 v[118:121], v[194:197], v[170:173], v[118:121]
	v_mfma_f32_16x16x32_f16 v[114:117], v[194:197], v[178:181], v[114:117]
	v_mfma_f32_16x16x32_f16 v[110:113], v[202:205], v[170:173], v[110:113]
	v_mfma_f32_16x16x32_f16 v[106:109], v[202:205], v[178:181], v[106:109]
	v_mfma_f32_16x16x32_f16 v[102:105], v[210:213], v[170:173], v[102:105]
	v_mfma_f32_16x16x32_f16 v[98:101], v[210:213], v[178:181], v[98:101]
	s_setprio 0
	s_barrier
	v_lshl_add_u64 v[232:233], v[134:135], 0, v[130:131]
	v_readfirstlane_b32 s9, v145
	v_lshl_add_u64 v[234:235], v[232:233], 0, s[4:5]
	s_mov_b32 m0, s9
	v_readfirstlane_b32 s9, v146
	ds_read_b128 v[214:217], v160
	ds_read_b128 v[218:221], v160 offset:1024
	ds_read_b128 v[222:225], v160 offset:2048
	ds_read_b128 v[226:229], v160 offset:3072
	global_load_lds_dwordx4 v[234:235], off
	v_lshl_add_u64 v[234:235], v[232:233], 0, s[6:7]
	s_mov_b32 m0, s9
	s_nop 0
	global_load_lds_dwordx4 v[234:235], off
	s_barrier
	s_waitcnt lgkmcnt(0)
	s_setprio 1
	s_waitcnt lgkmcnt(0)
	s_setprio 0
	v_readfirstlane_b32 s9, v142
	v_lshl_add_u64 v[234:235], v[230:231], 0, s[4:5]
	s_mov_b32 m0, s9
	v_readfirstlane_b32 s9, v147
	s_barrier
	ds_read_b128 v[182:185], v141 offset:16384
	ds_read_b128 v[186:189], v141 offset:17408
	ds_read_b128 v[190:193], v140 offset:16384
	ds_read_b128 v[194:197], v140 offset:17408
	ds_read_b128 v[198:201], v139 offset:16384
	ds_read_b128 v[202:205], v139 offset:17408
	ds_read_b128 v[206:209], v138 offset:16384
	ds_read_b128 v[210:213], v138 offset:17408
	global_load_lds_dwordx4 v[234:235], off
	v_lshl_add_u64 v[234:235], v[230:231], 0, s[6:7]
	s_mov_b32 m0, s9
	s_nop 0
	global_load_lds_dwordx4 v[234:235], off
	s_barrier
	s_waitcnt lgkmcnt(0)
	s_setprio 1
	s_waitcnt lgkmcnt(0)
	s_setprio 0
	s_barrier
	v_readfirstlane_b32 s9, v150
	v_lshl_add_u64 v[166:167], v[232:233], 0, s[20:21]
	s_mov_b32 m0, s9
	v_readfirstlane_b32 s9, v152
	global_load_lds_dwordx4 v[166:167], off
	v_lshl_add_u64 v[166:167], v[232:233], 0, s[22:23]
	s_mov_b32 m0, s9
	s_nop 0
	global_load_lds_dwordx4 v[166:167], off
	s_waitcnt vmcnt(6)
	s_barrier
	s_setprio 1
	v_mfma_f32_16x16x32_f16 v[30:33], v[182:185], v[214:217], v[30:33]
	v_mfma_f32_16x16x32_f16 v[26:29], v[182:185], v[222:225], v[26:29]
	v_mfma_f32_16x16x32_f16 v[22:25], v[190:193], v[214:217], v[22:25]
	v_mfma_f32_16x16x32_f16 v[18:21], v[190:193], v[222:225], v[18:21]
	v_mfma_f32_16x16x32_f16 v[14:17], v[198:201], v[214:217], v[14:17]
	v_mfma_f32_16x16x32_f16 v[10:13], v[198:201], v[222:225], v[10:13]
	v_mfma_f32_16x16x32_f16 v[6:9], v[206:209], v[214:217], v[6:9]
	v_mfma_f32_16x16x32_f16 v[2:5], v[206:209], v[222:225], v[2:5]
	v_mfma_f32_16x16x32_f16 v[30:33], v[186:189], v[218:221], v[30:33]
	v_mfma_f32_16x16x32_f16 v[26:29], v[186:189], v[226:229], v[26:29]
	v_mfma_f32_16x16x32_f16 v[22:25], v[194:197], v[218:221], v[22:25]
	v_mfma_f32_16x16x32_f16 v[18:21], v[194:197], v[226:229], v[18:21]
	v_mfma_f32_16x16x32_f16 v[14:17], v[202:205], v[218:221], v[14:17]
	v_mfma_f32_16x16x32_f16 v[10:13], v[202:205], v[226:229], v[10:13]
	v_mfma_f32_16x16x32_f16 v[6:9], v[210:213], v[218:221], v[6:9]
	v_mfma_f32_16x16x32_f16 v[2:5], v[210:213], v[226:229], v[2:5]
	s_setprio 0
	s_barrier
	ds_read_b128 v[166:169], v151
	ds_read_b128 v[170:173], v151 offset:1024
	ds_read_b128 v[174:177], v151 offset:2048
	ds_read_b128 v[178:181], v151 offset:3072
	v_readfirstlane_b32 s9, v153
	v_lshl_add_u64 v[214:215], v[230:231], 0, s[20:21]
	s_mov_b32 m0, s9
	v_readfirstlane_b32 s9, v154
	ds_read_b128 v[182:185], v141 offset:32768
	ds_read_b128 v[186:189], v141 offset:33792
	ds_read_b128 v[190:193], v140 offset:32768
	ds_read_b128 v[194:197], v140 offset:33792
	ds_read_b128 v[198:201], v139 offset:32768
	ds_read_b128 v[202:205], v139 offset:33792
	ds_read_b128 v[206:209], v138 offset:32768
	ds_read_b128 v[210:213], v138 offset:33792
	global_load_lds_dwordx4 v[214:215], off
	v_lshl_add_u64 v[214:215], v[230:231], 0, s[22:23]
	s_mov_b32 m0, s9
	s_nop 0
	global_load_lds_dwordx4 v[214:215], off
	s_waitcnt lgkmcnt(8)
	s_barrier
	s_waitcnt lgkmcnt(0)
	s_setprio 1
	s_waitcnt lgkmcnt(0)
	v_mfma_f32_16x16x32_f16 v[126:129], v[182:185], v[166:169], v[126:129]
	v_mfma_f32_16x16x32_f16 v[122:125], v[182:185], v[174:177], v[122:125]
	v_mfma_f32_16x16x32_f16 v[118:121], v[190:193], v[166:169], v[118:121]
	v_mfma_f32_16x16x32_f16 v[114:117], v[190:193], v[174:177], v[114:117]
	v_mfma_f32_16x16x32_f16 v[110:113], v[198:201], v[166:169], v[110:113]
	v_mfma_f32_16x16x32_f16 v[106:109], v[198:201], v[174:177], v[106:109]
	v_mfma_f32_16x16x32_f16 v[102:105], v[206:209], v[166:169], v[102:105]
	v_mfma_f32_16x16x32_f16 v[98:101], v[206:209], v[174:177], v[98:101]
	v_mfma_f32_16x16x32_f16 v[126:129], v[186:189], v[170:173], v[126:129]
	v_mfma_f32_16x16x32_f16 v[122:125], v[186:189], v[178:181], v[122:125]
	v_mfma_f32_16x16x32_f16 v[118:121], v[194:197], v[170:173], v[118:121]
	v_mfma_f32_16x16x32_f16 v[114:117], v[194:197], v[178:181], v[114:117]
	v_mfma_f32_16x16x32_f16 v[110:113], v[202:205], v[170:173], v[110:113]
	v_mfma_f32_16x16x32_f16 v[106:109], v[202:205], v[178:181], v[106:109]
	v_mfma_f32_16x16x32_f16 v[102:105], v[210:213], v[170:173], v[102:105]
	v_mfma_f32_16x16x32_f16 v[98:101], v[210:213], v[178:181], v[98:101]
	s_setprio 0
	s_barrier
	v_readfirstlane_b32 s9, v155
	v_lshl_add_u64 v[234:235], v[232:233], 0, s[24:25]
	s_mov_b32 m0, s9
	v_readfirstlane_b32 s9, v156
	ds_read_b128 v[214:217], v144
	ds_read_b128 v[218:221], v144 offset:1024
	ds_read_b128 v[222:225], v144 offset:2048
	ds_read_b128 v[226:229], v144 offset:3072
	global_load_lds_dwordx4 v[234:235], off
	v_lshl_add_u64 v[234:235], v[232:233], 0, s[26:27]
	s_mov_b32 m0, s9
	s_nop 0
	global_load_lds_dwordx4 v[234:235], off
	s_barrier
	s_waitcnt lgkmcnt(0)
	s_setprio 1
	s_waitcnt lgkmcnt(0)
	s_setprio 0
	v_readfirstlane_b32 s9, v157
	v_lshl_add_u64 v[234:235], v[230:231], 0, s[24:25]
	s_mov_b32 m0, s9
	v_readfirstlane_b32 s9, v158
	s_barrier
	ds_read_b128 v[182:185], v141 offset:49152
	ds_read_b128 v[186:189], v141 offset:50176
	ds_read_b128 v[190:193], v140 offset:49152
	ds_read_b128 v[194:197], v140 offset:50176
	ds_read_b128 v[198:201], v139 offset:49152
	ds_read_b128 v[202:205], v139 offset:50176
	ds_read_b128 v[206:209], v138 offset:49152
	ds_read_b128 v[210:213], v138 offset:50176
	global_load_lds_dwordx4 v[234:235], off
	v_lshl_add_u64 v[230:231], v[230:231], 0, s[26:27]
	s_mov_b32 m0, s9
	s_nop 0
	global_load_lds_dwordx4 v[230:231], off
	s_barrier
	s_waitcnt lgkmcnt(0)
	s_setprio 1
	s_waitcnt lgkmcnt(0)
	s_setprio 0
	s_barrier
	v_readfirstlane_b32 s9, v159
	v_lshl_add_u64 v[166:167], v[232:233], 0, s[28:29]
	s_mov_b32 m0, s9
	v_readfirstlane_b32 s9, v161
	global_load_lds_dwordx4 v[166:167], off
	v_lshl_add_u64 v[166:167], v[232:233], 0, s[30:31]
	s_mov_b32 m0, s9
	s_nop 0
	global_load_lds_dwordx4 v[166:167], off
	s_waitcnt vmcnt(6)
	s_barrier
	s_setprio 1
	v_mfma_f32_16x16x32_f16 v[30:33], v[182:185], v[214:217], v[30:33]
	v_mfma_f32_16x16x32_f16 v[26:29], v[182:185], v[222:225], v[26:29]
	v_mfma_f32_16x16x32_f16 v[22:25], v[190:193], v[214:217], v[22:25]
	v_mfma_f32_16x16x32_f16 v[18:21], v[190:193], v[222:225], v[18:21]
	v_mfma_f32_16x16x32_f16 v[14:17], v[198:201], v[214:217], v[14:17]
	v_mfma_f32_16x16x32_f16 v[10:13], v[198:201], v[222:225], v[10:13]
	v_mfma_f32_16x16x32_f16 v[6:9], v[206:209], v[214:217], v[6:9]
	v_mfma_f32_16x16x32_f16 v[2:5], v[206:209], v[222:225], v[2:5]
	v_mfma_f32_16x16x32_f16 v[30:33], v[186:189], v[218:221], v[30:33]
	v_mfma_f32_16x16x32_f16 v[26:29], v[186:189], v[226:229], v[26:29]
	v_mfma_f32_16x16x32_f16 v[22:25], v[194:197], v[218:221], v[22:25]
	v_mfma_f32_16x16x32_f16 v[18:21], v[194:197], v[226:229], v[18:21]
	v_mfma_f32_16x16x32_f16 v[14:17], v[202:205], v[218:221], v[14:17]
	v_mfma_f32_16x16x32_f16 v[10:13], v[202:205], v[226:229], v[10:13]
	v_mfma_f32_16x16x32_f16 v[6:9], v[210:213], v[218:221], v[6:9]
	v_mfma_f32_16x16x32_f16 v[2:5], v[210:213], v[226:229], v[2:5]
	s_setprio 0
	s_add_i32 s3, s3, 2
	v_lshl_add_u64 v[134:135], v[134:135], 0, s[4:5]
	s_cmp_lt_u32 s3, 12
	v_lshl_add_u64 v[136:137], v[136:137], 0, s[4:5]
	s_barrier
	s_cbranch_scc1 .LBB7_3
	v_cmp_gt_u32_e32 vcc, 0x100, v0
	s_and_saveexec_b64 s[4:5], vcc
	s_cbranch_execz .Lop_deskew
	s_barrier
.Lop_deskew:
	s_or_b64 exec, exec, s[4:5]
	v_lshl_add_u64 v[230:231], v[136:137], 0, v[130:131]
	v_readfirstlane_b32 s9, v163
	v_lshl_add_u64 v[182:183], v[230:231], 0, s[16:17]
	s_mov_b32 m0, s9
	v_readfirstlane_b32 s9, v164
	global_load_lds_dwordx4 v[182:183], off
	v_lshl_add_u64 v[182:183], v[230:231], 0, s[18:19]
	s_mov_b32 m0, s9
	s_nop 0
	global_load_lds_dwordx4 v[182:183], off
	ds_read_b128 v[166:169], v162
	ds_read_b128 v[170:173], v162 offset:1024
	ds_read_b128 v[174:177], v162 offset:2048
	ds_read_b128 v[178:181], v162 offset:3072
	ds_read_b128 v[182:185], v141
	ds_read_b128 v[186:189], v141 offset:1024
	ds_read_b128 v[190:193], v140
	ds_read_b128 v[194:197], v140 offset:1024
	ds_read_b128 v[198:201], v139
	ds_read_b128 v[202:205], v139 offset:1024
	ds_read_b128 v[206:209], v138
	ds_read_b128 v[210:213], v138 offset:1024
	s_waitcnt lgkmcnt(0)
	v_mfma_f32_16x16x32_f16 v[126:129], v[182:185], v[166:169], v[126:129]
	v_mfma_f32_16x16x32_f16 v[122:125], v[182:185], v[174:177], v[122:125]
	v_mfma_f32_16x16x32_f16 v[118:121], v[190:193], v[166:169], v[118:121]
	v_mfma_f32_16x16x32_f16 v[114:117], v[190:193], v[174:177], v[114:117]
	v_mfma_f32_16x16x32_f16 v[110:113], v[198:201], v[166:169], v[110:113]
	v_mfma_f32_16x16x32_f16 v[106:109], v[198:201], v[174:177], v[106:109]
	v_mfma_f32_16x16x32_f16 v[102:105], v[206:209], v[166:169], v[102:105]
	v_mfma_f32_16x16x32_f16 v[98:101], v[206:209], v[174:177], v[98:101]
	v_mfma_f32_16x16x32_f16 v[126:129], v[186:189], v[170:173], v[126:129]
	v_mfma_f32_16x16x32_f16 v[122:125], v[186:189], v[178:181], v[122:125]
	v_mfma_f32_16x16x32_f16 v[118:121], v[194:197], v[170:173], v[118:121]
	v_mfma_f32_16x16x32_f16 v[114:117], v[194:197], v[178:181], v[114:117]
	v_mfma_f32_16x16x32_f16 v[110:113], v[202:205], v[170:173], v[110:113]
	v_mfma_f32_16x16x32_f16 v[106:109], v[202:205], v[178:181], v[106:109]
	v_mfma_f32_16x16x32_f16 v[102:105], v[210:213], v[170:173], v[102:105]
	v_mfma_f32_16x16x32_f16 v[98:101], v[210:213], v[178:181], v[98:101]
	s_nop 7
	ds_read_b128 v[214:217], v160
	ds_read_b128 v[218:221], v160 offset:1024
	ds_read_b128 v[222:225], v160 offset:2048
	ds_read_b128 v[226:229], v160 offset:3072
	ds_read_b128 v[182:185], v141 offset:16384
	ds_read_b128 v[186:189], v141 offset:17408
	ds_read_b128 v[190:193], v140 offset:16384
	ds_read_b128 v[194:197], v140 offset:17408
	ds_read_b128 v[198:201], v139 offset:16384
	ds_read_b128 v[202:205], v139 offset:17408
	ds_read_b128 v[206:209], v138 offset:16384
	ds_read_b128 v[210:213], v138 offset:17408
	s_waitcnt lgkmcnt(0)
	v_mfma_f32_16x16x32_f16 v[30:33], v[182:185], v[214:217], v[30:33]
	v_mfma_f32_16x16x32_f16 v[26:29], v[182:185], v[222:225], v[26:29]
	v_mfma_f32_16x16x32_f16 v[22:25], v[190:193], v[214:217], v[22:25]
	v_mfma_f32_16x16x32_f16 v[18:21], v[190:193], v[222:225], v[18:21]
	v_mfma_f32_16x16x32_f16 v[14:17], v[198:201], v[214:217], v[14:17]
	v_mfma_f32_16x16x32_f16 v[10:13], v[198:201], v[222:225], v[10:13]
	v_mfma_f32_16x16x32_f16 v[6:9], v[206:209], v[214:217], v[6:9]
	v_mfma_f32_16x16x32_f16 v[2:5], v[206:209], v[222:225], v[2:5]
	v_mfma_f32_16x16x32_f16 v[30:33], v[186:189], v[218:221], v[30:33]
	v_mfma_f32_16x16x32_f16 v[26:29], v[186:189], v[226:229], v[26:29]
	v_mfma_f32_16x16x32_f16 v[22:25], v[194:197], v[218:221], v[22:25]
	v_mfma_f32_16x16x32_f16 v[18:21], v[194:197], v[226:229], v[18:21]
	v_mfma_f32_16x16x32_f16 v[14:17], v[202:205], v[218:221], v[14:17]
	v_mfma_f32_16x16x32_f16 v[10:13], v[202:205], v[226:229], v[10:13]
	v_mfma_f32_16x16x32_f16 v[6:9], v[210:213], v[218:221], v[6:9]
	v_mfma_f32_16x16x32_f16 v[2:5], v[210:213], v[226:229], v[2:5]
	s_nop 7
	s_waitcnt vmcnt(0)
	s_barrier
	ds_read_b128 v[166:169], v151
	ds_read_b128 v[170:173], v151 offset:1024
	ds_read_b128 v[174:177], v151 offset:2048
	ds_read_b128 v[178:181], v151 offset:3072
	ds_read_b128 v[182:185], v141 offset:32768
	ds_read_b128 v[186:189], v141 offset:33792
	ds_read_b128 v[190:193], v140 offset:32768
	ds_read_b128 v[194:197], v140 offset:33792
	ds_read_b128 v[198:201], v139 offset:32768
	ds_read_b128 v[202:205], v139 offset:33792
	ds_read_b128 v[206:209], v138 offset:32768
	ds_read_b128 v[210:213], v138 offset:33792
	s_waitcnt lgkmcnt(0)
	v_mfma_f32_16x16x32_f16 v[126:129], v[182:185], v[166:169], v[126:129]
	v_mfma_f32_16x16x32_f16 v[122:125], v[182:185], v[174:177], v[122:125]
	v_mfma_f32_16x16x32_f16 v[118:121], v[190:193], v[166:169], v[118:121]
	v_mfma_f32_16x16x32_f16 v[114:117], v[190:193], v[174:177], v[114:117]
	v_mfma_f32_16x16x32_f16 v[110:113], v[198:201], v[166:169], v[110:113]
	v_mfma_f32_16x16x32_f16 v[106:109], v[198:201], v[174:177], v[106:109]
	v_mfma_f32_16x16x32_f16 v[102:105], v[206:209], v[166:169], v[102:105]
	v_mfma_f32_16x16x32_f16 v[98:101], v[206:209], v[174:177], v[98:101]
	v_mfma_f32_16x16x32_f16 v[126:129], v[186:189], v[170:173], v[126:129]
	v_mfma_f32_16x16x32_f16 v[122:125], v[186:189], v[178:181], v[122:125]
	v_mfma_f32_16x16x32_f16 v[118:121], v[194:197], v[170:173], v[118:121]
	v_mfma_f32_16x16x32_f16 v[114:117], v[194:197], v[178:181], v[114:117]
	v_mfma_f32_16x16x32_f16 v[110:113], v[202:205], v[170:173], v[110:113]
	v_mfma_f32_16x16x32_f16 v[106:109], v[202:205], v[178:181], v[106:109]
	v_mfma_f32_16x16x32_f16 v[102:105], v[210:213], v[170:173], v[102:105]
	v_mfma_f32_16x16x32_f16 v[98:101], v[210:213], v[178:181], v[98:101]
	s_nop 7
	ds_read_b128 v[214:217], v144
	ds_read_b128 v[218:221], v144 offset:1024
	ds_read_b128 v[222:225], v144 offset:2048
	ds_read_b128 v[226:229], v144 offset:3072
	ds_read_b128 v[182:185], v141 offset:49152
	ds_read_b128 v[186:189], v141 offset:50176
	ds_read_b128 v[190:193], v140 offset:49152
	ds_read_b128 v[194:197], v140 offset:50176
	ds_read_b128 v[198:201], v139 offset:49152
	ds_read_b128 v[202:205], v139 offset:50176
	ds_read_b128 v[206:209], v138 offset:49152
	ds_read_b128 v[210:213], v138 offset:50176
	s_waitcnt lgkmcnt(0)
	v_mfma_f32_16x16x32_f16 v[30:33], v[182:185], v[214:217], v[30:33]
	v_mfma_f32_16x16x32_f16 v[26:29], v[182:185], v[222:225], v[26:29]
	v_mfma_f32_16x16x32_f16 v[22:25], v[190:193], v[214:217], v[22:25]
	v_mfma_f32_16x16x32_f16 v[18:21], v[190:193], v[222:225], v[18:21]
	v_mfma_f32_16x16x32_f16 v[14:17], v[198:201], v[214:217], v[14:17]
	v_mfma_f32_16x16x32_f16 v[10:13], v[198:201], v[222:225], v[10:13]
	v_mfma_f32_16x16x32_f16 v[6:9], v[206:209], v[214:217], v[6:9]
	v_mfma_f32_16x16x32_f16 v[2:5], v[206:209], v[222:225], v[2:5]
	v_mfma_f32_16x16x32_f16 v[30:33], v[186:189], v[218:221], v[30:33]
	v_mfma_f32_16x16x32_f16 v[26:29], v[186:189], v[226:229], v[26:29]
	v_mfma_f32_16x16x32_f16 v[22:25], v[194:197], v[218:221], v[22:25]
	v_mfma_f32_16x16x32_f16 v[18:21], v[194:197], v[226:229], v[18:21]
	v_mfma_f32_16x16x32_f16 v[14:17], v[202:205], v[218:221], v[14:17]
	v_mfma_f32_16x16x32_f16 v[10:13], v[202:205], v[226:229], v[10:13]
	v_mfma_f32_16x16x32_f16 v[6:9], v[210:213], v[218:221], v[6:9]
	v_mfma_f32_16x16x32_f16 v[2:5], v[210:213], v[226:229], v[2:5]
	s_load_dword s20, s[0:1], 0x20
	s_load_dwordx2 s[10:11], s[0:1], 0x10
	v_and_b32_e32 v130, 15, v0
	v_bfe_u32 v131, v0, 6, 2
	v_lshl_add_u32 v130, v131, 5, v130
	v_add_u32_e32 v130, s33, v130
	v_bfe_u32 v131, v0, 4, 2
	v_lshrrev_b32_e32 v132, 8, v0
	v_lshlrev_b32_e32 v131, 2, v131
	v_lshl_add_u32 v131, v132, 6, v131
	v_add_u32_e32 v131, s8, v131
	v_lshlrev_b32_e32 v131, 2, v131
	v_lshl_add_u32 v130, v130, 12, v131
	v_mov_b32_e32 v131, 0
	s_mov_b64 s[4:5], 0x10000
	s_waitcnt lgkmcnt(0)
	v_lshl_add_u64 v[130:131], s[10:11], 0, v[130:131]
	v_lshl_add_u64 v[132:133], v[130:131], 0, s[4:5]
	s_nop 7
	s_nop 7
	v_pk_add_f32 v[126:127], v[126:127], v[30:31]
	v_pk_add_f32 v[128:129], v[128:129], v[32:33]
	v_pk_mul_f32 v[126:127], v[126:127], s[20:21] op_sel_hi:[1,0]
	v_pk_mul_f32 v[128:129], v[128:129], s[20:21] op_sel_hi:[1,0]
	global_store_dwordx4 v[130:131], v[126:129], off nt
	v_pk_add_f32 v[122:123], v[122:123], v[26:27]
	v_pk_add_f32 v[124:125], v[124:125], v[28:29]
	v_pk_mul_f32 v[122:123], v[122:123], s[20:21] op_sel_hi:[1,0]
	v_pk_mul_f32 v[124:125], v[124:125], s[20:21] op_sel_hi:[1,0]
	global_store_dwordx4 v[132:133], v[122:125], off nt
	v_pk_add_f32 v[118:119], v[118:119], v[22:23]
	v_pk_add_f32 v[120:121], v[120:121], v[24:25]
	v_pk_mul_f32 v[118:119], v[118:119], s[20:21] op_sel_hi:[1,0]
	v_pk_mul_f32 v[120:121], v[120:121], s[20:21] op_sel_hi:[1,0]
	global_store_dwordx4 v[130:131], v[118:121], off offset:64 nt
	v_pk_add_f32 v[114:115], v[114:115], v[18:19]
	v_pk_add_f32 v[116:117], v[116:117], v[20:21]
	v_pk_mul_f32 v[114:115], v[114:115], s[20:21] op_sel_hi:[1,0]
	v_pk_mul_f32 v[116:117], v[116:117], s[20:21] op_sel_hi:[1,0]
	global_store_dwordx4 v[132:133], v[114:117], off offset:64 nt
	v_pk_add_f32 v[110:111], v[110:111], v[14:15]
	v_pk_add_f32 v[112:113], v[112:113], v[16:17]
	v_pk_mul_f32 v[110:111], v[110:111], s[20:21] op_sel_hi:[1,0]
	v_pk_mul_f32 v[112:113], v[112:113], s[20:21] op_sel_hi:[1,0]
	global_store_dwordx4 v[130:131], v[110:113], off offset:128 nt
	v_pk_add_f32 v[106:107], v[106:107], v[10:11]
	v_pk_add_f32 v[108:109], v[108:109], v[12:13]
	v_pk_mul_f32 v[106:107], v[106:107], s[20:21] op_sel_hi:[1,0]
	v_pk_mul_f32 v[108:109], v[108:109], s[20:21] op_sel_hi:[1,0]
	global_store_dwordx4 v[132:133], v[106:109], off offset:128 nt
	v_pk_add_f32 v[102:103], v[102:103], v[6:7]
	v_pk_add_f32 v[104:105], v[104:105], v[8:9]
	v_pk_mul_f32 v[102:103], v[102:103], s[20:21] op_sel_hi:[1,0]
	v_pk_mul_f32 v[104:105], v[104:105], s[20:21] op_sel_hi:[1,0]
	global_store_dwordx4 v[130:131], v[102:105], off offset:192 nt
	v_pk_add_f32 v[98:99], v[98:99], v[2:3]
	v_pk_add_f32 v[100:101], v[100:101], v[4:5]
	v_pk_mul_f32 v[98:99], v[98:99], s[20:21] op_sel_hi:[1,0]
	v_pk_mul_f32 v[100:101], v[100:101], s[20:21] op_sel_hi:[1,0]
	global_store_dwordx4 v[132:133], v[98:101], off offset:192 nt
	s_endpgm
	.p2alignl 8, 3212836864
